# routing: per-token expert rank via one 64-bit integer compare per expert on unique (score, index) keys instead of a scalar readlane/compare/mask loop
# speedup vs baseline: 1.0357x; 1.0102x over previous
; #define LAS __attribute__((address_space(3)))
; __device__ __forceinline__ void phase_nrr(const Frame& F, const Args& a, int l, const bf16_t* XA, const float* g, const float* modl, unsigned char* XN8) {
;     ...
;         __syncthreads();
; #pragma unroll
;         for (int rb = 0; rb < 4; ++rb) *(LAS f32x4*)(Pl + (size_t)((kq * 64 + 16 * rb + fr) * NE + 16 * eb + 4 * fq)) = acc[rb];
;         __syncthreads();
;         const float bias = rbias[lane];
; #pragma unroll
;         for (int i = 0; i < 8; ++i) { const int t = tb + i;
;             const float lg = Pl[(w * 8 + i) * NE + lane] + Pl[(64 + w * 8 + i) * NE + lane]; const float sc = 1.f / (1.f + __expf(-lg)); const float bb = sc + bias;
;             float m1 = bb; m1 = fmaxf(m1, __shfl_xor(m1, 1)); m1 = fmaxf(m1, __shfl_xor(m1, 2)); m1 = fmaxf(m1, __shfl_xor(m1, 4));
;             const unsigned long long eq = __ballot(bb == m1); const int gbase = lane & ~7; const unsigned grpmask = (unsigned)((eq >> gbase) & 0xffull);
;             const int first = gbase + __builtin_ctz(grpmask);
;             float m2 = (lane == first) ? -INFINITY : bb; m2 = fmaxf(m2, __shfl_xor(m2, 1)); m2 = fmaxf(m2, __shfl_xor(m2, 2)); m2 = fmaxf(m2, __shfl_xor(m2, 4));
;             const float gsum = m1 + m2; const int gq = lane >> 3;
;             int grank = 0;
; #pragma unroll
;             for (int g2 = 0; g2 < 8; ++g2) { const float v = __int_as_float(__builtin_amdgcn_readlane(__float_as_int(gsum), g2 * 8)); grank += (v > gsum || (v == gsum && g2 < gq)) ? 1 : 0; }
;             const bool keep = grank < 4; const float val = keep ? bb : -INFINITY;
;             int rank = 0;
; #pragma unroll 8
;             for (int e2 = 0; e2 < 64; ++e2) { const float v = __int_as_float(__builtin_amdgcn_readlane(__float_as_int(val), e2)); rank += (v > val || (v == val && e2 < lane)) ? 1 : 0; }
.LBB0_535:
	s_barrier
	ds_write_b128 v242, v[110:113]
	ds_write_b128 v242, v[118:121] offset:4096
	s_nop 0
	ds_write_b128 v242, v[126:129] offset:8192
	s_nop 1
	ds_write_b128 v242, v[130:133] offset:12288
	s_waitcnt lgkmcnt(0)
	s_barrier
	global_load_dword v3, v[198:199], off
	s_waitcnt vmcnt(15)
	v_add_u32_e32 v4, s76, v226
	ds_read2st64_b32 v[6:7], v4 offset1:64
	s_mov_b32 s3, 0
	s_waitcnt lgkmcnt(0)
	v_add_f32_e32 v2, v6, v7
	v_mul_f32_e32 v2, 0xbfb8aa3b, v2
	v_exp_f32_e32 v2, v2
	s_nop 0
	v_add_f32_e32 v2, 1.0, v2
	v_div_scale_f32 v5, s[22:23], v2, v2, 1.0
	v_rcp_f32_e32 v6, v5
	s_nop 0
	v_fma_f32 v7, -v5, v6, 1.0
	v_fmac_f32_e32 v6, v7, v6
	v_div_scale_f32 v7, vcc, 1.0, v2, 1.0
	v_mul_f32_e32 v8, v7, v6
	v_fma_f32 v9, -v5, v8, v7
	v_fmac_f32_e32 v8, v9, v6
	v_fma_f32 v5, -v5, v8, v7
	v_div_fmas_f32 v5, v5, v6, v8
	v_div_fixup_f32 v2, v5, v2, 1.0
	s_waitcnt vmcnt(0)
	v_add_f32_e32 v5, v3, v2
	ds_bpermute_b32 v6, v1, v5
	s_waitcnt lgkmcnt(0)
	v_max_f32_e32 v6, v6, v6
	v_max_f32_e32 v6, v5, v6
	ds_bpermute_b32 v7, v201, v6
	s_waitcnt lgkmcnt(0)
	v_max_f32_e32 v7, v7, v7
	v_max_f32_e32 v6, v6, v7
	ds_bpermute_b32 v7, v220, v6
	s_waitcnt lgkmcnt(0)
	v_max_f32_e32 v7, v7, v7
	v_max_f32_e32 v8, v6, v7
	v_cmp_eq_f32_e32 vcc, v5, v8
	s_nop 1
	v_lshrrev_b64 v[6:7], v200, vcc
	v_ffbl_b32_sdwa v6, v6 dst_sel:DWORD dst_unused:UNUSED_PAD src0_sel:BYTE_0
	v_add_u32_e32 v6, v6, v200
	v_cmp_ne_u32_e32 vcc, v230, v6
	s_nop 1
	v_cndmask_b32_e32 v6, v245, v5, vcc
	ds_bpermute_b32 v7, v1, v6
	s_waitcnt lgkmcnt(0)
	v_max_f32_e32 v7, v7, v7
	v_max_f32_e32 v6, v6, v7
	ds_bpermute_b32 v7, v201, v6
	s_waitcnt lgkmcnt(0)
	v_max_f32_e32 v7, v7, v7
	v_max_f32_e32 v6, v6, v7
	ds_bpermute_b32 v7, v220, v6
	s_waitcnt lgkmcnt(0)
	v_max_f32_e32 v7, v7, v7
	v_max_f32_e32 v6, v6, v7
	v_add_f32_e32 v6, v8, v6
	s_nop 0
	v_readlane_b32 s5, v6, 0
	s_nop 1
	v_cmp_eq_f32_e64 s[22:23], s5, v6
	v_cmp_gt_f32_e32 vcc, s5, v6
	s_and_b64 s[22:23], s[6:7], s[22:23]
	s_or_b64 s[22:23], vcc, s[22:23]
	v_readlane_b32 s5, v6, 8
	v_cndmask_b32_e64 v7, 0, 1, s[22:23]
	s_nop 0
	v_cmp_eq_f32_e64 s[22:23], s5, v6
	v_cmp_gt_f32_e32 vcc, s5, v6
	s_and_b64 s[22:23], s[8:9], s[22:23]
	s_or_b64 s[22:23], vcc, s[22:23]
	v_readlane_b32 s5, v6, 16
	v_cndmask_b32_e64 v8, 0, 1, s[22:23]
	s_nop 0
	v_cmp_eq_f32_e64 s[22:23], s5, v6
	v_cmp_gt_f32_e32 vcc, s5, v6
	s_and_b64 s[22:23], s[10:11], s[22:23]
	s_or_b64 s[22:23], vcc, s[22:23]
	v_readlane_b32 s5, v6, 24
	v_cndmask_b32_e64 v9, 0, 1, s[22:23]
	s_nop 0
	v_cmp_eq_f32_e64 s[22:23], s5, v6
	v_cmp_gt_f32_e32 vcc, s5, v6
	s_and_b64 s[22:23], s[12:13], s[22:23]
	s_or_b64 s[22:23], vcc, s[22:23]
	v_readlane_b32 s5, v6, 32
	v_cndmask_b32_e64 v10, 0, 1, s[22:23]
	s_nop 0
	v_cmp_eq_f32_e64 s[22:23], s5, v6
	v_cmp_gt_f32_e32 vcc, s5, v6
	s_and_b64 s[22:23], s[14:15], s[22:23]
	s_or_b64 s[22:23], vcc, s[22:23]
	v_readlane_b32 s5, v6, 40
	v_cndmask_b32_e64 v11, 0, 1, s[22:23]
	s_nop 0
	v_cmp_eq_f32_e64 s[22:23], s5, v6
	v_cmp_gt_f32_e32 vcc, s5, v6
	s_and_b64 s[22:23], s[16:17], s[22:23]
	s_or_b64 s[22:23], vcc, s[22:23]
	v_readlane_b32 s5, v6, 48
	v_cndmask_b32_e64 v12, 0, 1, s[22:23]
	s_nop 0
	v_cmp_eq_f32_e64 s[22:23], s5, v6
	v_cmp_gt_f32_e32 vcc, s5, v6
	s_and_b64 s[22:23], s[18:19], s[22:23]
	v_readlane_b32 s5, v6, 56
	s_or_b64 s[22:23], vcc, s[22:23]
	v_cndmask_b32_e64 v13, 0, 1, s[22:23]
	v_cmp_gt_f32_e32 vcc, s5, v6
	s_nop 1
	v_cndmask_b32_e64 v6, 0, 1, vcc
	v_add_u32_e32 v6, v8, v6
	v_add3_u32 v6, v6, v7, v9
	v_add3_u32 v6, v6, v10, v11
	v_add3_u32 v6, v6, v12, v13
	v_cmp_gt_u32_e32 vcc, 4, v6
	v_mov_b32_e32 v6, 0
	s_nop 0
	v_cndmask_b32_e32 v5, v245, v5, vcc
	v_ashrrev_i32_e32 v9, 31, v5
	v_sub_u32_e32 v8, 63, v230
	v_and_b32_e32 v9, 0x7fffffff, v9
	v_xor_b32_e32 v9, v5, v9
	s_nop 0
	v_readlane_b32 s25, v9, 0
	s_movk_i32 s24, 63
	v_readlane_b32 s23, v9, 1
	s_movk_i32 s22, 62
	v_cmp_gt_i64_e32 vcc, s[24:25], v[8:9]
	v_readlane_b32 s25, v9, 2
	s_movk_i32 s24, 61
	v_addc_co_u32_e32 v6, vcc, 0, v6, vcc
	v_cmp_gt_i64_e32 vcc, s[22:23], v[8:9]
	v_readlane_b32 s23, v9, 3
	s_movk_i32 s22, 60
	v_addc_co_u32_e32 v6, vcc, 0, v6, vcc
	v_cmp_gt_i64_e32 vcc, s[24:25], v[8:9]
	v_readlane_b32 s25, v9, 4
	s_movk_i32 s24, 59
	v_addc_co_u32_e32 v6, vcc, 0, v6, vcc
	v_cmp_gt_i64_e32 vcc, s[22:23], v[8:9]
	v_readlane_b32 s23, v9, 5
	s_movk_i32 s22, 58
	v_addc_co_u32_e32 v6, vcc, 0, v6, vcc
	v_cmp_gt_i64_e32 vcc, s[24:25], v[8:9]
	v_readlane_b32 s25, v9, 6
	s_movk_i32 s24, 57
	v_addc_co_u32_e32 v6, vcc, 0, v6, vcc
	v_cmp_gt_i64_e32 vcc, s[22:23], v[8:9]
	v_readlane_b32 s23, v9, 7
	s_movk_i32 s22, 56
	v_addc_co_u32_e32 v6, vcc, 0, v6, vcc
	v_cmp_gt_i64_e32 vcc, s[24:25], v[8:9]
	v_readlane_b32 s25, v9, 8
	s_movk_i32 s24, 55
	v_addc_co_u32_e32 v6, vcc, 0, v6, vcc
	v_cmp_gt_i64_e32 vcc, s[22:23], v[8:9]
	v_readlane_b32 s23, v9, 9
	s_movk_i32 s22, 54
	v_addc_co_u32_e32 v6, vcc, 0, v6, vcc
	v_cmp_gt_i64_e32 vcc, s[24:25], v[8:9]
	v_readlane_b32 s25, v9, 10
	s_movk_i32 s24, 53
	v_addc_co_u32_e32 v6, vcc, 0, v6, vcc
	v_cmp_gt_i64_e32 vcc, s[22:23], v[8:9]
	v_readlane_b32 s23, v9, 11
	s_movk_i32 s22, 52
	v_addc_co_u32_e32 v6, vcc, 0, v6, vcc
	v_cmp_gt_i64_e32 vcc, s[24:25], v[8:9]
	v_readlane_b32 s25, v9, 12
	s_movk_i32 s24, 51
	v_addc_co_u32_e32 v6, vcc, 0, v6, vcc
	v_cmp_gt_i64_e32 vcc, s[22:23], v[8:9]
	v_readlane_b32 s23, v9, 13
	s_movk_i32 s22, 50
	v_addc_co_u32_e32 v6, vcc, 0, v6, vcc
	v_cmp_gt_i64_e32 vcc, s[24:25], v[8:9]
	v_readlane_b32 s25, v9, 14
	s_movk_i32 s24, 49
	v_addc_co_u32_e32 v6, vcc, 0, v6, vcc
	v_cmp_gt_i64_e32 vcc, s[22:23], v[8:9]
	v_readlane_b32 s23, v9, 15
	s_movk_i32 s22, 48
	v_addc_co_u32_e32 v6, vcc, 0, v6, vcc
	v_cmp_gt_i64_e32 vcc, s[24:25], v[8:9]
; __device__ __forceinline__ void phase_nrr(const Frame& F, const Args& a, int l, const bf16_t* XA, const float* g, const float* modl, unsigned char* XN8) {
;     ...
;             for (int e2 = 0; e2 < 64; ++e2) { const float v = __int_as_float(__builtin_amdgcn_readlane(__float_as_int(val), e2)); rank += (v > val || (v == val && e2 < lane)) ? 1 : 0; }
;             const bool sel = rank < TOPK;
;             const float ssum = wave_sum(sel ? sc : 0.f);
;             if (sel) { const int p = atomicAdd((int*)(hist + lane), 1); top_e[t * TOPK + rank] = lane; gate[t * TOPK + rank] = sc / ssum * 2.5f; lpos[t * TOPK + rank] = p; }
	v_readlane_b32 s25, v9, 16
	s_movk_i32 s24, 47
	v_addc_co_u32_e32 v6, vcc, 0, v6, vcc
	v_cmp_gt_i64_e32 vcc, s[22:23], v[8:9]
	v_readlane_b32 s23, v9, 17
	s_movk_i32 s22, 46
	v_addc_co_u32_e32 v6, vcc, 0, v6, vcc
	v_cmp_gt_i64_e32 vcc, s[24:25], v[8:9]
	v_readlane_b32 s25, v9, 18
	s_movk_i32 s24, 45
	v_addc_co_u32_e32 v6, vcc, 0, v6, vcc
	v_cmp_gt_i64_e32 vcc, s[22:23], v[8:9]
	v_readlane_b32 s23, v9, 19
	s_movk_i32 s22, 44
	v_addc_co_u32_e32 v6, vcc, 0, v6, vcc
	v_cmp_gt_i64_e32 vcc, s[24:25], v[8:9]
	v_readlane_b32 s25, v9, 20
	s_movk_i32 s24, 43
	v_addc_co_u32_e32 v6, vcc, 0, v6, vcc
	v_cmp_gt_i64_e32 vcc, s[22:23], v[8:9]
	v_readlane_b32 s23, v9, 21
	s_movk_i32 s22, 42
	v_addc_co_u32_e32 v6, vcc, 0, v6, vcc
	v_cmp_gt_i64_e32 vcc, s[24:25], v[8:9]
	v_readlane_b32 s25, v9, 22
	s_movk_i32 s24, 41
	v_addc_co_u32_e32 v6, vcc, 0, v6, vcc
	v_cmp_gt_i64_e32 vcc, s[22:23], v[8:9]
	v_readlane_b32 s23, v9, 23
	s_movk_i32 s22, 40
	v_addc_co_u32_e32 v6, vcc, 0, v6, vcc
	v_cmp_gt_i64_e32 vcc, s[24:25], v[8:9]
	v_readlane_b32 s25, v9, 24
	s_movk_i32 s24, 39
	v_addc_co_u32_e32 v6, vcc, 0, v6, vcc
	v_cmp_gt_i64_e32 vcc, s[22:23], v[8:9]
	v_readlane_b32 s23, v9, 25
	s_movk_i32 s22, 38
	v_addc_co_u32_e32 v6, vcc, 0, v6, vcc
	v_cmp_gt_i64_e32 vcc, s[24:25], v[8:9]
	v_readlane_b32 s25, v9, 26
	s_movk_i32 s24, 37
	v_addc_co_u32_e32 v6, vcc, 0, v6, vcc
	v_cmp_gt_i64_e32 vcc, s[22:23], v[8:9]
	v_readlane_b32 s23, v9, 27
	s_movk_i32 s22, 36
	v_addc_co_u32_e32 v6, vcc, 0, v6, vcc
	v_cmp_gt_i64_e32 vcc, s[24:25], v[8:9]
	v_readlane_b32 s25, v9, 28
	s_movk_i32 s24, 35
	v_addc_co_u32_e32 v6, vcc, 0, v6, vcc
	v_cmp_gt_i64_e32 vcc, s[22:23], v[8:9]
	v_readlane_b32 s23, v9, 29
	s_movk_i32 s22, 34
	v_addc_co_u32_e32 v6, vcc, 0, v6, vcc
	v_cmp_gt_i64_e32 vcc, s[24:25], v[8:9]
	v_readlane_b32 s25, v9, 30
	s_movk_i32 s24, 33
	v_addc_co_u32_e32 v6, vcc, 0, v6, vcc
	v_cmp_gt_i64_e32 vcc, s[22:23], v[8:9]
	v_readlane_b32 s23, v9, 31
	s_movk_i32 s22, 32
	v_addc_co_u32_e32 v6, vcc, 0, v6, vcc
	v_cmp_gt_i64_e32 vcc, s[24:25], v[8:9]
	v_readlane_b32 s25, v9, 32
	s_movk_i32 s24, 31
	v_addc_co_u32_e32 v6, vcc, 0, v6, vcc
	v_cmp_gt_i64_e32 vcc, s[22:23], v[8:9]
	v_readlane_b32 s23, v9, 33
	s_movk_i32 s22, 30
	v_addc_co_u32_e32 v6, vcc, 0, v6, vcc
	v_cmp_gt_i64_e32 vcc, s[24:25], v[8:9]
	v_readlane_b32 s25, v9, 34
	s_movk_i32 s24, 29
	v_addc_co_u32_e32 v6, vcc, 0, v6, vcc
	v_cmp_gt_i64_e32 vcc, s[22:23], v[8:9]
	v_readlane_b32 s23, v9, 35
	s_movk_i32 s22, 28
	v_addc_co_u32_e32 v6, vcc, 0, v6, vcc
	v_cmp_gt_i64_e32 vcc, s[24:25], v[8:9]
	v_readlane_b32 s25, v9, 36
	s_movk_i32 s24, 27
	v_addc_co_u32_e32 v6, vcc, 0, v6, vcc
	v_cmp_gt_i64_e32 vcc, s[22:23], v[8:9]
	v_readlane_b32 s23, v9, 37
	s_movk_i32 s22, 26
	v_addc_co_u32_e32 v6, vcc, 0, v6, vcc
	v_cmp_gt_i64_e32 vcc, s[24:25], v[8:9]
	v_readlane_b32 s25, v9, 38
	s_movk_i32 s24, 25
	v_addc_co_u32_e32 v6, vcc, 0, v6, vcc
	v_cmp_gt_i64_e32 vcc, s[22:23], v[8:9]
	v_readlane_b32 s23, v9, 39
	s_movk_i32 s22, 24
	v_addc_co_u32_e32 v6, vcc, 0, v6, vcc
	v_cmp_gt_i64_e32 vcc, s[24:25], v[8:9]
	v_readlane_b32 s25, v9, 40
	s_movk_i32 s24, 23
	v_addc_co_u32_e32 v6, vcc, 0, v6, vcc
	v_cmp_gt_i64_e32 vcc, s[22:23], v[8:9]
	v_readlane_b32 s23, v9, 41
	s_movk_i32 s22, 22
	v_addc_co_u32_e32 v6, vcc, 0, v6, vcc
	v_cmp_gt_i64_e32 vcc, s[24:25], v[8:9]
	v_readlane_b32 s25, v9, 42
	s_movk_i32 s24, 21
	v_addc_co_u32_e32 v6, vcc, 0, v6, vcc
	v_cmp_gt_i64_e32 vcc, s[22:23], v[8:9]
	v_readlane_b32 s23, v9, 43
	s_movk_i32 s22, 20
	v_addc_co_u32_e32 v6, vcc, 0, v6, vcc
	v_cmp_gt_i64_e32 vcc, s[24:25], v[8:9]
	v_readlane_b32 s25, v9, 44
	s_movk_i32 s24, 19
	v_addc_co_u32_e32 v6, vcc, 0, v6, vcc
	v_cmp_gt_i64_e32 vcc, s[22:23], v[8:9]
	v_readlane_b32 s23, v9, 45
	s_movk_i32 s22, 18
	v_addc_co_u32_e32 v6, vcc, 0, v6, vcc
	v_cmp_gt_i64_e32 vcc, s[24:25], v[8:9]
	v_readlane_b32 s25, v9, 46
	s_movk_i32 s24, 17
	v_addc_co_u32_e32 v6, vcc, 0, v6, vcc
	v_cmp_gt_i64_e32 vcc, s[22:23], v[8:9]
	v_readlane_b32 s23, v9, 47
	s_movk_i32 s22, 16
	v_addc_co_u32_e32 v6, vcc, 0, v6, vcc
	v_cmp_gt_i64_e32 vcc, s[24:25], v[8:9]
	v_readlane_b32 s25, v9, 48
	s_movk_i32 s24, 15
	v_addc_co_u32_e32 v6, vcc, 0, v6, vcc
	v_cmp_gt_i64_e32 vcc, s[22:23], v[8:9]
	v_readlane_b32 s23, v9, 49
	s_movk_i32 s22, 14
	v_addc_co_u32_e32 v6, vcc, 0, v6, vcc
	v_cmp_gt_i64_e32 vcc, s[24:25], v[8:9]
	v_readlane_b32 s25, v9, 50
	s_movk_i32 s24, 13
	v_addc_co_u32_e32 v6, vcc, 0, v6, vcc
	v_cmp_gt_i64_e32 vcc, s[22:23], v[8:9]
	v_readlane_b32 s23, v9, 51
	s_movk_i32 s22, 12
	v_addc_co_u32_e32 v6, vcc, 0, v6, vcc
	v_cmp_gt_i64_e32 vcc, s[24:25], v[8:9]
	v_readlane_b32 s25, v9, 52
	s_movk_i32 s24, 11
	v_addc_co_u32_e32 v6, vcc, 0, v6, vcc
	v_cmp_gt_i64_e32 vcc, s[22:23], v[8:9]
	v_readlane_b32 s23, v9, 53
	s_movk_i32 s22, 10
	v_addc_co_u32_e32 v6, vcc, 0, v6, vcc
	v_cmp_gt_i64_e32 vcc, s[24:25], v[8:9]
	v_readlane_b32 s25, v9, 54
	s_movk_i32 s24, 9
	v_addc_co_u32_e32 v6, vcc, 0, v6, vcc
	v_cmp_gt_i64_e32 vcc, s[22:23], v[8:9]
	v_readlane_b32 s23, v9, 55
	s_movk_i32 s22, 8
	v_addc_co_u32_e32 v6, vcc, 0, v6, vcc
	v_cmp_gt_i64_e32 vcc, s[24:25], v[8:9]
	v_readlane_b32 s25, v9, 56
	s_movk_i32 s24, 7
	v_addc_co_u32_e32 v6, vcc, 0, v6, vcc
	v_cmp_gt_i64_e32 vcc, s[22:23], v[8:9]
	v_readlane_b32 s23, v9, 57
	s_movk_i32 s22, 6
	v_addc_co_u32_e32 v6, vcc, 0, v6, vcc
	v_cmp_gt_i64_e32 vcc, s[24:25], v[8:9]
	v_readlane_b32 s25, v9, 58
	s_movk_i32 s24, 5
	v_addc_co_u32_e32 v6, vcc, 0, v6, vcc
	v_cmp_gt_i64_e32 vcc, s[22:23], v[8:9]
	v_readlane_b32 s23, v9, 59
	s_movk_i32 s22, 4
	v_addc_co_u32_e32 v6, vcc, 0, v6, vcc
	v_cmp_gt_i64_e32 vcc, s[24:25], v[8:9]
	v_readlane_b32 s25, v9, 60
	s_movk_i32 s24, 3
	v_addc_co_u32_e32 v6, vcc, 0, v6, vcc
	v_cmp_gt_i64_e32 vcc, s[22:23], v[8:9]
	v_readlane_b32 s23, v9, 61
	s_movk_i32 s22, 2
	v_addc_co_u32_e32 v6, vcc, 0, v6, vcc
	v_cmp_gt_i64_e32 vcc, s[24:25], v[8:9]
	v_readlane_b32 s25, v9, 62
	s_movk_i32 s24, 1
	v_addc_co_u32_e32 v6, vcc, 0, v6, vcc
	v_cmp_gt_i64_e32 vcc, s[22:23], v[8:9]
	v_readlane_b32 s23, v9, 63
	s_movk_i32 s22, 0
	v_addc_co_u32_e32 v6, vcc, 0, v6, vcc
	v_cmp_gt_i64_e32 vcc, s[24:25], v[8:9]
	s_nop 1
	v_addc_co_u32_e32 v6, vcc, 0, v6, vcc
	v_cmp_gt_i64_e32 vcc, s[22:23], v[8:9]
	s_nop 1
	v_addc_co_u32_e32 v6, vcc, 0, v6, vcc
	v_cmp_gt_u32_e32 vcc, 6, v6
	s_mul_i32 s36, s44, 6
	s_nop 0
	v_cndmask_b32_e32 v5, 0, v2, vcc
	ds_bpermute_b32 v7, v1, v5
	s_waitcnt lgkmcnt(0)
	v_add_f32_e32 v5, v5, v7
	ds_bpermute_b32 v7, v201, v5
	s_waitcnt lgkmcnt(0)
	v_add_f32_e32 v5, v5, v7
	ds_bpermute_b32 v7, v220, v5
	s_waitcnt lgkmcnt(0)
	v_add_f32_e32 v5, v5, v7
	ds_bpermute_b32 v7, v221, v5
	s_waitcnt lgkmcnt(0)
	v_add_f32_e32 v5, v5, v7
	ds_bpermute_b32 v7, v222, v5
	s_waitcnt lgkmcnt(0)
	v_add_f32_e32 v5, v5, v7
	ds_bpermute_b32 v7, v223, v5
	s_and_saveexec_b64 s[22:23], vcc
	s_cbranch_execz .LBB0_539
; __device__ __forceinline__ void phase_nrr(const Frame& F, const Args& a, int l, const bf16_t* XA, const float* g, const float* modl, unsigned char* XN8) {
;     ...
;         for (int i = 0; i < 8; ++i) { const int t = tb + i;
;             const float lg = Pl[(w * 8 + i) * NE + lane] + Pl[(64 + w * 8 + i) * NE + lane]; const float sc = 1.f / (1.f + __expf(-lg)); const float bb = sc + bias;
;             float m1 = bb; m1 = fmaxf(m1, __shfl_xor(m1, 1)); m1 = fmaxf(m1, __shfl_xor(m1, 2)); m1 = fmaxf(m1, __shfl_xor(m1, 4));
;             const unsigned long long eq = __ballot(bb == m1); const int gbase = lane & ~7; const unsigned grpmask = (unsigned)((eq >> gbase) & 0xffull);
;             const int first = gbase + __builtin_ctz(grpmask);
;             float m2 = (lane == first) ? -INFINITY : bb; m2 = fmaxf(m2, __shfl_xor(m2, 1)); m2 = fmaxf(m2, __shfl_xor(m2, 2)); m2 = fmaxf(m2, __shfl_xor(m2, 4));
;             const float gsum = m1 + m2; const int gq = lane >> 3;
;             int grank = 0;
; #pragma unroll
;             for (int g2 = 0; g2 < 8; ++g2) { const float v = __int_as_float(__builtin_amdgcn_readlane(__float_as_int(gsum), g2 * 8)); grank += (v > gsum || (v == gsum && g2 < gq)) ? 1 : 0; }
;             const bool keep = grank < 4; const float val = keep ? bb : -INFINITY;
;             int rank = 0;
; #pragma unroll 8
;             for (int e2 = 0; e2 < 64; ++e2) { const float v = __int_as_float(__builtin_amdgcn_readlane(__float_as_int(val), e2)); rank += (v > val || (v == val && e2 < lane)) ? 1 : 0; }
;             const bool sel = rank < TOPK;
;             const float ssum = wave_sum(sel ? sc : 0.f);
;             if (sel) { const int p = atomicAdd((int*)(hist + lane), 1); top_e[t * TOPK + rank] = lane; gate[t * TOPK + rank] = sc / ssum * 2.5f; lpos[t * TOPK + rank] = p; }
	s_waitcnt lgkmcnt(0)
	v_add_f32_e32 v5, v5, v7
	v_div_scale_f32 v11, s[24:25], v5, v5, v2
	v_or_b32_e32 v6, s36, v6
	v_rcp_f32_e32 v12, v11
	v_ashrrev_i32_e32 v7, 31, v6
	v_lshlrev_b64 v[6:7], 2, v[6:7]
	v_lshl_add_u64 v[8:9], s[26:27], 0, v[6:7]
	ds_add_rtn_u32 v10, v227, v243
	global_store_dword v[8:9], v230, off
	v_fma_f32 v8, -v11, v12, 1.0
	v_fmac_f32_e32 v12, v8, v12
	v_div_scale_f32 v8, vcc, v2, v5, v2
	v_mul_f32_e32 v9, v8, v12
	v_fma_f32 v13, -v11, v9, v8
	v_fmac_f32_e32 v9, v13, v12
	v_fma_f32 v8, -v11, v9, v8
	v_div_fmas_f32 v8, v8, v12, v9
	v_div_fixup_f32 v2, v8, v5, v2
	v_mul_f32_e32 v2, 0x40200000, v2
	v_lshl_add_u64 v[8:9], s[28:29], 0, v[6:7]
	v_lshl_add_u64 v[6:7], s[30:31], 0, v[6:7]
	global_store_dword v[8:9], v2, off
	s_waitcnt lgkmcnt(0)
	global_store_dword v[6:7], v10, off
.LBB0_539:
	s_or_b64 exec, exec, s[22:23]
	v_add_u32_e32 v2, s77, v226
	ds_read_b32 v2, v2
	ds_read_b32 v5, v4 offset:16640
	s_mov_b32 s3, 0
	s_waitcnt lgkmcnt(0)
	v_add_f32_e32 v2, v2, v5
	v_mul_f32_e32 v2, 0xbfb8aa3b, v2
	v_exp_f32_e32 v2, v2
	s_nop 0
	v_add_f32_e32 v2, 1.0, v2
	v_div_scale_f32 v5, s[22:23], v2, v2, 1.0
	v_rcp_f32_e32 v6, v5
	s_nop 0
	v_fma_f32 v7, -v5, v6, 1.0
	v_fmac_f32_e32 v6, v7, v6
	v_div_scale_f32 v7, vcc, 1.0, v2, 1.0
	v_mul_f32_e32 v8, v7, v6
	v_fma_f32 v9, -v5, v8, v7
	v_fmac_f32_e32 v8, v9, v6
	v_fma_f32 v5, -v5, v8, v7
	v_div_fmas_f32 v5, v5, v6, v8
	v_div_fixup_f32 v5, v5, v2, 1.0
	v_add_f32_e32 v2, v3, v5
	ds_bpermute_b32 v6, v1, v2
	s_waitcnt lgkmcnt(0)
	v_max_f32_e32 v6, v6, v6
	v_max_f32_e32 v6, v2, v6
	ds_bpermute_b32 v7, v201, v6
	s_waitcnt lgkmcnt(0)
	v_max_f32_e32 v7, v7, v7
	v_max_f32_e32 v6, v6, v7
	ds_bpermute_b32 v7, v220, v6
	s_waitcnt lgkmcnt(0)
	v_max_f32_e32 v7, v7, v7
	v_max_f32_e32 v8, v6, v7
	v_cmp_eq_f32_e32 vcc, v2, v8
	s_nop 1
	v_lshrrev_b64 v[6:7], v200, vcc
	v_ffbl_b32_sdwa v6, v6 dst_sel:DWORD dst_unused:UNUSED_PAD src0_sel:BYTE_0
	v_add_u32_e32 v6, v6, v200
	v_cmp_ne_u32_e32 vcc, v230, v6
	s_nop 1
	v_cndmask_b32_e32 v6, v245, v2, vcc
	ds_bpermute_b32 v7, v1, v6
	s_waitcnt lgkmcnt(0)
	v_max_f32_e32 v7, v7, v7
	v_max_f32_e32 v6, v6, v7
	ds_bpermute_b32 v7, v201, v6
	s_waitcnt lgkmcnt(0)
	v_max_f32_e32 v7, v7, v7
	v_max_f32_e32 v6, v6, v7
	ds_bpermute_b32 v7, v220, v6
	s_waitcnt lgkmcnt(0)
	v_max_f32_e32 v7, v7, v7
	v_max_f32_e32 v6, v6, v7
	v_add_f32_e32 v6, v8, v6
	s_nop 0
	v_readlane_b32 s5, v6, 0
	s_nop 1
	v_cmp_eq_f32_e64 s[22:23], s5, v6
	v_cmp_gt_f32_e32 vcc, s5, v6
	s_and_b64 s[22:23], s[6:7], s[22:23]
	s_or_b64 s[22:23], vcc, s[22:23]
	v_readlane_b32 s5, v6, 8
	v_cndmask_b32_e64 v7, 0, 1, s[22:23]
	s_nop 0
	v_cmp_eq_f32_e64 s[22:23], s5, v6
	v_cmp_gt_f32_e32 vcc, s5, v6
	s_and_b64 s[22:23], s[8:9], s[22:23]
	s_or_b64 s[22:23], vcc, s[22:23]
	v_readlane_b32 s5, v6, 16
	v_cndmask_b32_e64 v8, 0, 1, s[22:23]
	s_nop 0
	v_cmp_eq_f32_e64 s[22:23], s5, v6
	v_cmp_gt_f32_e32 vcc, s5, v6
	s_and_b64 s[22:23], s[10:11], s[22:23]
	s_or_b64 s[22:23], vcc, s[22:23]
	v_readlane_b32 s5, v6, 24
	v_cndmask_b32_e64 v9, 0, 1, s[22:23]
	s_nop 0
	v_cmp_eq_f32_e64 s[22:23], s5, v6
	v_cmp_gt_f32_e32 vcc, s5, v6
	s_and_b64 s[22:23], s[12:13], s[22:23]
	s_or_b64 s[22:23], vcc, s[22:23]
	v_readlane_b32 s5, v6, 32
	v_cndmask_b32_e64 v10, 0, 1, s[22:23]
	s_nop 0
	v_cmp_eq_f32_e64 s[22:23], s5, v6
	v_cmp_gt_f32_e32 vcc, s5, v6
	s_and_b64 s[22:23], s[14:15], s[22:23]
	s_or_b64 s[22:23], vcc, s[22:23]
	v_readlane_b32 s5, v6, 40
	v_cndmask_b32_e64 v11, 0, 1, s[22:23]
	s_nop 0
	v_cmp_eq_f32_e64 s[22:23], s5, v6
	v_cmp_gt_f32_e32 vcc, s5, v6
	s_and_b64 s[22:23], s[16:17], s[22:23]
	s_or_b64 s[22:23], vcc, s[22:23]
	v_readlane_b32 s5, v6, 48
	v_cndmask_b32_e64 v12, 0, 1, s[22:23]
	s_nop 0
	v_cmp_eq_f32_e64 s[22:23], s5, v6
	v_cmp_gt_f32_e32 vcc, s5, v6
	s_and_b64 s[22:23], s[18:19], s[22:23]
	v_readlane_b32 s5, v6, 56
	s_or_b64 s[22:23], vcc, s[22:23]
	v_cndmask_b32_e64 v13, 0, 1, s[22:23]
	v_cmp_gt_f32_e32 vcc, s5, v6
	s_nop 1
	v_cndmask_b32_e64 v6, 0, 1, vcc
	v_add_u32_e32 v6, v8, v6
	v_add3_u32 v6, v6, v7, v9
	v_add3_u32 v6, v6, v10, v11
	v_add3_u32 v6, v6, v12, v13
	v_cmp_gt_u32_e32 vcc, 4, v6
	s_nop 1
	v_cndmask_b32_e32 v6, v245, v2, vcc
	v_mov_b32_e32 v2, 0
	v_ashrrev_i32_e32 v9, 31, v6
	v_sub_u32_e32 v8, 63, v230
	v_and_b32_e32 v9, 0x7fffffff, v9
	v_xor_b32_e32 v9, v6, v9
	s_nop 0
	v_readlane_b32 s25, v9, 0
	s_movk_i32 s24, 63
	v_readlane_b32 s23, v9, 1
	s_movk_i32 s22, 62
	v_cmp_gt_i64_e32 vcc, s[24:25], v[8:9]
	v_readlane_b32 s25, v9, 2
	s_movk_i32 s24, 61
	v_addc_co_u32_e32 v2, vcc, 0, v2, vcc
	v_cmp_gt_i64_e32 vcc, s[22:23], v[8:9]
	v_readlane_b32 s23, v9, 3
	s_movk_i32 s22, 60
	v_addc_co_u32_e32 v2, vcc, 0, v2, vcc
	v_cmp_gt_i64_e32 vcc, s[24:25], v[8:9]
	v_readlane_b32 s25, v9, 4
	s_movk_i32 s24, 59
	v_addc_co_u32_e32 v2, vcc, 0, v2, vcc
	v_cmp_gt_i64_e32 vcc, s[22:23], v[8:9]
	v_readlane_b32 s23, v9, 5
	s_movk_i32 s22, 58
	v_addc_co_u32_e32 v2, vcc, 0, v2, vcc
	v_cmp_gt_i64_e32 vcc, s[24:25], v[8:9]
	v_readlane_b32 s25, v9, 6
	s_movk_i32 s24, 57
	v_addc_co_u32_e32 v2, vcc, 0, v2, vcc
	v_cmp_gt_i64_e32 vcc, s[22:23], v[8:9]
	v_readlane_b32 s23, v9, 7
	s_movk_i32 s22, 56
	v_addc_co_u32_e32 v2, vcc, 0, v2, vcc
	v_cmp_gt_i64_e32 vcc, s[24:25], v[8:9]
	v_readlane_b32 s25, v9, 8
	s_movk_i32 s24, 55
	v_addc_co_u32_e32 v2, vcc, 0, v2, vcc
	v_cmp_gt_i64_e32 vcc, s[22:23], v[8:9]
	v_readlane_b32 s23, v9, 9
	s_movk_i32 s22, 54
	v_addc_co_u32_e32 v2, vcc, 0, v2, vcc
	v_cmp_gt_i64_e32 vcc, s[24:25], v[8:9]
	v_readlane_b32 s25, v9, 10
	s_movk_i32 s24, 53
	v_addc_co_u32_e32 v2, vcc, 0, v2, vcc
	v_cmp_gt_i64_e32 vcc, s[22:23], v[8:9]
	v_readlane_b32 s23, v9, 11
	s_movk_i32 s22, 52
	v_addc_co_u32_e32 v2, vcc, 0, v2, vcc
; __device__ __forceinline__ void phase_nrr(const Frame& F, const Args& a, int l, const bf16_t* XA, const float* g, const float* modl, unsigned char* XN8) {
;     ...
;             for (int e2 = 0; e2 < 64; ++e2) { const float v = __int_as_float(__builtin_amdgcn_readlane(__float_as_int(val), e2)); rank += (v > val || (v == val && e2 < lane)) ? 1 : 0; }
;             const bool sel = rank < TOPK;
;             const float ssum = wave_sum(sel ? sc : 0.f);
	v_cmp_gt_i64_e32 vcc, s[24:25], v[8:9]
	v_readlane_b32 s25, v9, 12
	s_movk_i32 s24, 51
	v_addc_co_u32_e32 v2, vcc, 0, v2, vcc
	v_cmp_gt_i64_e32 vcc, s[22:23], v[8:9]
	v_readlane_b32 s23, v9, 13
	s_movk_i32 s22, 50
	v_addc_co_u32_e32 v2, vcc, 0, v2, vcc
	v_cmp_gt_i64_e32 vcc, s[24:25], v[8:9]
	v_readlane_b32 s25, v9, 14
	s_movk_i32 s24, 49
	v_addc_co_u32_e32 v2, vcc, 0, v2, vcc
	v_cmp_gt_i64_e32 vcc, s[22:23], v[8:9]
	v_readlane_b32 s23, v9, 15
	s_movk_i32 s22, 48
	v_addc_co_u32_e32 v2, vcc, 0, v2, vcc
	v_cmp_gt_i64_e32 vcc, s[24:25], v[8:9]
	v_readlane_b32 s25, v9, 16
	s_movk_i32 s24, 47
	v_addc_co_u32_e32 v2, vcc, 0, v2, vcc
	v_cmp_gt_i64_e32 vcc, s[22:23], v[8:9]
	v_readlane_b32 s23, v9, 17
	s_movk_i32 s22, 46
	v_addc_co_u32_e32 v2, vcc, 0, v2, vcc
	v_cmp_gt_i64_e32 vcc, s[24:25], v[8:9]
	v_readlane_b32 s25, v9, 18
	s_movk_i32 s24, 45
	v_addc_co_u32_e32 v2, vcc, 0, v2, vcc
	v_cmp_gt_i64_e32 vcc, s[22:23], v[8:9]
	v_readlane_b32 s23, v9, 19
	s_movk_i32 s22, 44
	v_addc_co_u32_e32 v2, vcc, 0, v2, vcc
	v_cmp_gt_i64_e32 vcc, s[24:25], v[8:9]
	v_readlane_b32 s25, v9, 20
	s_movk_i32 s24, 43
	v_addc_co_u32_e32 v2, vcc, 0, v2, vcc
	v_cmp_gt_i64_e32 vcc, s[22:23], v[8:9]
	v_readlane_b32 s23, v9, 21
	s_movk_i32 s22, 42
	v_addc_co_u32_e32 v2, vcc, 0, v2, vcc
	v_cmp_gt_i64_e32 vcc, s[24:25], v[8:9]
	v_readlane_b32 s25, v9, 22
	s_movk_i32 s24, 41
	v_addc_co_u32_e32 v2, vcc, 0, v2, vcc
	v_cmp_gt_i64_e32 vcc, s[22:23], v[8:9]
	v_readlane_b32 s23, v9, 23
	s_movk_i32 s22, 40
	v_addc_co_u32_e32 v2, vcc, 0, v2, vcc
	v_cmp_gt_i64_e32 vcc, s[24:25], v[8:9]
	v_readlane_b32 s25, v9, 24
	s_movk_i32 s24, 39
	v_addc_co_u32_e32 v2, vcc, 0, v2, vcc
	v_cmp_gt_i64_e32 vcc, s[22:23], v[8:9]
	v_readlane_b32 s23, v9, 25
	s_movk_i32 s22, 38
	v_addc_co_u32_e32 v2, vcc, 0, v2, vcc
	v_cmp_gt_i64_e32 vcc, s[24:25], v[8:9]
	v_readlane_b32 s25, v9, 26
	s_movk_i32 s24, 37
	v_addc_co_u32_e32 v2, vcc, 0, v2, vcc
	v_cmp_gt_i64_e32 vcc, s[22:23], v[8:9]
	v_readlane_b32 s23, v9, 27
	s_movk_i32 s22, 36
	v_addc_co_u32_e32 v2, vcc, 0, v2, vcc
	v_cmp_gt_i64_e32 vcc, s[24:25], v[8:9]
	v_readlane_b32 s25, v9, 28
	s_movk_i32 s24, 35
	v_addc_co_u32_e32 v2, vcc, 0, v2, vcc
	v_cmp_gt_i64_e32 vcc, s[22:23], v[8:9]
	v_readlane_b32 s23, v9, 29
	s_movk_i32 s22, 34
	v_addc_co_u32_e32 v2, vcc, 0, v2, vcc
	v_cmp_gt_i64_e32 vcc, s[24:25], v[8:9]
	v_readlane_b32 s25, v9, 30
	s_movk_i32 s24, 33
	v_addc_co_u32_e32 v2, vcc, 0, v2, vcc
	v_cmp_gt_i64_e32 vcc, s[22:23], v[8:9]
	v_readlane_b32 s23, v9, 31
	s_movk_i32 s22, 32
	v_addc_co_u32_e32 v2, vcc, 0, v2, vcc
	v_cmp_gt_i64_e32 vcc, s[24:25], v[8:9]
	v_readlane_b32 s25, v9, 32
	s_movk_i32 s24, 31
	v_addc_co_u32_e32 v2, vcc, 0, v2, vcc
	v_cmp_gt_i64_e32 vcc, s[22:23], v[8:9]
	v_readlane_b32 s23, v9, 33
	s_movk_i32 s22, 30
	v_addc_co_u32_e32 v2, vcc, 0, v2, vcc
	v_cmp_gt_i64_e32 vcc, s[24:25], v[8:9]
	v_readlane_b32 s25, v9, 34
	s_movk_i32 s24, 29
	v_addc_co_u32_e32 v2, vcc, 0, v2, vcc
	v_cmp_gt_i64_e32 vcc, s[22:23], v[8:9]
	v_readlane_b32 s23, v9, 35
	s_movk_i32 s22, 28
	v_addc_co_u32_e32 v2, vcc, 0, v2, vcc
	v_cmp_gt_i64_e32 vcc, s[24:25], v[8:9]
	v_readlane_b32 s25, v9, 36
	s_movk_i32 s24, 27
	v_addc_co_u32_e32 v2, vcc, 0, v2, vcc
	v_cmp_gt_i64_e32 vcc, s[22:23], v[8:9]
	v_readlane_b32 s23, v9, 37
	s_movk_i32 s22, 26
	v_addc_co_u32_e32 v2, vcc, 0, v2, vcc
	v_cmp_gt_i64_e32 vcc, s[24:25], v[8:9]
	v_readlane_b32 s25, v9, 38
	s_movk_i32 s24, 25
	v_addc_co_u32_e32 v2, vcc, 0, v2, vcc
	v_cmp_gt_i64_e32 vcc, s[22:23], v[8:9]
	v_readlane_b32 s23, v9, 39
	s_movk_i32 s22, 24
	v_addc_co_u32_e32 v2, vcc, 0, v2, vcc
	v_cmp_gt_i64_e32 vcc, s[24:25], v[8:9]
	v_readlane_b32 s25, v9, 40
	s_movk_i32 s24, 23
	v_addc_co_u32_e32 v2, vcc, 0, v2, vcc
	v_cmp_gt_i64_e32 vcc, s[22:23], v[8:9]
	v_readlane_b32 s23, v9, 41
	s_movk_i32 s22, 22
	v_addc_co_u32_e32 v2, vcc, 0, v2, vcc
	v_cmp_gt_i64_e32 vcc, s[24:25], v[8:9]
	v_readlane_b32 s25, v9, 42
	s_movk_i32 s24, 21
	v_addc_co_u32_e32 v2, vcc, 0, v2, vcc
	v_cmp_gt_i64_e32 vcc, s[22:23], v[8:9]
	v_readlane_b32 s23, v9, 43
	s_movk_i32 s22, 20
	v_addc_co_u32_e32 v2, vcc, 0, v2, vcc
	v_cmp_gt_i64_e32 vcc, s[24:25], v[8:9]
	v_readlane_b32 s25, v9, 44
	s_movk_i32 s24, 19
	v_addc_co_u32_e32 v2, vcc, 0, v2, vcc
	v_cmp_gt_i64_e32 vcc, s[22:23], v[8:9]
	v_readlane_b32 s23, v9, 45
	s_movk_i32 s22, 18
	v_addc_co_u32_e32 v2, vcc, 0, v2, vcc
	v_cmp_gt_i64_e32 vcc, s[24:25], v[8:9]
	v_readlane_b32 s25, v9, 46
	s_movk_i32 s24, 17
	v_addc_co_u32_e32 v2, vcc, 0, v2, vcc
	v_cmp_gt_i64_e32 vcc, s[22:23], v[8:9]
	v_readlane_b32 s23, v9, 47
	s_movk_i32 s22, 16
	v_addc_co_u32_e32 v2, vcc, 0, v2, vcc
	v_cmp_gt_i64_e32 vcc, s[24:25], v[8:9]
	v_readlane_b32 s25, v9, 48
	s_movk_i32 s24, 15
	v_addc_co_u32_e32 v2, vcc, 0, v2, vcc
	v_cmp_gt_i64_e32 vcc, s[22:23], v[8:9]
	v_readlane_b32 s23, v9, 49
	s_movk_i32 s22, 14
	v_addc_co_u32_e32 v2, vcc, 0, v2, vcc
	v_cmp_gt_i64_e32 vcc, s[24:25], v[8:9]
	v_readlane_b32 s25, v9, 50
	s_movk_i32 s24, 13
	v_addc_co_u32_e32 v2, vcc, 0, v2, vcc
	v_cmp_gt_i64_e32 vcc, s[22:23], v[8:9]
	v_readlane_b32 s23, v9, 51
	s_movk_i32 s22, 12
	v_addc_co_u32_e32 v2, vcc, 0, v2, vcc
	v_cmp_gt_i64_e32 vcc, s[24:25], v[8:9]
	v_readlane_b32 s25, v9, 52
	s_movk_i32 s24, 11
	v_addc_co_u32_e32 v2, vcc, 0, v2, vcc
	v_cmp_gt_i64_e32 vcc, s[22:23], v[8:9]
	v_readlane_b32 s23, v9, 53
	s_movk_i32 s22, 10
	v_addc_co_u32_e32 v2, vcc, 0, v2, vcc
	v_cmp_gt_i64_e32 vcc, s[24:25], v[8:9]
	v_readlane_b32 s25, v9, 54
	s_movk_i32 s24, 9
	v_addc_co_u32_e32 v2, vcc, 0, v2, vcc
	v_cmp_gt_i64_e32 vcc, s[22:23], v[8:9]
	v_readlane_b32 s23, v9, 55
	s_movk_i32 s22, 8
	v_addc_co_u32_e32 v2, vcc, 0, v2, vcc
	v_cmp_gt_i64_e32 vcc, s[24:25], v[8:9]
	v_readlane_b32 s25, v9, 56
	s_movk_i32 s24, 7
	v_addc_co_u32_e32 v2, vcc, 0, v2, vcc
	v_cmp_gt_i64_e32 vcc, s[22:23], v[8:9]
	v_readlane_b32 s23, v9, 57
	s_movk_i32 s22, 6
	v_addc_co_u32_e32 v2, vcc, 0, v2, vcc
	v_cmp_gt_i64_e32 vcc, s[24:25], v[8:9]
	v_readlane_b32 s25, v9, 58
	s_movk_i32 s24, 5
	v_addc_co_u32_e32 v2, vcc, 0, v2, vcc
	v_cmp_gt_i64_e32 vcc, s[22:23], v[8:9]
	v_readlane_b32 s23, v9, 59
	s_movk_i32 s22, 4
	v_addc_co_u32_e32 v2, vcc, 0, v2, vcc
	v_cmp_gt_i64_e32 vcc, s[24:25], v[8:9]
	v_readlane_b32 s25, v9, 60
	s_movk_i32 s24, 3
	v_addc_co_u32_e32 v2, vcc, 0, v2, vcc
	v_cmp_gt_i64_e32 vcc, s[22:23], v[8:9]
	v_readlane_b32 s23, v9, 61
	s_movk_i32 s22, 2
	v_addc_co_u32_e32 v2, vcc, 0, v2, vcc
	v_cmp_gt_i64_e32 vcc, s[24:25], v[8:9]
	v_readlane_b32 s25, v9, 62
	s_movk_i32 s24, 1
	v_addc_co_u32_e32 v2, vcc, 0, v2, vcc
	v_cmp_gt_i64_e32 vcc, s[22:23], v[8:9]
	v_readlane_b32 s23, v9, 63
	s_movk_i32 s22, 0
	v_addc_co_u32_e32 v2, vcc, 0, v2, vcc
	v_cmp_gt_i64_e32 vcc, s[24:25], v[8:9]
	s_nop 1
	v_addc_co_u32_e32 v2, vcc, 0, v2, vcc
	v_cmp_gt_i64_e32 vcc, s[22:23], v[8:9]
	s_nop 1
	v_addc_co_u32_e32 v2, vcc, 0, v2, vcc
	v_cmp_gt_u32_e32 vcc, 6, v2
	s_nop 1
	v_cndmask_b32_e32 v6, 0, v5, vcc
	ds_bpermute_b32 v7, v1, v6
	s_waitcnt lgkmcnt(0)
; __device__ __forceinline__ void phase_nrr(const Frame& F, const Args& a, int l, const bf16_t* XA, const float* g, const float* modl, unsigned char* XN8) {
;     ...
;         for (int i = 0; i < 8; ++i) { const int t = tb + i;
;             const float lg = Pl[(w * 8 + i) * NE + lane] + Pl[(64 + w * 8 + i) * NE + lane]; const float sc = 1.f / (1.f + __expf(-lg)); const float bb = sc + bias;
;             float m1 = bb; m1 = fmaxf(m1, __shfl_xor(m1, 1)); m1 = fmaxf(m1, __shfl_xor(m1, 2)); m1 = fmaxf(m1, __shfl_xor(m1, 4));
;             const unsigned long long eq = __ballot(bb == m1); const int gbase = lane & ~7; const unsigned grpmask = (unsigned)((eq >> gbase) & 0xffull);
;             const int first = gbase + __builtin_ctz(grpmask);
;             float m2 = (lane == first) ? -INFINITY : bb; m2 = fmaxf(m2, __shfl_xor(m2, 1)); m2 = fmaxf(m2, __shfl_xor(m2, 2)); m2 = fmaxf(m2, __shfl_xor(m2, 4));
;             const float gsum = m1 + m2; const int gq = lane >> 3;
;             int grank = 0;
; #pragma unroll
;             for (int g2 = 0; g2 < 8; ++g2) { const float v = __int_as_float(__builtin_amdgcn_readlane(__float_as_int(gsum), g2 * 8)); grank += (v > gsum || (v == gsum && g2 < gq)) ? 1 : 0; }
;             const bool keep = grank < 4; const float val = keep ? bb : -INFINITY;
;             int rank = 0;
; #pragma unroll 8
;             for (int e2 = 0; e2 < 64; ++e2) { const float v = __int_as_float(__builtin_amdgcn_readlane(__float_as_int(val), e2)); rank += (v > val || (v == val && e2 < lane)) ? 1 : 0; }
;     ...
;             const float ssum = wave_sum(sel ? sc : 0.f);
;             if (sel) { const int p = atomicAdd((int*)(hist + lane), 1); top_e[t * TOPK + rank] = lane; gate[t * TOPK + rank] = sc / ssum * 2.5f; lpos[t * TOPK + rank] = p; }
	v_add_f32_e32 v6, v6, v7
	ds_bpermute_b32 v7, v201, v6
	s_waitcnt lgkmcnt(0)
	v_add_f32_e32 v6, v6, v7
	ds_bpermute_b32 v7, v220, v6
	s_waitcnt lgkmcnt(0)
	v_add_f32_e32 v6, v6, v7
	ds_bpermute_b32 v7, v221, v6
	s_waitcnt lgkmcnt(0)
	v_add_f32_e32 v6, v6, v7
	ds_bpermute_b32 v7, v222, v6
	s_waitcnt lgkmcnt(0)
	v_add_f32_e32 v6, v6, v7
	ds_bpermute_b32 v7, v223, v6
	s_and_saveexec_b64 s[22:23], vcc
	s_cbranch_execz .LBB0_543
	s_waitcnt lgkmcnt(0)
	v_add_f32_e32 v10, v6, v7
	v_mad_u64_u32 v[6:7], s[24:25], s42, 6, v[2:3]
	v_div_scale_f32 v2, s[24:25], v10, v10, v5
	v_rcp_f32_e32 v12, v2
	v_ashrrev_i32_e32 v7, 31, v6
	v_lshlrev_b64 v[6:7], 2, v[6:7]
	v_lshl_add_u64 v[8:9], s[26:27], 0, v[6:7]
	ds_add_rtn_u32 v11, v227, v243
	global_store_dword v[8:9], v230, off
	v_fma_f32 v8, -v2, v12, 1.0
	v_fmac_f32_e32 v12, v8, v12
	v_div_scale_f32 v8, vcc, v5, v10, v5
	v_mul_f32_e32 v9, v8, v12
	v_fma_f32 v13, -v2, v9, v8
	v_fmac_f32_e32 v9, v13, v12
	v_fma_f32 v2, -v2, v9, v8
	v_div_fmas_f32 v2, v2, v12, v9
	v_div_fixup_f32 v2, v2, v10, v5
	v_mul_f32_e32 v2, 0x40200000, v2
	v_lshl_add_u64 v[8:9], s[28:29], 0, v[6:7]
	v_lshl_add_u64 v[6:7], s[30:31], 0, v[6:7]
	global_store_dword v[8:9], v2, off
	s_waitcnt lgkmcnt(0)
	global_store_dword v[6:7], v11, off
.LBB0_543:
	s_or_b64 exec, exec, s[22:23]
	v_add_u32_e32 v2, s78, v226
	ds_read_b32 v2, v2
	ds_read_b32 v5, v4 offset:16896
	s_mov_b32 s3, 0
	s_waitcnt lgkmcnt(0)
	v_add_f32_e32 v2, v2, v5
	v_mul_f32_e32 v2, 0xbfb8aa3b, v2
	v_exp_f32_e32 v2, v2
	s_nop 0
	v_add_f32_e32 v2, 1.0, v2
	v_div_scale_f32 v5, s[22:23], v2, v2, 1.0
	v_rcp_f32_e32 v6, v5
	s_nop 0
	v_fma_f32 v7, -v5, v6, 1.0
	v_fmac_f32_e32 v6, v7, v6
	v_div_scale_f32 v7, vcc, 1.0, v2, 1.0
	v_mul_f32_e32 v8, v7, v6
	v_fma_f32 v9, -v5, v8, v7
	v_fmac_f32_e32 v8, v9, v6
	v_fma_f32 v5, -v5, v8, v7
	v_div_fmas_f32 v5, v5, v6, v8
	v_div_fixup_f32 v5, v5, v2, 1.0
	v_add_f32_e32 v2, v3, v5
	ds_bpermute_b32 v6, v1, v2
	s_waitcnt lgkmcnt(0)
	v_max_f32_e32 v6, v6, v6
	v_max_f32_e32 v6, v2, v6
	ds_bpermute_b32 v7, v201, v6
	s_waitcnt lgkmcnt(0)
	v_max_f32_e32 v7, v7, v7
	v_max_f32_e32 v6, v6, v7
	ds_bpermute_b32 v7, v220, v6
	s_waitcnt lgkmcnt(0)
	v_max_f32_e32 v7, v7, v7
	v_max_f32_e32 v8, v6, v7
	v_cmp_eq_f32_e32 vcc, v2, v8
	s_nop 1
	v_lshrrev_b64 v[6:7], v200, vcc
	v_ffbl_b32_sdwa v6, v6 dst_sel:DWORD dst_unused:UNUSED_PAD src0_sel:BYTE_0
	v_add_u32_e32 v6, v6, v200
	v_cmp_ne_u32_e32 vcc, v230, v6
	s_nop 1
	v_cndmask_b32_e32 v6, v245, v2, vcc
	ds_bpermute_b32 v7, v1, v6
	s_waitcnt lgkmcnt(0)
	v_max_f32_e32 v7, v7, v7
	v_max_f32_e32 v6, v6, v7
	ds_bpermute_b32 v7, v201, v6
	s_waitcnt lgkmcnt(0)
	v_max_f32_e32 v7, v7, v7
	v_max_f32_e32 v6, v6, v7
	ds_bpermute_b32 v7, v220, v6
	s_waitcnt lgkmcnt(0)
	v_max_f32_e32 v7, v7, v7
	v_max_f32_e32 v6, v6, v7
	v_add_f32_e32 v6, v8, v6
	s_nop 0
	v_readlane_b32 s5, v6, 0
	s_nop 1
	v_cmp_eq_f32_e64 s[22:23], s5, v6
	v_cmp_gt_f32_e32 vcc, s5, v6
	s_and_b64 s[22:23], s[6:7], s[22:23]
	s_or_b64 s[22:23], vcc, s[22:23]
	v_readlane_b32 s5, v6, 8
	v_cndmask_b32_e64 v7, 0, 1, s[22:23]
	s_nop 0
	v_cmp_eq_f32_e64 s[22:23], s5, v6
	v_cmp_gt_f32_e32 vcc, s5, v6
	s_and_b64 s[22:23], s[8:9], s[22:23]
	s_or_b64 s[22:23], vcc, s[22:23]
	v_readlane_b32 s5, v6, 16
	v_cndmask_b32_e64 v8, 0, 1, s[22:23]
	s_nop 0
	v_cmp_eq_f32_e64 s[22:23], s5, v6
	v_cmp_gt_f32_e32 vcc, s5, v6
	s_and_b64 s[22:23], s[10:11], s[22:23]
	s_or_b64 s[22:23], vcc, s[22:23]
	v_readlane_b32 s5, v6, 24
	v_cndmask_b32_e64 v9, 0, 1, s[22:23]
	s_nop 0
	v_cmp_eq_f32_e64 s[22:23], s5, v6
	v_cmp_gt_f32_e32 vcc, s5, v6
	s_and_b64 s[22:23], s[12:13], s[22:23]
	s_or_b64 s[22:23], vcc, s[22:23]
	v_readlane_b32 s5, v6, 32
	v_cndmask_b32_e64 v10, 0, 1, s[22:23]
	s_nop 0
	v_cmp_eq_f32_e64 s[22:23], s5, v6
	v_cmp_gt_f32_e32 vcc, s5, v6
	s_and_b64 s[22:23], s[14:15], s[22:23]
	s_or_b64 s[22:23], vcc, s[22:23]
	v_readlane_b32 s5, v6, 40
	v_cndmask_b32_e64 v11, 0, 1, s[22:23]
	s_nop 0
	v_cmp_eq_f32_e64 s[22:23], s5, v6
	v_cmp_gt_f32_e32 vcc, s5, v6
	s_and_b64 s[22:23], s[16:17], s[22:23]
	s_or_b64 s[22:23], vcc, s[22:23]
	v_readlane_b32 s5, v6, 48
	v_cndmask_b32_e64 v12, 0, 1, s[22:23]
	s_nop 0
	v_cmp_eq_f32_e64 s[22:23], s5, v6
	v_cmp_gt_f32_e32 vcc, s5, v6
	s_and_b64 s[22:23], s[18:19], s[22:23]
	v_readlane_b32 s5, v6, 56
	s_or_b64 s[22:23], vcc, s[22:23]
	v_cndmask_b32_e64 v13, 0, 1, s[22:23]
	v_cmp_gt_f32_e32 vcc, s5, v6
	s_nop 1
	v_cndmask_b32_e64 v6, 0, 1, vcc
	v_add_u32_e32 v6, v8, v6
	v_add3_u32 v6, v6, v7, v9
	v_add3_u32 v6, v6, v10, v11
	v_add3_u32 v6, v6, v12, v13
	v_cmp_gt_u32_e32 vcc, 4, v6
	s_nop 1
	v_cndmask_b32_e32 v6, v245, v2, vcc
	v_mov_b32_e32 v2, 0
	v_ashrrev_i32_e32 v9, 31, v6
	v_sub_u32_e32 v8, 63, v230
	v_and_b32_e32 v9, 0x7fffffff, v9
	v_xor_b32_e32 v9, v6, v9
	s_nop 0
	v_readlane_b32 s25, v9, 0
	s_movk_i32 s24, 63
	v_readlane_b32 s23, v9, 1
	s_movk_i32 s22, 62
	v_cmp_gt_i64_e32 vcc, s[24:25], v[8:9]
	v_readlane_b32 s25, v9, 2
	s_movk_i32 s24, 61
	v_addc_co_u32_e32 v2, vcc, 0, v2, vcc
	v_cmp_gt_i64_e32 vcc, s[22:23], v[8:9]
	v_readlane_b32 s23, v9, 3
	s_movk_i32 s22, 60
	v_addc_co_u32_e32 v2, vcc, 0, v2, vcc
	v_cmp_gt_i64_e32 vcc, s[24:25], v[8:9]
	v_readlane_b32 s25, v9, 4
	s_movk_i32 s24, 59
	v_addc_co_u32_e32 v2, vcc, 0, v2, vcc
	v_cmp_gt_i64_e32 vcc, s[22:23], v[8:9]
	v_readlane_b32 s23, v9, 5
	s_movk_i32 s22, 58
	v_addc_co_u32_e32 v2, vcc, 0, v2, vcc
	v_cmp_gt_i64_e32 vcc, s[24:25], v[8:9]
	v_readlane_b32 s25, v9, 6
	s_movk_i32 s24, 57
	v_addc_co_u32_e32 v2, vcc, 0, v2, vcc
	v_cmp_gt_i64_e32 vcc, s[22:23], v[8:9]
	v_readlane_b32 s23, v9, 7
	s_movk_i32 s22, 56
	v_addc_co_u32_e32 v2, vcc, 0, v2, vcc
	v_cmp_gt_i64_e32 vcc, s[24:25], v[8:9]
	v_readlane_b32 s25, v9, 8
; __device__ __forceinline__ void phase_nrr(const Frame& F, const Args& a, int l, const bf16_t* XA, const float* g, const float* modl, unsigned char* XN8) {
;     ...
;             for (int e2 = 0; e2 < 64; ++e2) { const float v = __int_as_float(__builtin_amdgcn_readlane(__float_as_int(val), e2)); rank += (v > val || (v == val && e2 < lane)) ? 1 : 0; }
	s_movk_i32 s24, 55
	v_addc_co_u32_e32 v2, vcc, 0, v2, vcc
	v_cmp_gt_i64_e32 vcc, s[22:23], v[8:9]
	v_readlane_b32 s23, v9, 9
	s_movk_i32 s22, 54
	v_addc_co_u32_e32 v2, vcc, 0, v2, vcc
	v_cmp_gt_i64_e32 vcc, s[24:25], v[8:9]
	v_readlane_b32 s25, v9, 10
	s_movk_i32 s24, 53
	v_addc_co_u32_e32 v2, vcc, 0, v2, vcc
	v_cmp_gt_i64_e32 vcc, s[22:23], v[8:9]
	v_readlane_b32 s23, v9, 11
	s_movk_i32 s22, 52
	v_addc_co_u32_e32 v2, vcc, 0, v2, vcc
	v_cmp_gt_i64_e32 vcc, s[24:25], v[8:9]
	v_readlane_b32 s25, v9, 12
	s_movk_i32 s24, 51
	v_addc_co_u32_e32 v2, vcc, 0, v2, vcc
	v_cmp_gt_i64_e32 vcc, s[22:23], v[8:9]
	v_readlane_b32 s23, v9, 13
	s_movk_i32 s22, 50
	v_addc_co_u32_e32 v2, vcc, 0, v2, vcc
	v_cmp_gt_i64_e32 vcc, s[24:25], v[8:9]
	v_readlane_b32 s25, v9, 14
	s_movk_i32 s24, 49
	v_addc_co_u32_e32 v2, vcc, 0, v2, vcc
	v_cmp_gt_i64_e32 vcc, s[22:23], v[8:9]
	v_readlane_b32 s23, v9, 15
	s_movk_i32 s22, 48
	v_addc_co_u32_e32 v2, vcc, 0, v2, vcc
	v_cmp_gt_i64_e32 vcc, s[24:25], v[8:9]
	v_readlane_b32 s25, v9, 16
	s_movk_i32 s24, 47
	v_addc_co_u32_e32 v2, vcc, 0, v2, vcc
	v_cmp_gt_i64_e32 vcc, s[22:23], v[8:9]
	v_readlane_b32 s23, v9, 17
	s_movk_i32 s22, 46
	v_addc_co_u32_e32 v2, vcc, 0, v2, vcc
	v_cmp_gt_i64_e32 vcc, s[24:25], v[8:9]
	v_readlane_b32 s25, v9, 18
	s_movk_i32 s24, 45
	v_addc_co_u32_e32 v2, vcc, 0, v2, vcc
	v_cmp_gt_i64_e32 vcc, s[22:23], v[8:9]
	v_readlane_b32 s23, v9, 19
	s_movk_i32 s22, 44
	v_addc_co_u32_e32 v2, vcc, 0, v2, vcc
	v_cmp_gt_i64_e32 vcc, s[24:25], v[8:9]
	v_readlane_b32 s25, v9, 20
	s_movk_i32 s24, 43
	v_addc_co_u32_e32 v2, vcc, 0, v2, vcc
	v_cmp_gt_i64_e32 vcc, s[22:23], v[8:9]
	v_readlane_b32 s23, v9, 21
	s_movk_i32 s22, 42
	v_addc_co_u32_e32 v2, vcc, 0, v2, vcc
	v_cmp_gt_i64_e32 vcc, s[24:25], v[8:9]
	v_readlane_b32 s25, v9, 22
	s_movk_i32 s24, 41
	v_addc_co_u32_e32 v2, vcc, 0, v2, vcc
	v_cmp_gt_i64_e32 vcc, s[22:23], v[8:9]
	v_readlane_b32 s23, v9, 23
	s_movk_i32 s22, 40
	v_addc_co_u32_e32 v2, vcc, 0, v2, vcc
	v_cmp_gt_i64_e32 vcc, s[24:25], v[8:9]
	v_readlane_b32 s25, v9, 24
	s_movk_i32 s24, 39
	v_addc_co_u32_e32 v2, vcc, 0, v2, vcc
	v_cmp_gt_i64_e32 vcc, s[22:23], v[8:9]
	v_readlane_b32 s23, v9, 25
	s_movk_i32 s22, 38
	v_addc_co_u32_e32 v2, vcc, 0, v2, vcc
	v_cmp_gt_i64_e32 vcc, s[24:25], v[8:9]
	v_readlane_b32 s25, v9, 26
	s_movk_i32 s24, 37
	v_addc_co_u32_e32 v2, vcc, 0, v2, vcc
	v_cmp_gt_i64_e32 vcc, s[22:23], v[8:9]
	v_readlane_b32 s23, v9, 27
	s_movk_i32 s22, 36
	v_addc_co_u32_e32 v2, vcc, 0, v2, vcc
	v_cmp_gt_i64_e32 vcc, s[24:25], v[8:9]
	v_readlane_b32 s25, v9, 28
	s_movk_i32 s24, 35
	v_addc_co_u32_e32 v2, vcc, 0, v2, vcc
	v_cmp_gt_i64_e32 vcc, s[22:23], v[8:9]
	v_readlane_b32 s23, v9, 29
	s_movk_i32 s22, 34
	v_addc_co_u32_e32 v2, vcc, 0, v2, vcc
	v_cmp_gt_i64_e32 vcc, s[24:25], v[8:9]
	v_readlane_b32 s25, v9, 30
	s_movk_i32 s24, 33
	v_addc_co_u32_e32 v2, vcc, 0, v2, vcc
	v_cmp_gt_i64_e32 vcc, s[22:23], v[8:9]
	v_readlane_b32 s23, v9, 31
	s_movk_i32 s22, 32
	v_addc_co_u32_e32 v2, vcc, 0, v2, vcc
	v_cmp_gt_i64_e32 vcc, s[24:25], v[8:9]
	v_readlane_b32 s25, v9, 32
	s_movk_i32 s24, 31
	v_addc_co_u32_e32 v2, vcc, 0, v2, vcc
	v_cmp_gt_i64_e32 vcc, s[22:23], v[8:9]
	v_readlane_b32 s23, v9, 33
	s_movk_i32 s22, 30
	v_addc_co_u32_e32 v2, vcc, 0, v2, vcc
	v_cmp_gt_i64_e32 vcc, s[24:25], v[8:9]
	v_readlane_b32 s25, v9, 34
	s_movk_i32 s24, 29
	v_addc_co_u32_e32 v2, vcc, 0, v2, vcc
	v_cmp_gt_i64_e32 vcc, s[22:23], v[8:9]
	v_readlane_b32 s23, v9, 35
	s_movk_i32 s22, 28
	v_addc_co_u32_e32 v2, vcc, 0, v2, vcc
	v_cmp_gt_i64_e32 vcc, s[24:25], v[8:9]
	v_readlane_b32 s25, v9, 36
	s_movk_i32 s24, 27
	v_addc_co_u32_e32 v2, vcc, 0, v2, vcc
	v_cmp_gt_i64_e32 vcc, s[22:23], v[8:9]
	v_readlane_b32 s23, v9, 37
	s_movk_i32 s22, 26
	v_addc_co_u32_e32 v2, vcc, 0, v2, vcc
	v_cmp_gt_i64_e32 vcc, s[24:25], v[8:9]
	v_readlane_b32 s25, v9, 38
	s_movk_i32 s24, 25
	v_addc_co_u32_e32 v2, vcc, 0, v2, vcc
	v_cmp_gt_i64_e32 vcc, s[22:23], v[8:9]
	v_readlane_b32 s23, v9, 39
	s_movk_i32 s22, 24
	v_addc_co_u32_e32 v2, vcc, 0, v2, vcc
	v_cmp_gt_i64_e32 vcc, s[24:25], v[8:9]
	v_readlane_b32 s25, v9, 40
	s_movk_i32 s24, 23
	v_addc_co_u32_e32 v2, vcc, 0, v2, vcc
	v_cmp_gt_i64_e32 vcc, s[22:23], v[8:9]
	v_readlane_b32 s23, v9, 41
	s_movk_i32 s22, 22
	v_addc_co_u32_e32 v2, vcc, 0, v2, vcc
	v_cmp_gt_i64_e32 vcc, s[24:25], v[8:9]
	v_readlane_b32 s25, v9, 42
	s_movk_i32 s24, 21
	v_addc_co_u32_e32 v2, vcc, 0, v2, vcc
	v_cmp_gt_i64_e32 vcc, s[22:23], v[8:9]
	v_readlane_b32 s23, v9, 43
	s_movk_i32 s22, 20
	v_addc_co_u32_e32 v2, vcc, 0, v2, vcc
	v_cmp_gt_i64_e32 vcc, s[24:25], v[8:9]
	v_readlane_b32 s25, v9, 44
	s_movk_i32 s24, 19
	v_addc_co_u32_e32 v2, vcc, 0, v2, vcc
	v_cmp_gt_i64_e32 vcc, s[22:23], v[8:9]
	v_readlane_b32 s23, v9, 45
	s_movk_i32 s22, 18
	v_addc_co_u32_e32 v2, vcc, 0, v2, vcc
	v_cmp_gt_i64_e32 vcc, s[24:25], v[8:9]
	v_readlane_b32 s25, v9, 46
	s_movk_i32 s24, 17
	v_addc_co_u32_e32 v2, vcc, 0, v2, vcc
	v_cmp_gt_i64_e32 vcc, s[22:23], v[8:9]
	v_readlane_b32 s23, v9, 47
	s_movk_i32 s22, 16
	v_addc_co_u32_e32 v2, vcc, 0, v2, vcc
	v_cmp_gt_i64_e32 vcc, s[24:25], v[8:9]
	v_readlane_b32 s25, v9, 48
	s_movk_i32 s24, 15
	v_addc_co_u32_e32 v2, vcc, 0, v2, vcc
	v_cmp_gt_i64_e32 vcc, s[22:23], v[8:9]
	v_readlane_b32 s23, v9, 49
	s_movk_i32 s22, 14
	v_addc_co_u32_e32 v2, vcc, 0, v2, vcc
	v_cmp_gt_i64_e32 vcc, s[24:25], v[8:9]
	v_readlane_b32 s25, v9, 50
	s_movk_i32 s24, 13
	v_addc_co_u32_e32 v2, vcc, 0, v2, vcc
	v_cmp_gt_i64_e32 vcc, s[22:23], v[8:9]
	v_readlane_b32 s23, v9, 51
	s_movk_i32 s22, 12
	v_addc_co_u32_e32 v2, vcc, 0, v2, vcc
	v_cmp_gt_i64_e32 vcc, s[24:25], v[8:9]
	v_readlane_b32 s25, v9, 52
	s_movk_i32 s24, 11
	v_addc_co_u32_e32 v2, vcc, 0, v2, vcc
; __device__ __forceinline__ void phase_nrr(const Frame& F, const Args& a, int l, const bf16_t* XA, const float* g, const float* modl, unsigned char* XN8) {
;     ...
;         for (int i = 0; i < 8; ++i) { const int t = tb + i;
;             const float lg = Pl[(w * 8 + i) * NE + lane] + Pl[(64 + w * 8 + i) * NE + lane]; const float sc = 1.f / (1.f + __expf(-lg)); const float bb = sc + bias;
;             float m1 = bb; m1 = fmaxf(m1, __shfl_xor(m1, 1)); m1 = fmaxf(m1, __shfl_xor(m1, 2)); m1 = fmaxf(m1, __shfl_xor(m1, 4));
;             const unsigned long long eq = __ballot(bb == m1); const int gbase = lane & ~7; const unsigned grpmask = (unsigned)((eq >> gbase) & 0xffull);
;             const int first = gbase + __builtin_ctz(grpmask);
;             float m2 = (lane == first) ? -INFINITY : bb; m2 = fmaxf(m2, __shfl_xor(m2, 1)); m2 = fmaxf(m2, __shfl_xor(m2, 2)); m2 = fmaxf(m2, __shfl_xor(m2, 4));
;     ...
;             int rank = 0;
; #pragma unroll 8
;             for (int e2 = 0; e2 < 64; ++e2) { const float v = __int_as_float(__builtin_amdgcn_readlane(__float_as_int(val), e2)); rank += (v > val || (v == val && e2 < lane)) ? 1 : 0; }
;             const bool sel = rank < TOPK;
;             const float ssum = wave_sum(sel ? sc : 0.f);
;             if (sel) { const int p = atomicAdd((int*)(hist + lane), 1); top_e[t * TOPK + rank] = lane; gate[t * TOPK + rank] = sc / ssum * 2.5f; lpos[t * TOPK + rank] = p; }
	v_cmp_gt_i64_e32 vcc, s[22:23], v[8:9]
	v_readlane_b32 s23, v9, 53
	s_movk_i32 s22, 10
	v_addc_co_u32_e32 v2, vcc, 0, v2, vcc
	v_cmp_gt_i64_e32 vcc, s[24:25], v[8:9]
	v_readlane_b32 s25, v9, 54
	s_movk_i32 s24, 9
	v_addc_co_u32_e32 v2, vcc, 0, v2, vcc
	v_cmp_gt_i64_e32 vcc, s[22:23], v[8:9]
	v_readlane_b32 s23, v9, 55
	s_movk_i32 s22, 8
	v_addc_co_u32_e32 v2, vcc, 0, v2, vcc
	v_cmp_gt_i64_e32 vcc, s[24:25], v[8:9]
	v_readlane_b32 s25, v9, 56
	s_movk_i32 s24, 7
	v_addc_co_u32_e32 v2, vcc, 0, v2, vcc
	v_cmp_gt_i64_e32 vcc, s[22:23], v[8:9]
	v_readlane_b32 s23, v9, 57
	s_movk_i32 s22, 6
	v_addc_co_u32_e32 v2, vcc, 0, v2, vcc
	v_cmp_gt_i64_e32 vcc, s[24:25], v[8:9]
	v_readlane_b32 s25, v9, 58
	s_movk_i32 s24, 5
	v_addc_co_u32_e32 v2, vcc, 0, v2, vcc
	v_cmp_gt_i64_e32 vcc, s[22:23], v[8:9]
	v_readlane_b32 s23, v9, 59
	s_movk_i32 s22, 4
	v_addc_co_u32_e32 v2, vcc, 0, v2, vcc
	v_cmp_gt_i64_e32 vcc, s[24:25], v[8:9]
	v_readlane_b32 s25, v9, 60
	s_movk_i32 s24, 3
	v_addc_co_u32_e32 v2, vcc, 0, v2, vcc
	v_cmp_gt_i64_e32 vcc, s[22:23], v[8:9]
	v_readlane_b32 s23, v9, 61
	s_movk_i32 s22, 2
	v_addc_co_u32_e32 v2, vcc, 0, v2, vcc
	v_cmp_gt_i64_e32 vcc, s[24:25], v[8:9]
	v_readlane_b32 s25, v9, 62
	s_movk_i32 s24, 1
	v_addc_co_u32_e32 v2, vcc, 0, v2, vcc
	v_cmp_gt_i64_e32 vcc, s[22:23], v[8:9]
	v_readlane_b32 s23, v9, 63
	s_movk_i32 s22, 0
	v_addc_co_u32_e32 v2, vcc, 0, v2, vcc
	v_cmp_gt_i64_e32 vcc, s[24:25], v[8:9]
	s_nop 1
	v_addc_co_u32_e32 v2, vcc, 0, v2, vcc
	v_cmp_gt_i64_e32 vcc, s[22:23], v[8:9]
	s_nop 1
	v_addc_co_u32_e32 v2, vcc, 0, v2, vcc
	v_cmp_gt_u32_e32 vcc, 6, v2
	s_nop 1
	v_cndmask_b32_e32 v6, 0, v5, vcc
	ds_bpermute_b32 v7, v1, v6
	s_waitcnt lgkmcnt(0)
	v_add_f32_e32 v6, v6, v7
	ds_bpermute_b32 v7, v201, v6
	s_waitcnt lgkmcnt(0)
	v_add_f32_e32 v6, v6, v7
	ds_bpermute_b32 v7, v220, v6
	s_waitcnt lgkmcnt(0)
	v_add_f32_e32 v6, v6, v7
	ds_bpermute_b32 v7, v221, v6
	s_waitcnt lgkmcnt(0)
	v_add_f32_e32 v6, v6, v7
	ds_bpermute_b32 v7, v222, v6
	s_waitcnt lgkmcnt(0)
	v_add_f32_e32 v6, v6, v7
	ds_bpermute_b32 v7, v223, v6
	s_and_saveexec_b64 s[22:23], vcc
	s_cbranch_execz .LBB0_547
	s_waitcnt lgkmcnt(0)
	v_add_f32_e32 v10, v6, v7
	v_mad_u64_u32 v[6:7], s[24:25], s40, 6, v[2:3]
	v_div_scale_f32 v2, s[24:25], v10, v10, v5
	v_rcp_f32_e32 v12, v2
	v_ashrrev_i32_e32 v7, 31, v6
	v_lshlrev_b64 v[6:7], 2, v[6:7]
	v_lshl_add_u64 v[8:9], s[26:27], 0, v[6:7]
	ds_add_rtn_u32 v11, v227, v243
	global_store_dword v[8:9], v230, off
	v_fma_f32 v8, -v2, v12, 1.0
	v_fmac_f32_e32 v12, v8, v12
	v_div_scale_f32 v8, vcc, v5, v10, v5
	v_mul_f32_e32 v9, v8, v12
	v_fma_f32 v13, -v2, v9, v8
	v_fmac_f32_e32 v9, v13, v12
	v_fma_f32 v2, -v2, v9, v8
	v_div_fmas_f32 v2, v2, v12, v9
	v_div_fixup_f32 v2, v2, v10, v5
	v_mul_f32_e32 v2, 0x40200000, v2
	v_lshl_add_u64 v[8:9], s[28:29], 0, v[6:7]
	v_lshl_add_u64 v[6:7], s[30:31], 0, v[6:7]
	global_store_dword v[8:9], v2, off
	s_waitcnt lgkmcnt(0)
	global_store_dword v[6:7], v11, off
.LBB0_547:
	s_or_b64 exec, exec, s[22:23]
	v_add_u32_e32 v2, s79, v226
	ds_read_b32 v2, v2
	ds_read_b32 v5, v4 offset:17152
	s_mov_b32 s3, 0
	s_waitcnt lgkmcnt(0)
	v_add_f32_e32 v2, v2, v5
	v_mul_f32_e32 v2, 0xbfb8aa3b, v2
	v_exp_f32_e32 v2, v2
	s_nop 0
	v_add_f32_e32 v2, 1.0, v2
	v_div_scale_f32 v5, s[22:23], v2, v2, 1.0
	v_rcp_f32_e32 v6, v5
	s_nop 0
	v_fma_f32 v7, -v5, v6, 1.0
	v_fmac_f32_e32 v6, v7, v6
	v_div_scale_f32 v7, vcc, 1.0, v2, 1.0
	v_mul_f32_e32 v8, v7, v6
	v_fma_f32 v9, -v5, v8, v7
	v_fmac_f32_e32 v8, v9, v6
	v_fma_f32 v5, -v5, v8, v7
	v_div_fmas_f32 v5, v5, v6, v8
	v_div_fixup_f32 v5, v5, v2, 1.0
	v_add_f32_e32 v2, v3, v5
	ds_bpermute_b32 v6, v1, v2
	s_waitcnt lgkmcnt(0)
	v_max_f32_e32 v6, v6, v6
	v_max_f32_e32 v6, v2, v6
	ds_bpermute_b32 v7, v201, v6
	s_waitcnt lgkmcnt(0)
	v_max_f32_e32 v7, v7, v7
	v_max_f32_e32 v6, v6, v7
	ds_bpermute_b32 v7, v220, v6
	s_waitcnt lgkmcnt(0)
	v_max_f32_e32 v7, v7, v7
	v_max_f32_e32 v8, v6, v7
	v_cmp_eq_f32_e32 vcc, v2, v8
	s_nop 1
	v_lshrrev_b64 v[6:7], v200, vcc
	v_ffbl_b32_sdwa v6, v6 dst_sel:DWORD dst_unused:UNUSED_PAD src0_sel:BYTE_0
	v_add_u32_e32 v6, v6, v200
	v_cmp_ne_u32_e32 vcc, v230, v6
	s_nop 1
	v_cndmask_b32_e32 v6, v245, v2, vcc
	ds_bpermute_b32 v7, v1, v6
	s_waitcnt lgkmcnt(0)
	v_max_f32_e32 v7, v7, v7
	v_max_f32_e32 v6, v6, v7
	ds_bpermute_b32 v7, v201, v6
	s_waitcnt lgkmcnt(0)
	v_max_f32_e32 v7, v7, v7
	v_max_f32_e32 v6, v6, v7
	ds_bpermute_b32 v7, v220, v6
	s_waitcnt lgkmcnt(0)
; __device__ __forceinline__ void phase_nrr(const Frame& F, const Args& a, int l, const bf16_t* XA, const float* g, const float* modl, unsigned char* XN8) {
;     ...
;             float m1 = bb; m1 = fmaxf(m1, __shfl_xor(m1, 1)); m1 = fmaxf(m1, __shfl_xor(m1, 2)); m1 = fmaxf(m1, __shfl_xor(m1, 4));
;             const unsigned long long eq = __ballot(bb == m1); const int gbase = lane & ~7; const unsigned grpmask = (unsigned)((eq >> gbase) & 0xffull);
;             const int first = gbase + __builtin_ctz(grpmask);
;             float m2 = (lane == first) ? -INFINITY : bb; m2 = fmaxf(m2, __shfl_xor(m2, 1)); m2 = fmaxf(m2, __shfl_xor(m2, 2)); m2 = fmaxf(m2, __shfl_xor(m2, 4));
;             const float gsum = m1 + m2; const int gq = lane >> 3;
;             int grank = 0;
; #pragma unroll
;             for (int g2 = 0; g2 < 8; ++g2) { const float v = __int_as_float(__builtin_amdgcn_readlane(__float_as_int(gsum), g2 * 8)); grank += (v > gsum || (v == gsum && g2 < gq)) ? 1 : 0; }
;             const bool keep = grank < 4; const float val = keep ? bb : -INFINITY;
;             int rank = 0;
; #pragma unroll 8
;             for (int e2 = 0; e2 < 64; ++e2) { const float v = __int_as_float(__builtin_amdgcn_readlane(__float_as_int(val), e2)); rank += (v > val || (v == val && e2 < lane)) ? 1 : 0; }
	v_max_f32_e32 v7, v7, v7
	v_max_f32_e32 v6, v6, v7
	v_add_f32_e32 v6, v8, v6
	s_nop 0
	v_readlane_b32 s5, v6, 0
	s_nop 1
	v_cmp_eq_f32_e64 s[22:23], s5, v6
	v_cmp_gt_f32_e32 vcc, s5, v6
	s_and_b64 s[22:23], s[6:7], s[22:23]
	s_or_b64 s[22:23], vcc, s[22:23]
	v_readlane_b32 s5, v6, 8
	v_cndmask_b32_e64 v7, 0, 1, s[22:23]
	s_nop 0
	v_cmp_eq_f32_e64 s[22:23], s5, v6
	v_cmp_gt_f32_e32 vcc, s5, v6
	s_and_b64 s[22:23], s[8:9], s[22:23]
	s_or_b64 s[22:23], vcc, s[22:23]
	v_readlane_b32 s5, v6, 16
	v_cndmask_b32_e64 v8, 0, 1, s[22:23]
	s_nop 0
	v_cmp_eq_f32_e64 s[22:23], s5, v6
	v_cmp_gt_f32_e32 vcc, s5, v6
	s_and_b64 s[22:23], s[10:11], s[22:23]
	s_or_b64 s[22:23], vcc, s[22:23]
	v_readlane_b32 s5, v6, 24
	v_cndmask_b32_e64 v9, 0, 1, s[22:23]
	s_nop 0
	v_cmp_eq_f32_e64 s[22:23], s5, v6
	v_cmp_gt_f32_e32 vcc, s5, v6
	s_and_b64 s[22:23], s[12:13], s[22:23]
	s_or_b64 s[22:23], vcc, s[22:23]
	v_readlane_b32 s5, v6, 32
	v_cndmask_b32_e64 v10, 0, 1, s[22:23]
	s_nop 0
	v_cmp_eq_f32_e64 s[22:23], s5, v6
	v_cmp_gt_f32_e32 vcc, s5, v6
	s_and_b64 s[22:23], s[14:15], s[22:23]
	s_or_b64 s[22:23], vcc, s[22:23]
	v_readlane_b32 s5, v6, 40
	v_cndmask_b32_e64 v11, 0, 1, s[22:23]
	s_nop 0
	v_cmp_eq_f32_e64 s[22:23], s5, v6
	v_cmp_gt_f32_e32 vcc, s5, v6
	s_and_b64 s[22:23], s[16:17], s[22:23]
	s_or_b64 s[22:23], vcc, s[22:23]
	v_readlane_b32 s5, v6, 48
	v_cndmask_b32_e64 v12, 0, 1, s[22:23]
	s_nop 0
	v_cmp_eq_f32_e64 s[22:23], s5, v6
	v_cmp_gt_f32_e32 vcc, s5, v6
	s_and_b64 s[22:23], s[18:19], s[22:23]
	v_readlane_b32 s5, v6, 56
	s_or_b64 s[22:23], vcc, s[22:23]
	v_cndmask_b32_e64 v13, 0, 1, s[22:23]
	v_cmp_gt_f32_e32 vcc, s5, v6
	s_nop 1
	v_cndmask_b32_e64 v6, 0, 1, vcc
	v_add_u32_e32 v6, v8, v6
	v_add3_u32 v6, v6, v7, v9
	v_add3_u32 v6, v6, v10, v11
	v_add3_u32 v6, v6, v12, v13
	v_cmp_gt_u32_e32 vcc, 4, v6
	s_nop 1
	v_cndmask_b32_e32 v6, v245, v2, vcc
	v_mov_b32_e32 v2, 0
	v_ashrrev_i32_e32 v9, 31, v6
	v_sub_u32_e32 v8, 63, v230
	v_and_b32_e32 v9, 0x7fffffff, v9
	v_xor_b32_e32 v9, v6, v9
	s_nop 0
	v_readlane_b32 s25, v9, 0
	s_movk_i32 s24, 63
	v_readlane_b32 s23, v9, 1
	s_movk_i32 s22, 62
	v_cmp_gt_i64_e32 vcc, s[24:25], v[8:9]
	v_readlane_b32 s25, v9, 2
	s_movk_i32 s24, 61
	v_addc_co_u32_e32 v2, vcc, 0, v2, vcc
	v_cmp_gt_i64_e32 vcc, s[22:23], v[8:9]
	v_readlane_b32 s23, v9, 3
	s_movk_i32 s22, 60
	v_addc_co_u32_e32 v2, vcc, 0, v2, vcc
	v_cmp_gt_i64_e32 vcc, s[24:25], v[8:9]
	v_readlane_b32 s25, v9, 4
	s_movk_i32 s24, 59
	v_addc_co_u32_e32 v2, vcc, 0, v2, vcc
	v_cmp_gt_i64_e32 vcc, s[22:23], v[8:9]
	v_readlane_b32 s23, v9, 5
	s_movk_i32 s22, 58
	v_addc_co_u32_e32 v2, vcc, 0, v2, vcc
	v_cmp_gt_i64_e32 vcc, s[24:25], v[8:9]
	v_readlane_b32 s25, v9, 6
	s_movk_i32 s24, 57
	v_addc_co_u32_e32 v2, vcc, 0, v2, vcc
	v_cmp_gt_i64_e32 vcc, s[22:23], v[8:9]
	v_readlane_b32 s23, v9, 7
	s_movk_i32 s22, 56
	v_addc_co_u32_e32 v2, vcc, 0, v2, vcc
	v_cmp_gt_i64_e32 vcc, s[24:25], v[8:9]
	v_readlane_b32 s25, v9, 8
	s_movk_i32 s24, 55
	v_addc_co_u32_e32 v2, vcc, 0, v2, vcc
	v_cmp_gt_i64_e32 vcc, s[22:23], v[8:9]
	v_readlane_b32 s23, v9, 9
	s_movk_i32 s22, 54
	v_addc_co_u32_e32 v2, vcc, 0, v2, vcc
	v_cmp_gt_i64_e32 vcc, s[24:25], v[8:9]
	v_readlane_b32 s25, v9, 10
	s_movk_i32 s24, 53
	v_addc_co_u32_e32 v2, vcc, 0, v2, vcc
	v_cmp_gt_i64_e32 vcc, s[22:23], v[8:9]
	v_readlane_b32 s23, v9, 11
	s_movk_i32 s22, 52
	v_addc_co_u32_e32 v2, vcc, 0, v2, vcc
	v_cmp_gt_i64_e32 vcc, s[24:25], v[8:9]
	v_readlane_b32 s25, v9, 12
	s_movk_i32 s24, 51
	v_addc_co_u32_e32 v2, vcc, 0, v2, vcc
	v_cmp_gt_i64_e32 vcc, s[22:23], v[8:9]
	v_readlane_b32 s23, v9, 13
	s_movk_i32 s22, 50
	v_addc_co_u32_e32 v2, vcc, 0, v2, vcc
	v_cmp_gt_i64_e32 vcc, s[24:25], v[8:9]
	v_readlane_b32 s25, v9, 14
	s_movk_i32 s24, 49
	v_addc_co_u32_e32 v2, vcc, 0, v2, vcc
	v_cmp_gt_i64_e32 vcc, s[22:23], v[8:9]
	v_readlane_b32 s23, v9, 15
	s_movk_i32 s22, 48
	v_addc_co_u32_e32 v2, vcc, 0, v2, vcc
	v_cmp_gt_i64_e32 vcc, s[24:25], v[8:9]
	v_readlane_b32 s25, v9, 16
	s_movk_i32 s24, 47
	v_addc_co_u32_e32 v2, vcc, 0, v2, vcc
	v_cmp_gt_i64_e32 vcc, s[22:23], v[8:9]
	v_readlane_b32 s23, v9, 17
	s_movk_i32 s22, 46
	v_addc_co_u32_e32 v2, vcc, 0, v2, vcc
	v_cmp_gt_i64_e32 vcc, s[24:25], v[8:9]
	v_readlane_b32 s25, v9, 18
	s_movk_i32 s24, 45
	v_addc_co_u32_e32 v2, vcc, 0, v2, vcc
	v_cmp_gt_i64_e32 vcc, s[22:23], v[8:9]
	v_readlane_b32 s23, v9, 19
	s_movk_i32 s22, 44
	v_addc_co_u32_e32 v2, vcc, 0, v2, vcc
	v_cmp_gt_i64_e32 vcc, s[24:25], v[8:9]
	v_readlane_b32 s25, v9, 20
	s_movk_i32 s24, 43
	v_addc_co_u32_e32 v2, vcc, 0, v2, vcc
	v_cmp_gt_i64_e32 vcc, s[22:23], v[8:9]
	v_readlane_b32 s23, v9, 21
	s_movk_i32 s22, 42
	v_addc_co_u32_e32 v2, vcc, 0, v2, vcc
	v_cmp_gt_i64_e32 vcc, s[24:25], v[8:9]
	v_readlane_b32 s25, v9, 22
	s_movk_i32 s24, 41
	v_addc_co_u32_e32 v2, vcc, 0, v2, vcc
	v_cmp_gt_i64_e32 vcc, s[22:23], v[8:9]
	v_readlane_b32 s23, v9, 23
	s_movk_i32 s22, 40
	v_addc_co_u32_e32 v2, vcc, 0, v2, vcc
	v_cmp_gt_i64_e32 vcc, s[24:25], v[8:9]
	v_readlane_b32 s25, v9, 24
	s_movk_i32 s24, 39
	v_addc_co_u32_e32 v2, vcc, 0, v2, vcc
	v_cmp_gt_i64_e32 vcc, s[22:23], v[8:9]
	v_readlane_b32 s23, v9, 25
	s_movk_i32 s22, 38
	v_addc_co_u32_e32 v2, vcc, 0, v2, vcc
	v_cmp_gt_i64_e32 vcc, s[24:25], v[8:9]
	v_readlane_b32 s25, v9, 26
	s_movk_i32 s24, 37
	v_addc_co_u32_e32 v2, vcc, 0, v2, vcc
	v_cmp_gt_i64_e32 vcc, s[22:23], v[8:9]
	v_readlane_b32 s23, v9, 27
	s_movk_i32 s22, 36
	v_addc_co_u32_e32 v2, vcc, 0, v2, vcc
	v_cmp_gt_i64_e32 vcc, s[24:25], v[8:9]
	v_readlane_b32 s25, v9, 28
	s_movk_i32 s24, 35
	v_addc_co_u32_e32 v2, vcc, 0, v2, vcc
	v_cmp_gt_i64_e32 vcc, s[22:23], v[8:9]
	v_readlane_b32 s23, v9, 29
	s_movk_i32 s22, 34
	v_addc_co_u32_e32 v2, vcc, 0, v2, vcc
; __device__ __forceinline__ void phase_nrr(const Frame& F, const Args& a, int l, const bf16_t* XA, const float* g, const float* modl, unsigned char* XN8) {
;     ...
;             int rank = 0;
; #pragma unroll 8
;             for (int e2 = 0; e2 < 64; ++e2) { const float v = __int_as_float(__builtin_amdgcn_readlane(__float_as_int(val), e2)); rank += (v > val || (v == val && e2 < lane)) ? 1 : 0; }
;             const bool sel = rank < TOPK;
;             const float ssum = wave_sum(sel ? sc : 0.f);
;             if (sel) { const int p = atomicAdd((int*)(hist + lane), 1); top_e[t * TOPK + rank] = lane; gate[t * TOPK + rank] = sc / ssum * 2.5f; lpos[t * TOPK + rank] = p; }
	v_cmp_gt_i64_e32 vcc, s[24:25], v[8:9]
	v_readlane_b32 s25, v9, 30
	s_movk_i32 s24, 33
	v_addc_co_u32_e32 v2, vcc, 0, v2, vcc
	v_cmp_gt_i64_e32 vcc, s[22:23], v[8:9]
	v_readlane_b32 s23, v9, 31
	s_movk_i32 s22, 32
	v_addc_co_u32_e32 v2, vcc, 0, v2, vcc
	v_cmp_gt_i64_e32 vcc, s[24:25], v[8:9]
	v_readlane_b32 s25, v9, 32
	s_movk_i32 s24, 31
	v_addc_co_u32_e32 v2, vcc, 0, v2, vcc
	v_cmp_gt_i64_e32 vcc, s[22:23], v[8:9]
	v_readlane_b32 s23, v9, 33
	s_movk_i32 s22, 30
	v_addc_co_u32_e32 v2, vcc, 0, v2, vcc
	v_cmp_gt_i64_e32 vcc, s[24:25], v[8:9]
	v_readlane_b32 s25, v9, 34
	s_movk_i32 s24, 29
	v_addc_co_u32_e32 v2, vcc, 0, v2, vcc
	v_cmp_gt_i64_e32 vcc, s[22:23], v[8:9]
	v_readlane_b32 s23, v9, 35
	s_movk_i32 s22, 28
	v_addc_co_u32_e32 v2, vcc, 0, v2, vcc
	v_cmp_gt_i64_e32 vcc, s[24:25], v[8:9]
	v_readlane_b32 s25, v9, 36
	s_movk_i32 s24, 27
	v_addc_co_u32_e32 v2, vcc, 0, v2, vcc
	v_cmp_gt_i64_e32 vcc, s[22:23], v[8:9]
	v_readlane_b32 s23, v9, 37
	s_movk_i32 s22, 26
	v_addc_co_u32_e32 v2, vcc, 0, v2, vcc
	v_cmp_gt_i64_e32 vcc, s[24:25], v[8:9]
	v_readlane_b32 s25, v9, 38
	s_movk_i32 s24, 25
	v_addc_co_u32_e32 v2, vcc, 0, v2, vcc
	v_cmp_gt_i64_e32 vcc, s[22:23], v[8:9]
	v_readlane_b32 s23, v9, 39
	s_movk_i32 s22, 24
	v_addc_co_u32_e32 v2, vcc, 0, v2, vcc
	v_cmp_gt_i64_e32 vcc, s[24:25], v[8:9]
	v_readlane_b32 s25, v9, 40
	s_movk_i32 s24, 23
	v_addc_co_u32_e32 v2, vcc, 0, v2, vcc
	v_cmp_gt_i64_e32 vcc, s[22:23], v[8:9]
	v_readlane_b32 s23, v9, 41
	s_movk_i32 s22, 22
	v_addc_co_u32_e32 v2, vcc, 0, v2, vcc
	v_cmp_gt_i64_e32 vcc, s[24:25], v[8:9]
	v_readlane_b32 s25, v9, 42
	s_movk_i32 s24, 21
	v_addc_co_u32_e32 v2, vcc, 0, v2, vcc
	v_cmp_gt_i64_e32 vcc, s[22:23], v[8:9]
	v_readlane_b32 s23, v9, 43
	s_movk_i32 s22, 20
	v_addc_co_u32_e32 v2, vcc, 0, v2, vcc
	v_cmp_gt_i64_e32 vcc, s[24:25], v[8:9]
	v_readlane_b32 s25, v9, 44
	s_movk_i32 s24, 19
	v_addc_co_u32_e32 v2, vcc, 0, v2, vcc
	v_cmp_gt_i64_e32 vcc, s[22:23], v[8:9]
	v_readlane_b32 s23, v9, 45
	s_movk_i32 s22, 18
	v_addc_co_u32_e32 v2, vcc, 0, v2, vcc
	v_cmp_gt_i64_e32 vcc, s[24:25], v[8:9]
	v_readlane_b32 s25, v9, 46
	s_movk_i32 s24, 17
	v_addc_co_u32_e32 v2, vcc, 0, v2, vcc
	v_cmp_gt_i64_e32 vcc, s[22:23], v[8:9]
	v_readlane_b32 s23, v9, 47
	s_movk_i32 s22, 16
	v_addc_co_u32_e32 v2, vcc, 0, v2, vcc
	v_cmp_gt_i64_e32 vcc, s[24:25], v[8:9]
	v_readlane_b32 s25, v9, 48
	s_movk_i32 s24, 15
	v_addc_co_u32_e32 v2, vcc, 0, v2, vcc
	v_cmp_gt_i64_e32 vcc, s[22:23], v[8:9]
	v_readlane_b32 s23, v9, 49
	s_movk_i32 s22, 14
	v_addc_co_u32_e32 v2, vcc, 0, v2, vcc
	v_cmp_gt_i64_e32 vcc, s[24:25], v[8:9]
	v_readlane_b32 s25, v9, 50
	s_movk_i32 s24, 13
	v_addc_co_u32_e32 v2, vcc, 0, v2, vcc
	v_cmp_gt_i64_e32 vcc, s[22:23], v[8:9]
	v_readlane_b32 s23, v9, 51
	s_movk_i32 s22, 12
	v_addc_co_u32_e32 v2, vcc, 0, v2, vcc
	v_cmp_gt_i64_e32 vcc, s[24:25], v[8:9]
	v_readlane_b32 s25, v9, 52
	s_movk_i32 s24, 11
	v_addc_co_u32_e32 v2, vcc, 0, v2, vcc
	v_cmp_gt_i64_e32 vcc, s[22:23], v[8:9]
	v_readlane_b32 s23, v9, 53
	s_movk_i32 s22, 10
	v_addc_co_u32_e32 v2, vcc, 0, v2, vcc
	v_cmp_gt_i64_e32 vcc, s[24:25], v[8:9]
	v_readlane_b32 s25, v9, 54
	s_movk_i32 s24, 9
	v_addc_co_u32_e32 v2, vcc, 0, v2, vcc
	v_cmp_gt_i64_e32 vcc, s[22:23], v[8:9]
	v_readlane_b32 s23, v9, 55
	s_movk_i32 s22, 8
	v_addc_co_u32_e32 v2, vcc, 0, v2, vcc
	v_cmp_gt_i64_e32 vcc, s[24:25], v[8:9]
	v_readlane_b32 s25, v9, 56
	s_movk_i32 s24, 7
	v_addc_co_u32_e32 v2, vcc, 0, v2, vcc
	v_cmp_gt_i64_e32 vcc, s[22:23], v[8:9]
	v_readlane_b32 s23, v9, 57
	s_movk_i32 s22, 6
	v_addc_co_u32_e32 v2, vcc, 0, v2, vcc
	v_cmp_gt_i64_e32 vcc, s[24:25], v[8:9]
	v_readlane_b32 s25, v9, 58
	s_movk_i32 s24, 5
	v_addc_co_u32_e32 v2, vcc, 0, v2, vcc
	v_cmp_gt_i64_e32 vcc, s[22:23], v[8:9]
	v_readlane_b32 s23, v9, 59
	s_movk_i32 s22, 4
	v_addc_co_u32_e32 v2, vcc, 0, v2, vcc
	v_cmp_gt_i64_e32 vcc, s[24:25], v[8:9]
	v_readlane_b32 s25, v9, 60
	s_movk_i32 s24, 3
	v_addc_co_u32_e32 v2, vcc, 0, v2, vcc
	v_cmp_gt_i64_e32 vcc, s[22:23], v[8:9]
	v_readlane_b32 s23, v9, 61
	s_movk_i32 s22, 2
	v_addc_co_u32_e32 v2, vcc, 0, v2, vcc
	v_cmp_gt_i64_e32 vcc, s[24:25], v[8:9]
	v_readlane_b32 s25, v9, 62
	s_movk_i32 s24, 1
	v_addc_co_u32_e32 v2, vcc, 0, v2, vcc
	v_cmp_gt_i64_e32 vcc, s[22:23], v[8:9]
	v_readlane_b32 s23, v9, 63
	s_movk_i32 s22, 0
	v_addc_co_u32_e32 v2, vcc, 0, v2, vcc
	v_cmp_gt_i64_e32 vcc, s[24:25], v[8:9]
	s_nop 1
	v_addc_co_u32_e32 v2, vcc, 0, v2, vcc
	v_cmp_gt_i64_e32 vcc, s[22:23], v[8:9]
	s_nop 1
	v_addc_co_u32_e32 v2, vcc, 0, v2, vcc
	v_cmp_gt_u32_e32 vcc, 6, v2
	s_nop 1
	v_cndmask_b32_e32 v6, 0, v5, vcc
	ds_bpermute_b32 v7, v1, v6
	s_waitcnt lgkmcnt(0)
	v_add_f32_e32 v6, v6, v7
	ds_bpermute_b32 v7, v201, v6
	s_waitcnt lgkmcnt(0)
	v_add_f32_e32 v6, v6, v7
	ds_bpermute_b32 v7, v220, v6
	s_waitcnt lgkmcnt(0)
	v_add_f32_e32 v6, v6, v7
	ds_bpermute_b32 v7, v221, v6
	s_waitcnt lgkmcnt(0)
	v_add_f32_e32 v6, v6, v7
	ds_bpermute_b32 v7, v222, v6
	s_waitcnt lgkmcnt(0)
	v_add_f32_e32 v6, v6, v7
	ds_bpermute_b32 v7, v223, v6
	s_and_saveexec_b64 s[22:23], vcc
	s_cbranch_execz .LBB0_551
	s_waitcnt lgkmcnt(0)
	v_add_f32_e32 v10, v6, v7
	v_mad_u64_u32 v[6:7], s[4:5], s4, 6, v[2:3]
	v_div_scale_f32 v2, s[4:5], v10, v10, v5
	v_rcp_f32_e32 v12, v2
	v_ashrrev_i32_e32 v7, 31, v6
	v_lshlrev_b64 v[6:7], 2, v[6:7]
	v_lshl_add_u64 v[8:9], s[26:27], 0, v[6:7]
	ds_add_rtn_u32 v11, v227, v243
	global_store_dword v[8:9], v230, off
	v_fma_f32 v8, -v2, v12, 1.0
	v_fmac_f32_e32 v12, v8, v12
	v_div_scale_f32 v8, vcc, v5, v10, v5
	v_mul_f32_e32 v9, v8, v12
	v_fma_f32 v13, -v2, v9, v8
	v_fmac_f32_e32 v9, v13, v12
	v_fma_f32 v2, -v2, v9, v8
	v_div_fmas_f32 v2, v2, v12, v9
	v_div_fixup_f32 v2, v2, v10, v5
	v_mul_f32_e32 v2, 0x40200000, v2
	v_lshl_add_u64 v[8:9], s[28:29], 0, v[6:7]
	v_lshl_add_u64 v[6:7], s[30:31], 0, v[6:7]
	global_store_dword v[8:9], v2, off
	s_waitcnt lgkmcnt(0)
	global_store_dword v[6:7], v11, off
; __device__ __forceinline__ void phase_nrr(const Frame& F, const Args& a, int l, const bf16_t* XA, const float* g, const float* modl, unsigned char* XN8) {
;     ...
;         for (int i = 0; i < 8; ++i) { const int t = tb + i;
;             const float lg = Pl[(w * 8 + i) * NE + lane] + Pl[(64 + w * 8 + i) * NE + lane]; const float sc = 1.f / (1.f + __expf(-lg)); const float bb = sc + bias;
;             float m1 = bb; m1 = fmaxf(m1, __shfl_xor(m1, 1)); m1 = fmaxf(m1, __shfl_xor(m1, 2)); m1 = fmaxf(m1, __shfl_xor(m1, 4));
;             const unsigned long long eq = __ballot(bb == m1); const int gbase = lane & ~7; const unsigned grpmask = (unsigned)((eq >> gbase) & 0xffull);
;             const int first = gbase + __builtin_ctz(grpmask);
;             float m2 = (lane == first) ? -INFINITY : bb; m2 = fmaxf(m2, __shfl_xor(m2, 1)); m2 = fmaxf(m2, __shfl_xor(m2, 2)); m2 = fmaxf(m2, __shfl_xor(m2, 4));
;             const float gsum = m1 + m2; const int gq = lane >> 3;
;             int grank = 0;
; #pragma unroll
;             for (int g2 = 0; g2 < 8; ++g2) { const float v = __int_as_float(__builtin_amdgcn_readlane(__float_as_int(gsum), g2 * 8)); grank += (v > gsum || (v == gsum && g2 < gq)) ? 1 : 0; }
;             const bool keep = grank < 4; const float val = keep ? bb : -INFINITY;
;             int rank = 0;
; #pragma unroll 8
;             for (int e2 = 0; e2 < 64; ++e2) { const float v = __int_as_float(__builtin_amdgcn_readlane(__float_as_int(val), e2)); rank += (v > val || (v == val && e2 < lane)) ? 1 : 0; }
.LBB0_551:
	s_or_b64 exec, exec, s[22:23]
	v_add_u32_e32 v2, s84, v226
	ds_read_b32 v2, v2
	ds_read_b32 v5, v4 offset:17408
	s_mov_b32 s3, 0
	s_waitcnt lgkmcnt(0)
	v_add_f32_e32 v2, v2, v5
	v_mul_f32_e32 v2, 0xbfb8aa3b, v2
	v_exp_f32_e32 v2, v2
	s_nop 0
	v_add_f32_e32 v2, 1.0, v2
	v_div_scale_f32 v5, s[4:5], v2, v2, 1.0
	v_rcp_f32_e32 v6, v5
	s_nop 0
	v_fma_f32 v7, -v5, v6, 1.0
	v_fmac_f32_e32 v6, v7, v6
	v_div_scale_f32 v7, vcc, 1.0, v2, 1.0
	v_mul_f32_e32 v8, v7, v6
	v_fma_f32 v9, -v5, v8, v7
	v_fmac_f32_e32 v8, v9, v6
	v_fma_f32 v5, -v5, v8, v7
	v_div_fmas_f32 v5, v5, v6, v8
	v_div_fixup_f32 v2, v5, v2, 1.0
	v_add_f32_e32 v5, v3, v2
	ds_bpermute_b32 v6, v1, v5
	s_waitcnt lgkmcnt(0)
	v_max_f32_e32 v6, v6, v6
	v_max_f32_e32 v6, v5, v6
	ds_bpermute_b32 v7, v201, v6
	s_waitcnt lgkmcnt(0)
	v_max_f32_e32 v7, v7, v7
	v_max_f32_e32 v6, v6, v7
	ds_bpermute_b32 v7, v220, v6
	s_waitcnt lgkmcnt(0)
	v_max_f32_e32 v7, v7, v7
	v_max_f32_e32 v8, v6, v7
	v_cmp_eq_f32_e32 vcc, v5, v8
	s_nop 1
	v_lshrrev_b64 v[6:7], v200, vcc
	v_ffbl_b32_sdwa v6, v6 dst_sel:DWORD dst_unused:UNUSED_PAD src0_sel:BYTE_0
	v_add_u32_e32 v6, v6, v200
	v_cmp_ne_u32_e32 vcc, v230, v6
	s_nop 1
	v_cndmask_b32_e32 v6, v245, v5, vcc
	ds_bpermute_b32 v7, v1, v6
	s_waitcnt lgkmcnt(0)
	v_max_f32_e32 v7, v7, v7
	v_max_f32_e32 v6, v6, v7
	ds_bpermute_b32 v7, v201, v6
	s_waitcnt lgkmcnt(0)
	v_max_f32_e32 v7, v7, v7
	v_max_f32_e32 v6, v6, v7
	ds_bpermute_b32 v7, v220, v6
	s_waitcnt lgkmcnt(0)
	v_max_f32_e32 v7, v7, v7
	v_max_f32_e32 v6, v6, v7
	v_add_f32_e32 v6, v8, v6
	s_nop 0
	v_readlane_b32 s4, v6, 0
	s_nop 1
	v_cmp_eq_f32_e64 s[22:23], s4, v6
	v_cmp_gt_f32_e32 vcc, s4, v6
	s_and_b64 s[4:5], s[6:7], s[22:23]
	s_or_b64 s[4:5], vcc, s[4:5]
	v_cndmask_b32_e64 v7, 0, 1, s[4:5]
	v_readlane_b32 s4, v6, 8
	s_nop 1
	v_cmp_eq_f32_e64 s[22:23], s4, v6
	v_cmp_gt_f32_e32 vcc, s4, v6
	s_and_b64 s[4:5], s[8:9], s[22:23]
	s_or_b64 s[4:5], vcc, s[4:5]
	v_cndmask_b32_e64 v8, 0, 1, s[4:5]
	v_readlane_b32 s4, v6, 16
	s_nop 1
	v_cmp_eq_f32_e64 s[22:23], s4, v6
	v_cmp_gt_f32_e32 vcc, s4, v6
	s_and_b64 s[4:5], s[10:11], s[22:23]
	s_or_b64 s[4:5], vcc, s[4:5]
	v_cndmask_b32_e64 v9, 0, 1, s[4:5]
	v_readlane_b32 s4, v6, 24
	s_nop 1
	v_cmp_eq_f32_e64 s[22:23], s4, v6
	v_cmp_gt_f32_e32 vcc, s4, v6
	s_and_b64 s[4:5], s[12:13], s[22:23]
	s_or_b64 s[4:5], vcc, s[4:5]
	v_cndmask_b32_e64 v10, 0, 1, s[4:5]
	v_readlane_b32 s4, v6, 32
	s_nop 1
	v_cmp_eq_f32_e64 s[22:23], s4, v6
	v_cmp_gt_f32_e32 vcc, s4, v6
	s_and_b64 s[4:5], s[14:15], s[22:23]
	s_or_b64 s[4:5], vcc, s[4:5]
	v_cndmask_b32_e64 v11, 0, 1, s[4:5]
	v_readlane_b32 s4, v6, 40
	s_nop 1
	v_cmp_eq_f32_e64 s[22:23], s4, v6
	v_cmp_gt_f32_e32 vcc, s4, v6
	s_and_b64 s[4:5], s[16:17], s[22:23]
	s_or_b64 s[4:5], vcc, s[4:5]
	v_cndmask_b32_e64 v12, 0, 1, s[4:5]
	v_readlane_b32 s4, v6, 48
	s_nop 1
	v_cmp_eq_f32_e64 s[22:23], s4, v6
	v_cmp_gt_f32_e32 vcc, s4, v6
	s_and_b64 s[4:5], s[18:19], s[22:23]
	s_or_b64 s[4:5], vcc, s[4:5]
	v_cndmask_b32_e64 v13, 0, 1, s[4:5]
	v_readlane_b32 s4, v6, 56
	s_nop 1
	v_cmp_gt_f32_e32 vcc, s4, v6
	s_nop 1
	v_cndmask_b32_e64 v6, 0, 1, vcc
	v_add_u32_e32 v6, v8, v6
	v_add3_u32 v6, v6, v7, v9
	v_add3_u32 v6, v6, v10, v11
	v_add3_u32 v6, v6, v12, v13
	v_cmp_gt_u32_e32 vcc, 4, v6
	v_mov_b32_e32 v6, 0
	s_nop 0
	v_cndmask_b32_e32 v5, v245, v5, vcc
	v_ashrrev_i32_e32 v9, 31, v5
	v_sub_u32_e32 v8, 63, v230
	v_and_b32_e32 v9, 0x7fffffff, v9
	v_xor_b32_e32 v9, v5, v9
	s_nop 0
	v_readlane_b32 s25, v9, 0
	s_movk_i32 s24, 63
	v_readlane_b32 s23, v9, 1
	s_movk_i32 s22, 62
	v_cmp_gt_i64_e32 vcc, s[24:25], v[8:9]
	v_readlane_b32 s25, v9, 2
	s_movk_i32 s24, 61
	v_addc_co_u32_e32 v6, vcc, 0, v6, vcc
	v_cmp_gt_i64_e32 vcc, s[22:23], v[8:9]
	v_readlane_b32 s23, v9, 3
	s_movk_i32 s22, 60
	v_addc_co_u32_e32 v6, vcc, 0, v6, vcc
	v_cmp_gt_i64_e32 vcc, s[24:25], v[8:9]
	v_readlane_b32 s25, v9, 4
	s_movk_i32 s24, 59
	v_addc_co_u32_e32 v6, vcc, 0, v6, vcc
	v_cmp_gt_i64_e32 vcc, s[22:23], v[8:9]
	v_readlane_b32 s23, v9, 5
	s_movk_i32 s22, 58
	v_addc_co_u32_e32 v6, vcc, 0, v6, vcc
	v_cmp_gt_i64_e32 vcc, s[24:25], v[8:9]
	v_readlane_b32 s25, v9, 6
	s_movk_i32 s24, 57
	v_addc_co_u32_e32 v6, vcc, 0, v6, vcc
	v_cmp_gt_i64_e32 vcc, s[22:23], v[8:9]
	v_readlane_b32 s23, v9, 7
	s_movk_i32 s22, 56
	v_addc_co_u32_e32 v6, vcc, 0, v6, vcc
	v_cmp_gt_i64_e32 vcc, s[24:25], v[8:9]
	v_readlane_b32 s25, v9, 8
	s_movk_i32 s24, 55
	v_addc_co_u32_e32 v6, vcc, 0, v6, vcc
	v_cmp_gt_i64_e32 vcc, s[22:23], v[8:9]
	v_readlane_b32 s23, v9, 9
	s_movk_i32 s22, 54
	v_addc_co_u32_e32 v6, vcc, 0, v6, vcc
	v_cmp_gt_i64_e32 vcc, s[24:25], v[8:9]
	v_readlane_b32 s25, v9, 10
	s_movk_i32 s24, 53
	v_addc_co_u32_e32 v6, vcc, 0, v6, vcc
	v_cmp_gt_i64_e32 vcc, s[22:23], v[8:9]
	v_readlane_b32 s23, v9, 11
	s_movk_i32 s22, 52
	v_addc_co_u32_e32 v6, vcc, 0, v6, vcc
	v_cmp_gt_i64_e32 vcc, s[24:25], v[8:9]
	v_readlane_b32 s25, v9, 12
	s_movk_i32 s24, 51
	v_addc_co_u32_e32 v6, vcc, 0, v6, vcc
	v_cmp_gt_i64_e32 vcc, s[22:23], v[8:9]
	v_readlane_b32 s23, v9, 13
	s_movk_i32 s22, 50
	v_addc_co_u32_e32 v6, vcc, 0, v6, vcc
	v_cmp_gt_i64_e32 vcc, s[24:25], v[8:9]
	v_readlane_b32 s25, v9, 14
	s_movk_i32 s24, 49
	v_addc_co_u32_e32 v6, vcc, 0, v6, vcc
	v_cmp_gt_i64_e32 vcc, s[22:23], v[8:9]
	v_readlane_b32 s23, v9, 15
	s_movk_i32 s22, 48
	v_addc_co_u32_e32 v6, vcc, 0, v6, vcc
	v_cmp_gt_i64_e32 vcc, s[24:25], v[8:9]
	v_readlane_b32 s25, v9, 16
	s_movk_i32 s24, 47
	v_addc_co_u32_e32 v6, vcc, 0, v6, vcc
	v_cmp_gt_i64_e32 vcc, s[22:23], v[8:9]
	v_readlane_b32 s23, v9, 17
	s_movk_i32 s22, 46
	v_addc_co_u32_e32 v6, vcc, 0, v6, vcc
	v_cmp_gt_i64_e32 vcc, s[24:25], v[8:9]
	v_readlane_b32 s25, v9, 18
	s_movk_i32 s24, 45
; __device__ __forceinline__ void phase_nrr(const Frame& F, const Args& a, int l, const bf16_t* XA, const float* g, const float* modl, unsigned char* XN8) {
;     ...
;             int rank = 0;
; #pragma unroll 8
;             for (int e2 = 0; e2 < 64; ++e2) { const float v = __int_as_float(__builtin_amdgcn_readlane(__float_as_int(val), e2)); rank += (v > val || (v == val && e2 < lane)) ? 1 : 0; }
;             const bool sel = rank < TOPK;
;             const float ssum = wave_sum(sel ? sc : 0.f);
	v_addc_co_u32_e32 v6, vcc, 0, v6, vcc
	v_cmp_gt_i64_e32 vcc, s[22:23], v[8:9]
	v_readlane_b32 s23, v9, 19
	s_movk_i32 s22, 44
	v_addc_co_u32_e32 v6, vcc, 0, v6, vcc
	v_cmp_gt_i64_e32 vcc, s[24:25], v[8:9]
	v_readlane_b32 s25, v9, 20
	s_movk_i32 s24, 43
	v_addc_co_u32_e32 v6, vcc, 0, v6, vcc
	v_cmp_gt_i64_e32 vcc, s[22:23], v[8:9]
	v_readlane_b32 s23, v9, 21
	s_movk_i32 s22, 42
	v_addc_co_u32_e32 v6, vcc, 0, v6, vcc
	v_cmp_gt_i64_e32 vcc, s[24:25], v[8:9]
	v_readlane_b32 s25, v9, 22
	s_movk_i32 s24, 41
	v_addc_co_u32_e32 v6, vcc, 0, v6, vcc
	v_cmp_gt_i64_e32 vcc, s[22:23], v[8:9]
	v_readlane_b32 s23, v9, 23
	s_movk_i32 s22, 40
	v_addc_co_u32_e32 v6, vcc, 0, v6, vcc
	v_cmp_gt_i64_e32 vcc, s[24:25], v[8:9]
	v_readlane_b32 s25, v9, 24
	s_movk_i32 s24, 39
	v_addc_co_u32_e32 v6, vcc, 0, v6, vcc
	v_cmp_gt_i64_e32 vcc, s[22:23], v[8:9]
	v_readlane_b32 s23, v9, 25
	s_movk_i32 s22, 38
	v_addc_co_u32_e32 v6, vcc, 0, v6, vcc
	v_cmp_gt_i64_e32 vcc, s[24:25], v[8:9]
	v_readlane_b32 s25, v9, 26
	s_movk_i32 s24, 37
	v_addc_co_u32_e32 v6, vcc, 0, v6, vcc
	v_cmp_gt_i64_e32 vcc, s[22:23], v[8:9]
	v_readlane_b32 s23, v9, 27
	s_movk_i32 s22, 36
	v_addc_co_u32_e32 v6, vcc, 0, v6, vcc
	v_cmp_gt_i64_e32 vcc, s[24:25], v[8:9]
	v_readlane_b32 s25, v9, 28
	s_movk_i32 s24, 35
	v_addc_co_u32_e32 v6, vcc, 0, v6, vcc
	v_cmp_gt_i64_e32 vcc, s[22:23], v[8:9]
	v_readlane_b32 s23, v9, 29
	s_movk_i32 s22, 34
	v_addc_co_u32_e32 v6, vcc, 0, v6, vcc
	v_cmp_gt_i64_e32 vcc, s[24:25], v[8:9]
	v_readlane_b32 s25, v9, 30
	s_movk_i32 s24, 33
	v_addc_co_u32_e32 v6, vcc, 0, v6, vcc
	v_cmp_gt_i64_e32 vcc, s[22:23], v[8:9]
	v_readlane_b32 s23, v9, 31
	s_movk_i32 s22, 32
	v_addc_co_u32_e32 v6, vcc, 0, v6, vcc
	v_cmp_gt_i64_e32 vcc, s[24:25], v[8:9]
	v_readlane_b32 s25, v9, 32
	s_movk_i32 s24, 31
	v_addc_co_u32_e32 v6, vcc, 0, v6, vcc
	v_cmp_gt_i64_e32 vcc, s[22:23], v[8:9]
	v_readlane_b32 s23, v9, 33
	s_movk_i32 s22, 30
	v_addc_co_u32_e32 v6, vcc, 0, v6, vcc
	v_cmp_gt_i64_e32 vcc, s[24:25], v[8:9]
	v_readlane_b32 s25, v9, 34
	s_movk_i32 s24, 29
	v_addc_co_u32_e32 v6, vcc, 0, v6, vcc
	v_cmp_gt_i64_e32 vcc, s[22:23], v[8:9]
	v_readlane_b32 s23, v9, 35
	s_movk_i32 s22, 28
	v_addc_co_u32_e32 v6, vcc, 0, v6, vcc
	v_cmp_gt_i64_e32 vcc, s[24:25], v[8:9]
	v_readlane_b32 s25, v9, 36
	s_movk_i32 s24, 27
	v_addc_co_u32_e32 v6, vcc, 0, v6, vcc
	v_cmp_gt_i64_e32 vcc, s[22:23], v[8:9]
	v_readlane_b32 s23, v9, 37
	s_movk_i32 s22, 26
	v_addc_co_u32_e32 v6, vcc, 0, v6, vcc
	v_cmp_gt_i64_e32 vcc, s[24:25], v[8:9]
	v_readlane_b32 s25, v9, 38
	s_movk_i32 s24, 25
	v_addc_co_u32_e32 v6, vcc, 0, v6, vcc
	v_cmp_gt_i64_e32 vcc, s[22:23], v[8:9]
	v_readlane_b32 s23, v9, 39
	s_movk_i32 s22, 24
	v_addc_co_u32_e32 v6, vcc, 0, v6, vcc
	v_cmp_gt_i64_e32 vcc, s[24:25], v[8:9]
	v_readlane_b32 s25, v9, 40
	s_movk_i32 s24, 23
	v_addc_co_u32_e32 v6, vcc, 0, v6, vcc
	v_cmp_gt_i64_e32 vcc, s[22:23], v[8:9]
	v_readlane_b32 s23, v9, 41
	s_movk_i32 s22, 22
	v_addc_co_u32_e32 v6, vcc, 0, v6, vcc
	v_cmp_gt_i64_e32 vcc, s[24:25], v[8:9]
	v_readlane_b32 s25, v9, 42
	s_movk_i32 s24, 21
	v_addc_co_u32_e32 v6, vcc, 0, v6, vcc
	v_cmp_gt_i64_e32 vcc, s[22:23], v[8:9]
	v_readlane_b32 s23, v9, 43
	s_movk_i32 s22, 20
	v_addc_co_u32_e32 v6, vcc, 0, v6, vcc
	v_cmp_gt_i64_e32 vcc, s[24:25], v[8:9]
	v_readlane_b32 s25, v9, 44
	s_movk_i32 s24, 19
	v_addc_co_u32_e32 v6, vcc, 0, v6, vcc
	v_cmp_gt_i64_e32 vcc, s[22:23], v[8:9]
	v_readlane_b32 s23, v9, 45
	s_movk_i32 s22, 18
	v_addc_co_u32_e32 v6, vcc, 0, v6, vcc
	v_cmp_gt_i64_e32 vcc, s[24:25], v[8:9]
	v_readlane_b32 s25, v9, 46
	s_movk_i32 s24, 17
	v_addc_co_u32_e32 v6, vcc, 0, v6, vcc
	v_cmp_gt_i64_e32 vcc, s[22:23], v[8:9]
	v_readlane_b32 s23, v9, 47
	s_movk_i32 s22, 16
	v_addc_co_u32_e32 v6, vcc, 0, v6, vcc
	v_cmp_gt_i64_e32 vcc, s[24:25], v[8:9]
	v_readlane_b32 s25, v9, 48
	s_movk_i32 s24, 15
	v_addc_co_u32_e32 v6, vcc, 0, v6, vcc
	v_cmp_gt_i64_e32 vcc, s[22:23], v[8:9]
	v_readlane_b32 s23, v9, 49
	s_movk_i32 s22, 14
	v_addc_co_u32_e32 v6, vcc, 0, v6, vcc
	v_cmp_gt_i64_e32 vcc, s[24:25], v[8:9]
	v_readlane_b32 s25, v9, 50
	s_movk_i32 s24, 13
	v_addc_co_u32_e32 v6, vcc, 0, v6, vcc
	v_cmp_gt_i64_e32 vcc, s[22:23], v[8:9]
	v_readlane_b32 s23, v9, 51
	s_movk_i32 s22, 12
	v_addc_co_u32_e32 v6, vcc, 0, v6, vcc
	v_cmp_gt_i64_e32 vcc, s[24:25], v[8:9]
	v_readlane_b32 s25, v9, 52
	s_movk_i32 s24, 11
	v_addc_co_u32_e32 v6, vcc, 0, v6, vcc
	v_cmp_gt_i64_e32 vcc, s[22:23], v[8:9]
	v_readlane_b32 s23, v9, 53
	s_movk_i32 s22, 10
	v_addc_co_u32_e32 v6, vcc, 0, v6, vcc
	v_cmp_gt_i64_e32 vcc, s[24:25], v[8:9]
	v_readlane_b32 s25, v9, 54
	s_movk_i32 s24, 9
	v_addc_co_u32_e32 v6, vcc, 0, v6, vcc
	v_cmp_gt_i64_e32 vcc, s[22:23], v[8:9]
	v_readlane_b32 s23, v9, 55
	s_movk_i32 s22, 8
	v_addc_co_u32_e32 v6, vcc, 0, v6, vcc
	v_cmp_gt_i64_e32 vcc, s[24:25], v[8:9]
	v_readlane_b32 s25, v9, 56
	s_movk_i32 s24, 7
	v_addc_co_u32_e32 v6, vcc, 0, v6, vcc
	v_cmp_gt_i64_e32 vcc, s[22:23], v[8:9]
	v_readlane_b32 s23, v9, 57
	s_movk_i32 s22, 6
	v_addc_co_u32_e32 v6, vcc, 0, v6, vcc
	v_cmp_gt_i64_e32 vcc, s[24:25], v[8:9]
	v_readlane_b32 s25, v9, 58
	s_movk_i32 s24, 5
	v_addc_co_u32_e32 v6, vcc, 0, v6, vcc
	v_cmp_gt_i64_e32 vcc, s[22:23], v[8:9]
	v_readlane_b32 s23, v9, 59
	s_movk_i32 s22, 4
	v_addc_co_u32_e32 v6, vcc, 0, v6, vcc
	v_cmp_gt_i64_e32 vcc, s[24:25], v[8:9]
	v_readlane_b32 s25, v9, 60
	s_movk_i32 s24, 3
	v_addc_co_u32_e32 v6, vcc, 0, v6, vcc
	v_cmp_gt_i64_e32 vcc, s[22:23], v[8:9]
	v_readlane_b32 s23, v9, 61
	s_movk_i32 s22, 2
	v_addc_co_u32_e32 v6, vcc, 0, v6, vcc
	v_cmp_gt_i64_e32 vcc, s[24:25], v[8:9]
	v_readlane_b32 s25, v9, 62
	s_movk_i32 s24, 1
	v_addc_co_u32_e32 v6, vcc, 0, v6, vcc
	v_cmp_gt_i64_e32 vcc, s[22:23], v[8:9]
	v_readlane_b32 s23, v9, 63
	s_movk_i32 s22, 0
	v_addc_co_u32_e32 v6, vcc, 0, v6, vcc
	v_cmp_gt_i64_e32 vcc, s[24:25], v[8:9]
	s_nop 1
	v_addc_co_u32_e32 v6, vcc, 0, v6, vcc
	v_cmp_gt_i64_e32 vcc, s[22:23], v[8:9]
	s_nop 1
	v_addc_co_u32_e32 v6, vcc, 0, v6, vcc
	v_cmp_gt_u32_e32 vcc, 6, v6
	s_nop 1
	v_cndmask_b32_e32 v5, 0, v2, vcc
	ds_bpermute_b32 v7, v1, v5
	s_waitcnt lgkmcnt(0)
	v_add_f32_e32 v5, v5, v7
	ds_bpermute_b32 v7, v201, v5
	s_waitcnt lgkmcnt(0)
	v_add_f32_e32 v5, v5, v7
	ds_bpermute_b32 v7, v220, v5
	s_waitcnt lgkmcnt(0)
	v_add_f32_e32 v5, v5, v7
	ds_bpermute_b32 v7, v221, v5
	s_waitcnt lgkmcnt(0)
	v_add_f32_e32 v5, v5, v7
	ds_bpermute_b32 v7, v222, v5
	s_waitcnt lgkmcnt(0)
	v_add_f32_e32 v5, v5, v7
	ds_bpermute_b32 v7, v223, v5
	s_and_saveexec_b64 s[4:5], vcc
	s_cbranch_execz .LBB0_555
; __device__ __forceinline__ void phase_nrr(const Frame& F, const Args& a, int l, const bf16_t* XA, const float* g, const float* modl, unsigned char* XN8) {
;     ...
;         for (int i = 0; i < 8; ++i) { const int t = tb + i;
;             const float lg = Pl[(w * 8 + i) * NE + lane] + Pl[(64 + w * 8 + i) * NE + lane]; const float sc = 1.f / (1.f + __expf(-lg)); const float bb = sc + bias;
;             float m1 = bb; m1 = fmaxf(m1, __shfl_xor(m1, 1)); m1 = fmaxf(m1, __shfl_xor(m1, 2)); m1 = fmaxf(m1, __shfl_xor(m1, 4));
;             const unsigned long long eq = __ballot(bb == m1); const int gbase = lane & ~7; const unsigned grpmask = (unsigned)((eq >> gbase) & 0xffull);
;             const int first = gbase + __builtin_ctz(grpmask);
;             float m2 = (lane == first) ? -INFINITY : bb; m2 = fmaxf(m2, __shfl_xor(m2, 1)); m2 = fmaxf(m2, __shfl_xor(m2, 2)); m2 = fmaxf(m2, __shfl_xor(m2, 4));
;             const float gsum = m1 + m2; const int gq = lane >> 3;
;             int grank = 0;
; #pragma unroll
;             for (int g2 = 0; g2 < 8; ++g2) { const float v = __int_as_float(__builtin_amdgcn_readlane(__float_as_int(gsum), g2 * 8)); grank += (v > gsum || (v == gsum && g2 < gq)) ? 1 : 0; }
;             const bool keep = grank < 4; const float val = keep ? bb : -INFINITY;
;             int rank = 0;
; #pragma unroll 8
;             for (int e2 = 0; e2 < 64; ++e2) { const float v = __int_as_float(__builtin_amdgcn_readlane(__float_as_int(val), e2)); rank += (v > val || (v == val && e2 < lane)) ? 1 : 0; }
;             const bool sel = rank < TOPK;
;             const float ssum = wave_sum(sel ? sc : 0.f);
;             if (sel) { const int p = atomicAdd((int*)(hist + lane), 1); top_e[t * TOPK + rank] = lane; gate[t * TOPK + rank] = sc / ssum * 2.5f; lpos[t * TOPK + rank] = p; }
	s_waitcnt lgkmcnt(0)
	v_add_f32_e32 v5, v5, v7
	s_mul_i32 s2, s2, 6
	v_or_b32_e32 v6, s2, v6
	v_div_scale_f32 v11, s[2:3], v5, v5, v2
	v_rcp_f32_e32 v12, v11
	v_ashrrev_i32_e32 v7, 31, v6
	v_lshlrev_b64 v[6:7], 2, v[6:7]
	v_lshl_add_u64 v[8:9], s[26:27], 0, v[6:7]
	ds_add_rtn_u32 v10, v227, v243
	global_store_dword v[8:9], v230, off
	v_fma_f32 v8, -v11, v12, 1.0
	v_fmac_f32_e32 v12, v8, v12
	v_div_scale_f32 v8, vcc, v2, v5, v2
	v_mul_f32_e32 v9, v8, v12
	v_fma_f32 v13, -v11, v9, v8
	v_fmac_f32_e32 v9, v13, v12
	v_fma_f32 v8, -v11, v9, v8
	v_div_fmas_f32 v8, v8, v12, v9
	v_div_fixup_f32 v2, v8, v5, v2
	v_mul_f32_e32 v2, 0x40200000, v2
	v_lshl_add_u64 v[8:9], s[28:29], 0, v[6:7]
	v_lshl_add_u64 v[6:7], s[30:31], 0, v[6:7]
	global_store_dword v[8:9], v2, off
	s_waitcnt lgkmcnt(0)
	global_store_dword v[6:7], v10, off
.LBB0_555:
	s_or_b64 exec, exec, s[4:5]
	v_add_u32_e32 v2, s85, v226
	ds_read_b32 v2, v2
	ds_read_b32 v5, v4 offset:17664
	s_waitcnt lgkmcnt(0)
	v_add_f32_e32 v2, v2, v5
	v_mul_f32_e32 v2, 0xbfb8aa3b, v2
	v_exp_f32_e32 v2, v2
	s_nop 0
	v_add_f32_e32 v2, 1.0, v2
	v_div_scale_f32 v5, s[2:3], v2, v2, 1.0
	v_rcp_f32_e32 v6, v5
	s_mov_b32 s2, 0
	v_fma_f32 v7, -v5, v6, 1.0
	v_fmac_f32_e32 v6, v7, v6
	v_div_scale_f32 v7, vcc, 1.0, v2, 1.0
	v_mul_f32_e32 v8, v7, v6
	v_fma_f32 v9, -v5, v8, v7
	v_fmac_f32_e32 v8, v9, v6
	v_fma_f32 v5, -v5, v8, v7
	v_div_fmas_f32 v5, v5, v6, v8
	v_div_fixup_f32 v2, v5, v2, 1.0
	v_add_f32_e32 v5, v3, v2
	ds_bpermute_b32 v6, v1, v5
	s_waitcnt lgkmcnt(0)
	v_max_f32_e32 v6, v6, v6
	v_max_f32_e32 v6, v5, v6
	ds_bpermute_b32 v7, v201, v6
	s_waitcnt lgkmcnt(0)
	v_max_f32_e32 v7, v7, v7
	v_max_f32_e32 v6, v6, v7
	ds_bpermute_b32 v7, v220, v6
	s_waitcnt lgkmcnt(0)
	v_max_f32_e32 v7, v7, v7
	v_max_f32_e32 v8, v6, v7
	v_cmp_eq_f32_e32 vcc, v5, v8
	s_nop 1
	v_lshrrev_b64 v[6:7], v200, vcc
	v_ffbl_b32_sdwa v6, v6 dst_sel:DWORD dst_unused:UNUSED_PAD src0_sel:BYTE_0
	v_add_u32_e32 v6, v6, v200
	v_cmp_ne_u32_e32 vcc, v230, v6
	s_nop 1
	v_cndmask_b32_e32 v6, v245, v5, vcc
	ds_bpermute_b32 v7, v1, v6
	s_waitcnt lgkmcnt(0)
	v_max_f32_e32 v7, v7, v7
	v_max_f32_e32 v6, v6, v7
	ds_bpermute_b32 v7, v201, v6
	s_waitcnt lgkmcnt(0)
	v_max_f32_e32 v7, v7, v7
	v_max_f32_e32 v6, v6, v7
	ds_bpermute_b32 v7, v220, v6
	s_waitcnt lgkmcnt(0)
	v_max_f32_e32 v7, v7, v7
	v_max_f32_e32 v6, v6, v7
	v_add_f32_e32 v6, v8, v6
	s_nop 0
	v_readlane_b32 s3, v6, 0
	s_nop 1
	v_cmp_eq_f32_e64 s[22:23], s3, v6
	v_cmp_gt_f32_e32 vcc, s3, v6
	s_and_b64 s[4:5], s[6:7], s[22:23]
	v_readlane_b32 s3, v6, 8
	s_or_b64 s[4:5], vcc, s[4:5]
	v_cndmask_b32_e64 v7, 0, 1, s[4:5]
	v_cmp_eq_f32_e64 s[22:23], s3, v6
	v_cmp_gt_f32_e32 vcc, s3, v6
	s_and_b64 s[4:5], s[8:9], s[22:23]
	v_readlane_b32 s3, v6, 16
	s_or_b64 s[4:5], vcc, s[4:5]
	v_cndmask_b32_e64 v8, 0, 1, s[4:5]
	v_cmp_eq_f32_e64 s[22:23], s3, v6
	v_cmp_gt_f32_e32 vcc, s3, v6
	s_and_b64 s[4:5], s[10:11], s[22:23]
	v_readlane_b32 s3, v6, 24
	s_or_b64 s[4:5], vcc, s[4:5]
	v_cndmask_b32_e64 v9, 0, 1, s[4:5]
	v_cmp_eq_f32_e64 s[22:23], s3, v6
	v_cmp_gt_f32_e32 vcc, s3, v6
	s_and_b64 s[4:5], s[12:13], s[22:23]
	v_readlane_b32 s3, v6, 32
	s_or_b64 s[4:5], vcc, s[4:5]
	v_cndmask_b32_e64 v10, 0, 1, s[4:5]
	v_cmp_eq_f32_e64 s[22:23], s3, v6
	v_cmp_gt_f32_e32 vcc, s3, v6
	s_and_b64 s[4:5], s[14:15], s[22:23]
	v_readlane_b32 s3, v6, 40
	s_or_b64 s[4:5], vcc, s[4:5]
	v_cndmask_b32_e64 v11, 0, 1, s[4:5]
	v_cmp_eq_f32_e64 s[22:23], s3, v6
	v_cmp_gt_f32_e32 vcc, s3, v6
	s_and_b64 s[4:5], s[16:17], s[22:23]
	v_readlane_b32 s3, v6, 48
	s_or_b64 s[4:5], vcc, s[4:5]
	v_cndmask_b32_e64 v12, 0, 1, s[4:5]
	v_cmp_eq_f32_e64 s[22:23], s3, v6
	v_cmp_gt_f32_e32 vcc, s3, v6
	s_and_b64 s[4:5], s[18:19], s[22:23]
	v_readlane_b32 s3, v6, 56
	s_or_b64 s[4:5], vcc, s[4:5]
	v_cndmask_b32_e64 v13, 0, 1, s[4:5]
	v_cmp_gt_f32_e32 vcc, s3, v6
	s_nop 1
	v_cndmask_b32_e64 v6, 0, 1, vcc
	v_add_u32_e32 v6, v8, v6
	v_add3_u32 v6, v6, v7, v9
	v_add3_u32 v6, v6, v10, v11
	v_add3_u32 v6, v6, v12, v13
	v_cmp_gt_u32_e32 vcc, 4, v6
	v_mov_b32_e32 v6, 0
	s_nop 0
	v_cndmask_b32_e32 v5, v245, v5, vcc
	v_ashrrev_i32_e32 v9, 31, v5
	v_sub_u32_e32 v8, 63, v230
	v_and_b32_e32 v9, 0x7fffffff, v9
	v_xor_b32_e32 v9, v5, v9
	s_nop 0
	v_readlane_b32 s25, v9, 0
	s_movk_i32 s24, 63
	v_readlane_b32 s23, v9, 1
	s_movk_i32 s22, 62
	v_cmp_gt_i64_e32 vcc, s[24:25], v[8:9]
	v_readlane_b32 s25, v9, 2
	s_movk_i32 s24, 61
	v_addc_co_u32_e32 v6, vcc, 0, v6, vcc
	v_cmp_gt_i64_e32 vcc, s[22:23], v[8:9]
	v_readlane_b32 s23, v9, 3
	s_movk_i32 s22, 60
	v_addc_co_u32_e32 v6, vcc, 0, v6, vcc
	v_cmp_gt_i64_e32 vcc, s[24:25], v[8:9]
	v_readlane_b32 s25, v9, 4
	s_movk_i32 s24, 59
	v_addc_co_u32_e32 v6, vcc, 0, v6, vcc
	v_cmp_gt_i64_e32 vcc, s[22:23], v[8:9]
	v_readlane_b32 s23, v9, 5
	s_movk_i32 s22, 58
	v_addc_co_u32_e32 v6, vcc, 0, v6, vcc
	v_cmp_gt_i64_e32 vcc, s[24:25], v[8:9]
	v_readlane_b32 s25, v9, 6
	s_movk_i32 s24, 57
	v_addc_co_u32_e32 v6, vcc, 0, v6, vcc
	v_cmp_gt_i64_e32 vcc, s[22:23], v[8:9]
	v_readlane_b32 s23, v9, 7
	s_movk_i32 s22, 56
	v_addc_co_u32_e32 v6, vcc, 0, v6, vcc
	v_cmp_gt_i64_e32 vcc, s[24:25], v[8:9]
	v_readlane_b32 s25, v9, 8
	s_movk_i32 s24, 55
	v_addc_co_u32_e32 v6, vcc, 0, v6, vcc
	v_cmp_gt_i64_e32 vcc, s[22:23], v[8:9]
	v_readlane_b32 s23, v9, 9
	s_movk_i32 s22, 54
	v_addc_co_u32_e32 v6, vcc, 0, v6, vcc
	v_cmp_gt_i64_e32 vcc, s[24:25], v[8:9]
	v_readlane_b32 s25, v9, 10
	s_movk_i32 s24, 53
	v_addc_co_u32_e32 v6, vcc, 0, v6, vcc
	v_cmp_gt_i64_e32 vcc, s[22:23], v[8:9]
	v_readlane_b32 s23, v9, 11
	s_movk_i32 s22, 52
	v_addc_co_u32_e32 v6, vcc, 0, v6, vcc
	v_cmp_gt_i64_e32 vcc, s[24:25], v[8:9]
	v_readlane_b32 s25, v9, 12
	s_movk_i32 s24, 51
; __device__ __forceinline__ void phase_nrr(const Frame& F, const Args& a, int l, const bf16_t* XA, const float* g, const float* modl, unsigned char* XN8) {
;     ...
;             int rank = 0;
; #pragma unroll 8
;             for (int e2 = 0; e2 < 64; ++e2) { const float v = __int_as_float(__builtin_amdgcn_readlane(__float_as_int(val), e2)); rank += (v > val || (v == val && e2 < lane)) ? 1 : 0; }
;             const bool sel = rank < TOPK;
;             const float ssum = wave_sum(sel ? sc : 0.f);
	v_addc_co_u32_e32 v6, vcc, 0, v6, vcc
	v_cmp_gt_i64_e32 vcc, s[22:23], v[8:9]
	v_readlane_b32 s23, v9, 13
	s_movk_i32 s22, 50
	v_addc_co_u32_e32 v6, vcc, 0, v6, vcc
	v_cmp_gt_i64_e32 vcc, s[24:25], v[8:9]
	v_readlane_b32 s25, v9, 14
	s_movk_i32 s24, 49
	v_addc_co_u32_e32 v6, vcc, 0, v6, vcc
	v_cmp_gt_i64_e32 vcc, s[22:23], v[8:9]
	v_readlane_b32 s23, v9, 15
	s_movk_i32 s22, 48
	v_addc_co_u32_e32 v6, vcc, 0, v6, vcc
	v_cmp_gt_i64_e32 vcc, s[24:25], v[8:9]
	v_readlane_b32 s25, v9, 16
	s_movk_i32 s24, 47
	v_addc_co_u32_e32 v6, vcc, 0, v6, vcc
	v_cmp_gt_i64_e32 vcc, s[22:23], v[8:9]
	v_readlane_b32 s23, v9, 17
	s_movk_i32 s22, 46
	v_addc_co_u32_e32 v6, vcc, 0, v6, vcc
	v_cmp_gt_i64_e32 vcc, s[24:25], v[8:9]
	v_readlane_b32 s25, v9, 18
	s_movk_i32 s24, 45
	v_addc_co_u32_e32 v6, vcc, 0, v6, vcc
	v_cmp_gt_i64_e32 vcc, s[22:23], v[8:9]
	v_readlane_b32 s23, v9, 19
	s_movk_i32 s22, 44
	v_addc_co_u32_e32 v6, vcc, 0, v6, vcc
	v_cmp_gt_i64_e32 vcc, s[24:25], v[8:9]
	v_readlane_b32 s25, v9, 20
	s_movk_i32 s24, 43
	v_addc_co_u32_e32 v6, vcc, 0, v6, vcc
	v_cmp_gt_i64_e32 vcc, s[22:23], v[8:9]
	v_readlane_b32 s23, v9, 21
	s_movk_i32 s22, 42
	v_addc_co_u32_e32 v6, vcc, 0, v6, vcc
	v_cmp_gt_i64_e32 vcc, s[24:25], v[8:9]
	v_readlane_b32 s25, v9, 22
	s_movk_i32 s24, 41
	v_addc_co_u32_e32 v6, vcc, 0, v6, vcc
	v_cmp_gt_i64_e32 vcc, s[22:23], v[8:9]
	v_readlane_b32 s23, v9, 23
	s_movk_i32 s22, 40
	v_addc_co_u32_e32 v6, vcc, 0, v6, vcc
	v_cmp_gt_i64_e32 vcc, s[24:25], v[8:9]
	v_readlane_b32 s25, v9, 24
	s_movk_i32 s24, 39
	v_addc_co_u32_e32 v6, vcc, 0, v6, vcc
	v_cmp_gt_i64_e32 vcc, s[22:23], v[8:9]
	v_readlane_b32 s23, v9, 25
	s_movk_i32 s22, 38
	v_addc_co_u32_e32 v6, vcc, 0, v6, vcc
	v_cmp_gt_i64_e32 vcc, s[24:25], v[8:9]
	v_readlane_b32 s25, v9, 26
	s_movk_i32 s24, 37
	v_addc_co_u32_e32 v6, vcc, 0, v6, vcc
	v_cmp_gt_i64_e32 vcc, s[22:23], v[8:9]
	v_readlane_b32 s23, v9, 27
	s_movk_i32 s22, 36
	v_addc_co_u32_e32 v6, vcc, 0, v6, vcc
	v_cmp_gt_i64_e32 vcc, s[24:25], v[8:9]
	v_readlane_b32 s25, v9, 28
	s_movk_i32 s24, 35
	v_addc_co_u32_e32 v6, vcc, 0, v6, vcc
	v_cmp_gt_i64_e32 vcc, s[22:23], v[8:9]
	v_readlane_b32 s23, v9, 29
	s_movk_i32 s22, 34
	v_addc_co_u32_e32 v6, vcc, 0, v6, vcc
	v_cmp_gt_i64_e32 vcc, s[24:25], v[8:9]
	v_readlane_b32 s25, v9, 30
	s_movk_i32 s24, 33
	v_addc_co_u32_e32 v6, vcc, 0, v6, vcc
	v_cmp_gt_i64_e32 vcc, s[22:23], v[8:9]
	v_readlane_b32 s23, v9, 31
	s_movk_i32 s22, 32
	v_addc_co_u32_e32 v6, vcc, 0, v6, vcc
	v_cmp_gt_i64_e32 vcc, s[24:25], v[8:9]
	v_readlane_b32 s25, v9, 32
	s_movk_i32 s24, 31
	v_addc_co_u32_e32 v6, vcc, 0, v6, vcc
	v_cmp_gt_i64_e32 vcc, s[22:23], v[8:9]
	v_readlane_b32 s23, v9, 33
	s_movk_i32 s22, 30
	v_addc_co_u32_e32 v6, vcc, 0, v6, vcc
	v_cmp_gt_i64_e32 vcc, s[24:25], v[8:9]
	v_readlane_b32 s25, v9, 34
	s_movk_i32 s24, 29
	v_addc_co_u32_e32 v6, vcc, 0, v6, vcc
	v_cmp_gt_i64_e32 vcc, s[22:23], v[8:9]
	v_readlane_b32 s23, v9, 35
	s_movk_i32 s22, 28
	v_addc_co_u32_e32 v6, vcc, 0, v6, vcc
	v_cmp_gt_i64_e32 vcc, s[24:25], v[8:9]
	v_readlane_b32 s25, v9, 36
	s_movk_i32 s24, 27
	v_addc_co_u32_e32 v6, vcc, 0, v6, vcc
	v_cmp_gt_i64_e32 vcc, s[22:23], v[8:9]
	v_readlane_b32 s23, v9, 37
	s_movk_i32 s22, 26
	v_addc_co_u32_e32 v6, vcc, 0, v6, vcc
	v_cmp_gt_i64_e32 vcc, s[24:25], v[8:9]
	v_readlane_b32 s25, v9, 38
	s_movk_i32 s24, 25
	v_addc_co_u32_e32 v6, vcc, 0, v6, vcc
	v_cmp_gt_i64_e32 vcc, s[22:23], v[8:9]
	v_readlane_b32 s23, v9, 39
	s_movk_i32 s22, 24
	v_addc_co_u32_e32 v6, vcc, 0, v6, vcc
	v_cmp_gt_i64_e32 vcc, s[24:25], v[8:9]
	v_readlane_b32 s25, v9, 40
	s_movk_i32 s24, 23
	v_addc_co_u32_e32 v6, vcc, 0, v6, vcc
	v_cmp_gt_i64_e32 vcc, s[22:23], v[8:9]
	v_readlane_b32 s23, v9, 41
	s_movk_i32 s22, 22
	v_addc_co_u32_e32 v6, vcc, 0, v6, vcc
	v_cmp_gt_i64_e32 vcc, s[24:25], v[8:9]
	v_readlane_b32 s25, v9, 42
	s_movk_i32 s24, 21
	v_addc_co_u32_e32 v6, vcc, 0, v6, vcc
	v_cmp_gt_i64_e32 vcc, s[22:23], v[8:9]
	v_readlane_b32 s23, v9, 43
	s_movk_i32 s22, 20
	v_addc_co_u32_e32 v6, vcc, 0, v6, vcc
	v_cmp_gt_i64_e32 vcc, s[24:25], v[8:9]
	v_readlane_b32 s25, v9, 44
	s_movk_i32 s24, 19
	v_addc_co_u32_e32 v6, vcc, 0, v6, vcc
	v_cmp_gt_i64_e32 vcc, s[22:23], v[8:9]
	v_readlane_b32 s23, v9, 45
	s_movk_i32 s22, 18
	v_addc_co_u32_e32 v6, vcc, 0, v6, vcc
	v_cmp_gt_i64_e32 vcc, s[24:25], v[8:9]
	v_readlane_b32 s25, v9, 46
	s_movk_i32 s24, 17
	v_addc_co_u32_e32 v6, vcc, 0, v6, vcc
	v_cmp_gt_i64_e32 vcc, s[22:23], v[8:9]
	v_readlane_b32 s23, v9, 47
	s_movk_i32 s22, 16
	v_addc_co_u32_e32 v6, vcc, 0, v6, vcc
	v_cmp_gt_i64_e32 vcc, s[24:25], v[8:9]
	v_readlane_b32 s25, v9, 48
	s_movk_i32 s24, 15
	v_addc_co_u32_e32 v6, vcc, 0, v6, vcc
	v_cmp_gt_i64_e32 vcc, s[22:23], v[8:9]
	v_readlane_b32 s23, v9, 49
	s_movk_i32 s22, 14
	v_addc_co_u32_e32 v6, vcc, 0, v6, vcc
	v_cmp_gt_i64_e32 vcc, s[24:25], v[8:9]
	v_readlane_b32 s25, v9, 50
	s_movk_i32 s24, 13
	v_addc_co_u32_e32 v6, vcc, 0, v6, vcc
	v_cmp_gt_i64_e32 vcc, s[22:23], v[8:9]
	v_readlane_b32 s23, v9, 51
	s_movk_i32 s22, 12
	v_addc_co_u32_e32 v6, vcc, 0, v6, vcc
	v_cmp_gt_i64_e32 vcc, s[24:25], v[8:9]
	v_readlane_b32 s25, v9, 52
	s_movk_i32 s24, 11
	v_addc_co_u32_e32 v6, vcc, 0, v6, vcc
	v_cmp_gt_i64_e32 vcc, s[22:23], v[8:9]
	v_readlane_b32 s23, v9, 53
	s_movk_i32 s22, 10
	v_addc_co_u32_e32 v6, vcc, 0, v6, vcc
	v_cmp_gt_i64_e32 vcc, s[24:25], v[8:9]
	v_readlane_b32 s25, v9, 54
	s_movk_i32 s24, 9
	v_addc_co_u32_e32 v6, vcc, 0, v6, vcc
	v_cmp_gt_i64_e32 vcc, s[22:23], v[8:9]
	v_readlane_b32 s23, v9, 55
	s_movk_i32 s22, 8
	v_addc_co_u32_e32 v6, vcc, 0, v6, vcc
	v_cmp_gt_i64_e32 vcc, s[24:25], v[8:9]
	v_readlane_b32 s25, v9, 56
	s_movk_i32 s24, 7
	v_addc_co_u32_e32 v6, vcc, 0, v6, vcc
	v_cmp_gt_i64_e32 vcc, s[22:23], v[8:9]
	v_readlane_b32 s23, v9, 57
	s_movk_i32 s22, 6
	v_addc_co_u32_e32 v6, vcc, 0, v6, vcc
	v_cmp_gt_i64_e32 vcc, s[24:25], v[8:9]
	v_readlane_b32 s25, v9, 58
	s_movk_i32 s24, 5
	v_addc_co_u32_e32 v6, vcc, 0, v6, vcc
	v_cmp_gt_i64_e32 vcc, s[22:23], v[8:9]
	v_readlane_b32 s23, v9, 59
	s_movk_i32 s22, 4
	v_addc_co_u32_e32 v6, vcc, 0, v6, vcc
	v_cmp_gt_i64_e32 vcc, s[24:25], v[8:9]
	v_readlane_b32 s25, v9, 60
	s_movk_i32 s24, 3
	v_addc_co_u32_e32 v6, vcc, 0, v6, vcc
	v_cmp_gt_i64_e32 vcc, s[22:23], v[8:9]
	v_readlane_b32 s23, v9, 61
	s_movk_i32 s22, 2
	v_addc_co_u32_e32 v6, vcc, 0, v6, vcc
	v_cmp_gt_i64_e32 vcc, s[24:25], v[8:9]
	v_readlane_b32 s25, v9, 62
	s_movk_i32 s24, 1
	v_addc_co_u32_e32 v6, vcc, 0, v6, vcc
	v_cmp_gt_i64_e32 vcc, s[22:23], v[8:9]
	v_readlane_b32 s23, v9, 63
	s_movk_i32 s22, 0
	v_addc_co_u32_e32 v6, vcc, 0, v6, vcc
	v_cmp_gt_i64_e32 vcc, s[24:25], v[8:9]
	s_nop 1
	v_addc_co_u32_e32 v6, vcc, 0, v6, vcc
	v_cmp_gt_i64_e32 vcc, s[22:23], v[8:9]
	s_nop 1
	v_addc_co_u32_e32 v6, vcc, 0, v6, vcc
	v_cmp_gt_u32_e32 vcc, 6, v6
	s_nop 1
	v_cndmask_b32_e32 v5, 0, v2, vcc
	ds_bpermute_b32 v7, v1, v5
	s_waitcnt lgkmcnt(0)
; __device__ __forceinline__ void phase_nrr(const Frame& F, const Args& a, int l, const bf16_t* XA, const float* g, const float* modl, unsigned char* XN8) {
;     ...
;         for (int i = 0; i < 8; ++i) { const int t = tb + i;
;             const float lg = Pl[(w * 8 + i) * NE + lane] + Pl[(64 + w * 8 + i) * NE + lane]; const float sc = 1.f / (1.f + __expf(-lg)); const float bb = sc + bias;
;             float m1 = bb; m1 = fmaxf(m1, __shfl_xor(m1, 1)); m1 = fmaxf(m1, __shfl_xor(m1, 2)); m1 = fmaxf(m1, __shfl_xor(m1, 4));
;             const unsigned long long eq = __ballot(bb == m1); const int gbase = lane & ~7; const unsigned grpmask = (unsigned)((eq >> gbase) & 0xffull);
;             const int first = gbase + __builtin_ctz(grpmask);
;             float m2 = (lane == first) ? -INFINITY : bb; m2 = fmaxf(m2, __shfl_xor(m2, 1)); m2 = fmaxf(m2, __shfl_xor(m2, 2)); m2 = fmaxf(m2, __shfl_xor(m2, 4));
;             const float gsum = m1 + m2; const int gq = lane >> 3;
;             int grank = 0;
; #pragma unroll
;             for (int g2 = 0; g2 < 8; ++g2) { const float v = __int_as_float(__builtin_amdgcn_readlane(__float_as_int(gsum), g2 * 8)); grank += (v > gsum || (v == gsum && g2 < gq)) ? 1 : 0; }
;             const bool keep = grank < 4; const float val = keep ? bb : -INFINITY;
;             int rank = 0;
; #pragma unroll 8
;             for (int e2 = 0; e2 < 64; ++e2) { const float v = __int_as_float(__builtin_amdgcn_readlane(__float_as_int(val), e2)); rank += (v > val || (v == val && e2 < lane)) ? 1 : 0; }
;     ...
;             const float ssum = wave_sum(sel ? sc : 0.f);
;             if (sel) { const int p = atomicAdd((int*)(hist + lane), 1); top_e[t * TOPK + rank] = lane; gate[t * TOPK + rank] = sc / ssum * 2.5f; lpos[t * TOPK + rank] = p; }
	v_add_f32_e32 v5, v5, v7
	ds_bpermute_b32 v7, v201, v5
	s_waitcnt lgkmcnt(0)
	v_add_f32_e32 v5, v5, v7
	ds_bpermute_b32 v7, v220, v5
	s_waitcnt lgkmcnt(0)
	v_add_f32_e32 v5, v5, v7
	ds_bpermute_b32 v7, v221, v5
	s_waitcnt lgkmcnt(0)
	v_add_f32_e32 v5, v5, v7
	ds_bpermute_b32 v7, v222, v5
	s_waitcnt lgkmcnt(0)
	v_add_f32_e32 v5, v5, v7
	ds_bpermute_b32 v7, v223, v5
	s_and_saveexec_b64 s[2:3], vcc
	s_cbranch_execz .LBB0_559
	s_waitcnt lgkmcnt(0)
	v_add_f32_e32 v5, v5, v7
	v_div_scale_f32 v11, s[4:5], v5, v5, v2
	v_add3_u32 v6, s36, 30, v6
	v_rcp_f32_e32 v12, v11
	v_ashrrev_i32_e32 v7, 31, v6
	v_lshlrev_b64 v[6:7], 2, v[6:7]
	v_lshl_add_u64 v[8:9], s[26:27], 0, v[6:7]
	ds_add_rtn_u32 v10, v227, v243
	global_store_dword v[8:9], v230, off
	v_fma_f32 v8, -v11, v12, 1.0
	v_fmac_f32_e32 v12, v8, v12
	v_div_scale_f32 v8, vcc, v2, v5, v2
	v_mul_f32_e32 v9, v8, v12
	v_fma_f32 v13, -v11, v9, v8
	v_fmac_f32_e32 v9, v13, v12
	v_fma_f32 v8, -v11, v9, v8
	v_div_fmas_f32 v8, v8, v12, v9
	v_div_fixup_f32 v2, v8, v5, v2
	v_mul_f32_e32 v2, 0x40200000, v2
	v_lshl_add_u64 v[8:9], s[28:29], 0, v[6:7]
	v_lshl_add_u64 v[6:7], s[30:31], 0, v[6:7]
	global_store_dword v[8:9], v2, off
	s_waitcnt lgkmcnt(0)
	global_store_dword v[6:7], v10, off
.LBB0_559:
	s_or_b64 exec, exec, s[2:3]
	v_add_u32_e32 v2, s86, v226
	ds_read_b32 v2, v2
	ds_read_b32 v5, v4 offset:17920
	s_waitcnt lgkmcnt(0)
	v_add_f32_e32 v2, v2, v5
	v_mul_f32_e32 v2, 0xbfb8aa3b, v2
	v_exp_f32_e32 v2, v2
	s_nop 0
	v_add_f32_e32 v2, 1.0, v2
	v_div_scale_f32 v5, s[2:3], v2, v2, 1.0
	v_rcp_f32_e32 v6, v5
	s_mov_b32 s2, 0
	v_fma_f32 v7, -v5, v6, 1.0
	v_fmac_f32_e32 v6, v7, v6
	v_div_scale_f32 v7, vcc, 1.0, v2, 1.0
	v_mul_f32_e32 v8, v7, v6
	v_fma_f32 v9, -v5, v8, v7
	v_fmac_f32_e32 v8, v9, v6
	v_fma_f32 v5, -v5, v8, v7
	v_div_fmas_f32 v5, v5, v6, v8
	v_div_fixup_f32 v2, v5, v2, 1.0
	v_add_f32_e32 v5, v3, v2
	ds_bpermute_b32 v6, v1, v5
	s_waitcnt lgkmcnt(0)
	v_max_f32_e32 v6, v6, v6
	v_max_f32_e32 v6, v5, v6
	ds_bpermute_b32 v7, v201, v6
	s_waitcnt lgkmcnt(0)
	v_max_f32_e32 v7, v7, v7
	v_max_f32_e32 v6, v6, v7
	ds_bpermute_b32 v7, v220, v6
	s_waitcnt lgkmcnt(0)
	v_max_f32_e32 v7, v7, v7
	v_max_f32_e32 v8, v6, v7
	v_cmp_eq_f32_e32 vcc, v5, v8
	s_nop 1
	v_lshrrev_b64 v[6:7], v200, vcc
	v_ffbl_b32_sdwa v6, v6 dst_sel:DWORD dst_unused:UNUSED_PAD src0_sel:BYTE_0
	v_add_u32_e32 v6, v6, v200
	v_cmp_ne_u32_e32 vcc, v230, v6
	s_nop 1
	v_cndmask_b32_e32 v6, v245, v5, vcc
	ds_bpermute_b32 v7, v1, v6
	s_waitcnt lgkmcnt(0)
	v_max_f32_e32 v7, v7, v7
	v_max_f32_e32 v6, v6, v7
	ds_bpermute_b32 v7, v201, v6
	s_waitcnt lgkmcnt(0)
	v_max_f32_e32 v7, v7, v7
	v_max_f32_e32 v6, v6, v7
	ds_bpermute_b32 v7, v220, v6
	s_waitcnt lgkmcnt(0)
	v_max_f32_e32 v7, v7, v7
	v_max_f32_e32 v6, v6, v7
	v_add_f32_e32 v6, v8, v6
	s_nop 0
	v_readlane_b32 s3, v6, 0
	s_nop 1
	v_cmp_eq_f32_e64 s[22:23], s3, v6
	v_cmp_gt_f32_e32 vcc, s3, v6
	s_and_b64 s[4:5], s[6:7], s[22:23]
	v_readlane_b32 s3, v6, 8
	s_or_b64 s[4:5], vcc, s[4:5]
	v_cndmask_b32_e64 v7, 0, 1, s[4:5]
	v_cmp_eq_f32_e64 s[22:23], s3, v6
	v_cmp_gt_f32_e32 vcc, s3, v6
	s_and_b64 s[4:5], s[8:9], s[22:23]
	v_readlane_b32 s3, v6, 16
	s_or_b64 s[4:5], vcc, s[4:5]
	v_cndmask_b32_e64 v8, 0, 1, s[4:5]
	v_cmp_eq_f32_e64 s[22:23], s3, v6
	v_cmp_gt_f32_e32 vcc, s3, v6
	s_and_b64 s[4:5], s[10:11], s[22:23]
	v_readlane_b32 s3, v6, 24
	s_or_b64 s[4:5], vcc, s[4:5]
	v_cndmask_b32_e64 v9, 0, 1, s[4:5]
	v_cmp_eq_f32_e64 s[22:23], s3, v6
	v_cmp_gt_f32_e32 vcc, s3, v6
	s_and_b64 s[4:5], s[12:13], s[22:23]
	v_readlane_b32 s3, v6, 32
	s_or_b64 s[4:5], vcc, s[4:5]
	v_cndmask_b32_e64 v10, 0, 1, s[4:5]
	v_cmp_eq_f32_e64 s[22:23], s3, v6
	v_cmp_gt_f32_e32 vcc, s3, v6
	s_and_b64 s[4:5], s[14:15], s[22:23]
	v_readlane_b32 s3, v6, 40
	s_or_b64 s[4:5], vcc, s[4:5]
	v_cndmask_b32_e64 v11, 0, 1, s[4:5]
	v_cmp_eq_f32_e64 s[22:23], s3, v6
	v_cmp_gt_f32_e32 vcc, s3, v6
	s_and_b64 s[4:5], s[16:17], s[22:23]
	v_readlane_b32 s3, v6, 48
	s_or_b64 s[4:5], vcc, s[4:5]
	v_cndmask_b32_e64 v12, 0, 1, s[4:5]
	v_cmp_eq_f32_e64 s[22:23], s3, v6
	v_cmp_gt_f32_e32 vcc, s3, v6
	s_and_b64 s[4:5], s[18:19], s[22:23]
	v_readlane_b32 s3, v6, 56
	s_or_b64 s[4:5], vcc, s[4:5]
	v_cndmask_b32_e64 v13, 0, 1, s[4:5]
	v_cmp_gt_f32_e32 vcc, s3, v6
	s_nop 1
	v_cndmask_b32_e64 v6, 0, 1, vcc
	v_add_u32_e32 v6, v8, v6
	v_add3_u32 v6, v6, v7, v9
	v_add3_u32 v6, v6, v10, v11
	v_add3_u32 v6, v6, v12, v13
	v_cmp_gt_u32_e32 vcc, 4, v6
	v_mov_b32_e32 v6, 0
	s_nop 0
	v_cndmask_b32_e32 v5, v245, v5, vcc
	v_ashrrev_i32_e32 v9, 31, v5
	v_sub_u32_e32 v8, 63, v230
	v_and_b32_e32 v9, 0x7fffffff, v9
	v_xor_b32_e32 v9, v5, v9
	s_nop 0
	v_readlane_b32 s25, v9, 0
	s_movk_i32 s24, 63
	v_readlane_b32 s23, v9, 1
	s_movk_i32 s22, 62
	v_cmp_gt_i64_e32 vcc, s[24:25], v[8:9]
	v_readlane_b32 s25, v9, 2
	s_movk_i32 s24, 61
	v_addc_co_u32_e32 v6, vcc, 0, v6, vcc
	v_cmp_gt_i64_e32 vcc, s[22:23], v[8:9]
	v_readlane_b32 s23, v9, 3
	s_movk_i32 s22, 60
	v_addc_co_u32_e32 v6, vcc, 0, v6, vcc
	v_cmp_gt_i64_e32 vcc, s[24:25], v[8:9]
	v_readlane_b32 s25, v9, 4
	s_movk_i32 s24, 59
	v_addc_co_u32_e32 v6, vcc, 0, v6, vcc
	v_cmp_gt_i64_e32 vcc, s[22:23], v[8:9]
	v_readlane_b32 s23, v9, 5
	s_movk_i32 s22, 58
	v_addc_co_u32_e32 v6, vcc, 0, v6, vcc
	v_cmp_gt_i64_e32 vcc, s[24:25], v[8:9]
	v_readlane_b32 s25, v9, 6
	s_movk_i32 s24, 57
	v_addc_co_u32_e32 v6, vcc, 0, v6, vcc
	v_cmp_gt_i64_e32 vcc, s[22:23], v[8:9]
	v_readlane_b32 s23, v9, 7
	s_movk_i32 s22, 56
	v_addc_co_u32_e32 v6, vcc, 0, v6, vcc
	v_cmp_gt_i64_e32 vcc, s[24:25], v[8:9]
	v_readlane_b32 s25, v9, 8
	s_movk_i32 s24, 55
	v_addc_co_u32_e32 v6, vcc, 0, v6, vcc
	v_cmp_gt_i64_e32 vcc, s[22:23], v[8:9]
	v_readlane_b32 s23, v9, 9
; __device__ __forceinline__ void phase_nrr(const Frame& F, const Args& a, int l, const bf16_t* XA, const float* g, const float* modl, unsigned char* XN8) {
;     ...
;             int rank = 0;
; #pragma unroll 8
;             for (int e2 = 0; e2 < 64; ++e2) { const float v = __int_as_float(__builtin_amdgcn_readlane(__float_as_int(val), e2)); rank += (v > val || (v == val && e2 < lane)) ? 1 : 0; }
	s_movk_i32 s22, 54
	v_addc_co_u32_e32 v6, vcc, 0, v6, vcc
	v_cmp_gt_i64_e32 vcc, s[24:25], v[8:9]
	v_readlane_b32 s25, v9, 10
	s_movk_i32 s24, 53
	v_addc_co_u32_e32 v6, vcc, 0, v6, vcc
	v_cmp_gt_i64_e32 vcc, s[22:23], v[8:9]
	v_readlane_b32 s23, v9, 11
	s_movk_i32 s22, 52
	v_addc_co_u32_e32 v6, vcc, 0, v6, vcc
	v_cmp_gt_i64_e32 vcc, s[24:25], v[8:9]
	v_readlane_b32 s25, v9, 12
	s_movk_i32 s24, 51
	v_addc_co_u32_e32 v6, vcc, 0, v6, vcc
	v_cmp_gt_i64_e32 vcc, s[22:23], v[8:9]
	v_readlane_b32 s23, v9, 13
	s_movk_i32 s22, 50
	v_addc_co_u32_e32 v6, vcc, 0, v6, vcc
	v_cmp_gt_i64_e32 vcc, s[24:25], v[8:9]
	v_readlane_b32 s25, v9, 14
	s_movk_i32 s24, 49
	v_addc_co_u32_e32 v6, vcc, 0, v6, vcc
	v_cmp_gt_i64_e32 vcc, s[22:23], v[8:9]
	v_readlane_b32 s23, v9, 15
	s_movk_i32 s22, 48
	v_addc_co_u32_e32 v6, vcc, 0, v6, vcc
	v_cmp_gt_i64_e32 vcc, s[24:25], v[8:9]
	v_readlane_b32 s25, v9, 16
	s_movk_i32 s24, 47
	v_addc_co_u32_e32 v6, vcc, 0, v6, vcc
	v_cmp_gt_i64_e32 vcc, s[22:23], v[8:9]
	v_readlane_b32 s23, v9, 17
	s_movk_i32 s22, 46
	v_addc_co_u32_e32 v6, vcc, 0, v6, vcc
	v_cmp_gt_i64_e32 vcc, s[24:25], v[8:9]
	v_readlane_b32 s25, v9, 18
	s_movk_i32 s24, 45
	v_addc_co_u32_e32 v6, vcc, 0, v6, vcc
	v_cmp_gt_i64_e32 vcc, s[22:23], v[8:9]
	v_readlane_b32 s23, v9, 19
	s_movk_i32 s22, 44
	v_addc_co_u32_e32 v6, vcc, 0, v6, vcc
	v_cmp_gt_i64_e32 vcc, s[24:25], v[8:9]
	v_readlane_b32 s25, v9, 20
	s_movk_i32 s24, 43
	v_addc_co_u32_e32 v6, vcc, 0, v6, vcc
	v_cmp_gt_i64_e32 vcc, s[22:23], v[8:9]
	v_readlane_b32 s23, v9, 21
	s_movk_i32 s22, 42
	v_addc_co_u32_e32 v6, vcc, 0, v6, vcc
	v_cmp_gt_i64_e32 vcc, s[24:25], v[8:9]
	v_readlane_b32 s25, v9, 22
	s_movk_i32 s24, 41
	v_addc_co_u32_e32 v6, vcc, 0, v6, vcc
	v_cmp_gt_i64_e32 vcc, s[22:23], v[8:9]
	v_readlane_b32 s23, v9, 23
	s_movk_i32 s22, 40
	v_addc_co_u32_e32 v6, vcc, 0, v6, vcc
	v_cmp_gt_i64_e32 vcc, s[24:25], v[8:9]
	v_readlane_b32 s25, v9, 24
	s_movk_i32 s24, 39
	v_addc_co_u32_e32 v6, vcc, 0, v6, vcc
	v_cmp_gt_i64_e32 vcc, s[22:23], v[8:9]
	v_readlane_b32 s23, v9, 25
	s_movk_i32 s22, 38
	v_addc_co_u32_e32 v6, vcc, 0, v6, vcc
	v_cmp_gt_i64_e32 vcc, s[24:25], v[8:9]
	v_readlane_b32 s25, v9, 26
	s_movk_i32 s24, 37
	v_addc_co_u32_e32 v6, vcc, 0, v6, vcc
	v_cmp_gt_i64_e32 vcc, s[22:23], v[8:9]
	v_readlane_b32 s23, v9, 27
	s_movk_i32 s22, 36
	v_addc_co_u32_e32 v6, vcc, 0, v6, vcc
	v_cmp_gt_i64_e32 vcc, s[24:25], v[8:9]
	v_readlane_b32 s25, v9, 28
	s_movk_i32 s24, 35
	v_addc_co_u32_e32 v6, vcc, 0, v6, vcc
	v_cmp_gt_i64_e32 vcc, s[22:23], v[8:9]
	v_readlane_b32 s23, v9, 29
	s_movk_i32 s22, 34
	v_addc_co_u32_e32 v6, vcc, 0, v6, vcc
	v_cmp_gt_i64_e32 vcc, s[24:25], v[8:9]
	v_readlane_b32 s25, v9, 30
	s_movk_i32 s24, 33
	v_addc_co_u32_e32 v6, vcc, 0, v6, vcc
	v_cmp_gt_i64_e32 vcc, s[22:23], v[8:9]
	v_readlane_b32 s23, v9, 31
	s_movk_i32 s22, 32
	v_addc_co_u32_e32 v6, vcc, 0, v6, vcc
	v_cmp_gt_i64_e32 vcc, s[24:25], v[8:9]
	v_readlane_b32 s25, v9, 32
	s_movk_i32 s24, 31
	v_addc_co_u32_e32 v6, vcc, 0, v6, vcc
	v_cmp_gt_i64_e32 vcc, s[22:23], v[8:9]
	v_readlane_b32 s23, v9, 33
	s_movk_i32 s22, 30
	v_addc_co_u32_e32 v6, vcc, 0, v6, vcc
	v_cmp_gt_i64_e32 vcc, s[24:25], v[8:9]
	v_readlane_b32 s25, v9, 34
	s_movk_i32 s24, 29
	v_addc_co_u32_e32 v6, vcc, 0, v6, vcc
	v_cmp_gt_i64_e32 vcc, s[22:23], v[8:9]
	v_readlane_b32 s23, v9, 35
	s_movk_i32 s22, 28
	v_addc_co_u32_e32 v6, vcc, 0, v6, vcc
	v_cmp_gt_i64_e32 vcc, s[24:25], v[8:9]
	v_readlane_b32 s25, v9, 36
	s_movk_i32 s24, 27
	v_addc_co_u32_e32 v6, vcc, 0, v6, vcc
	v_cmp_gt_i64_e32 vcc, s[22:23], v[8:9]
	v_readlane_b32 s23, v9, 37
	s_movk_i32 s22, 26
	v_addc_co_u32_e32 v6, vcc, 0, v6, vcc
	v_cmp_gt_i64_e32 vcc, s[24:25], v[8:9]
	v_readlane_b32 s25, v9, 38
	s_movk_i32 s24, 25
	v_addc_co_u32_e32 v6, vcc, 0, v6, vcc
	v_cmp_gt_i64_e32 vcc, s[22:23], v[8:9]
	v_readlane_b32 s23, v9, 39
	s_movk_i32 s22, 24
	v_addc_co_u32_e32 v6, vcc, 0, v6, vcc
	v_cmp_gt_i64_e32 vcc, s[24:25], v[8:9]
	v_readlane_b32 s25, v9, 40
	s_movk_i32 s24, 23
	v_addc_co_u32_e32 v6, vcc, 0, v6, vcc
	v_cmp_gt_i64_e32 vcc, s[22:23], v[8:9]
	v_readlane_b32 s23, v9, 41
	s_movk_i32 s22, 22
	v_addc_co_u32_e32 v6, vcc, 0, v6, vcc
	v_cmp_gt_i64_e32 vcc, s[24:25], v[8:9]
	v_readlane_b32 s25, v9, 42
	s_movk_i32 s24, 21
	v_addc_co_u32_e32 v6, vcc, 0, v6, vcc
	v_cmp_gt_i64_e32 vcc, s[22:23], v[8:9]
	v_readlane_b32 s23, v9, 43
	s_movk_i32 s22, 20
	v_addc_co_u32_e32 v6, vcc, 0, v6, vcc
	v_cmp_gt_i64_e32 vcc, s[24:25], v[8:9]
	v_readlane_b32 s25, v9, 44
	s_movk_i32 s24, 19
	v_addc_co_u32_e32 v6, vcc, 0, v6, vcc
	v_cmp_gt_i64_e32 vcc, s[22:23], v[8:9]
	v_readlane_b32 s23, v9, 45
	s_movk_i32 s22, 18
	v_addc_co_u32_e32 v6, vcc, 0, v6, vcc
	v_cmp_gt_i64_e32 vcc, s[24:25], v[8:9]
	v_readlane_b32 s25, v9, 46
	s_movk_i32 s24, 17
	v_addc_co_u32_e32 v6, vcc, 0, v6, vcc
	v_cmp_gt_i64_e32 vcc, s[22:23], v[8:9]
	v_readlane_b32 s23, v9, 47
	s_movk_i32 s22, 16
	v_addc_co_u32_e32 v6, vcc, 0, v6, vcc
	v_cmp_gt_i64_e32 vcc, s[24:25], v[8:9]
	v_readlane_b32 s25, v9, 48
	s_movk_i32 s24, 15
	v_addc_co_u32_e32 v6, vcc, 0, v6, vcc
	v_cmp_gt_i64_e32 vcc, s[22:23], v[8:9]
	v_readlane_b32 s23, v9, 49
	s_movk_i32 s22, 14
	v_addc_co_u32_e32 v6, vcc, 0, v6, vcc
	v_cmp_gt_i64_e32 vcc, s[24:25], v[8:9]
	v_readlane_b32 s25, v9, 50
	s_movk_i32 s24, 13
	v_addc_co_u32_e32 v6, vcc, 0, v6, vcc
	v_cmp_gt_i64_e32 vcc, s[22:23], v[8:9]
	v_readlane_b32 s23, v9, 51
	s_movk_i32 s22, 12
	v_addc_co_u32_e32 v6, vcc, 0, v6, vcc
	v_cmp_gt_i64_e32 vcc, s[24:25], v[8:9]
	v_readlane_b32 s25, v9, 52
	s_movk_i32 s24, 11
	v_addc_co_u32_e32 v6, vcc, 0, v6, vcc
	v_cmp_gt_i64_e32 vcc, s[22:23], v[8:9]
	v_readlane_b32 s23, v9, 53
	s_movk_i32 s22, 10
	v_addc_co_u32_e32 v6, vcc, 0, v6, vcc
; __device__ __forceinline__ void phase_nrr(const Frame& F, const Args& a, int l, const bf16_t* XA, const float* g, const float* modl, unsigned char* XN8) {
;     ...
;         for (int i = 0; i < 8; ++i) { const int t = tb + i;
;             const float lg = Pl[(w * 8 + i) * NE + lane] + Pl[(64 + w * 8 + i) * NE + lane]; const float sc = 1.f / (1.f + __expf(-lg)); const float bb = sc + bias;
;             float m1 = bb; m1 = fmaxf(m1, __shfl_xor(m1, 1)); m1 = fmaxf(m1, __shfl_xor(m1, 2)); m1 = fmaxf(m1, __shfl_xor(m1, 4));
;             const unsigned long long eq = __ballot(bb == m1); const int gbase = lane & ~7; const unsigned grpmask = (unsigned)((eq >> gbase) & 0xffull);
;             const int first = gbase + __builtin_ctz(grpmask);
;             float m2 = (lane == first) ? -INFINITY : bb; m2 = fmaxf(m2, __shfl_xor(m2, 1)); m2 = fmaxf(m2, __shfl_xor(m2, 2)); m2 = fmaxf(m2, __shfl_xor(m2, 4));
;     ...
;             int rank = 0;
; #pragma unroll 8
;             for (int e2 = 0; e2 < 64; ++e2) { const float v = __int_as_float(__builtin_amdgcn_readlane(__float_as_int(val), e2)); rank += (v > val || (v == val && e2 < lane)) ? 1 : 0; }
;             const bool sel = rank < TOPK;
;             const float ssum = wave_sum(sel ? sc : 0.f);
;             if (sel) { const int p = atomicAdd((int*)(hist + lane), 1); top_e[t * TOPK + rank] = lane; gate[t * TOPK + rank] = sc / ssum * 2.5f; lpos[t * TOPK + rank] = p; }
	v_cmp_gt_i64_e32 vcc, s[24:25], v[8:9]
	v_readlane_b32 s25, v9, 54
	s_movk_i32 s24, 9
	v_addc_co_u32_e32 v6, vcc, 0, v6, vcc
	v_cmp_gt_i64_e32 vcc, s[22:23], v[8:9]
	v_readlane_b32 s23, v9, 55
	s_movk_i32 s22, 8
	v_addc_co_u32_e32 v6, vcc, 0, v6, vcc
	v_cmp_gt_i64_e32 vcc, s[24:25], v[8:9]
	v_readlane_b32 s25, v9, 56
	s_movk_i32 s24, 7
	v_addc_co_u32_e32 v6, vcc, 0, v6, vcc
	v_cmp_gt_i64_e32 vcc, s[22:23], v[8:9]
	v_readlane_b32 s23, v9, 57
	s_movk_i32 s22, 6
	v_addc_co_u32_e32 v6, vcc, 0, v6, vcc
	v_cmp_gt_i64_e32 vcc, s[24:25], v[8:9]
	v_readlane_b32 s25, v9, 58
	s_movk_i32 s24, 5
	v_addc_co_u32_e32 v6, vcc, 0, v6, vcc
	v_cmp_gt_i64_e32 vcc, s[22:23], v[8:9]
	v_readlane_b32 s23, v9, 59
	s_movk_i32 s22, 4
	v_addc_co_u32_e32 v6, vcc, 0, v6, vcc
	v_cmp_gt_i64_e32 vcc, s[24:25], v[8:9]
	v_readlane_b32 s25, v9, 60
	s_movk_i32 s24, 3
	v_addc_co_u32_e32 v6, vcc, 0, v6, vcc
	v_cmp_gt_i64_e32 vcc, s[22:23], v[8:9]
	v_readlane_b32 s23, v9, 61
	s_movk_i32 s22, 2
	v_addc_co_u32_e32 v6, vcc, 0, v6, vcc
	v_cmp_gt_i64_e32 vcc, s[24:25], v[8:9]
	v_readlane_b32 s25, v9, 62
	s_movk_i32 s24, 1
	v_addc_co_u32_e32 v6, vcc, 0, v6, vcc
	v_cmp_gt_i64_e32 vcc, s[22:23], v[8:9]
	v_readlane_b32 s23, v9, 63
	s_movk_i32 s22, 0
	v_addc_co_u32_e32 v6, vcc, 0, v6, vcc
	v_cmp_gt_i64_e32 vcc, s[24:25], v[8:9]
	s_nop 1
	v_addc_co_u32_e32 v6, vcc, 0, v6, vcc
	v_cmp_gt_i64_e32 vcc, s[22:23], v[8:9]
	s_nop 1
	v_addc_co_u32_e32 v6, vcc, 0, v6, vcc
	v_cmp_gt_u32_e32 vcc, 6, v6
	s_nop 1
	v_cndmask_b32_e32 v5, 0, v2, vcc
	ds_bpermute_b32 v7, v1, v5
	s_waitcnt lgkmcnt(0)
	v_add_f32_e32 v5, v5, v7
	ds_bpermute_b32 v7, v201, v5
	s_waitcnt lgkmcnt(0)
	v_add_f32_e32 v5, v5, v7
	ds_bpermute_b32 v7, v220, v5
	s_waitcnt lgkmcnt(0)
	v_add_f32_e32 v5, v5, v7
	ds_bpermute_b32 v7, v221, v5
	s_waitcnt lgkmcnt(0)
	v_add_f32_e32 v5, v5, v7
	ds_bpermute_b32 v7, v222, v5
	s_waitcnt lgkmcnt(0)
	v_add_f32_e32 v5, v5, v7
	ds_bpermute_b32 v7, v223, v5
	s_and_saveexec_b64 s[2:3], vcc
	s_cbranch_execz .LBB0_563
	s_waitcnt lgkmcnt(0)
	v_add_f32_e32 v5, v5, v7
	v_div_scale_f32 v11, s[4:5], v5, v5, v2
	v_add3_u32 v6, s36, 36, v6
	v_rcp_f32_e32 v12, v11
	v_ashrrev_i32_e32 v7, 31, v6
	v_lshlrev_b64 v[6:7], 2, v[6:7]
	v_lshl_add_u64 v[8:9], s[26:27], 0, v[6:7]
	ds_add_rtn_u32 v10, v227, v243
	global_store_dword v[8:9], v230, off
	v_fma_f32 v8, -v11, v12, 1.0
	v_fmac_f32_e32 v12, v8, v12
	v_div_scale_f32 v8, vcc, v2, v5, v2
	v_mul_f32_e32 v9, v8, v12
	v_fma_f32 v13, -v11, v9, v8
	v_fmac_f32_e32 v9, v13, v12
	v_fma_f32 v8, -v11, v9, v8
	v_div_fmas_f32 v8, v8, v12, v9
	v_div_fixup_f32 v2, v8, v5, v2
	v_mul_f32_e32 v2, 0x40200000, v2
	v_lshl_add_u64 v[8:9], s[28:29], 0, v[6:7]
	v_lshl_add_u64 v[6:7], s[30:31], 0, v[6:7]
	global_store_dword v[8:9], v2, off
	s_waitcnt lgkmcnt(0)
	global_store_dword v[6:7], v10, off
.LBB0_563:
	s_or_b64 exec, exec, s[2:3]
	v_add_u32_e32 v2, s87, v226
	ds_read_b32 v2, v2
	ds_read_b32 v4, v4 offset:18176
	s_waitcnt lgkmcnt(0)
	v_add_f32_e32 v2, v2, v4
	v_mul_f32_e32 v2, 0xbfb8aa3b, v2
	v_exp_f32_e32 v2, v2
	s_nop 0
	v_add_f32_e32 v2, 1.0, v2
	v_div_scale_f32 v4, s[2:3], v2, v2, 1.0
	v_rcp_f32_e32 v5, v4
	s_mov_b32 s2, 0
	v_fma_f32 v6, -v4, v5, 1.0
	v_fmac_f32_e32 v5, v6, v5
	v_div_scale_f32 v6, vcc, 1.0, v2, 1.0
	v_mul_f32_e32 v7, v6, v5
	v_fma_f32 v8, -v4, v7, v6
	v_fmac_f32_e32 v7, v8, v5
	v_fma_f32 v4, -v4, v7, v6
	v_div_fmas_f32 v4, v4, v5, v7
	v_div_fixup_f32 v2, v4, v2, 1.0
	v_add_f32_e32 v3, v3, v2
	ds_bpermute_b32 v4, v1, v3
	s_waitcnt lgkmcnt(0)
	v_max_f32_e32 v4, v4, v4
	v_max_f32_e32 v4, v3, v4
	ds_bpermute_b32 v5, v201, v4
	s_waitcnt lgkmcnt(0)
	v_max_f32_e32 v5, v5, v5
	v_max_f32_e32 v4, v4, v5
	ds_bpermute_b32 v5, v220, v4
	s_waitcnt lgkmcnt(0)
	v_max_f32_e32 v5, v5, v5
	v_max_f32_e32 v6, v4, v5
	v_cmp_eq_f32_e32 vcc, v3, v6
	s_nop 1
	v_lshrrev_b64 v[4:5], v200, vcc
	v_ffbl_b32_sdwa v4, v4 dst_sel:DWORD dst_unused:UNUSED_PAD src0_sel:BYTE_0
	v_add_u32_e32 v4, v4, v200
	v_cmp_ne_u32_e32 vcc, v230, v4
	s_nop 1
	v_cndmask_b32_e32 v4, v245, v3, vcc
	ds_bpermute_b32 v5, v1, v4
	s_waitcnt lgkmcnt(0)
	v_max_f32_e32 v5, v5, v5
	v_max_f32_e32 v4, v4, v5
	ds_bpermute_b32 v5, v201, v4
	s_waitcnt lgkmcnt(0)
	v_max_f32_e32 v5, v5, v5
	v_max_f32_e32 v4, v4, v5
	ds_bpermute_b32 v5, v220, v4
	s_waitcnt lgkmcnt(0)
; __device__ __forceinline__ void phase_nrr(const Frame& F, const Args& a, int l, const bf16_t* XA, const float* g, const float* modl, unsigned char* XN8) {
;     ...
;             const float gsum = m1 + m2; const int gq = lane >> 3;
;             int grank = 0;
; #pragma unroll
;             for (int g2 = 0; g2 < 8; ++g2) { const float v = __int_as_float(__builtin_amdgcn_readlane(__float_as_int(gsum), g2 * 8)); grank += (v > gsum || (v == gsum && g2 < gq)) ? 1 : 0; }
;             const bool keep = grank < 4; const float val = keep ? bb : -INFINITY;
;             int rank = 0;
; #pragma unroll 8
;             for (int e2 = 0; e2 < 64; ++e2) { const float v = __int_as_float(__builtin_amdgcn_readlane(__float_as_int(val), e2)); rank += (v > val || (v == val && e2 < lane)) ? 1 : 0; }
	v_max_f32_e32 v5, v5, v5
	v_max_f32_e32 v4, v4, v5
	v_add_f32_e32 v4, v6, v4
	s_nop 0
	v_readlane_b32 s3, v4, 0
	s_nop 1
	v_cmp_eq_f32_e64 s[22:23], s3, v4
	v_cmp_gt_f32_e32 vcc, s3, v4
	s_and_b64 s[4:5], s[6:7], s[22:23]
	v_readlane_b32 s3, v4, 8
	s_or_b64 s[4:5], vcc, s[4:5]
	v_cndmask_b32_e64 v5, 0, 1, s[4:5]
	v_cmp_eq_f32_e64 s[22:23], s3, v4
	v_cmp_gt_f32_e32 vcc, s3, v4
	s_and_b64 s[4:5], s[8:9], s[22:23]
	v_readlane_b32 s3, v4, 16
	s_or_b64 s[4:5], vcc, s[4:5]
	v_cndmask_b32_e64 v6, 0, 1, s[4:5]
	v_cmp_eq_f32_e64 s[22:23], s3, v4
	v_cmp_gt_f32_e32 vcc, s3, v4
	s_and_b64 s[4:5], s[10:11], s[22:23]
	v_readlane_b32 s3, v4, 24
	s_or_b64 s[4:5], vcc, s[4:5]
	v_cndmask_b32_e64 v7, 0, 1, s[4:5]
	v_cmp_eq_f32_e64 s[22:23], s3, v4
	v_cmp_gt_f32_e32 vcc, s3, v4
	s_and_b64 s[4:5], s[12:13], s[22:23]
	v_readlane_b32 s3, v4, 32
	s_or_b64 s[4:5], vcc, s[4:5]
	v_cndmask_b32_e64 v8, 0, 1, s[4:5]
	v_cmp_eq_f32_e64 s[22:23], s3, v4
	v_cmp_gt_f32_e32 vcc, s3, v4
	s_and_b64 s[4:5], s[14:15], s[22:23]
	v_readlane_b32 s3, v4, 40
	s_or_b64 s[4:5], vcc, s[4:5]
	v_cndmask_b32_e64 v9, 0, 1, s[4:5]
	v_cmp_eq_f32_e64 s[22:23], s3, v4
	v_cmp_gt_f32_e32 vcc, s3, v4
	s_and_b64 s[4:5], s[16:17], s[22:23]
	v_readlane_b32 s3, v4, 48
	s_or_b64 s[4:5], vcc, s[4:5]
	v_cndmask_b32_e64 v10, 0, 1, s[4:5]
	v_cmp_eq_f32_e64 s[22:23], s3, v4
	v_cmp_gt_f32_e32 vcc, s3, v4
	s_and_b64 s[4:5], s[18:19], s[22:23]
	v_readlane_b32 s3, v4, 56
	s_or_b64 s[4:5], vcc, s[4:5]
	v_cndmask_b32_e64 v11, 0, 1, s[4:5]
	v_cmp_gt_f32_e32 vcc, s3, v4
	s_nop 1
	v_cndmask_b32_e64 v4, 0, 1, vcc
	v_add_u32_e32 v4, v6, v4
	v_add3_u32 v4, v4, v5, v7
	v_add3_u32 v4, v4, v8, v9
	v_add3_u32 v4, v4, v10, v11
	v_cmp_gt_u32_e32 vcc, 4, v4
	v_mov_b32_e32 v4, 0
	s_nop 0
	v_cndmask_b32_e32 v3, v245, v3, vcc
	v_ashrrev_i32_e32 v9, 31, v3
	v_sub_u32_e32 v8, 63, v230
	v_and_b32_e32 v9, 0x7fffffff, v9
	v_xor_b32_e32 v9, v3, v9
	s_nop 0
	v_readlane_b32 s25, v9, 0
	s_movk_i32 s24, 63
	v_readlane_b32 s23, v9, 1
	s_movk_i32 s22, 62
	v_cmp_gt_i64_e32 vcc, s[24:25], v[8:9]
	v_readlane_b32 s25, v9, 2
	s_movk_i32 s24, 61
	v_addc_co_u32_e32 v4, vcc, 0, v4, vcc
	v_cmp_gt_i64_e32 vcc, s[22:23], v[8:9]
	v_readlane_b32 s23, v9, 3
	s_movk_i32 s22, 60
	v_addc_co_u32_e32 v4, vcc, 0, v4, vcc
	v_cmp_gt_i64_e32 vcc, s[24:25], v[8:9]
	v_readlane_b32 s25, v9, 4
	s_movk_i32 s24, 59
	v_addc_co_u32_e32 v4, vcc, 0, v4, vcc
	v_cmp_gt_i64_e32 vcc, s[22:23], v[8:9]
	v_readlane_b32 s23, v9, 5
	s_movk_i32 s22, 58
	v_addc_co_u32_e32 v4, vcc, 0, v4, vcc
	v_cmp_gt_i64_e32 vcc, s[24:25], v[8:9]
	v_readlane_b32 s25, v9, 6
	s_movk_i32 s24, 57
	v_addc_co_u32_e32 v4, vcc, 0, v4, vcc
	v_cmp_gt_i64_e32 vcc, s[22:23], v[8:9]
	v_readlane_b32 s23, v9, 7
	s_movk_i32 s22, 56
	v_addc_co_u32_e32 v4, vcc, 0, v4, vcc
	v_cmp_gt_i64_e32 vcc, s[24:25], v[8:9]
	v_readlane_b32 s25, v9, 8
	s_movk_i32 s24, 55
	v_addc_co_u32_e32 v4, vcc, 0, v4, vcc
	v_cmp_gt_i64_e32 vcc, s[22:23], v[8:9]
	v_readlane_b32 s23, v9, 9
	s_movk_i32 s22, 54
	v_addc_co_u32_e32 v4, vcc, 0, v4, vcc
	v_cmp_gt_i64_e32 vcc, s[24:25], v[8:9]
	v_readlane_b32 s25, v9, 10
	s_movk_i32 s24, 53
	v_addc_co_u32_e32 v4, vcc, 0, v4, vcc
	v_cmp_gt_i64_e32 vcc, s[22:23], v[8:9]
	v_readlane_b32 s23, v9, 11
	s_movk_i32 s22, 52
	v_addc_co_u32_e32 v4, vcc, 0, v4, vcc
	v_cmp_gt_i64_e32 vcc, s[24:25], v[8:9]
	v_readlane_b32 s25, v9, 12
	s_movk_i32 s24, 51
	v_addc_co_u32_e32 v4, vcc, 0, v4, vcc
	v_cmp_gt_i64_e32 vcc, s[22:23], v[8:9]
	v_readlane_b32 s23, v9, 13
	s_movk_i32 s22, 50
	v_addc_co_u32_e32 v4, vcc, 0, v4, vcc
	v_cmp_gt_i64_e32 vcc, s[24:25], v[8:9]
	v_readlane_b32 s25, v9, 14
	s_movk_i32 s24, 49
	v_addc_co_u32_e32 v4, vcc, 0, v4, vcc
	v_cmp_gt_i64_e32 vcc, s[22:23], v[8:9]
	v_readlane_b32 s23, v9, 15
	s_movk_i32 s22, 48
	v_addc_co_u32_e32 v4, vcc, 0, v4, vcc
	v_cmp_gt_i64_e32 vcc, s[24:25], v[8:9]
	v_readlane_b32 s25, v9, 16
	s_movk_i32 s24, 47
	v_addc_co_u32_e32 v4, vcc, 0, v4, vcc
	v_cmp_gt_i64_e32 vcc, s[22:23], v[8:9]
	v_readlane_b32 s23, v9, 17
	s_movk_i32 s22, 46
	v_addc_co_u32_e32 v4, vcc, 0, v4, vcc
	v_cmp_gt_i64_e32 vcc, s[24:25], v[8:9]
	v_readlane_b32 s25, v9, 18
	s_movk_i32 s24, 45
	v_addc_co_u32_e32 v4, vcc, 0, v4, vcc
	v_cmp_gt_i64_e32 vcc, s[22:23], v[8:9]
	v_readlane_b32 s23, v9, 19
	s_movk_i32 s22, 44
	v_addc_co_u32_e32 v4, vcc, 0, v4, vcc
	v_cmp_gt_i64_e32 vcc, s[24:25], v[8:9]
	v_readlane_b32 s25, v9, 20
	s_movk_i32 s24, 43
	v_addc_co_u32_e32 v4, vcc, 0, v4, vcc
	v_cmp_gt_i64_e32 vcc, s[22:23], v[8:9]
	v_readlane_b32 s23, v9, 21
	s_movk_i32 s22, 42
	v_addc_co_u32_e32 v4, vcc, 0, v4, vcc
	v_cmp_gt_i64_e32 vcc, s[24:25], v[8:9]
	v_readlane_b32 s25, v9, 22
	s_movk_i32 s24, 41
	v_addc_co_u32_e32 v4, vcc, 0, v4, vcc
	v_cmp_gt_i64_e32 vcc, s[22:23], v[8:9]
	v_readlane_b32 s23, v9, 23
	s_movk_i32 s22, 40
	v_addc_co_u32_e32 v4, vcc, 0, v4, vcc
	v_cmp_gt_i64_e32 vcc, s[24:25], v[8:9]
	v_readlane_b32 s25, v9, 24
	s_movk_i32 s24, 39
	v_addc_co_u32_e32 v4, vcc, 0, v4, vcc
	v_cmp_gt_i64_e32 vcc, s[22:23], v[8:9]
	v_readlane_b32 s23, v9, 25
	s_movk_i32 s22, 38
	v_addc_co_u32_e32 v4, vcc, 0, v4, vcc
	v_cmp_gt_i64_e32 vcc, s[24:25], v[8:9]
	v_readlane_b32 s25, v9, 26
	s_movk_i32 s24, 37
	v_addc_co_u32_e32 v4, vcc, 0, v4, vcc
	v_cmp_gt_i64_e32 vcc, s[22:23], v[8:9]
	v_readlane_b32 s23, v9, 27
	s_movk_i32 s22, 36
	v_addc_co_u32_e32 v4, vcc, 0, v4, vcc
	v_cmp_gt_i64_e32 vcc, s[24:25], v[8:9]
	v_readlane_b32 s25, v9, 28
	s_movk_i32 s24, 35
	v_addc_co_u32_e32 v4, vcc, 0, v4, vcc
	v_cmp_gt_i64_e32 vcc, s[22:23], v[8:9]
	v_readlane_b32 s23, v9, 29
	s_movk_i32 s22, 34
	v_addc_co_u32_e32 v4, vcc, 0, v4, vcc
	v_cmp_gt_i64_e32 vcc, s[24:25], v[8:9]
	v_readlane_b32 s25, v9, 30
	s_movk_i32 s24, 33
; __device__ __forceinline__ void phase_nrr(const Frame& F, const Args& a, int l, const bf16_t* XA, const float* g, const float* modl, unsigned char* XN8) {
;     ...
;             int rank = 0;
; #pragma unroll 8
;             for (int e2 = 0; e2 < 64; ++e2) { const float v = __int_as_float(__builtin_amdgcn_readlane(__float_as_int(val), e2)); rank += (v > val || (v == val && e2 < lane)) ? 1 : 0; }
;             const bool sel = rank < TOPK;
;             const float ssum = wave_sum(sel ? sc : 0.f);
;             if (sel) { const int p = atomicAdd((int*)(hist + lane), 1); top_e[t * TOPK + rank] = lane; gate[t * TOPK + rank] = sc / ssum * 2.5f; lpos[t * TOPK + rank] = p; }
	v_addc_co_u32_e32 v4, vcc, 0, v4, vcc
	v_cmp_gt_i64_e32 vcc, s[22:23], v[8:9]
	v_readlane_b32 s23, v9, 31
	s_movk_i32 s22, 32
	v_addc_co_u32_e32 v4, vcc, 0, v4, vcc
	v_cmp_gt_i64_e32 vcc, s[24:25], v[8:9]
	v_readlane_b32 s25, v9, 32
	s_movk_i32 s24, 31
	v_addc_co_u32_e32 v4, vcc, 0, v4, vcc
	v_cmp_gt_i64_e32 vcc, s[22:23], v[8:9]
	v_readlane_b32 s23, v9, 33
	s_movk_i32 s22, 30
	v_addc_co_u32_e32 v4, vcc, 0, v4, vcc
	v_cmp_gt_i64_e32 vcc, s[24:25], v[8:9]
	v_readlane_b32 s25, v9, 34
	s_movk_i32 s24, 29
	v_addc_co_u32_e32 v4, vcc, 0, v4, vcc
	v_cmp_gt_i64_e32 vcc, s[22:23], v[8:9]
	v_readlane_b32 s23, v9, 35
	s_movk_i32 s22, 28
	v_addc_co_u32_e32 v4, vcc, 0, v4, vcc
	v_cmp_gt_i64_e32 vcc, s[24:25], v[8:9]
	v_readlane_b32 s25, v9, 36
	s_movk_i32 s24, 27
	v_addc_co_u32_e32 v4, vcc, 0, v4, vcc
	v_cmp_gt_i64_e32 vcc, s[22:23], v[8:9]
	v_readlane_b32 s23, v9, 37
	s_movk_i32 s22, 26
	v_addc_co_u32_e32 v4, vcc, 0, v4, vcc
	v_cmp_gt_i64_e32 vcc, s[24:25], v[8:9]
	v_readlane_b32 s25, v9, 38
	s_movk_i32 s24, 25
	v_addc_co_u32_e32 v4, vcc, 0, v4, vcc
	v_cmp_gt_i64_e32 vcc, s[22:23], v[8:9]
	v_readlane_b32 s23, v9, 39
	s_movk_i32 s22, 24
	v_addc_co_u32_e32 v4, vcc, 0, v4, vcc
	v_cmp_gt_i64_e32 vcc, s[24:25], v[8:9]
	v_readlane_b32 s25, v9, 40
	s_movk_i32 s24, 23
	v_addc_co_u32_e32 v4, vcc, 0, v4, vcc
	v_cmp_gt_i64_e32 vcc, s[22:23], v[8:9]
	v_readlane_b32 s23, v9, 41
	s_movk_i32 s22, 22
	v_addc_co_u32_e32 v4, vcc, 0, v4, vcc
	v_cmp_gt_i64_e32 vcc, s[24:25], v[8:9]
	v_readlane_b32 s25, v9, 42
	s_movk_i32 s24, 21
	v_addc_co_u32_e32 v4, vcc, 0, v4, vcc
	v_cmp_gt_i64_e32 vcc, s[22:23], v[8:9]
	v_readlane_b32 s23, v9, 43
	s_movk_i32 s22, 20
	v_addc_co_u32_e32 v4, vcc, 0, v4, vcc
	v_cmp_gt_i64_e32 vcc, s[24:25], v[8:9]
	v_readlane_b32 s25, v9, 44
	s_movk_i32 s24, 19
	v_addc_co_u32_e32 v4, vcc, 0, v4, vcc
	v_cmp_gt_i64_e32 vcc, s[22:23], v[8:9]
	v_readlane_b32 s23, v9, 45
	s_movk_i32 s22, 18
	v_addc_co_u32_e32 v4, vcc, 0, v4, vcc
	v_cmp_gt_i64_e32 vcc, s[24:25], v[8:9]
	v_readlane_b32 s25, v9, 46
	s_movk_i32 s24, 17
	v_addc_co_u32_e32 v4, vcc, 0, v4, vcc
	v_cmp_gt_i64_e32 vcc, s[22:23], v[8:9]
	v_readlane_b32 s23, v9, 47
	s_movk_i32 s22, 16
	v_addc_co_u32_e32 v4, vcc, 0, v4, vcc
	v_cmp_gt_i64_e32 vcc, s[24:25], v[8:9]
	v_readlane_b32 s25, v9, 48
	s_movk_i32 s24, 15
	v_addc_co_u32_e32 v4, vcc, 0, v4, vcc
	v_cmp_gt_i64_e32 vcc, s[22:23], v[8:9]
	v_readlane_b32 s23, v9, 49
	s_movk_i32 s22, 14
	v_addc_co_u32_e32 v4, vcc, 0, v4, vcc
	v_cmp_gt_i64_e32 vcc, s[24:25], v[8:9]
	v_readlane_b32 s25, v9, 50
	s_movk_i32 s24, 13
	v_addc_co_u32_e32 v4, vcc, 0, v4, vcc
	v_cmp_gt_i64_e32 vcc, s[22:23], v[8:9]
	v_readlane_b32 s23, v9, 51
	s_movk_i32 s22, 12
	v_addc_co_u32_e32 v4, vcc, 0, v4, vcc
	v_cmp_gt_i64_e32 vcc, s[24:25], v[8:9]
	v_readlane_b32 s25, v9, 52
	s_movk_i32 s24, 11
	v_addc_co_u32_e32 v4, vcc, 0, v4, vcc
	v_cmp_gt_i64_e32 vcc, s[22:23], v[8:9]
	v_readlane_b32 s23, v9, 53
	s_movk_i32 s22, 10
	v_addc_co_u32_e32 v4, vcc, 0, v4, vcc
	v_cmp_gt_i64_e32 vcc, s[24:25], v[8:9]
	v_readlane_b32 s25, v9, 54
	s_movk_i32 s24, 9
	v_addc_co_u32_e32 v4, vcc, 0, v4, vcc
	v_cmp_gt_i64_e32 vcc, s[22:23], v[8:9]
	v_readlane_b32 s23, v9, 55
	s_movk_i32 s22, 8
	v_addc_co_u32_e32 v4, vcc, 0, v4, vcc
	v_cmp_gt_i64_e32 vcc, s[24:25], v[8:9]
	v_readlane_b32 s25, v9, 56
	s_movk_i32 s24, 7
	v_addc_co_u32_e32 v4, vcc, 0, v4, vcc
	v_cmp_gt_i64_e32 vcc, s[22:23], v[8:9]
	v_readlane_b32 s23, v9, 57
	s_movk_i32 s22, 6
	v_addc_co_u32_e32 v4, vcc, 0, v4, vcc
	v_cmp_gt_i64_e32 vcc, s[24:25], v[8:9]
	v_readlane_b32 s25, v9, 58
	s_movk_i32 s24, 5
	v_addc_co_u32_e32 v4, vcc, 0, v4, vcc
	v_cmp_gt_i64_e32 vcc, s[22:23], v[8:9]
	v_readlane_b32 s23, v9, 59
	s_movk_i32 s22, 4
	v_addc_co_u32_e32 v4, vcc, 0, v4, vcc
	v_cmp_gt_i64_e32 vcc, s[24:25], v[8:9]
	v_readlane_b32 s25, v9, 60
	s_movk_i32 s24, 3
	v_addc_co_u32_e32 v4, vcc, 0, v4, vcc
	v_cmp_gt_i64_e32 vcc, s[22:23], v[8:9]
	v_readlane_b32 s23, v9, 61
	s_movk_i32 s22, 2
	v_addc_co_u32_e32 v4, vcc, 0, v4, vcc
	v_cmp_gt_i64_e32 vcc, s[24:25], v[8:9]
	v_readlane_b32 s25, v9, 62
	s_movk_i32 s24, 1
	v_addc_co_u32_e32 v4, vcc, 0, v4, vcc
	v_cmp_gt_i64_e32 vcc, s[22:23], v[8:9]
	v_readlane_b32 s23, v9, 63
	s_movk_i32 s22, 0
	v_addc_co_u32_e32 v4, vcc, 0, v4, vcc
	v_cmp_gt_i64_e32 vcc, s[24:25], v[8:9]
	s_nop 1
	v_addc_co_u32_e32 v4, vcc, 0, v4, vcc
	v_cmp_gt_i64_e32 vcc, s[22:23], v[8:9]
	s_nop 1
	v_addc_co_u32_e32 v4, vcc, 0, v4, vcc
	v_cmp_gt_u32_e32 vcc, 6, v4
	s_nop 1
	v_cndmask_b32_e32 v3, 0, v2, vcc
	ds_bpermute_b32 v5, v1, v3
	s_waitcnt lgkmcnt(0)
	v_add_f32_e32 v3, v3, v5
	ds_bpermute_b32 v5, v201, v3
	s_waitcnt lgkmcnt(0)
	v_add_f32_e32 v3, v3, v5
	ds_bpermute_b32 v5, v220, v3
	s_waitcnt lgkmcnt(0)
	v_add_f32_e32 v3, v3, v5
	ds_bpermute_b32 v5, v221, v3
	s_waitcnt lgkmcnt(0)
	v_add_f32_e32 v3, v3, v5
	ds_bpermute_b32 v5, v222, v3
	s_waitcnt lgkmcnt(0)
	v_add_f32_e32 v3, v3, v5
	ds_bpermute_b32 v5, v223, v3
	s_and_saveexec_b64 s[2:3], vcc
	s_cbranch_execz .LBB0_567
	s_waitcnt lgkmcnt(0)
	v_add_f32_e32 v3, v3, v5
	v_div_scale_f32 v9, s[4:5], v3, v3, v2
	v_add3_u32 v4, s36, 42, v4
	v_rcp_f32_e32 v10, v9
	v_ashrrev_i32_e32 v5, 31, v4
	v_lshlrev_b64 v[4:5], 2, v[4:5]
	v_lshl_add_u64 v[6:7], s[26:27], 0, v[4:5]
	ds_add_rtn_u32 v8, v227, v243
	global_store_dword v[6:7], v230, off
	v_fma_f32 v6, -v9, v10, 1.0
	v_fmac_f32_e32 v10, v6, v10
	v_div_scale_f32 v6, vcc, v2, v3, v2
	v_mul_f32_e32 v7, v6, v10
	v_fma_f32 v11, -v9, v7, v6
	v_fmac_f32_e32 v7, v11, v10
	v_fma_f32 v6, -v9, v7, v6
	v_div_fmas_f32 v6, v6, v10, v7
	v_div_fixup_f32 v2, v6, v3, v2
	v_mul_f32_e32 v6, 0x40200000, v2
	v_lshl_add_u64 v[2:3], s[28:29], 0, v[4:5]
	global_store_dword v[2:3], v6, off
	v_lshl_add_u64 v[2:3], s[30:31], 0, v[4:5]
	s_waitcnt lgkmcnt(0)
	global_store_dword v[2:3], v8, off

; #define LAS __attribute__((address_space(3)))
; __device__ __forceinline__ void phase_nrr(const Frame& F, const Args& a, int l, const bf16_t* XA, const float* g, const float* modl, unsigned char* XN8) {
;     ...
; #pragma unroll
;         for (int rb = 0; rb < 4; ++rb) *(LAS f32x4*)(Pl + (size_t)((kq * 64 + 16 * rb + fr) * NE + 16 * eb + 4 * fq)) = acc[rb];
;         __syncthreads();
;         const float bias = rbias[lane];
; #pragma unroll
;         for (int i = 0; i < 8; ++i) { const int t = tb + i;
;             const float lg = Pl[(w * 8 + i) * NE + lane] + Pl[(64 + w * 8 + i) * NE + lane]; const float sc = 1.f / (1.f + __expf(-lg)); const float bb = sc + bias;
;             float m1 = bb; m1 = fmaxf(m1, __shfl_xor(m1, 1)); m1 = fmaxf(m1, __shfl_xor(m1, 2)); m1 = fmaxf(m1, __shfl_xor(m1, 4));
;             const unsigned long long eq = __ballot(bb == m1); const int gbase = lane & ~7; const unsigned grpmask = (unsigned)((eq >> gbase) & 0xffull);
;             const int first = gbase + __builtin_ctz(grpmask);
;             float m2 = (lane == first) ? -INFINITY : bb; m2 = fmaxf(m2, __shfl_xor(m2, 1)); m2 = fmaxf(m2, __shfl_xor(m2, 2)); m2 = fmaxf(m2, __shfl_xor(m2, 4));
;             const float gsum = m1 + m2; const int gq = lane >> 3;
;             int grank = 0;
; #pragma unroll
;             for (int g2 = 0; g2 < 8; ++g2) { const float v = __int_as_float(__builtin_amdgcn_readlane(__float_as_int(gsum), g2 * 8)); grank += (v > gsum || (v == gsum && g2 < gq)) ? 1 : 0; }
;             const bool keep = grank < 4; const float val = keep ? bb : -INFINITY;
;             int rank = 0;
; #pragma unroll 8
;             for (int e2 = 0; e2 < 64; ++e2) { const float v = __int_as_float(__builtin_amdgcn_readlane(__float_as_int(val), e2)); rank += (v > val || (v == val && e2 < lane)) ? 1 : 0; }
.LBB0_1308:
	s_barrier
	ds_write_b128 v242, v[110:113]
	ds_write_b128 v242, v[118:121] offset:4096
	s_nop 0
	ds_write_b128 v242, v[126:129] offset:8192
	s_nop 1
	ds_write_b128 v242, v[130:133] offset:12288
	s_waitcnt lgkmcnt(0)
	s_barrier
	global_load_dword v3, v[198:199], off offset:256
	s_waitcnt vmcnt(15)
	v_add_u32_e32 v4, s33, v226
	ds_read2st64_b32 v[6:7], v4 offset1:64
	s_mov_b32 s3, 0
	s_waitcnt lgkmcnt(0)
	v_add_f32_e32 v2, v6, v7
	v_mul_f32_e32 v2, 0xbfb8aa3b, v2
	v_exp_f32_e32 v2, v2
	s_nop 0
	v_add_f32_e32 v2, 1.0, v2
	v_div_scale_f32 v5, s[20:21], v2, v2, 1.0
	v_rcp_f32_e32 v6, v5
	s_nop 0
	v_fma_f32 v7, -v5, v6, 1.0
	v_fmac_f32_e32 v6, v7, v6
	v_div_scale_f32 v7, vcc, 1.0, v2, 1.0
	v_mul_f32_e32 v8, v7, v6
	v_fma_f32 v9, -v5, v8, v7
	v_fmac_f32_e32 v8, v9, v6
	v_fma_f32 v5, -v5, v8, v7
	v_div_fmas_f32 v5, v5, v6, v8
	v_div_fixup_f32 v2, v5, v2, 1.0
	s_waitcnt vmcnt(0)
	v_add_f32_e32 v5, v3, v2
	ds_bpermute_b32 v6, v1, v5
	s_waitcnt lgkmcnt(0)
	v_max_f32_e32 v6, v6, v6
	v_max_f32_e32 v6, v5, v6
	ds_bpermute_b32 v7, v201, v6
	s_waitcnt lgkmcnt(0)
	v_max_f32_e32 v7, v7, v7
	v_max_f32_e32 v6, v6, v7
	ds_bpermute_b32 v7, v220, v6
	s_waitcnt lgkmcnt(0)
	v_max_f32_e32 v7, v7, v7
	v_max_f32_e32 v8, v6, v7
	v_cmp_eq_f32_e32 vcc, v5, v8
	s_nop 1
	v_lshrrev_b64 v[6:7], v200, vcc
	v_ffbl_b32_sdwa v6, v6 dst_sel:DWORD dst_unused:UNUSED_PAD src0_sel:BYTE_0
	v_add_u32_e32 v6, v6, v200
	v_cmp_ne_u32_e32 vcc, v230, v6
	s_nop 1
	v_cndmask_b32_e32 v6, v245, v5, vcc
	ds_bpermute_b32 v7, v1, v6
	s_waitcnt lgkmcnt(0)
	v_max_f32_e32 v7, v7, v7
	v_max_f32_e32 v6, v6, v7
	ds_bpermute_b32 v7, v201, v6
	s_waitcnt lgkmcnt(0)
	v_max_f32_e32 v7, v7, v7
	v_max_f32_e32 v6, v6, v7
	ds_bpermute_b32 v7, v220, v6
	s_waitcnt lgkmcnt(0)
	v_max_f32_e32 v7, v7, v7
	v_max_f32_e32 v6, v6, v7
	v_add_f32_e32 v6, v8, v6
	s_nop 0
	v_readlane_b32 s5, v6, 0
	s_nop 1
	v_cmp_eq_f32_e64 s[20:21], s5, v6
	v_cmp_gt_f32_e32 vcc, s5, v6
	s_and_b64 s[20:21], s[0:1], s[20:21]
	s_or_b64 s[20:21], vcc, s[20:21]
	v_readlane_b32 s5, v6, 8
	v_cndmask_b32_e64 v7, 0, 1, s[20:21]
	s_nop 0
	v_cmp_eq_f32_e64 s[20:21], s5, v6
	v_cmp_gt_f32_e32 vcc, s5, v6
	s_and_b64 s[20:21], s[6:7], s[20:21]
	s_or_b64 s[20:21], vcc, s[20:21]
	v_readlane_b32 s5, v6, 16
	v_cndmask_b32_e64 v8, 0, 1, s[20:21]
	s_nop 0
	v_cmp_eq_f32_e64 s[20:21], s5, v6
	v_cmp_gt_f32_e32 vcc, s5, v6
	s_and_b64 s[20:21], s[8:9], s[20:21]
	s_or_b64 s[20:21], vcc, s[20:21]
	v_readlane_b32 s5, v6, 24
	v_cndmask_b32_e64 v9, 0, 1, s[20:21]
	s_nop 0
	v_cmp_eq_f32_e64 s[20:21], s5, v6
	v_cmp_gt_f32_e32 vcc, s5, v6
	s_and_b64 s[20:21], s[10:11], s[20:21]
	s_or_b64 s[20:21], vcc, s[20:21]
	v_readlane_b32 s5, v6, 32
	v_cndmask_b32_e64 v10, 0, 1, s[20:21]
	s_nop 0
	v_cmp_eq_f32_e64 s[20:21], s5, v6
	v_cmp_gt_f32_e32 vcc, s5, v6
	s_and_b64 s[20:21], s[12:13], s[20:21]
	s_or_b64 s[20:21], vcc, s[20:21]
	v_readlane_b32 s5, v6, 40
	v_cndmask_b32_e64 v11, 0, 1, s[20:21]
	s_nop 0
	v_cmp_eq_f32_e64 s[20:21], s5, v6
	v_cmp_gt_f32_e32 vcc, s5, v6
	s_and_b64 s[20:21], s[14:15], s[20:21]
	s_or_b64 s[20:21], vcc, s[20:21]
	v_readlane_b32 s5, v6, 48
	v_cndmask_b32_e64 v12, 0, 1, s[20:21]
	s_nop 0
	v_cmp_eq_f32_e64 s[20:21], s5, v6
	v_cmp_gt_f32_e32 vcc, s5, v6
	s_and_b64 s[20:21], s[16:17], s[20:21]
	v_readlane_b32 s5, v6, 56
	s_or_b64 s[20:21], vcc, s[20:21]
	v_cndmask_b32_e64 v13, 0, 1, s[20:21]
	v_cmp_gt_f32_e32 vcc, s5, v6
	s_nop 1
	v_cndmask_b32_e64 v6, 0, 1, vcc
	v_add_u32_e32 v6, v8, v6
	v_add3_u32 v6, v6, v7, v9
	v_add3_u32 v6, v6, v10, v11
	v_add3_u32 v6, v6, v12, v13
	v_cmp_gt_u32_e32 vcc, 4, v6
	v_mov_b32_e32 v6, 0
	s_nop 0
	v_cndmask_b32_e32 v5, v245, v5, vcc
	v_ashrrev_i32_e32 v9, 31, v5
	v_sub_u32_e32 v8, 63, v230
	v_and_b32_e32 v9, 0x7fffffff, v9
	v_xor_b32_e32 v9, v5, v9
	s_nop 0
	v_readlane_b32 s23, v9, 0
	s_movk_i32 s22, 63
	v_readlane_b32 s21, v9, 1
	s_movk_i32 s20, 62
	v_cmp_gt_i64_e32 vcc, s[22:23], v[8:9]
	v_readlane_b32 s23, v9, 2
	s_movk_i32 s22, 61
	v_addc_co_u32_e32 v6, vcc, 0, v6, vcc
	v_cmp_gt_i64_e32 vcc, s[20:21], v[8:9]
	v_readlane_b32 s21, v9, 3
	s_movk_i32 s20, 60
	v_addc_co_u32_e32 v6, vcc, 0, v6, vcc
	v_cmp_gt_i64_e32 vcc, s[22:23], v[8:9]
	v_readlane_b32 s23, v9, 4
	s_movk_i32 s22, 59
	v_addc_co_u32_e32 v6, vcc, 0, v6, vcc
	v_cmp_gt_i64_e32 vcc, s[20:21], v[8:9]
	v_readlane_b32 s21, v9, 5
	s_movk_i32 s20, 58
	v_addc_co_u32_e32 v6, vcc, 0, v6, vcc
	v_cmp_gt_i64_e32 vcc, s[22:23], v[8:9]
	v_readlane_b32 s23, v9, 6
	s_movk_i32 s22, 57
	v_addc_co_u32_e32 v6, vcc, 0, v6, vcc
	v_cmp_gt_i64_e32 vcc, s[20:21], v[8:9]
	v_readlane_b32 s21, v9, 7
	s_movk_i32 s20, 56
	v_addc_co_u32_e32 v6, vcc, 0, v6, vcc
	v_cmp_gt_i64_e32 vcc, s[22:23], v[8:9]
	v_readlane_b32 s23, v9, 8
	s_movk_i32 s22, 55
	v_addc_co_u32_e32 v6, vcc, 0, v6, vcc
	v_cmp_gt_i64_e32 vcc, s[20:21], v[8:9]
	v_readlane_b32 s21, v9, 9
	s_movk_i32 s20, 54
	v_addc_co_u32_e32 v6, vcc, 0, v6, vcc
	v_cmp_gt_i64_e32 vcc, s[22:23], v[8:9]
	v_readlane_b32 s23, v9, 10
	s_movk_i32 s22, 53
	v_addc_co_u32_e32 v6, vcc, 0, v6, vcc
	v_cmp_gt_i64_e32 vcc, s[20:21], v[8:9]
	v_readlane_b32 s21, v9, 11
	s_movk_i32 s20, 52
	v_addc_co_u32_e32 v6, vcc, 0, v6, vcc
	v_cmp_gt_i64_e32 vcc, s[22:23], v[8:9]
	v_readlane_b32 s23, v9, 12
	s_movk_i32 s22, 51
	v_addc_co_u32_e32 v6, vcc, 0, v6, vcc
	v_cmp_gt_i64_e32 vcc, s[20:21], v[8:9]
	v_readlane_b32 s21, v9, 13
	s_movk_i32 s20, 50
	v_addc_co_u32_e32 v6, vcc, 0, v6, vcc
	v_cmp_gt_i64_e32 vcc, s[22:23], v[8:9]
	v_readlane_b32 s23, v9, 14
	s_movk_i32 s22, 49
	v_addc_co_u32_e32 v6, vcc, 0, v6, vcc
	v_cmp_gt_i64_e32 vcc, s[20:21], v[8:9]
	v_readlane_b32 s21, v9, 15
	s_movk_i32 s20, 48
	v_addc_co_u32_e32 v6, vcc, 0, v6, vcc
	v_cmp_gt_i64_e32 vcc, s[22:23], v[8:9]
; __device__ __forceinline__ void phase_nrr(const Frame& F, const Args& a, int l, const bf16_t* XA, const float* g, const float* modl, unsigned char* XN8) {
;     ...
;             int rank = 0;
; #pragma unroll 8
;             for (int e2 = 0; e2 < 64; ++e2) { const float v = __int_as_float(__builtin_amdgcn_readlane(__float_as_int(val), e2)); rank += (v > val || (v == val && e2 < lane)) ? 1 : 0; }
;             const bool sel = rank < TOPK;
;             const float ssum = wave_sum(sel ? sc : 0.f);
;             if (sel) { const int p = atomicAdd((int*)(hist + lane), 1); top_e[t * TOPK + rank] = lane; gate[t * TOPK + rank] = sc / ssum * 2.5f; lpos[t * TOPK + rank] = p; }
	v_readlane_b32 s23, v9, 16
	s_movk_i32 s22, 47
	v_addc_co_u32_e32 v6, vcc, 0, v6, vcc
	v_cmp_gt_i64_e32 vcc, s[20:21], v[8:9]
	v_readlane_b32 s21, v9, 17
	s_movk_i32 s20, 46
	v_addc_co_u32_e32 v6, vcc, 0, v6, vcc
	v_cmp_gt_i64_e32 vcc, s[22:23], v[8:9]
	v_readlane_b32 s23, v9, 18
	s_movk_i32 s22, 45
	v_addc_co_u32_e32 v6, vcc, 0, v6, vcc
	v_cmp_gt_i64_e32 vcc, s[20:21], v[8:9]
	v_readlane_b32 s21, v9, 19
	s_movk_i32 s20, 44
	v_addc_co_u32_e32 v6, vcc, 0, v6, vcc
	v_cmp_gt_i64_e32 vcc, s[22:23], v[8:9]
	v_readlane_b32 s23, v9, 20
	s_movk_i32 s22, 43
	v_addc_co_u32_e32 v6, vcc, 0, v6, vcc
	v_cmp_gt_i64_e32 vcc, s[20:21], v[8:9]
	v_readlane_b32 s21, v9, 21
	s_movk_i32 s20, 42
	v_addc_co_u32_e32 v6, vcc, 0, v6, vcc
	v_cmp_gt_i64_e32 vcc, s[22:23], v[8:9]
	v_readlane_b32 s23, v9, 22
	s_movk_i32 s22, 41
	v_addc_co_u32_e32 v6, vcc, 0, v6, vcc
	v_cmp_gt_i64_e32 vcc, s[20:21], v[8:9]
	v_readlane_b32 s21, v9, 23
	s_movk_i32 s20, 40
	v_addc_co_u32_e32 v6, vcc, 0, v6, vcc
	v_cmp_gt_i64_e32 vcc, s[22:23], v[8:9]
	v_readlane_b32 s23, v9, 24
	s_movk_i32 s22, 39
	v_addc_co_u32_e32 v6, vcc, 0, v6, vcc
	v_cmp_gt_i64_e32 vcc, s[20:21], v[8:9]
	v_readlane_b32 s21, v9, 25
	s_movk_i32 s20, 38
	v_addc_co_u32_e32 v6, vcc, 0, v6, vcc
	v_cmp_gt_i64_e32 vcc, s[22:23], v[8:9]
	v_readlane_b32 s23, v9, 26
	s_movk_i32 s22, 37
	v_addc_co_u32_e32 v6, vcc, 0, v6, vcc
	v_cmp_gt_i64_e32 vcc, s[20:21], v[8:9]
	v_readlane_b32 s21, v9, 27
	s_movk_i32 s20, 36
	v_addc_co_u32_e32 v6, vcc, 0, v6, vcc
	v_cmp_gt_i64_e32 vcc, s[22:23], v[8:9]
	v_readlane_b32 s23, v9, 28
	s_movk_i32 s22, 35
	v_addc_co_u32_e32 v6, vcc, 0, v6, vcc
	v_cmp_gt_i64_e32 vcc, s[20:21], v[8:9]
	v_readlane_b32 s21, v9, 29
	s_movk_i32 s20, 34
	v_addc_co_u32_e32 v6, vcc, 0, v6, vcc
	v_cmp_gt_i64_e32 vcc, s[22:23], v[8:9]
	v_readlane_b32 s23, v9, 30
	s_movk_i32 s22, 33
	v_addc_co_u32_e32 v6, vcc, 0, v6, vcc
	v_cmp_gt_i64_e32 vcc, s[20:21], v[8:9]
	v_readlane_b32 s21, v9, 31
	s_movk_i32 s20, 32
	v_addc_co_u32_e32 v6, vcc, 0, v6, vcc
	v_cmp_gt_i64_e32 vcc, s[22:23], v[8:9]
	v_readlane_b32 s23, v9, 32
	s_movk_i32 s22, 31
	v_addc_co_u32_e32 v6, vcc, 0, v6, vcc
	v_cmp_gt_i64_e32 vcc, s[20:21], v[8:9]
	v_readlane_b32 s21, v9, 33
	s_movk_i32 s20, 30
	v_addc_co_u32_e32 v6, vcc, 0, v6, vcc
	v_cmp_gt_i64_e32 vcc, s[22:23], v[8:9]
	v_readlane_b32 s23, v9, 34
	s_movk_i32 s22, 29
	v_addc_co_u32_e32 v6, vcc, 0, v6, vcc
	v_cmp_gt_i64_e32 vcc, s[20:21], v[8:9]
	v_readlane_b32 s21, v9, 35
	s_movk_i32 s20, 28
	v_addc_co_u32_e32 v6, vcc, 0, v6, vcc
	v_cmp_gt_i64_e32 vcc, s[22:23], v[8:9]
	v_readlane_b32 s23, v9, 36
	s_movk_i32 s22, 27
	v_addc_co_u32_e32 v6, vcc, 0, v6, vcc
	v_cmp_gt_i64_e32 vcc, s[20:21], v[8:9]
	v_readlane_b32 s21, v9, 37
	s_movk_i32 s20, 26
	v_addc_co_u32_e32 v6, vcc, 0, v6, vcc
	v_cmp_gt_i64_e32 vcc, s[22:23], v[8:9]
	v_readlane_b32 s23, v9, 38
	s_movk_i32 s22, 25
	v_addc_co_u32_e32 v6, vcc, 0, v6, vcc
	v_cmp_gt_i64_e32 vcc, s[20:21], v[8:9]
	v_readlane_b32 s21, v9, 39
	s_movk_i32 s20, 24
	v_addc_co_u32_e32 v6, vcc, 0, v6, vcc
	v_cmp_gt_i64_e32 vcc, s[22:23], v[8:9]
	v_readlane_b32 s23, v9, 40
	s_movk_i32 s22, 23
	v_addc_co_u32_e32 v6, vcc, 0, v6, vcc
	v_cmp_gt_i64_e32 vcc, s[20:21], v[8:9]
	v_readlane_b32 s21, v9, 41
	s_movk_i32 s20, 22
	v_addc_co_u32_e32 v6, vcc, 0, v6, vcc
	v_cmp_gt_i64_e32 vcc, s[22:23], v[8:9]
	v_readlane_b32 s23, v9, 42
	s_movk_i32 s22, 21
	v_addc_co_u32_e32 v6, vcc, 0, v6, vcc
	v_cmp_gt_i64_e32 vcc, s[20:21], v[8:9]
	v_readlane_b32 s21, v9, 43
	s_movk_i32 s20, 20
	v_addc_co_u32_e32 v6, vcc, 0, v6, vcc
	v_cmp_gt_i64_e32 vcc, s[22:23], v[8:9]
	v_readlane_b32 s23, v9, 44
	s_movk_i32 s22, 19
	v_addc_co_u32_e32 v6, vcc, 0, v6, vcc
	v_cmp_gt_i64_e32 vcc, s[20:21], v[8:9]
	v_readlane_b32 s21, v9, 45
	s_movk_i32 s20, 18
	v_addc_co_u32_e32 v6, vcc, 0, v6, vcc
	v_cmp_gt_i64_e32 vcc, s[22:23], v[8:9]
	v_readlane_b32 s23, v9, 46
	s_movk_i32 s22, 17
	v_addc_co_u32_e32 v6, vcc, 0, v6, vcc
	v_cmp_gt_i64_e32 vcc, s[20:21], v[8:9]
	v_readlane_b32 s21, v9, 47
	s_movk_i32 s20, 16
	v_addc_co_u32_e32 v6, vcc, 0, v6, vcc
	v_cmp_gt_i64_e32 vcc, s[22:23], v[8:9]
	v_readlane_b32 s23, v9, 48
	s_movk_i32 s22, 15
	v_addc_co_u32_e32 v6, vcc, 0, v6, vcc
	v_cmp_gt_i64_e32 vcc, s[20:21], v[8:9]
	v_readlane_b32 s21, v9, 49
	s_movk_i32 s20, 14
	v_addc_co_u32_e32 v6, vcc, 0, v6, vcc
	v_cmp_gt_i64_e32 vcc, s[22:23], v[8:9]
	v_readlane_b32 s23, v9, 50
	s_movk_i32 s22, 13
	v_addc_co_u32_e32 v6, vcc, 0, v6, vcc
	v_cmp_gt_i64_e32 vcc, s[20:21], v[8:9]
	v_readlane_b32 s21, v9, 51
	s_movk_i32 s20, 12
	v_addc_co_u32_e32 v6, vcc, 0, v6, vcc
	v_cmp_gt_i64_e32 vcc, s[22:23], v[8:9]
	v_readlane_b32 s23, v9, 52
	s_movk_i32 s22, 11
	v_addc_co_u32_e32 v6, vcc, 0, v6, vcc
	v_cmp_gt_i64_e32 vcc, s[20:21], v[8:9]
	v_readlane_b32 s21, v9, 53
	s_movk_i32 s20, 10
	v_addc_co_u32_e32 v6, vcc, 0, v6, vcc
	v_cmp_gt_i64_e32 vcc, s[22:23], v[8:9]
	v_readlane_b32 s23, v9, 54
	s_movk_i32 s22, 9
	v_addc_co_u32_e32 v6, vcc, 0, v6, vcc
	v_cmp_gt_i64_e32 vcc, s[20:21], v[8:9]
	v_readlane_b32 s21, v9, 55
	s_movk_i32 s20, 8
	v_addc_co_u32_e32 v6, vcc, 0, v6, vcc
	v_cmp_gt_i64_e32 vcc, s[22:23], v[8:9]
	v_readlane_b32 s23, v9, 56
	s_movk_i32 s22, 7
	v_addc_co_u32_e32 v6, vcc, 0, v6, vcc
	v_cmp_gt_i64_e32 vcc, s[20:21], v[8:9]
	v_readlane_b32 s21, v9, 57
	s_movk_i32 s20, 6
	v_addc_co_u32_e32 v6, vcc, 0, v6, vcc
	v_cmp_gt_i64_e32 vcc, s[22:23], v[8:9]
	v_readlane_b32 s23, v9, 58
	s_movk_i32 s22, 5
	v_addc_co_u32_e32 v6, vcc, 0, v6, vcc
	v_cmp_gt_i64_e32 vcc, s[20:21], v[8:9]
	v_readlane_b32 s21, v9, 59
	s_movk_i32 s20, 4
	v_addc_co_u32_e32 v6, vcc, 0, v6, vcc
	v_cmp_gt_i64_e32 vcc, s[22:23], v[8:9]
	v_readlane_b32 s23, v9, 60
	s_movk_i32 s22, 3
	v_addc_co_u32_e32 v6, vcc, 0, v6, vcc
	v_cmp_gt_i64_e32 vcc, s[20:21], v[8:9]
	v_readlane_b32 s21, v9, 61
	s_movk_i32 s20, 2
	v_addc_co_u32_e32 v6, vcc, 0, v6, vcc
	v_cmp_gt_i64_e32 vcc, s[22:23], v[8:9]
	v_readlane_b32 s23, v9, 62
	s_movk_i32 s22, 1
	v_addc_co_u32_e32 v6, vcc, 0, v6, vcc
	v_cmp_gt_i64_e32 vcc, s[20:21], v[8:9]
	v_readlane_b32 s21, v9, 63
	s_movk_i32 s20, 0
	v_addc_co_u32_e32 v6, vcc, 0, v6, vcc
	v_cmp_gt_i64_e32 vcc, s[22:23], v[8:9]
	s_nop 1
	v_addc_co_u32_e32 v6, vcc, 0, v6, vcc
	v_cmp_gt_i64_e32 vcc, s[20:21], v[8:9]
	s_nop 1
	v_addc_co_u32_e32 v6, vcc, 0, v6, vcc
	v_cmp_gt_u32_e32 vcc, 6, v6
	s_mul_i32 s50, s24, 6
	s_nop 0
	v_cndmask_b32_e32 v5, 0, v2, vcc
	ds_bpermute_b32 v7, v1, v5
	s_waitcnt lgkmcnt(0)
	v_add_f32_e32 v5, v5, v7
	ds_bpermute_b32 v7, v201, v5
	s_waitcnt lgkmcnt(0)
	v_add_f32_e32 v5, v5, v7
	ds_bpermute_b32 v7, v220, v5
	s_waitcnt lgkmcnt(0)
	v_add_f32_e32 v5, v5, v7
	ds_bpermute_b32 v7, v221, v5
	s_waitcnt lgkmcnt(0)
	v_add_f32_e32 v5, v5, v7
	ds_bpermute_b32 v7, v222, v5
	s_waitcnt lgkmcnt(0)
	v_add_f32_e32 v5, v5, v7
	ds_bpermute_b32 v7, v223, v5
	s_and_saveexec_b64 s[20:21], vcc
	s_cbranch_execz .LBB0_1312
; __device__ __forceinline__ void phase_nrr(const Frame& F, const Args& a, int l, const bf16_t* XA, const float* g, const float* modl, unsigned char* XN8) {
;     ...
;         for (int i = 0; i < 8; ++i) { const int t = tb + i;
;             const float lg = Pl[(w * 8 + i) * NE + lane] + Pl[(64 + w * 8 + i) * NE + lane]; const float sc = 1.f / (1.f + __expf(-lg)); const float bb = sc + bias;
;             float m1 = bb; m1 = fmaxf(m1, __shfl_xor(m1, 1)); m1 = fmaxf(m1, __shfl_xor(m1, 2)); m1 = fmaxf(m1, __shfl_xor(m1, 4));
;             const unsigned long long eq = __ballot(bb == m1); const int gbase = lane & ~7; const unsigned grpmask = (unsigned)((eq >> gbase) & 0xffull);
;             const int first = gbase + __builtin_ctz(grpmask);
;             float m2 = (lane == first) ? -INFINITY : bb; m2 = fmaxf(m2, __shfl_xor(m2, 1)); m2 = fmaxf(m2, __shfl_xor(m2, 2)); m2 = fmaxf(m2, __shfl_xor(m2, 4));
;             const float gsum = m1 + m2; const int gq = lane >> 3;
;             int grank = 0;
; #pragma unroll
;             for (int g2 = 0; g2 < 8; ++g2) { const float v = __int_as_float(__builtin_amdgcn_readlane(__float_as_int(gsum), g2 * 8)); grank += (v > gsum || (v == gsum && g2 < gq)) ? 1 : 0; }
;             const bool keep = grank < 4; const float val = keep ? bb : -INFINITY;
;             int rank = 0;
; #pragma unroll 8
;             for (int e2 = 0; e2 < 64; ++e2) { const float v = __int_as_float(__builtin_amdgcn_readlane(__float_as_int(val), e2)); rank += (v > val || (v == val && e2 < lane)) ? 1 : 0; }
;     ...
;             if (sel) { const int p = atomicAdd((int*)(hist + lane), 1); top_e[t * TOPK + rank] = lane; gate[t * TOPK + rank] = sc / ssum * 2.5f; lpos[t * TOPK + rank] = p; }
	s_waitcnt lgkmcnt(0)
	v_add_f32_e32 v5, v5, v7
	v_div_scale_f32 v11, s[22:23], v5, v5, v2
	v_or_b32_e32 v6, s50, v6
	v_rcp_f32_e32 v12, v11
	v_ashrrev_i32_e32 v7, 31, v6
	v_lshlrev_b64 v[6:7], 2, v[6:7]
	v_lshl_add_u64 v[8:9], s[42:43], 0, v[6:7]
	ds_add_rtn_u32 v10, v227, v243
	global_store_dword v[8:9], v230, off
	v_fma_f32 v8, -v11, v12, 1.0
	v_fmac_f32_e32 v12, v8, v12
	v_div_scale_f32 v8, vcc, v2, v5, v2
	v_mul_f32_e32 v9, v8, v12
	v_fma_f32 v13, -v11, v9, v8
	v_fmac_f32_e32 v9, v13, v12
	v_fma_f32 v8, -v11, v9, v8
	v_div_fmas_f32 v8, v8, v12, v9
	v_div_fixup_f32 v2, v8, v5, v2
	v_mul_f32_e32 v2, 0x40200000, v2
	v_lshl_add_u64 v[8:9], s[44:45], 0, v[6:7]
	v_lshl_add_u64 v[6:7], s[46:47], 0, v[6:7]
	global_store_dword v[8:9], v2, off
	s_waitcnt lgkmcnt(0)
	global_store_dword v[6:7], v10, off
.LBB0_1312:
	s_or_b64 exec, exec, s[20:21]
	v_add_u32_e32 v2, s76, v226
	ds_read_b32 v2, v2
	ds_read_b32 v5, v4 offset:16640
	s_mov_b32 s3, 0
	s_waitcnt lgkmcnt(0)
	v_add_f32_e32 v2, v2, v5
	v_mul_f32_e32 v2, 0xbfb8aa3b, v2
	v_exp_f32_e32 v2, v2
	s_nop 0
	v_add_f32_e32 v2, 1.0, v2
	v_div_scale_f32 v5, s[20:21], v2, v2, 1.0
	v_rcp_f32_e32 v6, v5
	v_div_scale_f32 v7, vcc, 1.0, v2, 1.0
	v_fma_f32 v8, -v5, v6, 1.0
	v_fmac_f32_e32 v6, v8, v6
	v_mul_f32_e32 v8, v7, v6
	v_fma_f32 v9, -v5, v8, v7
	v_fmac_f32_e32 v8, v9, v6
	v_fma_f32 v5, -v5, v8, v7
	v_div_fmas_f32 v5, v5, v6, v8
	v_div_fixup_f32 v5, v5, v2, 1.0
	v_add_f32_e32 v2, v3, v5
	ds_bpermute_b32 v6, v1, v2
	s_waitcnt lgkmcnt(0)
	v_max_f32_e32 v6, v6, v6
	v_max_f32_e32 v6, v2, v6
	ds_bpermute_b32 v7, v201, v6
	s_waitcnt lgkmcnt(0)
	v_max_f32_e32 v7, v7, v7
	v_max_f32_e32 v6, v6, v7
	ds_bpermute_b32 v7, v220, v6
	s_waitcnt lgkmcnt(0)
	v_max_f32_e32 v7, v7, v7
	v_max_f32_e32 v8, v6, v7
	v_cmp_eq_f32_e32 vcc, v2, v8
	s_nop 1
	v_lshrrev_b64 v[6:7], v200, vcc
	v_ffbl_b32_sdwa v6, v6 dst_sel:DWORD dst_unused:UNUSED_PAD src0_sel:BYTE_0
	v_add_u32_e32 v6, v6, v200
	v_cmp_ne_u32_e32 vcc, v230, v6
	s_nop 1
	v_cndmask_b32_e32 v6, v245, v2, vcc
	ds_bpermute_b32 v7, v1, v6
	s_waitcnt lgkmcnt(0)
	v_max_f32_e32 v7, v7, v7
	v_max_f32_e32 v6, v6, v7
	ds_bpermute_b32 v7, v201, v6
	s_waitcnt lgkmcnt(0)
	v_max_f32_e32 v7, v7, v7
	v_max_f32_e32 v6, v6, v7
	ds_bpermute_b32 v7, v220, v6
	s_waitcnt lgkmcnt(0)
	v_max_f32_e32 v7, v7, v7
	v_max_f32_e32 v6, v6, v7
	v_add_f32_e32 v6, v8, v6
	s_nop 0
	v_readlane_b32 s5, v6, 0
	v_readlane_b32 s24, v6, 8
	v_readlane_b32 s28, v6, 16
	v_cmp_eq_f32_e64 s[20:21], s5, v6
	v_cmp_gt_f32_e32 vcc, s5, v6
	v_cmp_gt_f32_e64 s[22:23], s24, v6
	v_cmp_eq_f32_e64 s[24:25], s24, v6
	s_and_b64 s[20:21], s[0:1], s[20:21]
	v_readlane_b32 s34, v6, 24
	v_cmp_gt_f32_e64 s[26:27], s28, v6
	v_cmp_eq_f32_e64 s[28:29], s28, v6
	s_and_b64 s[24:25], s[6:7], s[24:25]
	s_or_b64 s[20:21], vcc, s[20:21]
	v_readlane_b32 s40, v6, 32
	v_cmp_gt_f32_e64 s[30:31], s34, v6
	v_cmp_eq_f32_e64 s[34:35], s34, v6
	s_and_b64 s[28:29], s[8:9], s[28:29]
	v_cndmask_b32_e64 v7, 0, 1, s[20:21]
	s_or_b64 s[20:21], s[22:23], s[24:25]
	v_cmp_gt_f32_e64 s[36:37], s40, v6
	v_cmp_eq_f32_e64 s[40:41], s40, v6
	s_and_b64 s[34:35], s[10:11], s[34:35]
	v_cndmask_b32_e64 v8, 0, 1, s[20:21]
	s_or_b64 s[20:21], s[26:27], s[28:29]
	s_and_b64 s[40:41], s[12:13], s[40:41]
	v_cndmask_b32_e64 v9, 0, 1, s[20:21]
	s_or_b64 s[20:21], s[30:31], s[34:35]
	v_readlane_b32 s55, v6, 40
	v_cndmask_b32_e64 v10, 0, 1, s[20:21]
	s_or_b64 s[20:21], s[36:37], s[40:41]
	v_cndmask_b32_e64 v11, 0, 1, s[20:21]
	v_cmp_eq_f32_e64 s[20:21], s55, v6
	v_cmp_gt_f32_e32 vcc, s55, v6
	s_and_b64 s[20:21], s[14:15], s[20:21]
	s_or_b64 s[20:21], vcc, s[20:21]
	v_readlane_b32 s5, v6, 48
	v_cndmask_b32_e64 v12, 0, 1, s[20:21]
	s_nop 0
	v_cmp_eq_f32_e64 s[20:21], s5, v6
	v_cmp_gt_f32_e32 vcc, s5, v6
	s_and_b64 s[20:21], s[16:17], s[20:21]
	v_readlane_b32 s5, v6, 56
	s_or_b64 s[20:21], vcc, s[20:21]
	v_cndmask_b32_e64 v13, 0, 1, s[20:21]
	v_cmp_gt_f32_e32 vcc, s5, v6
	s_nop 1
	v_cndmask_b32_e64 v6, 0, 1, vcc
	v_add_u32_e32 v6, v8, v6
	v_add3_u32 v6, v6, v7, v9
	v_add3_u32 v6, v6, v10, v11
	v_add3_u32 v6, v6, v12, v13
	v_cmp_gt_u32_e32 vcc, 4, v6
	s_nop 1
	v_cndmask_b32_e32 v6, v245, v2, vcc
	v_mov_b32_e32 v2, 0
	v_ashrrev_i32_e32 v9, 31, v6
	v_sub_u32_e32 v8, 63, v230
	v_and_b32_e32 v9, 0x7fffffff, v9
	v_xor_b32_e32 v9, v6, v9
	s_nop 0
	v_readlane_b32 s23, v9, 0
	s_movk_i32 s22, 63
	v_readlane_b32 s21, v9, 1
	s_movk_i32 s20, 62
	v_cmp_gt_i64_e32 vcc, s[22:23], v[8:9]
	v_readlane_b32 s23, v9, 2
	s_movk_i32 s22, 61
	v_addc_co_u32_e32 v2, vcc, 0, v2, vcc
	v_cmp_gt_i64_e32 vcc, s[20:21], v[8:9]
	v_readlane_b32 s21, v9, 3
	s_movk_i32 s20, 60
	v_addc_co_u32_e32 v2, vcc, 0, v2, vcc
	v_cmp_gt_i64_e32 vcc, s[22:23], v[8:9]
	v_readlane_b32 s23, v9, 4
	s_movk_i32 s22, 59
	v_addc_co_u32_e32 v2, vcc, 0, v2, vcc
	v_cmp_gt_i64_e32 vcc, s[20:21], v[8:9]
	v_readlane_b32 s21, v9, 5
	s_movk_i32 s20, 58
	v_addc_co_u32_e32 v2, vcc, 0, v2, vcc
	v_cmp_gt_i64_e32 vcc, s[22:23], v[8:9]
	v_readlane_b32 s23, v9, 6
	s_movk_i32 s22, 57
	v_addc_co_u32_e32 v2, vcc, 0, v2, vcc
	v_cmp_gt_i64_e32 vcc, s[20:21], v[8:9]
	v_readlane_b32 s21, v9, 7
	s_movk_i32 s20, 56
	v_addc_co_u32_e32 v2, vcc, 0, v2, vcc
	v_cmp_gt_i64_e32 vcc, s[22:23], v[8:9]
	v_readlane_b32 s23, v9, 8
	s_movk_i32 s22, 55
	v_addc_co_u32_e32 v2, vcc, 0, v2, vcc
	v_cmp_gt_i64_e32 vcc, s[20:21], v[8:9]
	v_readlane_b32 s21, v9, 9
	s_movk_i32 s20, 54
	v_addc_co_u32_e32 v2, vcc, 0, v2, vcc
	v_cmp_gt_i64_e32 vcc, s[22:23], v[8:9]
	v_readlane_b32 s23, v9, 10
	s_movk_i32 s22, 53
	v_addc_co_u32_e32 v2, vcc, 0, v2, vcc
	v_cmp_gt_i64_e32 vcc, s[20:21], v[8:9]
	v_readlane_b32 s21, v9, 11
	s_movk_i32 s20, 52
	v_addc_co_u32_e32 v2, vcc, 0, v2, vcc
; __device__ __forceinline__ void phase_nrr(const Frame& F, const Args& a, int l, const bf16_t* XA, const float* g, const float* modl, unsigned char* XN8) {
;     ...
;             int rank = 0;
; #pragma unroll 8
;             for (int e2 = 0; e2 < 64; ++e2) { const float v = __int_as_float(__builtin_amdgcn_readlane(__float_as_int(val), e2)); rank += (v > val || (v == val && e2 < lane)) ? 1 : 0; }
;             const bool sel = rank < TOPK;
;             const float ssum = wave_sum(sel ? sc : 0.f);
	v_cmp_gt_i64_e32 vcc, s[22:23], v[8:9]
	v_readlane_b32 s23, v9, 12
	s_movk_i32 s22, 51
	v_addc_co_u32_e32 v2, vcc, 0, v2, vcc
	v_cmp_gt_i64_e32 vcc, s[20:21], v[8:9]
	v_readlane_b32 s21, v9, 13
	s_movk_i32 s20, 50
	v_addc_co_u32_e32 v2, vcc, 0, v2, vcc
	v_cmp_gt_i64_e32 vcc, s[22:23], v[8:9]
	v_readlane_b32 s23, v9, 14
	s_movk_i32 s22, 49
	v_addc_co_u32_e32 v2, vcc, 0, v2, vcc
	v_cmp_gt_i64_e32 vcc, s[20:21], v[8:9]
	v_readlane_b32 s21, v9, 15
	s_movk_i32 s20, 48
	v_addc_co_u32_e32 v2, vcc, 0, v2, vcc
	v_cmp_gt_i64_e32 vcc, s[22:23], v[8:9]
	v_readlane_b32 s23, v9, 16
	s_movk_i32 s22, 47
	v_addc_co_u32_e32 v2, vcc, 0, v2, vcc
	v_cmp_gt_i64_e32 vcc, s[20:21], v[8:9]
	v_readlane_b32 s21, v9, 17
	s_movk_i32 s20, 46
	v_addc_co_u32_e32 v2, vcc, 0, v2, vcc
	v_cmp_gt_i64_e32 vcc, s[22:23], v[8:9]
	v_readlane_b32 s23, v9, 18
	s_movk_i32 s22, 45
	v_addc_co_u32_e32 v2, vcc, 0, v2, vcc
	v_cmp_gt_i64_e32 vcc, s[20:21], v[8:9]
	v_readlane_b32 s21, v9, 19
	s_movk_i32 s20, 44
	v_addc_co_u32_e32 v2, vcc, 0, v2, vcc
	v_cmp_gt_i64_e32 vcc, s[22:23], v[8:9]
	v_readlane_b32 s23, v9, 20
	s_movk_i32 s22, 43
	v_addc_co_u32_e32 v2, vcc, 0, v2, vcc
	v_cmp_gt_i64_e32 vcc, s[20:21], v[8:9]
	v_readlane_b32 s21, v9, 21
	s_movk_i32 s20, 42
	v_addc_co_u32_e32 v2, vcc, 0, v2, vcc
	v_cmp_gt_i64_e32 vcc, s[22:23], v[8:9]
	v_readlane_b32 s23, v9, 22
	s_movk_i32 s22, 41
	v_addc_co_u32_e32 v2, vcc, 0, v2, vcc
	v_cmp_gt_i64_e32 vcc, s[20:21], v[8:9]
	v_readlane_b32 s21, v9, 23
	s_movk_i32 s20, 40
	v_addc_co_u32_e32 v2, vcc, 0, v2, vcc
	v_cmp_gt_i64_e32 vcc, s[22:23], v[8:9]
	v_readlane_b32 s23, v9, 24
	s_movk_i32 s22, 39
	v_addc_co_u32_e32 v2, vcc, 0, v2, vcc
	v_cmp_gt_i64_e32 vcc, s[20:21], v[8:9]
	v_readlane_b32 s21, v9, 25
	s_movk_i32 s20, 38
	v_addc_co_u32_e32 v2, vcc, 0, v2, vcc
	v_cmp_gt_i64_e32 vcc, s[22:23], v[8:9]
	v_readlane_b32 s23, v9, 26
	s_movk_i32 s22, 37
	v_addc_co_u32_e32 v2, vcc, 0, v2, vcc
	v_cmp_gt_i64_e32 vcc, s[20:21], v[8:9]
	v_readlane_b32 s21, v9, 27
	s_movk_i32 s20, 36
	v_addc_co_u32_e32 v2, vcc, 0, v2, vcc
	v_cmp_gt_i64_e32 vcc, s[22:23], v[8:9]
	v_readlane_b32 s23, v9, 28
	s_movk_i32 s22, 35
	v_addc_co_u32_e32 v2, vcc, 0, v2, vcc
	v_cmp_gt_i64_e32 vcc, s[20:21], v[8:9]
	v_readlane_b32 s21, v9, 29
	s_movk_i32 s20, 34
	v_addc_co_u32_e32 v2, vcc, 0, v2, vcc
	v_cmp_gt_i64_e32 vcc, s[22:23], v[8:9]
	v_readlane_b32 s23, v9, 30
	s_movk_i32 s22, 33
	v_addc_co_u32_e32 v2, vcc, 0, v2, vcc
	v_cmp_gt_i64_e32 vcc, s[20:21], v[8:9]
	v_readlane_b32 s21, v9, 31
	s_movk_i32 s20, 32
	v_addc_co_u32_e32 v2, vcc, 0, v2, vcc
	v_cmp_gt_i64_e32 vcc, s[22:23], v[8:9]
	v_readlane_b32 s23, v9, 32
	s_movk_i32 s22, 31
	v_addc_co_u32_e32 v2, vcc, 0, v2, vcc
	v_cmp_gt_i64_e32 vcc, s[20:21], v[8:9]
	v_readlane_b32 s21, v9, 33
	s_movk_i32 s20, 30
	v_addc_co_u32_e32 v2, vcc, 0, v2, vcc
	v_cmp_gt_i64_e32 vcc, s[22:23], v[8:9]
	v_readlane_b32 s23, v9, 34
	s_movk_i32 s22, 29
	v_addc_co_u32_e32 v2, vcc, 0, v2, vcc
	v_cmp_gt_i64_e32 vcc, s[20:21], v[8:9]
	v_readlane_b32 s21, v9, 35
	s_movk_i32 s20, 28
	v_addc_co_u32_e32 v2, vcc, 0, v2, vcc
	v_cmp_gt_i64_e32 vcc, s[22:23], v[8:9]
	v_readlane_b32 s23, v9, 36
	s_movk_i32 s22, 27
	v_addc_co_u32_e32 v2, vcc, 0, v2, vcc
	v_cmp_gt_i64_e32 vcc, s[20:21], v[8:9]
	v_readlane_b32 s21, v9, 37
	s_movk_i32 s20, 26
	v_addc_co_u32_e32 v2, vcc, 0, v2, vcc
	v_cmp_gt_i64_e32 vcc, s[22:23], v[8:9]
	v_readlane_b32 s23, v9, 38
	s_movk_i32 s22, 25
	v_addc_co_u32_e32 v2, vcc, 0, v2, vcc
	v_cmp_gt_i64_e32 vcc, s[20:21], v[8:9]
	v_readlane_b32 s21, v9, 39
	s_movk_i32 s20, 24
	v_addc_co_u32_e32 v2, vcc, 0, v2, vcc
	v_cmp_gt_i64_e32 vcc, s[22:23], v[8:9]
	v_readlane_b32 s23, v9, 40
	s_movk_i32 s22, 23
	v_addc_co_u32_e32 v2, vcc, 0, v2, vcc
	v_cmp_gt_i64_e32 vcc, s[20:21], v[8:9]
	v_readlane_b32 s21, v9, 41
	s_movk_i32 s20, 22
	v_addc_co_u32_e32 v2, vcc, 0, v2, vcc
	v_cmp_gt_i64_e32 vcc, s[22:23], v[8:9]
	v_readlane_b32 s23, v9, 42
	s_movk_i32 s22, 21
	v_addc_co_u32_e32 v2, vcc, 0, v2, vcc
	v_cmp_gt_i64_e32 vcc, s[20:21], v[8:9]
	v_readlane_b32 s21, v9, 43
	s_movk_i32 s20, 20
	v_addc_co_u32_e32 v2, vcc, 0, v2, vcc
	v_cmp_gt_i64_e32 vcc, s[22:23], v[8:9]
	v_readlane_b32 s23, v9, 44
	s_movk_i32 s22, 19
	v_addc_co_u32_e32 v2, vcc, 0, v2, vcc
	v_cmp_gt_i64_e32 vcc, s[20:21], v[8:9]
	v_readlane_b32 s21, v9, 45
	s_movk_i32 s20, 18
	v_addc_co_u32_e32 v2, vcc, 0, v2, vcc
	v_cmp_gt_i64_e32 vcc, s[22:23], v[8:9]
	v_readlane_b32 s23, v9, 46
	s_movk_i32 s22, 17
	v_addc_co_u32_e32 v2, vcc, 0, v2, vcc
	v_cmp_gt_i64_e32 vcc, s[20:21], v[8:9]
	v_readlane_b32 s21, v9, 47
	s_movk_i32 s20, 16
	v_addc_co_u32_e32 v2, vcc, 0, v2, vcc
	v_cmp_gt_i64_e32 vcc, s[22:23], v[8:9]
	v_readlane_b32 s23, v9, 48
	s_movk_i32 s22, 15
	v_addc_co_u32_e32 v2, vcc, 0, v2, vcc
	v_cmp_gt_i64_e32 vcc, s[20:21], v[8:9]
	v_readlane_b32 s21, v9, 49
	s_movk_i32 s20, 14
	v_addc_co_u32_e32 v2, vcc, 0, v2, vcc
	v_cmp_gt_i64_e32 vcc, s[22:23], v[8:9]
	v_readlane_b32 s23, v9, 50
	s_movk_i32 s22, 13
	v_addc_co_u32_e32 v2, vcc, 0, v2, vcc
	v_cmp_gt_i64_e32 vcc, s[20:21], v[8:9]
	v_readlane_b32 s21, v9, 51
	s_movk_i32 s20, 12
	v_addc_co_u32_e32 v2, vcc, 0, v2, vcc
	v_cmp_gt_i64_e32 vcc, s[22:23], v[8:9]
	v_readlane_b32 s23, v9, 52
	s_movk_i32 s22, 11
	v_addc_co_u32_e32 v2, vcc, 0, v2, vcc
	v_cmp_gt_i64_e32 vcc, s[20:21], v[8:9]
	v_readlane_b32 s21, v9, 53
	s_movk_i32 s20, 10
	v_addc_co_u32_e32 v2, vcc, 0, v2, vcc
	v_cmp_gt_i64_e32 vcc, s[22:23], v[8:9]
	v_readlane_b32 s23, v9, 54
	s_movk_i32 s22, 9
	v_addc_co_u32_e32 v2, vcc, 0, v2, vcc
	v_cmp_gt_i64_e32 vcc, s[20:21], v[8:9]
	v_readlane_b32 s21, v9, 55
	s_movk_i32 s20, 8
	v_addc_co_u32_e32 v2, vcc, 0, v2, vcc
	v_cmp_gt_i64_e32 vcc, s[22:23], v[8:9]
	v_readlane_b32 s23, v9, 56
	s_movk_i32 s22, 7
	v_addc_co_u32_e32 v2, vcc, 0, v2, vcc
	v_cmp_gt_i64_e32 vcc, s[20:21], v[8:9]
	v_readlane_b32 s21, v9, 57
	s_movk_i32 s20, 6
	v_addc_co_u32_e32 v2, vcc, 0, v2, vcc
	v_cmp_gt_i64_e32 vcc, s[22:23], v[8:9]
	v_readlane_b32 s23, v9, 58
	s_movk_i32 s22, 5
	v_addc_co_u32_e32 v2, vcc, 0, v2, vcc
	v_cmp_gt_i64_e32 vcc, s[20:21], v[8:9]
	v_readlane_b32 s21, v9, 59
	s_movk_i32 s20, 4
	v_addc_co_u32_e32 v2, vcc, 0, v2, vcc
	v_cmp_gt_i64_e32 vcc, s[22:23], v[8:9]
	v_readlane_b32 s23, v9, 60
	s_movk_i32 s22, 3
	v_addc_co_u32_e32 v2, vcc, 0, v2, vcc
	v_cmp_gt_i64_e32 vcc, s[20:21], v[8:9]
	v_readlane_b32 s21, v9, 61
	s_movk_i32 s20, 2
	v_addc_co_u32_e32 v2, vcc, 0, v2, vcc
	v_cmp_gt_i64_e32 vcc, s[22:23], v[8:9]
	v_readlane_b32 s23, v9, 62
	s_movk_i32 s22, 1
	v_addc_co_u32_e32 v2, vcc, 0, v2, vcc
	v_cmp_gt_i64_e32 vcc, s[20:21], v[8:9]
	v_readlane_b32 s21, v9, 63
	s_movk_i32 s20, 0
	v_addc_co_u32_e32 v2, vcc, 0, v2, vcc
	v_cmp_gt_i64_e32 vcc, s[22:23], v[8:9]
	s_nop 1
	v_addc_co_u32_e32 v2, vcc, 0, v2, vcc
	v_cmp_gt_i64_e32 vcc, s[20:21], v[8:9]
	s_nop 1
	v_addc_co_u32_e32 v2, vcc, 0, v2, vcc
	v_cmp_gt_u32_e32 vcc, 6, v2
	s_nop 1
	v_cndmask_b32_e32 v6, 0, v5, vcc
	ds_bpermute_b32 v7, v1, v6
	s_waitcnt lgkmcnt(0)
; __device__ __forceinline__ void phase_nrr(const Frame& F, const Args& a, int l, const bf16_t* XA, const float* g, const float* modl, unsigned char* XN8) {
;     ...
;         for (int i = 0; i < 8; ++i) { const int t = tb + i;
;             const float lg = Pl[(w * 8 + i) * NE + lane] + Pl[(64 + w * 8 + i) * NE + lane]; const float sc = 1.f / (1.f + __expf(-lg)); const float bb = sc + bias;
;             float m1 = bb; m1 = fmaxf(m1, __shfl_xor(m1, 1)); m1 = fmaxf(m1, __shfl_xor(m1, 2)); m1 = fmaxf(m1, __shfl_xor(m1, 4));
;             const unsigned long long eq = __ballot(bb == m1); const int gbase = lane & ~7; const unsigned grpmask = (unsigned)((eq >> gbase) & 0xffull);
;             const int first = gbase + __builtin_ctz(grpmask);
;             float m2 = (lane == first) ? -INFINITY : bb; m2 = fmaxf(m2, __shfl_xor(m2, 1)); m2 = fmaxf(m2, __shfl_xor(m2, 2)); m2 = fmaxf(m2, __shfl_xor(m2, 4));
;             const float gsum = m1 + m2; const int gq = lane >> 3;
;             int grank = 0;
; #pragma unroll
;             for (int g2 = 0; g2 < 8; ++g2) { const float v = __int_as_float(__builtin_amdgcn_readlane(__float_as_int(gsum), g2 * 8)); grank += (v > gsum || (v == gsum && g2 < gq)) ? 1 : 0; }
;             const bool keep = grank < 4; const float val = keep ? bb : -INFINITY;
;             int rank = 0;
; #pragma unroll 8
;             for (int e2 = 0; e2 < 64; ++e2) { const float v = __int_as_float(__builtin_amdgcn_readlane(__float_as_int(val), e2)); rank += (v > val || (v == val && e2 < lane)) ? 1 : 0; }
;     ...
;             const float ssum = wave_sum(sel ? sc : 0.f);
;             if (sel) { const int p = atomicAdd((int*)(hist + lane), 1); top_e[t * TOPK + rank] = lane; gate[t * TOPK + rank] = sc / ssum * 2.5f; lpos[t * TOPK + rank] = p; }
	v_add_f32_e32 v6, v6, v7
	ds_bpermute_b32 v7, v201, v6
	s_waitcnt lgkmcnt(0)
	v_add_f32_e32 v6, v6, v7
	ds_bpermute_b32 v7, v220, v6
	s_waitcnt lgkmcnt(0)
	v_add_f32_e32 v6, v6, v7
	ds_bpermute_b32 v7, v221, v6
	s_waitcnt lgkmcnt(0)
	v_add_f32_e32 v6, v6, v7
	ds_bpermute_b32 v7, v222, v6
	s_waitcnt lgkmcnt(0)
	v_add_f32_e32 v6, v6, v7
	ds_bpermute_b32 v7, v223, v6
	s_and_saveexec_b64 s[20:21], vcc
	s_cbranch_execz .LBB0_1316
	s_waitcnt lgkmcnt(0)
	v_add_f32_e32 v10, v6, v7
	v_mad_u64_u32 v[6:7], s[22:23], s56, 6, v[2:3]
	v_div_scale_f32 v2, s[22:23], v10, v10, v5
	v_rcp_f32_e32 v12, v2
	v_ashrrev_i32_e32 v7, 31, v6
	v_lshlrev_b64 v[6:7], 2, v[6:7]
	v_lshl_add_u64 v[8:9], s[42:43], 0, v[6:7]
	ds_add_rtn_u32 v11, v227, v243
	global_store_dword v[8:9], v230, off
	v_fma_f32 v8, -v2, v12, 1.0
	v_fmac_f32_e32 v12, v8, v12
	v_div_scale_f32 v8, vcc, v5, v10, v5
	v_mul_f32_e32 v9, v8, v12
	v_fma_f32 v13, -v2, v9, v8
	v_fmac_f32_e32 v9, v13, v12
	v_fma_f32 v2, -v2, v9, v8
	v_div_fmas_f32 v2, v2, v12, v9
	v_div_fixup_f32 v2, v2, v10, v5
	v_mul_f32_e32 v2, 0x40200000, v2
	v_lshl_add_u64 v[8:9], s[44:45], 0, v[6:7]
	v_lshl_add_u64 v[6:7], s[46:47], 0, v[6:7]
	global_store_dword v[8:9], v2, off
	s_waitcnt lgkmcnt(0)
	global_store_dword v[6:7], v11, off
.LBB0_1316:
	s_or_b64 exec, exec, s[20:21]
	v_add_u32_e32 v2, s77, v226
	ds_read_b32 v2, v2
	ds_read_b32 v5, v4 offset:16896
	s_mov_b32 s3, 0
	s_waitcnt lgkmcnt(0)
	v_add_f32_e32 v2, v2, v5
	v_mul_f32_e32 v2, 0xbfb8aa3b, v2
	v_exp_f32_e32 v2, v2
	s_nop 0
	v_add_f32_e32 v2, 1.0, v2
	v_div_scale_f32 v5, s[20:21], v2, v2, 1.0
	v_rcp_f32_e32 v6, v5
	v_div_scale_f32 v7, vcc, 1.0, v2, 1.0
	v_fma_f32 v8, -v5, v6, 1.0
	v_fmac_f32_e32 v6, v8, v6
	v_mul_f32_e32 v8, v7, v6
	v_fma_f32 v9, -v5, v8, v7
	v_fmac_f32_e32 v8, v9, v6
	v_fma_f32 v5, -v5, v8, v7
	v_div_fmas_f32 v5, v5, v6, v8
	v_div_fixup_f32 v5, v5, v2, 1.0
	v_add_f32_e32 v2, v3, v5
	ds_bpermute_b32 v6, v1, v2
	s_waitcnt lgkmcnt(0)
	v_max_f32_e32 v6, v6, v6
	v_max_f32_e32 v6, v2, v6
	ds_bpermute_b32 v7, v201, v6
	s_waitcnt lgkmcnt(0)
	v_max_f32_e32 v7, v7, v7
	v_max_f32_e32 v6, v6, v7
	ds_bpermute_b32 v7, v220, v6
	s_waitcnt lgkmcnt(0)
	v_max_f32_e32 v7, v7, v7
	v_max_f32_e32 v8, v6, v7
	v_cmp_eq_f32_e32 vcc, v2, v8
	s_nop 1
	v_lshrrev_b64 v[6:7], v200, vcc
	v_ffbl_b32_sdwa v6, v6 dst_sel:DWORD dst_unused:UNUSED_PAD src0_sel:BYTE_0
	v_add_u32_e32 v6, v6, v200
	v_cmp_ne_u32_e32 vcc, v230, v6
	s_nop 1
	v_cndmask_b32_e32 v6, v245, v2, vcc
	ds_bpermute_b32 v7, v1, v6
	s_waitcnt lgkmcnt(0)
	v_max_f32_e32 v7, v7, v7
	v_max_f32_e32 v6, v6, v7
	ds_bpermute_b32 v7, v201, v6
	s_waitcnt lgkmcnt(0)
	v_max_f32_e32 v7, v7, v7
	v_max_f32_e32 v6, v6, v7
	ds_bpermute_b32 v7, v220, v6
	s_waitcnt lgkmcnt(0)
	v_max_f32_e32 v7, v7, v7
	v_max_f32_e32 v6, v6, v7
	v_add_f32_e32 v6, v8, v6
	s_nop 0
	v_readlane_b32 s5, v6, 0
	v_readlane_b32 s24, v6, 8
	v_readlane_b32 s28, v6, 16
	v_cmp_eq_f32_e64 s[20:21], s5, v6
	v_cmp_gt_f32_e32 vcc, s5, v6
	v_cmp_gt_f32_e64 s[22:23], s24, v6
	v_cmp_eq_f32_e64 s[24:25], s24, v6
	s_and_b64 s[20:21], s[0:1], s[20:21]
	v_readlane_b32 s34, v6, 24
	v_cmp_gt_f32_e64 s[26:27], s28, v6
	v_cmp_eq_f32_e64 s[28:29], s28, v6
	s_and_b64 s[24:25], s[6:7], s[24:25]
	s_or_b64 s[20:21], vcc, s[20:21]
	v_readlane_b32 s40, v6, 32
	v_cmp_gt_f32_e64 s[30:31], s34, v6
	v_cmp_eq_f32_e64 s[34:35], s34, v6
	s_and_b64 s[28:29], s[8:9], s[28:29]
	v_cndmask_b32_e64 v7, 0, 1, s[20:21]
	s_or_b64 s[20:21], s[22:23], s[24:25]
	v_cmp_gt_f32_e64 s[36:37], s40, v6
	v_cmp_eq_f32_e64 s[40:41], s40, v6
	s_and_b64 s[34:35], s[10:11], s[34:35]
	v_cndmask_b32_e64 v8, 0, 1, s[20:21]
	s_or_b64 s[20:21], s[26:27], s[28:29]
	s_and_b64 s[40:41], s[12:13], s[40:41]
	v_cndmask_b32_e64 v9, 0, 1, s[20:21]
	s_or_b64 s[20:21], s[30:31], s[34:35]
	v_readlane_b32 s55, v6, 40
	v_cndmask_b32_e64 v10, 0, 1, s[20:21]
	s_or_b64 s[20:21], s[36:37], s[40:41]
	v_cndmask_b32_e64 v11, 0, 1, s[20:21]
	v_cmp_eq_f32_e64 s[20:21], s55, v6
	v_cmp_gt_f32_e32 vcc, s55, v6
	s_and_b64 s[20:21], s[14:15], s[20:21]
	s_or_b64 s[20:21], vcc, s[20:21]
	v_readlane_b32 s5, v6, 48
	v_cndmask_b32_e64 v12, 0, 1, s[20:21]
	s_nop 0
	v_cmp_eq_f32_e64 s[20:21], s5, v6
	v_cmp_gt_f32_e32 vcc, s5, v6
	s_and_b64 s[20:21], s[16:17], s[20:21]
	v_readlane_b32 s5, v6, 56
	s_or_b64 s[20:21], vcc, s[20:21]
	v_cndmask_b32_e64 v13, 0, 1, s[20:21]
	v_cmp_gt_f32_e32 vcc, s5, v6
	s_nop 1
	v_cndmask_b32_e64 v6, 0, 1, vcc
	v_add_u32_e32 v6, v8, v6
	v_add3_u32 v6, v6, v7, v9
	v_add3_u32 v6, v6, v10, v11
	v_add3_u32 v6, v6, v12, v13
	v_cmp_gt_u32_e32 vcc, 4, v6
	s_nop 1
	v_cndmask_b32_e32 v6, v245, v2, vcc
	v_mov_b32_e32 v2, 0
	v_ashrrev_i32_e32 v9, 31, v6
	v_sub_u32_e32 v8, 63, v230
	v_and_b32_e32 v9, 0x7fffffff, v9
	v_xor_b32_e32 v9, v6, v9
	s_nop 0
	v_readlane_b32 s23, v9, 0
	s_movk_i32 s22, 63
	v_readlane_b32 s21, v9, 1
	s_movk_i32 s20, 62
	v_cmp_gt_i64_e32 vcc, s[22:23], v[8:9]
	v_readlane_b32 s23, v9, 2
	s_movk_i32 s22, 61
	v_addc_co_u32_e32 v2, vcc, 0, v2, vcc
	v_cmp_gt_i64_e32 vcc, s[20:21], v[8:9]
	v_readlane_b32 s21, v9, 3
	s_movk_i32 s20, 60
	v_addc_co_u32_e32 v2, vcc, 0, v2, vcc
	v_cmp_gt_i64_e32 vcc, s[22:23], v[8:9]
	v_readlane_b32 s23, v9, 4
	s_movk_i32 s22, 59
	v_addc_co_u32_e32 v2, vcc, 0, v2, vcc
	v_cmp_gt_i64_e32 vcc, s[20:21], v[8:9]
	v_readlane_b32 s21, v9, 5
	s_movk_i32 s20, 58
	v_addc_co_u32_e32 v2, vcc, 0, v2, vcc
	v_cmp_gt_i64_e32 vcc, s[22:23], v[8:9]
	v_readlane_b32 s23, v9, 6
	s_movk_i32 s22, 57
	v_addc_co_u32_e32 v2, vcc, 0, v2, vcc
	v_cmp_gt_i64_e32 vcc, s[20:21], v[8:9]
	v_readlane_b32 s21, v9, 7
	s_movk_i32 s20, 56
	v_addc_co_u32_e32 v2, vcc, 0, v2, vcc
	v_cmp_gt_i64_e32 vcc, s[22:23], v[8:9]
	v_readlane_b32 s23, v9, 8
; __device__ __forceinline__ void phase_nrr(const Frame& F, const Args& a, int l, const bf16_t* XA, const float* g, const float* modl, unsigned char* XN8) {
;     ...
;             int rank = 0;
; #pragma unroll 8
;             for (int e2 = 0; e2 < 64; ++e2) { const float v = __int_as_float(__builtin_amdgcn_readlane(__float_as_int(val), e2)); rank += (v > val || (v == val && e2 < lane)) ? 1 : 0; }
	s_movk_i32 s22, 55
	v_addc_co_u32_e32 v2, vcc, 0, v2, vcc
	v_cmp_gt_i64_e32 vcc, s[20:21], v[8:9]
	v_readlane_b32 s21, v9, 9
	s_movk_i32 s20, 54
	v_addc_co_u32_e32 v2, vcc, 0, v2, vcc
	v_cmp_gt_i64_e32 vcc, s[22:23], v[8:9]
	v_readlane_b32 s23, v9, 10
	s_movk_i32 s22, 53
	v_addc_co_u32_e32 v2, vcc, 0, v2, vcc
	v_cmp_gt_i64_e32 vcc, s[20:21], v[8:9]
	v_readlane_b32 s21, v9, 11
	s_movk_i32 s20, 52
	v_addc_co_u32_e32 v2, vcc, 0, v2, vcc
	v_cmp_gt_i64_e32 vcc, s[22:23], v[8:9]
	v_readlane_b32 s23, v9, 12
	s_movk_i32 s22, 51
	v_addc_co_u32_e32 v2, vcc, 0, v2, vcc
	v_cmp_gt_i64_e32 vcc, s[20:21], v[8:9]
	v_readlane_b32 s21, v9, 13
	s_movk_i32 s20, 50
	v_addc_co_u32_e32 v2, vcc, 0, v2, vcc
	v_cmp_gt_i64_e32 vcc, s[22:23], v[8:9]
	v_readlane_b32 s23, v9, 14
	s_movk_i32 s22, 49
	v_addc_co_u32_e32 v2, vcc, 0, v2, vcc
	v_cmp_gt_i64_e32 vcc, s[20:21], v[8:9]
	v_readlane_b32 s21, v9, 15
	s_movk_i32 s20, 48
	v_addc_co_u32_e32 v2, vcc, 0, v2, vcc
	v_cmp_gt_i64_e32 vcc, s[22:23], v[8:9]
	v_readlane_b32 s23, v9, 16
	s_movk_i32 s22, 47
	v_addc_co_u32_e32 v2, vcc, 0, v2, vcc
	v_cmp_gt_i64_e32 vcc, s[20:21], v[8:9]
	v_readlane_b32 s21, v9, 17
	s_movk_i32 s20, 46
	v_addc_co_u32_e32 v2, vcc, 0, v2, vcc
	v_cmp_gt_i64_e32 vcc, s[22:23], v[8:9]
	v_readlane_b32 s23, v9, 18
	s_movk_i32 s22, 45
	v_addc_co_u32_e32 v2, vcc, 0, v2, vcc
	v_cmp_gt_i64_e32 vcc, s[20:21], v[8:9]
	v_readlane_b32 s21, v9, 19
	s_movk_i32 s20, 44
	v_addc_co_u32_e32 v2, vcc, 0, v2, vcc
	v_cmp_gt_i64_e32 vcc, s[22:23], v[8:9]
	v_readlane_b32 s23, v9, 20
	s_movk_i32 s22, 43
	v_addc_co_u32_e32 v2, vcc, 0, v2, vcc
	v_cmp_gt_i64_e32 vcc, s[20:21], v[8:9]
	v_readlane_b32 s21, v9, 21
	s_movk_i32 s20, 42
	v_addc_co_u32_e32 v2, vcc, 0, v2, vcc
	v_cmp_gt_i64_e32 vcc, s[22:23], v[8:9]
	v_readlane_b32 s23, v9, 22
	s_movk_i32 s22, 41
	v_addc_co_u32_e32 v2, vcc, 0, v2, vcc
	v_cmp_gt_i64_e32 vcc, s[20:21], v[8:9]
	v_readlane_b32 s21, v9, 23
	s_movk_i32 s20, 40
	v_addc_co_u32_e32 v2, vcc, 0, v2, vcc
	v_cmp_gt_i64_e32 vcc, s[22:23], v[8:9]
	v_readlane_b32 s23, v9, 24
	s_movk_i32 s22, 39
	v_addc_co_u32_e32 v2, vcc, 0, v2, vcc
	v_cmp_gt_i64_e32 vcc, s[20:21], v[8:9]
	v_readlane_b32 s21, v9, 25
	s_movk_i32 s20, 38
	v_addc_co_u32_e32 v2, vcc, 0, v2, vcc
	v_cmp_gt_i64_e32 vcc, s[22:23], v[8:9]
	v_readlane_b32 s23, v9, 26
	s_movk_i32 s22, 37
	v_addc_co_u32_e32 v2, vcc, 0, v2, vcc
	v_cmp_gt_i64_e32 vcc, s[20:21], v[8:9]
	v_readlane_b32 s21, v9, 27
	s_movk_i32 s20, 36
	v_addc_co_u32_e32 v2, vcc, 0, v2, vcc
	v_cmp_gt_i64_e32 vcc, s[22:23], v[8:9]
	v_readlane_b32 s23, v9, 28
	s_movk_i32 s22, 35
	v_addc_co_u32_e32 v2, vcc, 0, v2, vcc
	v_cmp_gt_i64_e32 vcc, s[20:21], v[8:9]
	v_readlane_b32 s21, v9, 29
	s_movk_i32 s20, 34
	v_addc_co_u32_e32 v2, vcc, 0, v2, vcc
	v_cmp_gt_i64_e32 vcc, s[22:23], v[8:9]
	v_readlane_b32 s23, v9, 30
	s_movk_i32 s22, 33
	v_addc_co_u32_e32 v2, vcc, 0, v2, vcc
	v_cmp_gt_i64_e32 vcc, s[20:21], v[8:9]
	v_readlane_b32 s21, v9, 31
	s_movk_i32 s20, 32
	v_addc_co_u32_e32 v2, vcc, 0, v2, vcc
	v_cmp_gt_i64_e32 vcc, s[22:23], v[8:9]
	v_readlane_b32 s23, v9, 32
	s_movk_i32 s22, 31
	v_addc_co_u32_e32 v2, vcc, 0, v2, vcc
	v_cmp_gt_i64_e32 vcc, s[20:21], v[8:9]
	v_readlane_b32 s21, v9, 33
	s_movk_i32 s20, 30
	v_addc_co_u32_e32 v2, vcc, 0, v2, vcc
	v_cmp_gt_i64_e32 vcc, s[22:23], v[8:9]
	v_readlane_b32 s23, v9, 34
	s_movk_i32 s22, 29
	v_addc_co_u32_e32 v2, vcc, 0, v2, vcc
	v_cmp_gt_i64_e32 vcc, s[20:21], v[8:9]
	v_readlane_b32 s21, v9, 35
	s_movk_i32 s20, 28
	v_addc_co_u32_e32 v2, vcc, 0, v2, vcc
	v_cmp_gt_i64_e32 vcc, s[22:23], v[8:9]
	v_readlane_b32 s23, v9, 36
	s_movk_i32 s22, 27
	v_addc_co_u32_e32 v2, vcc, 0, v2, vcc
	v_cmp_gt_i64_e32 vcc, s[20:21], v[8:9]
	v_readlane_b32 s21, v9, 37
	s_movk_i32 s20, 26
	v_addc_co_u32_e32 v2, vcc, 0, v2, vcc
	v_cmp_gt_i64_e32 vcc, s[22:23], v[8:9]
	v_readlane_b32 s23, v9, 38
	s_movk_i32 s22, 25
	v_addc_co_u32_e32 v2, vcc, 0, v2, vcc
	v_cmp_gt_i64_e32 vcc, s[20:21], v[8:9]
	v_readlane_b32 s21, v9, 39
	s_movk_i32 s20, 24
	v_addc_co_u32_e32 v2, vcc, 0, v2, vcc
	v_cmp_gt_i64_e32 vcc, s[22:23], v[8:9]
	v_readlane_b32 s23, v9, 40
	s_movk_i32 s22, 23
	v_addc_co_u32_e32 v2, vcc, 0, v2, vcc
	v_cmp_gt_i64_e32 vcc, s[20:21], v[8:9]
	v_readlane_b32 s21, v9, 41
	s_movk_i32 s20, 22
	v_addc_co_u32_e32 v2, vcc, 0, v2, vcc
	v_cmp_gt_i64_e32 vcc, s[22:23], v[8:9]
	v_readlane_b32 s23, v9, 42
	s_movk_i32 s22, 21
	v_addc_co_u32_e32 v2, vcc, 0, v2, vcc
	v_cmp_gt_i64_e32 vcc, s[20:21], v[8:9]
	v_readlane_b32 s21, v9, 43
	s_movk_i32 s20, 20
	v_addc_co_u32_e32 v2, vcc, 0, v2, vcc
	v_cmp_gt_i64_e32 vcc, s[22:23], v[8:9]
	v_readlane_b32 s23, v9, 44
	s_movk_i32 s22, 19
	v_addc_co_u32_e32 v2, vcc, 0, v2, vcc
	v_cmp_gt_i64_e32 vcc, s[20:21], v[8:9]
	v_readlane_b32 s21, v9, 45
	s_movk_i32 s20, 18
	v_addc_co_u32_e32 v2, vcc, 0, v2, vcc
	v_cmp_gt_i64_e32 vcc, s[22:23], v[8:9]
	v_readlane_b32 s23, v9, 46
	s_movk_i32 s22, 17
	v_addc_co_u32_e32 v2, vcc, 0, v2, vcc
	v_cmp_gt_i64_e32 vcc, s[20:21], v[8:9]
	v_readlane_b32 s21, v9, 47
	s_movk_i32 s20, 16
	v_addc_co_u32_e32 v2, vcc, 0, v2, vcc
	v_cmp_gt_i64_e32 vcc, s[22:23], v[8:9]
	v_readlane_b32 s23, v9, 48
	s_movk_i32 s22, 15
	v_addc_co_u32_e32 v2, vcc, 0, v2, vcc
	v_cmp_gt_i64_e32 vcc, s[20:21], v[8:9]
	v_readlane_b32 s21, v9, 49
	s_movk_i32 s20, 14
	v_addc_co_u32_e32 v2, vcc, 0, v2, vcc
	v_cmp_gt_i64_e32 vcc, s[22:23], v[8:9]
	v_readlane_b32 s23, v9, 50
	s_movk_i32 s22, 13
	v_addc_co_u32_e32 v2, vcc, 0, v2, vcc
	v_cmp_gt_i64_e32 vcc, s[20:21], v[8:9]
	v_readlane_b32 s21, v9, 51
	s_movk_i32 s20, 12
	v_addc_co_u32_e32 v2, vcc, 0, v2, vcc
	v_cmp_gt_i64_e32 vcc, s[22:23], v[8:9]
	v_readlane_b32 s23, v9, 52
	s_movk_i32 s22, 11
	v_addc_co_u32_e32 v2, vcc, 0, v2, vcc
; __device__ __forceinline__ void phase_nrr(const Frame& F, const Args& a, int l, const bf16_t* XA, const float* g, const float* modl, unsigned char* XN8) {
;     ...
;         for (int i = 0; i < 8; ++i) { const int t = tb + i;
;             const float lg = Pl[(w * 8 + i) * NE + lane] + Pl[(64 + w * 8 + i) * NE + lane]; const float sc = 1.f / (1.f + __expf(-lg)); const float bb = sc + bias;
;             float m1 = bb; m1 = fmaxf(m1, __shfl_xor(m1, 1)); m1 = fmaxf(m1, __shfl_xor(m1, 2)); m1 = fmaxf(m1, __shfl_xor(m1, 4));
;             const unsigned long long eq = __ballot(bb == m1); const int gbase = lane & ~7; const unsigned grpmask = (unsigned)((eq >> gbase) & 0xffull);
;             const int first = gbase + __builtin_ctz(grpmask);
;             float m2 = (lane == first) ? -INFINITY : bb; m2 = fmaxf(m2, __shfl_xor(m2, 1)); m2 = fmaxf(m2, __shfl_xor(m2, 2)); m2 = fmaxf(m2, __shfl_xor(m2, 4));
;     ...
;             int rank = 0;
; #pragma unroll 8
;             for (int e2 = 0; e2 < 64; ++e2) { const float v = __int_as_float(__builtin_amdgcn_readlane(__float_as_int(val), e2)); rank += (v > val || (v == val && e2 < lane)) ? 1 : 0; }
;             const bool sel = rank < TOPK;
;             const float ssum = wave_sum(sel ? sc : 0.f);
;             if (sel) { const int p = atomicAdd((int*)(hist + lane), 1); top_e[t * TOPK + rank] = lane; gate[t * TOPK + rank] = sc / ssum * 2.5f; lpos[t * TOPK + rank] = p; }
	v_cmp_gt_i64_e32 vcc, s[20:21], v[8:9]
	v_readlane_b32 s21, v9, 53
	s_movk_i32 s20, 10
	v_addc_co_u32_e32 v2, vcc, 0, v2, vcc
	v_cmp_gt_i64_e32 vcc, s[22:23], v[8:9]
	v_readlane_b32 s23, v9, 54
	s_movk_i32 s22, 9
	v_addc_co_u32_e32 v2, vcc, 0, v2, vcc
	v_cmp_gt_i64_e32 vcc, s[20:21], v[8:9]
	v_readlane_b32 s21, v9, 55
	s_movk_i32 s20, 8
	v_addc_co_u32_e32 v2, vcc, 0, v2, vcc
	v_cmp_gt_i64_e32 vcc, s[22:23], v[8:9]
	v_readlane_b32 s23, v9, 56
	s_movk_i32 s22, 7
	v_addc_co_u32_e32 v2, vcc, 0, v2, vcc
	v_cmp_gt_i64_e32 vcc, s[20:21], v[8:9]
	v_readlane_b32 s21, v9, 57
	s_movk_i32 s20, 6
	v_addc_co_u32_e32 v2, vcc, 0, v2, vcc
	v_cmp_gt_i64_e32 vcc, s[22:23], v[8:9]
	v_readlane_b32 s23, v9, 58
	s_movk_i32 s22, 5
	v_addc_co_u32_e32 v2, vcc, 0, v2, vcc
	v_cmp_gt_i64_e32 vcc, s[20:21], v[8:9]
	v_readlane_b32 s21, v9, 59
	s_movk_i32 s20, 4
	v_addc_co_u32_e32 v2, vcc, 0, v2, vcc
	v_cmp_gt_i64_e32 vcc, s[22:23], v[8:9]
	v_readlane_b32 s23, v9, 60
	s_movk_i32 s22, 3
	v_addc_co_u32_e32 v2, vcc, 0, v2, vcc
	v_cmp_gt_i64_e32 vcc, s[20:21], v[8:9]
	v_readlane_b32 s21, v9, 61
	s_movk_i32 s20, 2
	v_addc_co_u32_e32 v2, vcc, 0, v2, vcc
	v_cmp_gt_i64_e32 vcc, s[22:23], v[8:9]
	v_readlane_b32 s23, v9, 62
	s_movk_i32 s22, 1
	v_addc_co_u32_e32 v2, vcc, 0, v2, vcc
	v_cmp_gt_i64_e32 vcc, s[20:21], v[8:9]
	v_readlane_b32 s21, v9, 63
	s_movk_i32 s20, 0
	v_addc_co_u32_e32 v2, vcc, 0, v2, vcc
	v_cmp_gt_i64_e32 vcc, s[22:23], v[8:9]
	s_nop 1
	v_addc_co_u32_e32 v2, vcc, 0, v2, vcc
	v_cmp_gt_i64_e32 vcc, s[20:21], v[8:9]
	s_nop 1
	v_addc_co_u32_e32 v2, vcc, 0, v2, vcc
	v_cmp_gt_u32_e32 vcc, 6, v2
	s_nop 1
	v_cndmask_b32_e32 v6, 0, v5, vcc
	ds_bpermute_b32 v7, v1, v6
	s_waitcnt lgkmcnt(0)
	v_add_f32_e32 v6, v6, v7
	ds_bpermute_b32 v7, v201, v6
	s_waitcnt lgkmcnt(0)
	v_add_f32_e32 v6, v6, v7
	ds_bpermute_b32 v7, v220, v6
	s_waitcnt lgkmcnt(0)
	v_add_f32_e32 v6, v6, v7
	ds_bpermute_b32 v7, v221, v6
	s_waitcnt lgkmcnt(0)
	v_add_f32_e32 v6, v6, v7
	ds_bpermute_b32 v7, v222, v6
	s_waitcnt lgkmcnt(0)
	v_add_f32_e32 v6, v6, v7
	ds_bpermute_b32 v7, v223, v6
	s_and_saveexec_b64 s[20:21], vcc
	s_cbranch_execz .LBB0_1320
	s_waitcnt lgkmcnt(0)
	v_add_f32_e32 v10, v6, v7
	v_mad_u64_u32 v[6:7], s[22:23], s54, 6, v[2:3]
	v_div_scale_f32 v2, s[22:23], v10, v10, v5
	v_rcp_f32_e32 v12, v2
	v_ashrrev_i32_e32 v7, 31, v6
	v_lshlrev_b64 v[6:7], 2, v[6:7]
	v_lshl_add_u64 v[8:9], s[42:43], 0, v[6:7]
	ds_add_rtn_u32 v11, v227, v243
	global_store_dword v[8:9], v230, off
	v_fma_f32 v8, -v2, v12, 1.0
	v_fmac_f32_e32 v12, v8, v12
	v_div_scale_f32 v8, vcc, v5, v10, v5
	v_mul_f32_e32 v9, v8, v12
	v_fma_f32 v13, -v2, v9, v8
	v_fmac_f32_e32 v9, v13, v12
	v_fma_f32 v2, -v2, v9, v8
	v_div_fmas_f32 v2, v2, v12, v9
	v_div_fixup_f32 v2, v2, v10, v5
	v_mul_f32_e32 v2, 0x40200000, v2
	v_lshl_add_u64 v[8:9], s[44:45], 0, v[6:7]
	v_lshl_add_u64 v[6:7], s[46:47], 0, v[6:7]
	global_store_dword v[8:9], v2, off
	s_waitcnt lgkmcnt(0)
	global_store_dword v[6:7], v11, off
.LBB0_1320:
	s_or_b64 exec, exec, s[20:21]
	v_add_u32_e32 v2, s78, v226
	ds_read_b32 v2, v2
	ds_read_b32 v5, v4 offset:17152
	s_mov_b32 s3, 0
	s_waitcnt lgkmcnt(0)
	v_add_f32_e32 v2, v2, v5
	v_mul_f32_e32 v2, 0xbfb8aa3b, v2
	v_exp_f32_e32 v2, v2
	s_nop 0
	v_add_f32_e32 v2, 1.0, v2
	v_div_scale_f32 v5, s[20:21], v2, v2, 1.0
	v_rcp_f32_e32 v6, v5
	v_div_scale_f32 v7, vcc, 1.0, v2, 1.0
	v_fma_f32 v8, -v5, v6, 1.0
	v_fmac_f32_e32 v6, v8, v6
	v_mul_f32_e32 v8, v7, v6
	v_fma_f32 v9, -v5, v8, v7
	v_fmac_f32_e32 v8, v9, v6
	v_fma_f32 v5, -v5, v8, v7
	v_div_fmas_f32 v5, v5, v6, v8
	v_div_fixup_f32 v5, v5, v2, 1.0
	v_add_f32_e32 v2, v3, v5
	ds_bpermute_b32 v6, v1, v2
	s_waitcnt lgkmcnt(0)
	v_max_f32_e32 v6, v6, v6
	v_max_f32_e32 v6, v2, v6
	ds_bpermute_b32 v7, v201, v6
	s_waitcnt lgkmcnt(0)
	v_max_f32_e32 v7, v7, v7
	v_max_f32_e32 v6, v6, v7
	ds_bpermute_b32 v7, v220, v6
	s_waitcnt lgkmcnt(0)
	v_max_f32_e32 v7, v7, v7
	v_max_f32_e32 v8, v6, v7
	v_cmp_eq_f32_e32 vcc, v2, v8
	s_nop 1
	v_lshrrev_b64 v[6:7], v200, vcc
	v_ffbl_b32_sdwa v6, v6 dst_sel:DWORD dst_unused:UNUSED_PAD src0_sel:BYTE_0
	v_add_u32_e32 v6, v6, v200
	v_cmp_ne_u32_e32 vcc, v230, v6
	s_nop 1
	v_cndmask_b32_e32 v6, v245, v2, vcc
	ds_bpermute_b32 v7, v1, v6
	s_waitcnt lgkmcnt(0)
	v_max_f32_e32 v7, v7, v7
	v_max_f32_e32 v6, v6, v7
	ds_bpermute_b32 v7, v201, v6
	s_waitcnt lgkmcnt(0)
	v_max_f32_e32 v7, v7, v7
	v_max_f32_e32 v6, v6, v7
	ds_bpermute_b32 v7, v220, v6
	s_waitcnt lgkmcnt(0)
; __device__ __forceinline__ void phase_nrr(const Frame& F, const Args& a, int l, const bf16_t* XA, const float* g, const float* modl, unsigned char* XN8) {
;     ...
;             const float gsum = m1 + m2; const int gq = lane >> 3;
;             int grank = 0;
; #pragma unroll
;             for (int g2 = 0; g2 < 8; ++g2) { const float v = __int_as_float(__builtin_amdgcn_readlane(__float_as_int(gsum), g2 * 8)); grank += (v > gsum || (v == gsum && g2 < gq)) ? 1 : 0; }
;             const bool keep = grank < 4; const float val = keep ? bb : -INFINITY;
;             int rank = 0;
; #pragma unroll 8
;             for (int e2 = 0; e2 < 64; ++e2) { const float v = __int_as_float(__builtin_amdgcn_readlane(__float_as_int(val), e2)); rank += (v > val || (v == val && e2 < lane)) ? 1 : 0; }
	v_max_f32_e32 v7, v7, v7
	v_max_f32_e32 v6, v6, v7
	v_add_f32_e32 v6, v8, v6
	s_nop 0
	v_readlane_b32 s5, v6, 0
	v_readlane_b32 s24, v6, 8
	v_readlane_b32 s28, v6, 16
	v_cmp_eq_f32_e64 s[20:21], s5, v6
	v_cmp_gt_f32_e32 vcc, s5, v6
	v_cmp_gt_f32_e64 s[22:23], s24, v6
	v_cmp_eq_f32_e64 s[24:25], s24, v6
	s_and_b64 s[20:21], s[0:1], s[20:21]
	v_readlane_b32 s34, v6, 24
	v_cmp_gt_f32_e64 s[26:27], s28, v6
	v_cmp_eq_f32_e64 s[28:29], s28, v6
	s_and_b64 s[24:25], s[6:7], s[24:25]
	s_or_b64 s[20:21], vcc, s[20:21]
	v_readlane_b32 s40, v6, 32
	v_cmp_gt_f32_e64 s[30:31], s34, v6
	v_cmp_eq_f32_e64 s[34:35], s34, v6
	s_and_b64 s[28:29], s[8:9], s[28:29]
	v_cndmask_b32_e64 v7, 0, 1, s[20:21]
	s_or_b64 s[20:21], s[22:23], s[24:25]
	v_cmp_gt_f32_e64 s[36:37], s40, v6
	v_cmp_eq_f32_e64 s[40:41], s40, v6
	s_and_b64 s[34:35], s[10:11], s[34:35]
	v_cndmask_b32_e64 v8, 0, 1, s[20:21]
	s_or_b64 s[20:21], s[26:27], s[28:29]
	s_and_b64 s[40:41], s[12:13], s[40:41]
	v_cndmask_b32_e64 v9, 0, 1, s[20:21]
	s_or_b64 s[20:21], s[30:31], s[34:35]
	v_readlane_b32 s54, v6, 40
	v_cndmask_b32_e64 v10, 0, 1, s[20:21]
	s_or_b64 s[20:21], s[36:37], s[40:41]
	v_cndmask_b32_e64 v11, 0, 1, s[20:21]
	v_cmp_eq_f32_e64 s[20:21], s54, v6
	v_cmp_gt_f32_e32 vcc, s54, v6
	s_and_b64 s[20:21], s[14:15], s[20:21]
	s_or_b64 s[20:21], vcc, s[20:21]
	v_readlane_b32 s5, v6, 48
	v_cndmask_b32_e64 v12, 0, 1, s[20:21]
	s_nop 0
	v_cmp_eq_f32_e64 s[20:21], s5, v6
	v_cmp_gt_f32_e32 vcc, s5, v6
	s_and_b64 s[20:21], s[16:17], s[20:21]
	v_readlane_b32 s5, v6, 56
	s_or_b64 s[20:21], vcc, s[20:21]
	v_cndmask_b32_e64 v13, 0, 1, s[20:21]
	v_cmp_gt_f32_e32 vcc, s5, v6
	s_nop 1
	v_cndmask_b32_e64 v6, 0, 1, vcc
	v_add_u32_e32 v6, v8, v6
	v_add3_u32 v6, v6, v7, v9
	v_add3_u32 v6, v6, v10, v11
	v_add3_u32 v6, v6, v12, v13
	v_cmp_gt_u32_e32 vcc, 4, v6
	s_nop 1
	v_cndmask_b32_e32 v6, v245, v2, vcc
	v_mov_b32_e32 v2, 0
	v_ashrrev_i32_e32 v9, 31, v6
	v_sub_u32_e32 v8, 63, v230
	v_and_b32_e32 v9, 0x7fffffff, v9
	v_xor_b32_e32 v9, v6, v9
	s_nop 0
	v_readlane_b32 s23, v9, 0
	s_movk_i32 s22, 63
	v_readlane_b32 s21, v9, 1
	s_movk_i32 s20, 62
	v_cmp_gt_i64_e32 vcc, s[22:23], v[8:9]
	v_readlane_b32 s23, v9, 2
	s_movk_i32 s22, 61
	v_addc_co_u32_e32 v2, vcc, 0, v2, vcc
	v_cmp_gt_i64_e32 vcc, s[20:21], v[8:9]
	v_readlane_b32 s21, v9, 3
	s_movk_i32 s20, 60
	v_addc_co_u32_e32 v2, vcc, 0, v2, vcc
	v_cmp_gt_i64_e32 vcc, s[22:23], v[8:9]
	v_readlane_b32 s23, v9, 4
	s_movk_i32 s22, 59
	v_addc_co_u32_e32 v2, vcc, 0, v2, vcc
	v_cmp_gt_i64_e32 vcc, s[20:21], v[8:9]
	v_readlane_b32 s21, v9, 5
	s_movk_i32 s20, 58
	v_addc_co_u32_e32 v2, vcc, 0, v2, vcc
	v_cmp_gt_i64_e32 vcc, s[22:23], v[8:9]
	v_readlane_b32 s23, v9, 6
	s_movk_i32 s22, 57
	v_addc_co_u32_e32 v2, vcc, 0, v2, vcc
	v_cmp_gt_i64_e32 vcc, s[20:21], v[8:9]
	v_readlane_b32 s21, v9, 7
	s_movk_i32 s20, 56
	v_addc_co_u32_e32 v2, vcc, 0, v2, vcc
	v_cmp_gt_i64_e32 vcc, s[22:23], v[8:9]
	v_readlane_b32 s23, v9, 8
	s_movk_i32 s22, 55
	v_addc_co_u32_e32 v2, vcc, 0, v2, vcc
	v_cmp_gt_i64_e32 vcc, s[20:21], v[8:9]
	v_readlane_b32 s21, v9, 9
	s_movk_i32 s20, 54
	v_addc_co_u32_e32 v2, vcc, 0, v2, vcc
	v_cmp_gt_i64_e32 vcc, s[22:23], v[8:9]
	v_readlane_b32 s23, v9, 10
	s_movk_i32 s22, 53
	v_addc_co_u32_e32 v2, vcc, 0, v2, vcc
	v_cmp_gt_i64_e32 vcc, s[20:21], v[8:9]
	v_readlane_b32 s21, v9, 11
	s_movk_i32 s20, 52
	v_addc_co_u32_e32 v2, vcc, 0, v2, vcc
	v_cmp_gt_i64_e32 vcc, s[22:23], v[8:9]
	v_readlane_b32 s23, v9, 12
	s_movk_i32 s22, 51
	v_addc_co_u32_e32 v2, vcc, 0, v2, vcc
	v_cmp_gt_i64_e32 vcc, s[20:21], v[8:9]
	v_readlane_b32 s21, v9, 13
	s_movk_i32 s20, 50
	v_addc_co_u32_e32 v2, vcc, 0, v2, vcc
	v_cmp_gt_i64_e32 vcc, s[22:23], v[8:9]
	v_readlane_b32 s23, v9, 14
	s_movk_i32 s22, 49
	v_addc_co_u32_e32 v2, vcc, 0, v2, vcc
	v_cmp_gt_i64_e32 vcc, s[20:21], v[8:9]
	v_readlane_b32 s21, v9, 15
	s_movk_i32 s20, 48
	v_addc_co_u32_e32 v2, vcc, 0, v2, vcc
	v_cmp_gt_i64_e32 vcc, s[22:23], v[8:9]
	v_readlane_b32 s23, v9, 16
	s_movk_i32 s22, 47
	v_addc_co_u32_e32 v2, vcc, 0, v2, vcc
	v_cmp_gt_i64_e32 vcc, s[20:21], v[8:9]
	v_readlane_b32 s21, v9, 17
	s_movk_i32 s20, 46
	v_addc_co_u32_e32 v2, vcc, 0, v2, vcc
	v_cmp_gt_i64_e32 vcc, s[22:23], v[8:9]
	v_readlane_b32 s23, v9, 18
	s_movk_i32 s22, 45
	v_addc_co_u32_e32 v2, vcc, 0, v2, vcc
	v_cmp_gt_i64_e32 vcc, s[20:21], v[8:9]
	v_readlane_b32 s21, v9, 19
	s_movk_i32 s20, 44
	v_addc_co_u32_e32 v2, vcc, 0, v2, vcc
	v_cmp_gt_i64_e32 vcc, s[22:23], v[8:9]
	v_readlane_b32 s23, v9, 20
	s_movk_i32 s22, 43
	v_addc_co_u32_e32 v2, vcc, 0, v2, vcc
	v_cmp_gt_i64_e32 vcc, s[20:21], v[8:9]
	v_readlane_b32 s21, v9, 21
	s_movk_i32 s20, 42
	v_addc_co_u32_e32 v2, vcc, 0, v2, vcc
	v_cmp_gt_i64_e32 vcc, s[22:23], v[8:9]
	v_readlane_b32 s23, v9, 22
	s_movk_i32 s22, 41
	v_addc_co_u32_e32 v2, vcc, 0, v2, vcc
	v_cmp_gt_i64_e32 vcc, s[20:21], v[8:9]
	v_readlane_b32 s21, v9, 23
	s_movk_i32 s20, 40
	v_addc_co_u32_e32 v2, vcc, 0, v2, vcc
	v_cmp_gt_i64_e32 vcc, s[22:23], v[8:9]
	v_readlane_b32 s23, v9, 24
	s_movk_i32 s22, 39
	v_addc_co_u32_e32 v2, vcc, 0, v2, vcc
	v_cmp_gt_i64_e32 vcc, s[20:21], v[8:9]
	v_readlane_b32 s21, v9, 25
	s_movk_i32 s20, 38
	v_addc_co_u32_e32 v2, vcc, 0, v2, vcc
	v_cmp_gt_i64_e32 vcc, s[22:23], v[8:9]
	v_readlane_b32 s23, v9, 26
	s_movk_i32 s22, 37
	v_addc_co_u32_e32 v2, vcc, 0, v2, vcc
	v_cmp_gt_i64_e32 vcc, s[20:21], v[8:9]
	v_readlane_b32 s21, v9, 27
	s_movk_i32 s20, 36
	v_addc_co_u32_e32 v2, vcc, 0, v2, vcc
	v_cmp_gt_i64_e32 vcc, s[22:23], v[8:9]
	v_readlane_b32 s23, v9, 28
	s_movk_i32 s22, 35
	v_addc_co_u32_e32 v2, vcc, 0, v2, vcc
	v_cmp_gt_i64_e32 vcc, s[20:21], v[8:9]
	v_readlane_b32 s21, v9, 29
	s_movk_i32 s20, 34
	v_addc_co_u32_e32 v2, vcc, 0, v2, vcc
; __device__ __forceinline__ void phase_nrr(const Frame& F, const Args& a, int l, const bf16_t* XA, const float* g, const float* modl, unsigned char* XN8) {
;     ...
;             int rank = 0;
; #pragma unroll 8
;             for (int e2 = 0; e2 < 64; ++e2) { const float v = __int_as_float(__builtin_amdgcn_readlane(__float_as_int(val), e2)); rank += (v > val || (v == val && e2 < lane)) ? 1 : 0; }
;             const bool sel = rank < TOPK;
;             const float ssum = wave_sum(sel ? sc : 0.f);
;             if (sel) { const int p = atomicAdd((int*)(hist + lane), 1); top_e[t * TOPK + rank] = lane; gate[t * TOPK + rank] = sc / ssum * 2.5f; lpos[t * TOPK + rank] = p; }
	v_cmp_gt_i64_e32 vcc, s[22:23], v[8:9]
	v_readlane_b32 s23, v9, 30
	s_movk_i32 s22, 33
	v_addc_co_u32_e32 v2, vcc, 0, v2, vcc
	v_cmp_gt_i64_e32 vcc, s[20:21], v[8:9]
	v_readlane_b32 s21, v9, 31
	s_movk_i32 s20, 32
	v_addc_co_u32_e32 v2, vcc, 0, v2, vcc
	v_cmp_gt_i64_e32 vcc, s[22:23], v[8:9]
	v_readlane_b32 s23, v9, 32
	s_movk_i32 s22, 31
	v_addc_co_u32_e32 v2, vcc, 0, v2, vcc
	v_cmp_gt_i64_e32 vcc, s[20:21], v[8:9]
	v_readlane_b32 s21, v9, 33
	s_movk_i32 s20, 30
	v_addc_co_u32_e32 v2, vcc, 0, v2, vcc
	v_cmp_gt_i64_e32 vcc, s[22:23], v[8:9]
	v_readlane_b32 s23, v9, 34
	s_movk_i32 s22, 29
	v_addc_co_u32_e32 v2, vcc, 0, v2, vcc
	v_cmp_gt_i64_e32 vcc, s[20:21], v[8:9]
	v_readlane_b32 s21, v9, 35
	s_movk_i32 s20, 28
	v_addc_co_u32_e32 v2, vcc, 0, v2, vcc
	v_cmp_gt_i64_e32 vcc, s[22:23], v[8:9]
	v_readlane_b32 s23, v9, 36
	s_movk_i32 s22, 27
	v_addc_co_u32_e32 v2, vcc, 0, v2, vcc
	v_cmp_gt_i64_e32 vcc, s[20:21], v[8:9]
	v_readlane_b32 s21, v9, 37
	s_movk_i32 s20, 26
	v_addc_co_u32_e32 v2, vcc, 0, v2, vcc
	v_cmp_gt_i64_e32 vcc, s[22:23], v[8:9]
	v_readlane_b32 s23, v9, 38
	s_movk_i32 s22, 25
	v_addc_co_u32_e32 v2, vcc, 0, v2, vcc
	v_cmp_gt_i64_e32 vcc, s[20:21], v[8:9]
	v_readlane_b32 s21, v9, 39
	s_movk_i32 s20, 24
	v_addc_co_u32_e32 v2, vcc, 0, v2, vcc
	v_cmp_gt_i64_e32 vcc, s[22:23], v[8:9]
	v_readlane_b32 s23, v9, 40
	s_movk_i32 s22, 23
	v_addc_co_u32_e32 v2, vcc, 0, v2, vcc
	v_cmp_gt_i64_e32 vcc, s[20:21], v[8:9]
	v_readlane_b32 s21, v9, 41
	s_movk_i32 s20, 22
	v_addc_co_u32_e32 v2, vcc, 0, v2, vcc
	v_cmp_gt_i64_e32 vcc, s[22:23], v[8:9]
	v_readlane_b32 s23, v9, 42
	s_movk_i32 s22, 21
	v_addc_co_u32_e32 v2, vcc, 0, v2, vcc
	v_cmp_gt_i64_e32 vcc, s[20:21], v[8:9]
	v_readlane_b32 s21, v9, 43
	s_movk_i32 s20, 20
	v_addc_co_u32_e32 v2, vcc, 0, v2, vcc
	v_cmp_gt_i64_e32 vcc, s[22:23], v[8:9]
	v_readlane_b32 s23, v9, 44
	s_movk_i32 s22, 19
	v_addc_co_u32_e32 v2, vcc, 0, v2, vcc
	v_cmp_gt_i64_e32 vcc, s[20:21], v[8:9]
	v_readlane_b32 s21, v9, 45
	s_movk_i32 s20, 18
	v_addc_co_u32_e32 v2, vcc, 0, v2, vcc
	v_cmp_gt_i64_e32 vcc, s[22:23], v[8:9]
	v_readlane_b32 s23, v9, 46
	s_movk_i32 s22, 17
	v_addc_co_u32_e32 v2, vcc, 0, v2, vcc
	v_cmp_gt_i64_e32 vcc, s[20:21], v[8:9]
	v_readlane_b32 s21, v9, 47
	s_movk_i32 s20, 16
	v_addc_co_u32_e32 v2, vcc, 0, v2, vcc
	v_cmp_gt_i64_e32 vcc, s[22:23], v[8:9]
	v_readlane_b32 s23, v9, 48
	s_movk_i32 s22, 15
	v_addc_co_u32_e32 v2, vcc, 0, v2, vcc
	v_cmp_gt_i64_e32 vcc, s[20:21], v[8:9]
	v_readlane_b32 s21, v9, 49
	s_movk_i32 s20, 14
	v_addc_co_u32_e32 v2, vcc, 0, v2, vcc
	v_cmp_gt_i64_e32 vcc, s[22:23], v[8:9]
	v_readlane_b32 s23, v9, 50
	s_movk_i32 s22, 13
	v_addc_co_u32_e32 v2, vcc, 0, v2, vcc
	v_cmp_gt_i64_e32 vcc, s[20:21], v[8:9]
	v_readlane_b32 s21, v9, 51
	s_movk_i32 s20, 12
	v_addc_co_u32_e32 v2, vcc, 0, v2, vcc
	v_cmp_gt_i64_e32 vcc, s[22:23], v[8:9]
	v_readlane_b32 s23, v9, 52
	s_movk_i32 s22, 11
	v_addc_co_u32_e32 v2, vcc, 0, v2, vcc
	v_cmp_gt_i64_e32 vcc, s[20:21], v[8:9]
	v_readlane_b32 s21, v9, 53
	s_movk_i32 s20, 10
	v_addc_co_u32_e32 v2, vcc, 0, v2, vcc
	v_cmp_gt_i64_e32 vcc, s[22:23], v[8:9]
	v_readlane_b32 s23, v9, 54
	s_movk_i32 s22, 9
	v_addc_co_u32_e32 v2, vcc, 0, v2, vcc
	v_cmp_gt_i64_e32 vcc, s[20:21], v[8:9]
	v_readlane_b32 s21, v9, 55
	s_movk_i32 s20, 8
	v_addc_co_u32_e32 v2, vcc, 0, v2, vcc
	v_cmp_gt_i64_e32 vcc, s[22:23], v[8:9]
	v_readlane_b32 s23, v9, 56
	s_movk_i32 s22, 7
	v_addc_co_u32_e32 v2, vcc, 0, v2, vcc
	v_cmp_gt_i64_e32 vcc, s[20:21], v[8:9]
	v_readlane_b32 s21, v9, 57
	s_movk_i32 s20, 6
	v_addc_co_u32_e32 v2, vcc, 0, v2, vcc
	v_cmp_gt_i64_e32 vcc, s[22:23], v[8:9]
	v_readlane_b32 s23, v9, 58
	s_movk_i32 s22, 5
	v_addc_co_u32_e32 v2, vcc, 0, v2, vcc
	v_cmp_gt_i64_e32 vcc, s[20:21], v[8:9]
	v_readlane_b32 s21, v9, 59
	s_movk_i32 s20, 4
	v_addc_co_u32_e32 v2, vcc, 0, v2, vcc
	v_cmp_gt_i64_e32 vcc, s[22:23], v[8:9]
	v_readlane_b32 s23, v9, 60
	s_movk_i32 s22, 3
	v_addc_co_u32_e32 v2, vcc, 0, v2, vcc
	v_cmp_gt_i64_e32 vcc, s[20:21], v[8:9]
	v_readlane_b32 s21, v9, 61
	s_movk_i32 s20, 2
	v_addc_co_u32_e32 v2, vcc, 0, v2, vcc
	v_cmp_gt_i64_e32 vcc, s[22:23], v[8:9]
	v_readlane_b32 s23, v9, 62
	s_movk_i32 s22, 1
	v_addc_co_u32_e32 v2, vcc, 0, v2, vcc
	v_cmp_gt_i64_e32 vcc, s[20:21], v[8:9]
	v_readlane_b32 s21, v9, 63
	s_movk_i32 s20, 0
	v_addc_co_u32_e32 v2, vcc, 0, v2, vcc
	v_cmp_gt_i64_e32 vcc, s[22:23], v[8:9]
	s_nop 1
	v_addc_co_u32_e32 v2, vcc, 0, v2, vcc
	v_cmp_gt_i64_e32 vcc, s[20:21], v[8:9]
	s_nop 1
	v_addc_co_u32_e32 v2, vcc, 0, v2, vcc
	v_cmp_gt_u32_e32 vcc, 6, v2
	s_nop 1
	v_cndmask_b32_e32 v6, 0, v5, vcc
	ds_bpermute_b32 v7, v1, v6
	s_waitcnt lgkmcnt(0)
	v_add_f32_e32 v6, v6, v7
	ds_bpermute_b32 v7, v201, v6
	s_waitcnt lgkmcnt(0)
	v_add_f32_e32 v6, v6, v7
	ds_bpermute_b32 v7, v220, v6
	s_waitcnt lgkmcnt(0)
	v_add_f32_e32 v6, v6, v7
	ds_bpermute_b32 v7, v221, v6
	s_waitcnt lgkmcnt(0)
	v_add_f32_e32 v6, v6, v7
	ds_bpermute_b32 v7, v222, v6
	s_waitcnt lgkmcnt(0)
	v_add_f32_e32 v6, v6, v7
	ds_bpermute_b32 v7, v223, v6
	s_and_saveexec_b64 s[20:21], vcc
	s_cbranch_execz .LBB0_1324
	s_waitcnt lgkmcnt(0)
	v_add_f32_e32 v10, v6, v7
	v_mad_u64_u32 v[6:7], s[4:5], s4, 6, v[2:3]
	v_div_scale_f32 v2, s[4:5], v10, v10, v5
	v_rcp_f32_e32 v12, v2
	v_ashrrev_i32_e32 v7, 31, v6
	v_lshlrev_b64 v[6:7], 2, v[6:7]
	v_lshl_add_u64 v[8:9], s[42:43], 0, v[6:7]
	ds_add_rtn_u32 v11, v227, v243
	global_store_dword v[8:9], v230, off
	v_fma_f32 v8, -v2, v12, 1.0
	v_fmac_f32_e32 v12, v8, v12
	v_div_scale_f32 v8, vcc, v5, v10, v5
	v_mul_f32_e32 v9, v8, v12
	v_fma_f32 v13, -v2, v9, v8
	v_fmac_f32_e32 v9, v13, v12
	v_fma_f32 v2, -v2, v9, v8
	v_div_fmas_f32 v2, v2, v12, v9
	v_div_fixup_f32 v2, v2, v10, v5
	v_mul_f32_e32 v2, 0x40200000, v2
	v_lshl_add_u64 v[8:9], s[44:45], 0, v[6:7]
	v_lshl_add_u64 v[6:7], s[46:47], 0, v[6:7]
	global_store_dword v[8:9], v2, off
	s_waitcnt lgkmcnt(0)
	global_store_dword v[6:7], v11, off
; __device__ __forceinline__ void phase_nrr(const Frame& F, const Args& a, int l, const bf16_t* XA, const float* g, const float* modl, unsigned char* XN8) {
;     ...
;         for (int i = 0; i < 8; ++i) { const int t = tb + i;
;             const float lg = Pl[(w * 8 + i) * NE + lane] + Pl[(64 + w * 8 + i) * NE + lane]; const float sc = 1.f / (1.f + __expf(-lg)); const float bb = sc + bias;
;             float m1 = bb; m1 = fmaxf(m1, __shfl_xor(m1, 1)); m1 = fmaxf(m1, __shfl_xor(m1, 2)); m1 = fmaxf(m1, __shfl_xor(m1, 4));
;             const unsigned long long eq = __ballot(bb == m1); const int gbase = lane & ~7; const unsigned grpmask = (unsigned)((eq >> gbase) & 0xffull);
;             const int first = gbase + __builtin_ctz(grpmask);
;             float m2 = (lane == first) ? -INFINITY : bb; m2 = fmaxf(m2, __shfl_xor(m2, 1)); m2 = fmaxf(m2, __shfl_xor(m2, 2)); m2 = fmaxf(m2, __shfl_xor(m2, 4));
;             const float gsum = m1 + m2; const int gq = lane >> 3;
;             int grank = 0;
; #pragma unroll
;             for (int g2 = 0; g2 < 8; ++g2) { const float v = __int_as_float(__builtin_amdgcn_readlane(__float_as_int(gsum), g2 * 8)); grank += (v > gsum || (v == gsum && g2 < gq)) ? 1 : 0; }
;             const bool keep = grank < 4; const float val = keep ? bb : -INFINITY;
;             int rank = 0;
; #pragma unroll 8
;             for (int e2 = 0; e2 < 64; ++e2) { const float v = __int_as_float(__builtin_amdgcn_readlane(__float_as_int(val), e2)); rank += (v > val || (v == val && e2 < lane)) ? 1 : 0; }
.LBB0_1324:
	s_or_b64 exec, exec, s[20:21]
	v_add_u32_e32 v2, s79, v226
	ds_read_b32 v2, v2
	ds_read_b32 v5, v4 offset:17408
	s_mov_b32 s3, 0
	s_waitcnt lgkmcnt(0)
	v_add_f32_e32 v2, v2, v5
	v_mul_f32_e32 v2, 0xbfb8aa3b, v2
	v_exp_f32_e32 v2, v2
	s_nop 0
	v_add_f32_e32 v2, 1.0, v2
	v_div_scale_f32 v5, s[4:5], v2, v2, 1.0
	v_rcp_f32_e32 v6, v5
	v_div_scale_f32 v7, vcc, 1.0, v2, 1.0
	v_fma_f32 v8, -v5, v6, 1.0
	v_fmac_f32_e32 v6, v8, v6
	v_mul_f32_e32 v8, v7, v6
	v_fma_f32 v9, -v5, v8, v7
	v_fmac_f32_e32 v8, v9, v6
	v_fma_f32 v5, -v5, v8, v7
	v_div_fmas_f32 v5, v5, v6, v8
	v_div_fixup_f32 v2, v5, v2, 1.0
	v_add_f32_e32 v5, v3, v2
	ds_bpermute_b32 v6, v1, v5
	s_waitcnt lgkmcnt(0)
	v_max_f32_e32 v6, v6, v6
	v_max_f32_e32 v6, v5, v6
	ds_bpermute_b32 v7, v201, v6
	s_waitcnt lgkmcnt(0)
	v_max_f32_e32 v7, v7, v7
	v_max_f32_e32 v6, v6, v7
	ds_bpermute_b32 v7, v220, v6
	s_waitcnt lgkmcnt(0)
	v_max_f32_e32 v7, v7, v7
	v_max_f32_e32 v8, v6, v7
	v_cmp_eq_f32_e32 vcc, v5, v8
	s_nop 1
	v_lshrrev_b64 v[6:7], v200, vcc
	v_ffbl_b32_sdwa v6, v6 dst_sel:DWORD dst_unused:UNUSED_PAD src0_sel:BYTE_0
	v_add_u32_e32 v6, v6, v200
	v_cmp_ne_u32_e32 vcc, v230, v6
	s_nop 1
	v_cndmask_b32_e32 v6, v245, v5, vcc
	ds_bpermute_b32 v7, v1, v6
	s_waitcnt lgkmcnt(0)
	v_max_f32_e32 v7, v7, v7
	v_max_f32_e32 v6, v6, v7
	ds_bpermute_b32 v7, v201, v6
	s_waitcnt lgkmcnt(0)
	v_max_f32_e32 v7, v7, v7
	v_max_f32_e32 v6, v6, v7
	ds_bpermute_b32 v7, v220, v6
	s_waitcnt lgkmcnt(0)
	v_max_f32_e32 v7, v7, v7
	v_max_f32_e32 v6, v6, v7
	v_add_f32_e32 v6, v8, v6
	s_nop 0
	v_readlane_b32 s4, v6, 0
	v_readlane_b32 s5, v6, 8
	v_readlane_b32 s28, v6, 16
	v_cmp_eq_f32_e64 s[20:21], s4, v6
	v_cmp_gt_f32_e32 vcc, s4, v6
	v_cmp_gt_f32_e64 s[22:23], s5, v6
	v_cmp_eq_f32_e64 s[24:25], s5, v6
	s_and_b64 s[4:5], s[0:1], s[20:21]
	v_readlane_b32 s34, v6, 24
	v_cmp_gt_f32_e64 s[26:27], s28, v6
	v_cmp_eq_f32_e64 s[28:29], s28, v6
	s_and_b64 s[20:21], s[6:7], s[24:25]
	s_or_b64 s[4:5], vcc, s[4:5]
	v_readlane_b32 s40, v6, 32
	v_cmp_gt_f32_e64 s[30:31], s34, v6
	v_cmp_eq_f32_e64 s[34:35], s34, v6
	s_and_b64 s[24:25], s[8:9], s[28:29]
	v_cndmask_b32_e64 v7, 0, 1, s[4:5]
	s_or_b64 s[4:5], s[22:23], s[20:21]
	v_cmp_gt_f32_e64 s[36:37], s40, v6
	v_cmp_eq_f32_e64 s[40:41], s40, v6
	s_and_b64 s[28:29], s[10:11], s[34:35]
	v_cndmask_b32_e64 v8, 0, 1, s[4:5]
	s_or_b64 s[4:5], s[26:27], s[24:25]
	v_readlane_b32 s54, v6, 40
	s_and_b64 s[34:35], s[12:13], s[40:41]
	v_cndmask_b32_e64 v9, 0, 1, s[4:5]
	s_or_b64 s[4:5], s[30:31], s[28:29]
	v_cndmask_b32_e64 v10, 0, 1, s[4:5]
	s_or_b64 s[4:5], s[36:37], s[34:35]
	v_cmp_eq_f32_e64 s[20:21], s54, v6
	v_cndmask_b32_e64 v11, 0, 1, s[4:5]
	v_cmp_gt_f32_e32 vcc, s54, v6
	s_and_b64 s[4:5], s[14:15], s[20:21]
	s_or_b64 s[4:5], vcc, s[4:5]
	v_cndmask_b32_e64 v12, 0, 1, s[4:5]
	v_readlane_b32 s4, v6, 48
	s_nop 1
	v_cmp_eq_f32_e64 s[20:21], s4, v6
	v_cmp_gt_f32_e32 vcc, s4, v6
	s_and_b64 s[4:5], s[16:17], s[20:21]
	s_or_b64 s[4:5], vcc, s[4:5]
	v_cndmask_b32_e64 v13, 0, 1, s[4:5]
	v_readlane_b32 s4, v6, 56
	s_nop 1
	v_cmp_gt_f32_e32 vcc, s4, v6
	s_nop 1
	v_cndmask_b32_e64 v6, 0, 1, vcc
	v_add_u32_e32 v6, v8, v6
	v_add3_u32 v6, v6, v7, v9
	v_add3_u32 v6, v6, v10, v11
	v_add3_u32 v6, v6, v12, v13
	v_cmp_gt_u32_e32 vcc, 4, v6
	v_mov_b32_e32 v6, 0
	s_nop 0
	v_cndmask_b32_e32 v5, v245, v5, vcc
	v_ashrrev_i32_e32 v9, 31, v5
	v_sub_u32_e32 v8, 63, v230
	v_and_b32_e32 v9, 0x7fffffff, v9
	v_xor_b32_e32 v9, v5, v9
	s_nop 0
	v_readlane_b32 s23, v9, 0
	s_movk_i32 s22, 63
	v_readlane_b32 s21, v9, 1
	s_movk_i32 s20, 62
	v_cmp_gt_i64_e32 vcc, s[22:23], v[8:9]
	v_readlane_b32 s23, v9, 2
	s_movk_i32 s22, 61
	v_addc_co_u32_e32 v6, vcc, 0, v6, vcc
	v_cmp_gt_i64_e32 vcc, s[20:21], v[8:9]
	v_readlane_b32 s21, v9, 3
	s_movk_i32 s20, 60
	v_addc_co_u32_e32 v6, vcc, 0, v6, vcc
	v_cmp_gt_i64_e32 vcc, s[22:23], v[8:9]
	v_readlane_b32 s23, v9, 4
	s_movk_i32 s22, 59
	v_addc_co_u32_e32 v6, vcc, 0, v6, vcc
	v_cmp_gt_i64_e32 vcc, s[20:21], v[8:9]
	v_readlane_b32 s21, v9, 5
	s_movk_i32 s20, 58
	v_addc_co_u32_e32 v6, vcc, 0, v6, vcc
	v_cmp_gt_i64_e32 vcc, s[22:23], v[8:9]
	v_readlane_b32 s23, v9, 6
	s_movk_i32 s22, 57
	v_addc_co_u32_e32 v6, vcc, 0, v6, vcc
	v_cmp_gt_i64_e32 vcc, s[20:21], v[8:9]
	v_readlane_b32 s21, v9, 7
	s_movk_i32 s20, 56
	v_addc_co_u32_e32 v6, vcc, 0, v6, vcc
	v_cmp_gt_i64_e32 vcc, s[22:23], v[8:9]
	v_readlane_b32 s23, v9, 8
	s_movk_i32 s22, 55
	v_addc_co_u32_e32 v6, vcc, 0, v6, vcc
	v_cmp_gt_i64_e32 vcc, s[20:21], v[8:9]
	v_readlane_b32 s21, v9, 9
	s_movk_i32 s20, 54
	v_addc_co_u32_e32 v6, vcc, 0, v6, vcc
	v_cmp_gt_i64_e32 vcc, s[22:23], v[8:9]
	v_readlane_b32 s23, v9, 10
	s_movk_i32 s22, 53
	v_addc_co_u32_e32 v6, vcc, 0, v6, vcc
	v_cmp_gt_i64_e32 vcc, s[20:21], v[8:9]
	v_readlane_b32 s21, v9, 11
	s_movk_i32 s20, 52
	v_addc_co_u32_e32 v6, vcc, 0, v6, vcc
	v_cmp_gt_i64_e32 vcc, s[22:23], v[8:9]
	v_readlane_b32 s23, v9, 12
	s_movk_i32 s22, 51
	v_addc_co_u32_e32 v6, vcc, 0, v6, vcc
	v_cmp_gt_i64_e32 vcc, s[20:21], v[8:9]
	v_readlane_b32 s21, v9, 13
	s_movk_i32 s20, 50
	v_addc_co_u32_e32 v6, vcc, 0, v6, vcc
	v_cmp_gt_i64_e32 vcc, s[22:23], v[8:9]
	v_readlane_b32 s23, v9, 14
	s_movk_i32 s22, 49
	v_addc_co_u32_e32 v6, vcc, 0, v6, vcc
	v_cmp_gt_i64_e32 vcc, s[20:21], v[8:9]
	v_readlane_b32 s21, v9, 15
	s_movk_i32 s20, 48
	v_addc_co_u32_e32 v6, vcc, 0, v6, vcc
	v_cmp_gt_i64_e32 vcc, s[22:23], v[8:9]
	v_readlane_b32 s23, v9, 16
	s_movk_i32 s22, 47
	v_addc_co_u32_e32 v6, vcc, 0, v6, vcc
	v_cmp_gt_i64_e32 vcc, s[20:21], v[8:9]
	v_readlane_b32 s21, v9, 17
	s_movk_i32 s20, 46
	v_addc_co_u32_e32 v6, vcc, 0, v6, vcc
	v_cmp_gt_i64_e32 vcc, s[22:23], v[8:9]
	v_readlane_b32 s23, v9, 18
	s_movk_i32 s22, 45
; __device__ __forceinline__ void phase_nrr(const Frame& F, const Args& a, int l, const bf16_t* XA, const float* g, const float* modl, unsigned char* XN8) {
;     ...
;             int rank = 0;
; #pragma unroll 8
;             for (int e2 = 0; e2 < 64; ++e2) { const float v = __int_as_float(__builtin_amdgcn_readlane(__float_as_int(val), e2)); rank += (v > val || (v == val && e2 < lane)) ? 1 : 0; }
;             const bool sel = rank < TOPK;
;             const float ssum = wave_sum(sel ? sc : 0.f);
;             if (sel) { const int p = atomicAdd((int*)(hist + lane), 1); top_e[t * TOPK + rank] = lane; gate[t * TOPK + rank] = sc / ssum * 2.5f; lpos[t * TOPK + rank] = p; }
	v_addc_co_u32_e32 v6, vcc, 0, v6, vcc
	v_cmp_gt_i64_e32 vcc, s[20:21], v[8:9]
	v_readlane_b32 s21, v9, 19
	s_movk_i32 s20, 44
	v_addc_co_u32_e32 v6, vcc, 0, v6, vcc
	v_cmp_gt_i64_e32 vcc, s[22:23], v[8:9]
	v_readlane_b32 s23, v9, 20
	s_movk_i32 s22, 43
	v_addc_co_u32_e32 v6, vcc, 0, v6, vcc
	v_cmp_gt_i64_e32 vcc, s[20:21], v[8:9]
	v_readlane_b32 s21, v9, 21
	s_movk_i32 s20, 42
	v_addc_co_u32_e32 v6, vcc, 0, v6, vcc
	v_cmp_gt_i64_e32 vcc, s[22:23], v[8:9]
	v_readlane_b32 s23, v9, 22
	s_movk_i32 s22, 41
	v_addc_co_u32_e32 v6, vcc, 0, v6, vcc
	v_cmp_gt_i64_e32 vcc, s[20:21], v[8:9]
	v_readlane_b32 s21, v9, 23
	s_movk_i32 s20, 40
	v_addc_co_u32_e32 v6, vcc, 0, v6, vcc
	v_cmp_gt_i64_e32 vcc, s[22:23], v[8:9]
	v_readlane_b32 s23, v9, 24
	s_movk_i32 s22, 39
	v_addc_co_u32_e32 v6, vcc, 0, v6, vcc
	v_cmp_gt_i64_e32 vcc, s[20:21], v[8:9]
	v_readlane_b32 s21, v9, 25
	s_movk_i32 s20, 38
	v_addc_co_u32_e32 v6, vcc, 0, v6, vcc
	v_cmp_gt_i64_e32 vcc, s[22:23], v[8:9]
	v_readlane_b32 s23, v9, 26
	s_movk_i32 s22, 37
	v_addc_co_u32_e32 v6, vcc, 0, v6, vcc
	v_cmp_gt_i64_e32 vcc, s[20:21], v[8:9]
	v_readlane_b32 s21, v9, 27
	s_movk_i32 s20, 36
	v_addc_co_u32_e32 v6, vcc, 0, v6, vcc
	v_cmp_gt_i64_e32 vcc, s[22:23], v[8:9]
	v_readlane_b32 s23, v9, 28
	s_movk_i32 s22, 35
	v_addc_co_u32_e32 v6, vcc, 0, v6, vcc
	v_cmp_gt_i64_e32 vcc, s[20:21], v[8:9]
	v_readlane_b32 s21, v9, 29
	s_movk_i32 s20, 34
	v_addc_co_u32_e32 v6, vcc, 0, v6, vcc
	v_cmp_gt_i64_e32 vcc, s[22:23], v[8:9]
	v_readlane_b32 s23, v9, 30
	s_movk_i32 s22, 33
	v_addc_co_u32_e32 v6, vcc, 0, v6, vcc
	v_cmp_gt_i64_e32 vcc, s[20:21], v[8:9]
	v_readlane_b32 s21, v9, 31
	s_movk_i32 s20, 32
	v_addc_co_u32_e32 v6, vcc, 0, v6, vcc
	v_cmp_gt_i64_e32 vcc, s[22:23], v[8:9]
	v_readlane_b32 s23, v9, 32
	s_movk_i32 s22, 31
	v_addc_co_u32_e32 v6, vcc, 0, v6, vcc
	v_cmp_gt_i64_e32 vcc, s[20:21], v[8:9]
	v_readlane_b32 s21, v9, 33
	s_movk_i32 s20, 30
	v_addc_co_u32_e32 v6, vcc, 0, v6, vcc
	v_cmp_gt_i64_e32 vcc, s[22:23], v[8:9]
	v_readlane_b32 s23, v9, 34
	s_movk_i32 s22, 29
	v_addc_co_u32_e32 v6, vcc, 0, v6, vcc
	v_cmp_gt_i64_e32 vcc, s[20:21], v[8:9]
	v_readlane_b32 s21, v9, 35
	s_movk_i32 s20, 28
	v_addc_co_u32_e32 v6, vcc, 0, v6, vcc
	v_cmp_gt_i64_e32 vcc, s[22:23], v[8:9]
	v_readlane_b32 s23, v9, 36
	s_movk_i32 s22, 27
	v_addc_co_u32_e32 v6, vcc, 0, v6, vcc
	v_cmp_gt_i64_e32 vcc, s[20:21], v[8:9]
	v_readlane_b32 s21, v9, 37
	s_movk_i32 s20, 26
	v_addc_co_u32_e32 v6, vcc, 0, v6, vcc
	v_cmp_gt_i64_e32 vcc, s[22:23], v[8:9]
	v_readlane_b32 s23, v9, 38
	s_movk_i32 s22, 25
	v_addc_co_u32_e32 v6, vcc, 0, v6, vcc
	v_cmp_gt_i64_e32 vcc, s[20:21], v[8:9]
	v_readlane_b32 s21, v9, 39
	s_movk_i32 s20, 24
	v_addc_co_u32_e32 v6, vcc, 0, v6, vcc
	v_cmp_gt_i64_e32 vcc, s[22:23], v[8:9]
	v_readlane_b32 s23, v9, 40
	s_movk_i32 s22, 23
	v_addc_co_u32_e32 v6, vcc, 0, v6, vcc
	v_cmp_gt_i64_e32 vcc, s[20:21], v[8:9]
	v_readlane_b32 s21, v9, 41
	s_movk_i32 s20, 22
	v_addc_co_u32_e32 v6, vcc, 0, v6, vcc
	v_cmp_gt_i64_e32 vcc, s[22:23], v[8:9]
	v_readlane_b32 s23, v9, 42
	s_movk_i32 s22, 21
	v_addc_co_u32_e32 v6, vcc, 0, v6, vcc
	v_cmp_gt_i64_e32 vcc, s[20:21], v[8:9]
	v_readlane_b32 s21, v9, 43
	s_movk_i32 s20, 20
	v_addc_co_u32_e32 v6, vcc, 0, v6, vcc
	v_cmp_gt_i64_e32 vcc, s[22:23], v[8:9]
	v_readlane_b32 s23, v9, 44
	s_movk_i32 s22, 19
	v_addc_co_u32_e32 v6, vcc, 0, v6, vcc
	v_cmp_gt_i64_e32 vcc, s[20:21], v[8:9]
	v_readlane_b32 s21, v9, 45
	s_movk_i32 s20, 18
	v_addc_co_u32_e32 v6, vcc, 0, v6, vcc
	v_cmp_gt_i64_e32 vcc, s[22:23], v[8:9]
	v_readlane_b32 s23, v9, 46
	s_movk_i32 s22, 17
	v_addc_co_u32_e32 v6, vcc, 0, v6, vcc
	v_cmp_gt_i64_e32 vcc, s[20:21], v[8:9]
	v_readlane_b32 s21, v9, 47
	s_movk_i32 s20, 16
	v_addc_co_u32_e32 v6, vcc, 0, v6, vcc
	v_cmp_gt_i64_e32 vcc, s[22:23], v[8:9]
	v_readlane_b32 s23, v9, 48
	s_movk_i32 s22, 15
	v_addc_co_u32_e32 v6, vcc, 0, v6, vcc
	v_cmp_gt_i64_e32 vcc, s[20:21], v[8:9]
	v_readlane_b32 s21, v9, 49
	s_movk_i32 s20, 14
	v_addc_co_u32_e32 v6, vcc, 0, v6, vcc
	v_cmp_gt_i64_e32 vcc, s[22:23], v[8:9]
	v_readlane_b32 s23, v9, 50
	s_movk_i32 s22, 13
	v_addc_co_u32_e32 v6, vcc, 0, v6, vcc
	v_cmp_gt_i64_e32 vcc, s[20:21], v[8:9]
	v_readlane_b32 s21, v9, 51
	s_movk_i32 s20, 12
	v_addc_co_u32_e32 v6, vcc, 0, v6, vcc
	v_cmp_gt_i64_e32 vcc, s[22:23], v[8:9]
	v_readlane_b32 s23, v9, 52
	s_movk_i32 s22, 11
	v_addc_co_u32_e32 v6, vcc, 0, v6, vcc
	v_cmp_gt_i64_e32 vcc, s[20:21], v[8:9]
	v_readlane_b32 s21, v9, 53
	s_movk_i32 s20, 10
	v_addc_co_u32_e32 v6, vcc, 0, v6, vcc
	v_cmp_gt_i64_e32 vcc, s[22:23], v[8:9]
	v_readlane_b32 s23, v9, 54
	s_movk_i32 s22, 9
	v_addc_co_u32_e32 v6, vcc, 0, v6, vcc
	v_cmp_gt_i64_e32 vcc, s[20:21], v[8:9]
	v_readlane_b32 s21, v9, 55
	s_movk_i32 s20, 8
	v_addc_co_u32_e32 v6, vcc, 0, v6, vcc
	v_cmp_gt_i64_e32 vcc, s[22:23], v[8:9]
	v_readlane_b32 s23, v9, 56
	s_movk_i32 s22, 7
	v_addc_co_u32_e32 v6, vcc, 0, v6, vcc
	v_cmp_gt_i64_e32 vcc, s[20:21], v[8:9]
	v_readlane_b32 s21, v9, 57
	s_movk_i32 s20, 6
	v_addc_co_u32_e32 v6, vcc, 0, v6, vcc
	v_cmp_gt_i64_e32 vcc, s[22:23], v[8:9]
	v_readlane_b32 s23, v9, 58
	s_movk_i32 s22, 5
	v_addc_co_u32_e32 v6, vcc, 0, v6, vcc
	v_cmp_gt_i64_e32 vcc, s[20:21], v[8:9]
	v_readlane_b32 s21, v9, 59
	s_movk_i32 s20, 4
	v_addc_co_u32_e32 v6, vcc, 0, v6, vcc
	v_cmp_gt_i64_e32 vcc, s[22:23], v[8:9]
	v_readlane_b32 s23, v9, 60
	s_movk_i32 s22, 3
	v_addc_co_u32_e32 v6, vcc, 0, v6, vcc
	v_cmp_gt_i64_e32 vcc, s[20:21], v[8:9]
	v_readlane_b32 s21, v9, 61
	s_movk_i32 s20, 2
	v_addc_co_u32_e32 v6, vcc, 0, v6, vcc
	v_cmp_gt_i64_e32 vcc, s[22:23], v[8:9]
	v_readlane_b32 s23, v9, 62
	s_movk_i32 s22, 1
	v_addc_co_u32_e32 v6, vcc, 0, v6, vcc
	v_cmp_gt_i64_e32 vcc, s[20:21], v[8:9]
	v_readlane_b32 s21, v9, 63
	s_movk_i32 s20, 0
	v_addc_co_u32_e32 v6, vcc, 0, v6, vcc
	v_cmp_gt_i64_e32 vcc, s[22:23], v[8:9]
	s_nop 1
	v_addc_co_u32_e32 v6, vcc, 0, v6, vcc
	v_cmp_gt_i64_e32 vcc, s[20:21], v[8:9]
	s_nop 1
	v_addc_co_u32_e32 v6, vcc, 0, v6, vcc
	v_cmp_gt_u32_e32 vcc, 6, v6
	s_nop 1
	v_cndmask_b32_e32 v5, 0, v2, vcc
	ds_bpermute_b32 v7, v1, v5
	s_waitcnt lgkmcnt(0)
	v_add_f32_e32 v5, v5, v7
	ds_bpermute_b32 v7, v201, v5
	s_waitcnt lgkmcnt(0)
	v_add_f32_e32 v5, v5, v7
	ds_bpermute_b32 v7, v220, v5
	s_waitcnt lgkmcnt(0)
	v_add_f32_e32 v5, v5, v7
	ds_bpermute_b32 v7, v221, v5
	s_waitcnt lgkmcnt(0)
	v_add_f32_e32 v5, v5, v7
	ds_bpermute_b32 v7, v222, v5
	s_waitcnt lgkmcnt(0)
	v_add_f32_e32 v5, v5, v7
	ds_bpermute_b32 v7, v223, v5
	s_and_saveexec_b64 s[4:5], vcc
	s_cbranch_execz .LBB0_1328
; __device__ __forceinline__ void phase_nrr(const Frame& F, const Args& a, int l, const bf16_t* XA, const float* g, const float* modl, unsigned char* XN8) {
;     ...
;         for (int i = 0; i < 8; ++i) { const int t = tb + i;
;             const float lg = Pl[(w * 8 + i) * NE + lane] + Pl[(64 + w * 8 + i) * NE + lane]; const float sc = 1.f / (1.f + __expf(-lg)); const float bb = sc + bias;
;             float m1 = bb; m1 = fmaxf(m1, __shfl_xor(m1, 1)); m1 = fmaxf(m1, __shfl_xor(m1, 2)); m1 = fmaxf(m1, __shfl_xor(m1, 4));
;             const unsigned long long eq = __ballot(bb == m1); const int gbase = lane & ~7; const unsigned grpmask = (unsigned)((eq >> gbase) & 0xffull);
;             const int first = gbase + __builtin_ctz(grpmask);
;             float m2 = (lane == first) ? -INFINITY : bb; m2 = fmaxf(m2, __shfl_xor(m2, 1)); m2 = fmaxf(m2, __shfl_xor(m2, 2)); m2 = fmaxf(m2, __shfl_xor(m2, 4));
;             const float gsum = m1 + m2; const int gq = lane >> 3;
;             int grank = 0;
; #pragma unroll
;             for (int g2 = 0; g2 < 8; ++g2) { const float v = __int_as_float(__builtin_amdgcn_readlane(__float_as_int(gsum), g2 * 8)); grank += (v > gsum || (v == gsum && g2 < gq)) ? 1 : 0; }
;             const bool keep = grank < 4; const float val = keep ? bb : -INFINITY;
;             int rank = 0;
; #pragma unroll 8
;             for (int e2 = 0; e2 < 64; ++e2) { const float v = __int_as_float(__builtin_amdgcn_readlane(__float_as_int(val), e2)); rank += (v > val || (v == val && e2 < lane)) ? 1 : 0; }
	s_waitcnt lgkmcnt(0)
	v_add_f32_e32 v5, v5, v7
	s_mul_i32 s2, s2, 6
	v_or_b32_e32 v6, s2, v6
	v_div_scale_f32 v11, s[2:3], v5, v5, v2
	v_rcp_f32_e32 v12, v11
	v_ashrrev_i32_e32 v7, 31, v6
	v_lshlrev_b64 v[6:7], 2, v[6:7]
	v_lshl_add_u64 v[8:9], s[42:43], 0, v[6:7]
	ds_add_rtn_u32 v10, v227, v243
	global_store_dword v[8:9], v230, off
	v_fma_f32 v8, -v11, v12, 1.0
	v_fmac_f32_e32 v12, v8, v12
	v_div_scale_f32 v8, vcc, v2, v5, v2
	v_mul_f32_e32 v9, v8, v12
	v_fma_f32 v13, -v11, v9, v8
	v_fmac_f32_e32 v9, v13, v12
	v_fma_f32 v8, -v11, v9, v8
	v_div_fmas_f32 v8, v8, v12, v9
	v_div_fixup_f32 v2, v8, v5, v2
	v_mul_f32_e32 v2, 0x40200000, v2
	v_lshl_add_u64 v[8:9], s[44:45], 0, v[6:7]
	v_lshl_add_u64 v[6:7], s[46:47], 0, v[6:7]
	global_store_dword v[8:9], v2, off
	s_waitcnt lgkmcnt(0)
	global_store_dword v[6:7], v10, off
.LBB0_1328:
	s_or_b64 exec, exec, s[4:5]
	v_add_u32_e32 v2, s80, v226
	ds_read_b32 v2, v2
	ds_read_b32 v5, v4 offset:17664
	s_waitcnt lgkmcnt(0)
	v_add_f32_e32 v2, v2, v5
	v_mul_f32_e32 v2, 0xbfb8aa3b, v2
	v_exp_f32_e32 v2, v2
	s_nop 0
	v_add_f32_e32 v2, 1.0, v2
	v_div_scale_f32 v5, s[2:3], v2, v2, 1.0
	v_rcp_f32_e32 v6, v5
	v_div_scale_f32 v7, vcc, 1.0, v2, 1.0
	s_mov_b32 s2, 0
	v_fma_f32 v8, -v5, v6, 1.0
	v_fmac_f32_e32 v6, v8, v6
	v_mul_f32_e32 v8, v7, v6
	v_fma_f32 v9, -v5, v8, v7
	v_fmac_f32_e32 v8, v9, v6
	v_fma_f32 v5, -v5, v8, v7
	v_div_fmas_f32 v5, v5, v6, v8
	v_div_fixup_f32 v2, v5, v2, 1.0
	v_add_f32_e32 v5, v3, v2
	ds_bpermute_b32 v6, v1, v5
	s_waitcnt lgkmcnt(0)
	v_max_f32_e32 v6, v6, v6
	v_max_f32_e32 v6, v5, v6
	ds_bpermute_b32 v7, v201, v6
	s_waitcnt lgkmcnt(0)
	v_max_f32_e32 v7, v7, v7
	v_max_f32_e32 v6, v6, v7
	ds_bpermute_b32 v7, v220, v6
	s_waitcnt lgkmcnt(0)
	v_max_f32_e32 v7, v7, v7
	v_max_f32_e32 v8, v6, v7
	v_cmp_eq_f32_e32 vcc, v5, v8
	s_nop 1
	v_lshrrev_b64 v[6:7], v200, vcc
	v_ffbl_b32_sdwa v6, v6 dst_sel:DWORD dst_unused:UNUSED_PAD src0_sel:BYTE_0
	v_add_u32_e32 v6, v6, v200
	v_cmp_ne_u32_e32 vcc, v230, v6
	s_nop 1
	v_cndmask_b32_e32 v6, v245, v5, vcc
	ds_bpermute_b32 v7, v1, v6
	s_waitcnt lgkmcnt(0)
	v_max_f32_e32 v7, v7, v7
	v_max_f32_e32 v6, v6, v7
	ds_bpermute_b32 v7, v201, v6
	s_waitcnt lgkmcnt(0)
	v_max_f32_e32 v7, v7, v7
	v_max_f32_e32 v6, v6, v7
	ds_bpermute_b32 v7, v220, v6
	s_waitcnt lgkmcnt(0)
	v_max_f32_e32 v7, v7, v7
	v_max_f32_e32 v6, v6, v7
	v_add_f32_e32 v6, v8, v6
	s_nop 0
	v_readlane_b32 s3, v6, 0
	v_readlane_b32 s4, v6, 8
	v_readlane_b32 s5, v6, 16
	v_cmp_eq_f32_e64 s[20:21], s3, v6
	v_cmp_gt_f32_e32 vcc, s3, v6
	v_cmp_gt_f32_e64 s[22:23], s4, v6
	v_cmp_eq_f32_e64 s[24:25], s4, v6
	v_cmp_gt_f32_e64 s[26:27], s5, v6
	v_cmp_eq_f32_e64 s[28:29], s5, v6
	s_and_b64 s[4:5], s[0:1], s[20:21]
	v_readlane_b32 s34, v6, 24
	s_and_b64 s[20:21], s[6:7], s[24:25]
	s_or_b64 s[4:5], vcc, s[4:5]
	v_readlane_b32 s40, v6, 32
	v_cmp_gt_f32_e64 s[30:31], s34, v6
	v_cmp_eq_f32_e64 s[34:35], s34, v6
	s_and_b64 s[24:25], s[8:9], s[28:29]
	v_cndmask_b32_e64 v7, 0, 1, s[4:5]
	s_or_b64 s[4:5], s[22:23], s[20:21]
	v_cmp_gt_f32_e64 s[36:37], s40, v6
	v_cmp_eq_f32_e64 s[40:41], s40, v6
	s_and_b64 s[28:29], s[10:11], s[34:35]
	v_cndmask_b32_e64 v8, 0, 1, s[4:5]
	s_or_b64 s[4:5], s[26:27], s[24:25]
	v_readlane_b32 s54, v6, 40
	s_and_b64 s[34:35], s[12:13], s[40:41]
	v_cndmask_b32_e64 v9, 0, 1, s[4:5]
	s_or_b64 s[4:5], s[30:31], s[28:29]
	v_cndmask_b32_e64 v10, 0, 1, s[4:5]
	s_or_b64 s[4:5], s[36:37], s[34:35]
	v_cmp_eq_f32_e64 s[20:21], s54, v6
	v_cndmask_b32_e64 v11, 0, 1, s[4:5]
	v_cmp_gt_f32_e32 vcc, s54, v6
	s_and_b64 s[4:5], s[14:15], s[20:21]
	v_readlane_b32 s3, v6, 48
	s_or_b64 s[4:5], vcc, s[4:5]
	v_cndmask_b32_e64 v12, 0, 1, s[4:5]
	v_cmp_eq_f32_e64 s[20:21], s3, v6
	v_cmp_gt_f32_e32 vcc, s3, v6
	s_and_b64 s[4:5], s[16:17], s[20:21]
	v_readlane_b32 s3, v6, 56
	s_or_b64 s[4:5], vcc, s[4:5]
	v_cndmask_b32_e64 v13, 0, 1, s[4:5]
	v_cmp_gt_f32_e32 vcc, s3, v6
	s_nop 1
	v_cndmask_b32_e64 v6, 0, 1, vcc
	v_add_u32_e32 v6, v8, v6
	v_add3_u32 v6, v6, v7, v9
	v_add3_u32 v6, v6, v10, v11
	v_add3_u32 v6, v6, v12, v13
	v_cmp_gt_u32_e32 vcc, 4, v6
	v_mov_b32_e32 v6, 0
	s_nop 0
	v_cndmask_b32_e32 v5, v245, v5, vcc
	v_ashrrev_i32_e32 v9, 31, v5
	v_sub_u32_e32 v8, 63, v230
	v_and_b32_e32 v9, 0x7fffffff, v9
	v_xor_b32_e32 v9, v5, v9
	s_nop 0
	v_readlane_b32 s23, v9, 0
	s_movk_i32 s22, 63
	v_readlane_b32 s21, v9, 1
	s_movk_i32 s20, 62
	v_cmp_gt_i64_e32 vcc, s[22:23], v[8:9]
	v_readlane_b32 s23, v9, 2
	s_movk_i32 s22, 61
	v_addc_co_u32_e32 v6, vcc, 0, v6, vcc
	v_cmp_gt_i64_e32 vcc, s[20:21], v[8:9]
	v_readlane_b32 s21, v9, 3
	s_movk_i32 s20, 60
	v_addc_co_u32_e32 v6, vcc, 0, v6, vcc
	v_cmp_gt_i64_e32 vcc, s[22:23], v[8:9]
	v_readlane_b32 s23, v9, 4
	s_movk_i32 s22, 59
	v_addc_co_u32_e32 v6, vcc, 0, v6, vcc
	v_cmp_gt_i64_e32 vcc, s[20:21], v[8:9]
	v_readlane_b32 s21, v9, 5
	s_movk_i32 s20, 58
	v_addc_co_u32_e32 v6, vcc, 0, v6, vcc
	v_cmp_gt_i64_e32 vcc, s[22:23], v[8:9]
	v_readlane_b32 s23, v9, 6
	s_movk_i32 s22, 57
	v_addc_co_u32_e32 v6, vcc, 0, v6, vcc
	v_cmp_gt_i64_e32 vcc, s[20:21], v[8:9]
	v_readlane_b32 s21, v9, 7
	s_movk_i32 s20, 56
	v_addc_co_u32_e32 v6, vcc, 0, v6, vcc
	v_cmp_gt_i64_e32 vcc, s[22:23], v[8:9]
	v_readlane_b32 s23, v9, 8
	s_movk_i32 s22, 55
	v_addc_co_u32_e32 v6, vcc, 0, v6, vcc
	v_cmp_gt_i64_e32 vcc, s[20:21], v[8:9]
	v_readlane_b32 s21, v9, 9
	s_movk_i32 s20, 54
	v_addc_co_u32_e32 v6, vcc, 0, v6, vcc
	v_cmp_gt_i64_e32 vcc, s[22:23], v[8:9]
	v_readlane_b32 s23, v9, 10
	s_movk_i32 s22, 53
	v_addc_co_u32_e32 v6, vcc, 0, v6, vcc
	v_cmp_gt_i64_e32 vcc, s[20:21], v[8:9]
	v_readlane_b32 s21, v9, 11
	s_movk_i32 s20, 52
	v_addc_co_u32_e32 v6, vcc, 0, v6, vcc
	v_cmp_gt_i64_e32 vcc, s[22:23], v[8:9]
; __device__ __forceinline__ void phase_nrr(const Frame& F, const Args& a, int l, const bf16_t* XA, const float* g, const float* modl, unsigned char* XN8) {
;     ...
;             int rank = 0;
; #pragma unroll 8
;             for (int e2 = 0; e2 < 64; ++e2) { const float v = __int_as_float(__builtin_amdgcn_readlane(__float_as_int(val), e2)); rank += (v > val || (v == val && e2 < lane)) ? 1 : 0; }
;             const bool sel = rank < TOPK;
;             const float ssum = wave_sum(sel ? sc : 0.f);
	v_readlane_b32 s23, v9, 12
	s_movk_i32 s22, 51
	v_addc_co_u32_e32 v6, vcc, 0, v6, vcc
	v_cmp_gt_i64_e32 vcc, s[20:21], v[8:9]
	v_readlane_b32 s21, v9, 13
	s_movk_i32 s20, 50
	v_addc_co_u32_e32 v6, vcc, 0, v6, vcc
	v_cmp_gt_i64_e32 vcc, s[22:23], v[8:9]
	v_readlane_b32 s23, v9, 14
	s_movk_i32 s22, 49
	v_addc_co_u32_e32 v6, vcc, 0, v6, vcc
	v_cmp_gt_i64_e32 vcc, s[20:21], v[8:9]
	v_readlane_b32 s21, v9, 15
	s_movk_i32 s20, 48
	v_addc_co_u32_e32 v6, vcc, 0, v6, vcc
	v_cmp_gt_i64_e32 vcc, s[22:23], v[8:9]
	v_readlane_b32 s23, v9, 16
	s_movk_i32 s22, 47
	v_addc_co_u32_e32 v6, vcc, 0, v6, vcc
	v_cmp_gt_i64_e32 vcc, s[20:21], v[8:9]
	v_readlane_b32 s21, v9, 17
	s_movk_i32 s20, 46
	v_addc_co_u32_e32 v6, vcc, 0, v6, vcc
	v_cmp_gt_i64_e32 vcc, s[22:23], v[8:9]
	v_readlane_b32 s23, v9, 18
	s_movk_i32 s22, 45
	v_addc_co_u32_e32 v6, vcc, 0, v6, vcc
	v_cmp_gt_i64_e32 vcc, s[20:21], v[8:9]
	v_readlane_b32 s21, v9, 19
	s_movk_i32 s20, 44
	v_addc_co_u32_e32 v6, vcc, 0, v6, vcc
	v_cmp_gt_i64_e32 vcc, s[22:23], v[8:9]
	v_readlane_b32 s23, v9, 20
	s_movk_i32 s22, 43
	v_addc_co_u32_e32 v6, vcc, 0, v6, vcc
	v_cmp_gt_i64_e32 vcc, s[20:21], v[8:9]
	v_readlane_b32 s21, v9, 21
	s_movk_i32 s20, 42
	v_addc_co_u32_e32 v6, vcc, 0, v6, vcc
	v_cmp_gt_i64_e32 vcc, s[22:23], v[8:9]
	v_readlane_b32 s23, v9, 22
	s_movk_i32 s22, 41
	v_addc_co_u32_e32 v6, vcc, 0, v6, vcc
	v_cmp_gt_i64_e32 vcc, s[20:21], v[8:9]
	v_readlane_b32 s21, v9, 23
	s_movk_i32 s20, 40
	v_addc_co_u32_e32 v6, vcc, 0, v6, vcc
	v_cmp_gt_i64_e32 vcc, s[22:23], v[8:9]
	v_readlane_b32 s23, v9, 24
	s_movk_i32 s22, 39
	v_addc_co_u32_e32 v6, vcc, 0, v6, vcc
	v_cmp_gt_i64_e32 vcc, s[20:21], v[8:9]
	v_readlane_b32 s21, v9, 25
	s_movk_i32 s20, 38
	v_addc_co_u32_e32 v6, vcc, 0, v6, vcc
	v_cmp_gt_i64_e32 vcc, s[22:23], v[8:9]
	v_readlane_b32 s23, v9, 26
	s_movk_i32 s22, 37
	v_addc_co_u32_e32 v6, vcc, 0, v6, vcc
	v_cmp_gt_i64_e32 vcc, s[20:21], v[8:9]
	v_readlane_b32 s21, v9, 27
	s_movk_i32 s20, 36
	v_addc_co_u32_e32 v6, vcc, 0, v6, vcc
	v_cmp_gt_i64_e32 vcc, s[22:23], v[8:9]
	v_readlane_b32 s23, v9, 28
	s_movk_i32 s22, 35
	v_addc_co_u32_e32 v6, vcc, 0, v6, vcc
	v_cmp_gt_i64_e32 vcc, s[20:21], v[8:9]
	v_readlane_b32 s21, v9, 29
	s_movk_i32 s20, 34
	v_addc_co_u32_e32 v6, vcc, 0, v6, vcc
	v_cmp_gt_i64_e32 vcc, s[22:23], v[8:9]
	v_readlane_b32 s23, v9, 30
	s_movk_i32 s22, 33
	v_addc_co_u32_e32 v6, vcc, 0, v6, vcc
	v_cmp_gt_i64_e32 vcc, s[20:21], v[8:9]
	v_readlane_b32 s21, v9, 31
	s_movk_i32 s20, 32
	v_addc_co_u32_e32 v6, vcc, 0, v6, vcc
	v_cmp_gt_i64_e32 vcc, s[22:23], v[8:9]
	v_readlane_b32 s23, v9, 32
	s_movk_i32 s22, 31
	v_addc_co_u32_e32 v6, vcc, 0, v6, vcc
	v_cmp_gt_i64_e32 vcc, s[20:21], v[8:9]
	v_readlane_b32 s21, v9, 33
	s_movk_i32 s20, 30
	v_addc_co_u32_e32 v6, vcc, 0, v6, vcc
	v_cmp_gt_i64_e32 vcc, s[22:23], v[8:9]
	v_readlane_b32 s23, v9, 34
	s_movk_i32 s22, 29
	v_addc_co_u32_e32 v6, vcc, 0, v6, vcc
	v_cmp_gt_i64_e32 vcc, s[20:21], v[8:9]
	v_readlane_b32 s21, v9, 35
	s_movk_i32 s20, 28
	v_addc_co_u32_e32 v6, vcc, 0, v6, vcc
	v_cmp_gt_i64_e32 vcc, s[22:23], v[8:9]
	v_readlane_b32 s23, v9, 36
	s_movk_i32 s22, 27
	v_addc_co_u32_e32 v6, vcc, 0, v6, vcc
	v_cmp_gt_i64_e32 vcc, s[20:21], v[8:9]
	v_readlane_b32 s21, v9, 37
	s_movk_i32 s20, 26
	v_addc_co_u32_e32 v6, vcc, 0, v6, vcc
	v_cmp_gt_i64_e32 vcc, s[22:23], v[8:9]
	v_readlane_b32 s23, v9, 38
	s_movk_i32 s22, 25
	v_addc_co_u32_e32 v6, vcc, 0, v6, vcc
	v_cmp_gt_i64_e32 vcc, s[20:21], v[8:9]
	v_readlane_b32 s21, v9, 39
	s_movk_i32 s20, 24
	v_addc_co_u32_e32 v6, vcc, 0, v6, vcc
	v_cmp_gt_i64_e32 vcc, s[22:23], v[8:9]
	v_readlane_b32 s23, v9, 40
	s_movk_i32 s22, 23
	v_addc_co_u32_e32 v6, vcc, 0, v6, vcc
	v_cmp_gt_i64_e32 vcc, s[20:21], v[8:9]
	v_readlane_b32 s21, v9, 41
	s_movk_i32 s20, 22
	v_addc_co_u32_e32 v6, vcc, 0, v6, vcc
	v_cmp_gt_i64_e32 vcc, s[22:23], v[8:9]
	v_readlane_b32 s23, v9, 42
	s_movk_i32 s22, 21
	v_addc_co_u32_e32 v6, vcc, 0, v6, vcc
	v_cmp_gt_i64_e32 vcc, s[20:21], v[8:9]
	v_readlane_b32 s21, v9, 43
	s_movk_i32 s20, 20
	v_addc_co_u32_e32 v6, vcc, 0, v6, vcc
	v_cmp_gt_i64_e32 vcc, s[22:23], v[8:9]
	v_readlane_b32 s23, v9, 44
	s_movk_i32 s22, 19
	v_addc_co_u32_e32 v6, vcc, 0, v6, vcc
	v_cmp_gt_i64_e32 vcc, s[20:21], v[8:9]
	v_readlane_b32 s21, v9, 45
	s_movk_i32 s20, 18
	v_addc_co_u32_e32 v6, vcc, 0, v6, vcc
	v_cmp_gt_i64_e32 vcc, s[22:23], v[8:9]
	v_readlane_b32 s23, v9, 46
	s_movk_i32 s22, 17
	v_addc_co_u32_e32 v6, vcc, 0, v6, vcc
	v_cmp_gt_i64_e32 vcc, s[20:21], v[8:9]
	v_readlane_b32 s21, v9, 47
	s_movk_i32 s20, 16
	v_addc_co_u32_e32 v6, vcc, 0, v6, vcc
	v_cmp_gt_i64_e32 vcc, s[22:23], v[8:9]
	v_readlane_b32 s23, v9, 48
	s_movk_i32 s22, 15
	v_addc_co_u32_e32 v6, vcc, 0, v6, vcc
	v_cmp_gt_i64_e32 vcc, s[20:21], v[8:9]
	v_readlane_b32 s21, v9, 49
	s_movk_i32 s20, 14
	v_addc_co_u32_e32 v6, vcc, 0, v6, vcc
	v_cmp_gt_i64_e32 vcc, s[22:23], v[8:9]
	v_readlane_b32 s23, v9, 50
	s_movk_i32 s22, 13
	v_addc_co_u32_e32 v6, vcc, 0, v6, vcc
	v_cmp_gt_i64_e32 vcc, s[20:21], v[8:9]
	v_readlane_b32 s21, v9, 51
	s_movk_i32 s20, 12
	v_addc_co_u32_e32 v6, vcc, 0, v6, vcc
	v_cmp_gt_i64_e32 vcc, s[22:23], v[8:9]
	v_readlane_b32 s23, v9, 52
	s_movk_i32 s22, 11
	v_addc_co_u32_e32 v6, vcc, 0, v6, vcc
	v_cmp_gt_i64_e32 vcc, s[20:21], v[8:9]
	v_readlane_b32 s21, v9, 53
	s_movk_i32 s20, 10
	v_addc_co_u32_e32 v6, vcc, 0, v6, vcc
	v_cmp_gt_i64_e32 vcc, s[22:23], v[8:9]
	v_readlane_b32 s23, v9, 54
	s_movk_i32 s22, 9
	v_addc_co_u32_e32 v6, vcc, 0, v6, vcc
	v_cmp_gt_i64_e32 vcc, s[20:21], v[8:9]
	v_readlane_b32 s21, v9, 55
	s_movk_i32 s20, 8
	v_addc_co_u32_e32 v6, vcc, 0, v6, vcc
	v_cmp_gt_i64_e32 vcc, s[22:23], v[8:9]
	v_readlane_b32 s23, v9, 56
	s_movk_i32 s22, 7
	v_addc_co_u32_e32 v6, vcc, 0, v6, vcc
	v_cmp_gt_i64_e32 vcc, s[20:21], v[8:9]
	v_readlane_b32 s21, v9, 57
	s_movk_i32 s20, 6
	v_addc_co_u32_e32 v6, vcc, 0, v6, vcc
	v_cmp_gt_i64_e32 vcc, s[22:23], v[8:9]
	v_readlane_b32 s23, v9, 58
	s_movk_i32 s22, 5
	v_addc_co_u32_e32 v6, vcc, 0, v6, vcc
	v_cmp_gt_i64_e32 vcc, s[20:21], v[8:9]
	v_readlane_b32 s21, v9, 59
	s_movk_i32 s20, 4
	v_addc_co_u32_e32 v6, vcc, 0, v6, vcc
	v_cmp_gt_i64_e32 vcc, s[22:23], v[8:9]
	v_readlane_b32 s23, v9, 60
	s_movk_i32 s22, 3
	v_addc_co_u32_e32 v6, vcc, 0, v6, vcc
	v_cmp_gt_i64_e32 vcc, s[20:21], v[8:9]
	v_readlane_b32 s21, v9, 61
	s_movk_i32 s20, 2
	v_addc_co_u32_e32 v6, vcc, 0, v6, vcc
	v_cmp_gt_i64_e32 vcc, s[22:23], v[8:9]
	v_readlane_b32 s23, v9, 62
	s_movk_i32 s22, 1
	v_addc_co_u32_e32 v6, vcc, 0, v6, vcc
	v_cmp_gt_i64_e32 vcc, s[20:21], v[8:9]
	v_readlane_b32 s21, v9, 63
	s_movk_i32 s20, 0
	v_addc_co_u32_e32 v6, vcc, 0, v6, vcc
	v_cmp_gt_i64_e32 vcc, s[22:23], v[8:9]
	s_nop 1
	v_addc_co_u32_e32 v6, vcc, 0, v6, vcc
	v_cmp_gt_i64_e32 vcc, s[20:21], v[8:9]
	s_nop 1
	v_addc_co_u32_e32 v6, vcc, 0, v6, vcc
	v_cmp_gt_u32_e32 vcc, 6, v6
	s_nop 1
	v_cndmask_b32_e32 v5, 0, v2, vcc
	ds_bpermute_b32 v7, v1, v5
	s_waitcnt lgkmcnt(0)
; __device__ __forceinline__ void phase_nrr(const Frame& F, const Args& a, int l, const bf16_t* XA, const float* g, const float* modl, unsigned char* XN8) {
;     ...
;         for (int i = 0; i < 8; ++i) { const int t = tb + i;
;             const float lg = Pl[(w * 8 + i) * NE + lane] + Pl[(64 + w * 8 + i) * NE + lane]; const float sc = 1.f / (1.f + __expf(-lg)); const float bb = sc + bias;
;             float m1 = bb; m1 = fmaxf(m1, __shfl_xor(m1, 1)); m1 = fmaxf(m1, __shfl_xor(m1, 2)); m1 = fmaxf(m1, __shfl_xor(m1, 4));
;             const unsigned long long eq = __ballot(bb == m1); const int gbase = lane & ~7; const unsigned grpmask = (unsigned)((eq >> gbase) & 0xffull);
;             const int first = gbase + __builtin_ctz(grpmask);
;             float m2 = (lane == first) ? -INFINITY : bb; m2 = fmaxf(m2, __shfl_xor(m2, 1)); m2 = fmaxf(m2, __shfl_xor(m2, 2)); m2 = fmaxf(m2, __shfl_xor(m2, 4));
;             const float gsum = m1 + m2; const int gq = lane >> 3;
;             int grank = 0;
; #pragma unroll
;             for (int g2 = 0; g2 < 8; ++g2) { const float v = __int_as_float(__builtin_amdgcn_readlane(__float_as_int(gsum), g2 * 8)); grank += (v > gsum || (v == gsum && g2 < gq)) ? 1 : 0; }
;             const bool keep = grank < 4; const float val = keep ? bb : -INFINITY;
;             int rank = 0;
; #pragma unroll 8
;             for (int e2 = 0; e2 < 64; ++e2) { const float v = __int_as_float(__builtin_amdgcn_readlane(__float_as_int(val), e2)); rank += (v > val || (v == val && e2 < lane)) ? 1 : 0; }
;             const bool sel = rank < TOPK;
;             const float ssum = wave_sum(sel ? sc : 0.f);
;             if (sel) { const int p = atomicAdd((int*)(hist + lane), 1); top_e[t * TOPK + rank] = lane; gate[t * TOPK + rank] = sc / ssum * 2.5f; lpos[t * TOPK + rank] = p; }
	v_add_f32_e32 v5, v5, v7
	ds_bpermute_b32 v7, v201, v5
	s_waitcnt lgkmcnt(0)
	v_add_f32_e32 v5, v5, v7
	ds_bpermute_b32 v7, v220, v5
	s_waitcnt lgkmcnt(0)
	v_add_f32_e32 v5, v5, v7
	ds_bpermute_b32 v7, v221, v5
	s_waitcnt lgkmcnt(0)
	v_add_f32_e32 v5, v5, v7
	ds_bpermute_b32 v7, v222, v5
	s_waitcnt lgkmcnt(0)
	v_add_f32_e32 v5, v5, v7
	ds_bpermute_b32 v7, v223, v5
	s_and_saveexec_b64 s[2:3], vcc
	s_cbranch_execz .LBB0_1332
	s_waitcnt lgkmcnt(0)
	v_add_f32_e32 v5, v5, v7
	v_div_scale_f32 v11, s[4:5], v5, v5, v2
	v_add3_u32 v6, s50, 30, v6
	v_rcp_f32_e32 v12, v11
	v_ashrrev_i32_e32 v7, 31, v6
	v_lshlrev_b64 v[6:7], 2, v[6:7]
	v_lshl_add_u64 v[8:9], s[42:43], 0, v[6:7]
	ds_add_rtn_u32 v10, v227, v243
	global_store_dword v[8:9], v230, off
	v_fma_f32 v8, -v11, v12, 1.0
	v_fmac_f32_e32 v12, v8, v12
	v_div_scale_f32 v8, vcc, v2, v5, v2
	v_mul_f32_e32 v9, v8, v12
	v_fma_f32 v13, -v11, v9, v8
	v_fmac_f32_e32 v9, v13, v12
	v_fma_f32 v8, -v11, v9, v8
	v_div_fmas_f32 v8, v8, v12, v9
	v_div_fixup_f32 v2, v8, v5, v2
	v_mul_f32_e32 v2, 0x40200000, v2
	v_lshl_add_u64 v[8:9], s[44:45], 0, v[6:7]
	v_lshl_add_u64 v[6:7], s[46:47], 0, v[6:7]
	global_store_dword v[8:9], v2, off
	s_waitcnt lgkmcnt(0)
	global_store_dword v[6:7], v10, off
.LBB0_1332:
	s_or_b64 exec, exec, s[2:3]
	v_add_u32_e32 v2, s81, v226
	ds_read_b32 v2, v2
	ds_read_b32 v5, v4 offset:17920
	s_waitcnt lgkmcnt(0)
	v_add_f32_e32 v2, v2, v5
	v_mul_f32_e32 v2, 0xbfb8aa3b, v2
	v_exp_f32_e32 v2, v2
	s_nop 0
	v_add_f32_e32 v2, 1.0, v2
	v_div_scale_f32 v5, s[2:3], v2, v2, 1.0
	v_rcp_f32_e32 v6, v5
	v_div_scale_f32 v7, vcc, 1.0, v2, 1.0
	s_mov_b32 s2, 0
	v_fma_f32 v8, -v5, v6, 1.0
	v_fmac_f32_e32 v6, v8, v6
	v_mul_f32_e32 v8, v7, v6
	v_fma_f32 v9, -v5, v8, v7
	v_fmac_f32_e32 v8, v9, v6
	v_fma_f32 v5, -v5, v8, v7
	v_div_fmas_f32 v5, v5, v6, v8
	v_div_fixup_f32 v2, v5, v2, 1.0
	v_add_f32_e32 v5, v3, v2
	ds_bpermute_b32 v6, v1, v5
	s_waitcnt lgkmcnt(0)
	v_max_f32_e32 v6, v6, v6
	v_max_f32_e32 v6, v5, v6
	ds_bpermute_b32 v7, v201, v6
	s_waitcnt lgkmcnt(0)
	v_max_f32_e32 v7, v7, v7
	v_max_f32_e32 v6, v6, v7
	ds_bpermute_b32 v7, v220, v6
	s_waitcnt lgkmcnt(0)
	v_max_f32_e32 v7, v7, v7
	v_max_f32_e32 v8, v6, v7
	v_cmp_eq_f32_e32 vcc, v5, v8
	s_nop 1
	v_lshrrev_b64 v[6:7], v200, vcc
	v_ffbl_b32_sdwa v6, v6 dst_sel:DWORD dst_unused:UNUSED_PAD src0_sel:BYTE_0
	v_add_u32_e32 v6, v6, v200
	v_cmp_ne_u32_e32 vcc, v230, v6
	s_nop 1
	v_cndmask_b32_e32 v6, v245, v5, vcc
	ds_bpermute_b32 v7, v1, v6
	s_waitcnt lgkmcnt(0)
	v_max_f32_e32 v7, v7, v7
	v_max_f32_e32 v6, v6, v7
	ds_bpermute_b32 v7, v201, v6
	s_waitcnt lgkmcnt(0)
	v_max_f32_e32 v7, v7, v7
	v_max_f32_e32 v6, v6, v7
	ds_bpermute_b32 v7, v220, v6
	s_waitcnt lgkmcnt(0)
	v_max_f32_e32 v7, v7, v7
	v_max_f32_e32 v6, v6, v7
	v_add_f32_e32 v6, v8, v6
	s_nop 0
	v_readlane_b32 s3, v6, 0
	v_readlane_b32 s4, v6, 8
	v_readlane_b32 s5, v6, 16
	v_cmp_eq_f32_e64 s[20:21], s3, v6
	v_cmp_gt_f32_e32 vcc, s3, v6
	v_cmp_gt_f32_e64 s[22:23], s4, v6
	v_cmp_eq_f32_e64 s[24:25], s4, v6
	v_cmp_gt_f32_e64 s[26:27], s5, v6
	v_cmp_eq_f32_e64 s[28:29], s5, v6
	s_and_b64 s[4:5], s[0:1], s[20:21]
	v_readlane_b32 s34, v6, 24
	s_and_b64 s[20:21], s[6:7], s[24:25]
	s_or_b64 s[4:5], vcc, s[4:5]
	v_readlane_b32 s40, v6, 32
	v_cmp_gt_f32_e64 s[30:31], s34, v6
	v_cmp_eq_f32_e64 s[34:35], s34, v6
	s_and_b64 s[24:25], s[8:9], s[28:29]
	v_cndmask_b32_e64 v7, 0, 1, s[4:5]
	s_or_b64 s[4:5], s[22:23], s[20:21]
	v_cmp_gt_f32_e64 s[36:37], s40, v6
	v_cmp_eq_f32_e64 s[40:41], s40, v6
	s_and_b64 s[28:29], s[10:11], s[34:35]
	v_cndmask_b32_e64 v8, 0, 1, s[4:5]
	s_or_b64 s[4:5], s[26:27], s[24:25]
	v_readlane_b32 s54, v6, 40
	s_and_b64 s[34:35], s[12:13], s[40:41]
	v_cndmask_b32_e64 v9, 0, 1, s[4:5]
	s_or_b64 s[4:5], s[30:31], s[28:29]
	v_cndmask_b32_e64 v10, 0, 1, s[4:5]
	s_or_b64 s[4:5], s[36:37], s[34:35]
	v_cmp_eq_f32_e64 s[20:21], s54, v6
	v_cndmask_b32_e64 v11, 0, 1, s[4:5]
	v_cmp_gt_f32_e32 vcc, s54, v6
	s_and_b64 s[4:5], s[14:15], s[20:21]
	v_readlane_b32 s3, v6, 48
	s_or_b64 s[4:5], vcc, s[4:5]
	v_cndmask_b32_e64 v12, 0, 1, s[4:5]
	v_cmp_eq_f32_e64 s[20:21], s3, v6
	v_cmp_gt_f32_e32 vcc, s3, v6
	s_and_b64 s[4:5], s[16:17], s[20:21]
	v_readlane_b32 s3, v6, 56
	s_or_b64 s[4:5], vcc, s[4:5]
	v_cndmask_b32_e64 v13, 0, 1, s[4:5]
	v_cmp_gt_f32_e32 vcc, s3, v6
	s_nop 1
	v_cndmask_b32_e64 v6, 0, 1, vcc
	v_add_u32_e32 v6, v8, v6
	v_add3_u32 v6, v6, v7, v9
	v_add3_u32 v6, v6, v10, v11
	v_add3_u32 v6, v6, v12, v13
	v_cmp_gt_u32_e32 vcc, 4, v6
	v_mov_b32_e32 v6, 0
	s_nop 0
	v_cndmask_b32_e32 v5, v245, v5, vcc
	v_ashrrev_i32_e32 v9, 31, v5
	v_sub_u32_e32 v8, 63, v230
	v_and_b32_e32 v9, 0x7fffffff, v9
	v_xor_b32_e32 v9, v5, v9
	s_nop 0
	v_readlane_b32 s23, v9, 0
	s_movk_i32 s22, 63
	v_readlane_b32 s21, v9, 1
	s_movk_i32 s20, 62
	v_cmp_gt_i64_e32 vcc, s[22:23], v[8:9]
	v_readlane_b32 s23, v9, 2
	s_movk_i32 s22, 61
	v_addc_co_u32_e32 v6, vcc, 0, v6, vcc
	v_cmp_gt_i64_e32 vcc, s[20:21], v[8:9]
	v_readlane_b32 s21, v9, 3
	s_movk_i32 s20, 60
	v_addc_co_u32_e32 v6, vcc, 0, v6, vcc
	v_cmp_gt_i64_e32 vcc, s[22:23], v[8:9]
	v_readlane_b32 s23, v9, 4
	s_movk_i32 s22, 59
	v_addc_co_u32_e32 v6, vcc, 0, v6, vcc
	v_cmp_gt_i64_e32 vcc, s[20:21], v[8:9]
	v_readlane_b32 s21, v9, 5
	s_movk_i32 s20, 58
	v_addc_co_u32_e32 v6, vcc, 0, v6, vcc
	v_cmp_gt_i64_e32 vcc, s[22:23], v[8:9]
	v_readlane_b32 s23, v9, 6
	s_movk_i32 s22, 57
	v_addc_co_u32_e32 v6, vcc, 0, v6, vcc
	v_cmp_gt_i64_e32 vcc, s[20:21], v[8:9]
	v_readlane_b32 s21, v9, 7
	s_movk_i32 s20, 56
	v_addc_co_u32_e32 v6, vcc, 0, v6, vcc
	v_cmp_gt_i64_e32 vcc, s[22:23], v[8:9]
	v_readlane_b32 s23, v9, 8
	s_movk_i32 s22, 55
	v_addc_co_u32_e32 v6, vcc, 0, v6, vcc
; __device__ __forceinline__ void phase_nrr(const Frame& F, const Args& a, int l, const bf16_t* XA, const float* g, const float* modl, unsigned char* XN8) {
;     ...
;             int rank = 0;
; #pragma unroll 8
;             for (int e2 = 0; e2 < 64; ++e2) { const float v = __int_as_float(__builtin_amdgcn_readlane(__float_as_int(val), e2)); rank += (v > val || (v == val && e2 < lane)) ? 1 : 0; }
	v_cmp_gt_i64_e32 vcc, s[20:21], v[8:9]
	v_readlane_b32 s21, v9, 9
	s_movk_i32 s20, 54
	v_addc_co_u32_e32 v6, vcc, 0, v6, vcc
	v_cmp_gt_i64_e32 vcc, s[22:23], v[8:9]
	v_readlane_b32 s23, v9, 10
	s_movk_i32 s22, 53
	v_addc_co_u32_e32 v6, vcc, 0, v6, vcc
	v_cmp_gt_i64_e32 vcc, s[20:21], v[8:9]
	v_readlane_b32 s21, v9, 11
	s_movk_i32 s20, 52
	v_addc_co_u32_e32 v6, vcc, 0, v6, vcc
	v_cmp_gt_i64_e32 vcc, s[22:23], v[8:9]
	v_readlane_b32 s23, v9, 12
	s_movk_i32 s22, 51
	v_addc_co_u32_e32 v6, vcc, 0, v6, vcc
	v_cmp_gt_i64_e32 vcc, s[20:21], v[8:9]
	v_readlane_b32 s21, v9, 13
	s_movk_i32 s20, 50
	v_addc_co_u32_e32 v6, vcc, 0, v6, vcc
	v_cmp_gt_i64_e32 vcc, s[22:23], v[8:9]
	v_readlane_b32 s23, v9, 14
	s_movk_i32 s22, 49
	v_addc_co_u32_e32 v6, vcc, 0, v6, vcc
	v_cmp_gt_i64_e32 vcc, s[20:21], v[8:9]
	v_readlane_b32 s21, v9, 15
	s_movk_i32 s20, 48
	v_addc_co_u32_e32 v6, vcc, 0, v6, vcc
	v_cmp_gt_i64_e32 vcc, s[22:23], v[8:9]
	v_readlane_b32 s23, v9, 16
	s_movk_i32 s22, 47
	v_addc_co_u32_e32 v6, vcc, 0, v6, vcc
	v_cmp_gt_i64_e32 vcc, s[20:21], v[8:9]
	v_readlane_b32 s21, v9, 17
	s_movk_i32 s20, 46
	v_addc_co_u32_e32 v6, vcc, 0, v6, vcc
	v_cmp_gt_i64_e32 vcc, s[22:23], v[8:9]
	v_readlane_b32 s23, v9, 18
	s_movk_i32 s22, 45
	v_addc_co_u32_e32 v6, vcc, 0, v6, vcc
	v_cmp_gt_i64_e32 vcc, s[20:21], v[8:9]
	v_readlane_b32 s21, v9, 19
	s_movk_i32 s20, 44
	v_addc_co_u32_e32 v6, vcc, 0, v6, vcc
	v_cmp_gt_i64_e32 vcc, s[22:23], v[8:9]
	v_readlane_b32 s23, v9, 20
	s_movk_i32 s22, 43
	v_addc_co_u32_e32 v6, vcc, 0, v6, vcc
	v_cmp_gt_i64_e32 vcc, s[20:21], v[8:9]
	v_readlane_b32 s21, v9, 21
	s_movk_i32 s20, 42
	v_addc_co_u32_e32 v6, vcc, 0, v6, vcc
	v_cmp_gt_i64_e32 vcc, s[22:23], v[8:9]
	v_readlane_b32 s23, v9, 22
	s_movk_i32 s22, 41
	v_addc_co_u32_e32 v6, vcc, 0, v6, vcc
	v_cmp_gt_i64_e32 vcc, s[20:21], v[8:9]
	v_readlane_b32 s21, v9, 23
	s_movk_i32 s20, 40
	v_addc_co_u32_e32 v6, vcc, 0, v6, vcc
	v_cmp_gt_i64_e32 vcc, s[22:23], v[8:9]
	v_readlane_b32 s23, v9, 24
	s_movk_i32 s22, 39
	v_addc_co_u32_e32 v6, vcc, 0, v6, vcc
	v_cmp_gt_i64_e32 vcc, s[20:21], v[8:9]
	v_readlane_b32 s21, v9, 25
	s_movk_i32 s20, 38
	v_addc_co_u32_e32 v6, vcc, 0, v6, vcc
	v_cmp_gt_i64_e32 vcc, s[22:23], v[8:9]
	v_readlane_b32 s23, v9, 26
	s_movk_i32 s22, 37
	v_addc_co_u32_e32 v6, vcc, 0, v6, vcc
	v_cmp_gt_i64_e32 vcc, s[20:21], v[8:9]
	v_readlane_b32 s21, v9, 27
	s_movk_i32 s20, 36
	v_addc_co_u32_e32 v6, vcc, 0, v6, vcc
	v_cmp_gt_i64_e32 vcc, s[22:23], v[8:9]
	v_readlane_b32 s23, v9, 28
	s_movk_i32 s22, 35
	v_addc_co_u32_e32 v6, vcc, 0, v6, vcc
	v_cmp_gt_i64_e32 vcc, s[20:21], v[8:9]
	v_readlane_b32 s21, v9, 29
	s_movk_i32 s20, 34
	v_addc_co_u32_e32 v6, vcc, 0, v6, vcc
	v_cmp_gt_i64_e32 vcc, s[22:23], v[8:9]
	v_readlane_b32 s23, v9, 30
	s_movk_i32 s22, 33
	v_addc_co_u32_e32 v6, vcc, 0, v6, vcc
	v_cmp_gt_i64_e32 vcc, s[20:21], v[8:9]
	v_readlane_b32 s21, v9, 31
	s_movk_i32 s20, 32
	v_addc_co_u32_e32 v6, vcc, 0, v6, vcc
	v_cmp_gt_i64_e32 vcc, s[22:23], v[8:9]
	v_readlane_b32 s23, v9, 32
	s_movk_i32 s22, 31
	v_addc_co_u32_e32 v6, vcc, 0, v6, vcc
	v_cmp_gt_i64_e32 vcc, s[20:21], v[8:9]
	v_readlane_b32 s21, v9, 33
	s_movk_i32 s20, 30
	v_addc_co_u32_e32 v6, vcc, 0, v6, vcc
	v_cmp_gt_i64_e32 vcc, s[22:23], v[8:9]
	v_readlane_b32 s23, v9, 34
	s_movk_i32 s22, 29
	v_addc_co_u32_e32 v6, vcc, 0, v6, vcc
	v_cmp_gt_i64_e32 vcc, s[20:21], v[8:9]
	v_readlane_b32 s21, v9, 35
	s_movk_i32 s20, 28
	v_addc_co_u32_e32 v6, vcc, 0, v6, vcc
	v_cmp_gt_i64_e32 vcc, s[22:23], v[8:9]
	v_readlane_b32 s23, v9, 36
	s_movk_i32 s22, 27
	v_addc_co_u32_e32 v6, vcc, 0, v6, vcc
	v_cmp_gt_i64_e32 vcc, s[20:21], v[8:9]
	v_readlane_b32 s21, v9, 37
	s_movk_i32 s20, 26
	v_addc_co_u32_e32 v6, vcc, 0, v6, vcc
	v_cmp_gt_i64_e32 vcc, s[22:23], v[8:9]
	v_readlane_b32 s23, v9, 38
	s_movk_i32 s22, 25
	v_addc_co_u32_e32 v6, vcc, 0, v6, vcc
	v_cmp_gt_i64_e32 vcc, s[20:21], v[8:9]
	v_readlane_b32 s21, v9, 39
	s_movk_i32 s20, 24
	v_addc_co_u32_e32 v6, vcc, 0, v6, vcc
	v_cmp_gt_i64_e32 vcc, s[22:23], v[8:9]
	v_readlane_b32 s23, v9, 40
	s_movk_i32 s22, 23
	v_addc_co_u32_e32 v6, vcc, 0, v6, vcc
	v_cmp_gt_i64_e32 vcc, s[20:21], v[8:9]
	v_readlane_b32 s21, v9, 41
	s_movk_i32 s20, 22
	v_addc_co_u32_e32 v6, vcc, 0, v6, vcc
	v_cmp_gt_i64_e32 vcc, s[22:23], v[8:9]
	v_readlane_b32 s23, v9, 42
	s_movk_i32 s22, 21
	v_addc_co_u32_e32 v6, vcc, 0, v6, vcc
	v_cmp_gt_i64_e32 vcc, s[20:21], v[8:9]
	v_readlane_b32 s21, v9, 43
	s_movk_i32 s20, 20
	v_addc_co_u32_e32 v6, vcc, 0, v6, vcc
	v_cmp_gt_i64_e32 vcc, s[22:23], v[8:9]
	v_readlane_b32 s23, v9, 44
	s_movk_i32 s22, 19
	v_addc_co_u32_e32 v6, vcc, 0, v6, vcc
	v_cmp_gt_i64_e32 vcc, s[20:21], v[8:9]
	v_readlane_b32 s21, v9, 45
	s_movk_i32 s20, 18
	v_addc_co_u32_e32 v6, vcc, 0, v6, vcc
	v_cmp_gt_i64_e32 vcc, s[22:23], v[8:9]
	v_readlane_b32 s23, v9, 46
	s_movk_i32 s22, 17
	v_addc_co_u32_e32 v6, vcc, 0, v6, vcc
	v_cmp_gt_i64_e32 vcc, s[20:21], v[8:9]
	v_readlane_b32 s21, v9, 47
	s_movk_i32 s20, 16
	v_addc_co_u32_e32 v6, vcc, 0, v6, vcc
	v_cmp_gt_i64_e32 vcc, s[22:23], v[8:9]
	v_readlane_b32 s23, v9, 48
	s_movk_i32 s22, 15
	v_addc_co_u32_e32 v6, vcc, 0, v6, vcc
	v_cmp_gt_i64_e32 vcc, s[20:21], v[8:9]
	v_readlane_b32 s21, v9, 49
	s_movk_i32 s20, 14
	v_addc_co_u32_e32 v6, vcc, 0, v6, vcc
	v_cmp_gt_i64_e32 vcc, s[22:23], v[8:9]
	v_readlane_b32 s23, v9, 50
	s_movk_i32 s22, 13
	v_addc_co_u32_e32 v6, vcc, 0, v6, vcc
	v_cmp_gt_i64_e32 vcc, s[20:21], v[8:9]
	v_readlane_b32 s21, v9, 51
	s_movk_i32 s20, 12
	v_addc_co_u32_e32 v6, vcc, 0, v6, vcc
	v_cmp_gt_i64_e32 vcc, s[22:23], v[8:9]
	v_readlane_b32 s23, v9, 52
	s_movk_i32 s22, 11
	v_addc_co_u32_e32 v6, vcc, 0, v6, vcc
	v_cmp_gt_i64_e32 vcc, s[20:21], v[8:9]
; __device__ __forceinline__ void phase_nrr(const Frame& F, const Args& a, int l, const bf16_t* XA, const float* g, const float* modl, unsigned char* XN8) {
;     ...
;         for (int i = 0; i < 8; ++i) { const int t = tb + i;
;             const float lg = Pl[(w * 8 + i) * NE + lane] + Pl[(64 + w * 8 + i) * NE + lane]; const float sc = 1.f / (1.f + __expf(-lg)); const float bb = sc + bias;
;             float m1 = bb; m1 = fmaxf(m1, __shfl_xor(m1, 1)); m1 = fmaxf(m1, __shfl_xor(m1, 2)); m1 = fmaxf(m1, __shfl_xor(m1, 4));
;             const unsigned long long eq = __ballot(bb == m1); const int gbase = lane & ~7; const unsigned grpmask = (unsigned)((eq >> gbase) & 0xffull);
;             const int first = gbase + __builtin_ctz(grpmask);
;             float m2 = (lane == first) ? -INFINITY : bb; m2 = fmaxf(m2, __shfl_xor(m2, 1)); m2 = fmaxf(m2, __shfl_xor(m2, 2)); m2 = fmaxf(m2, __shfl_xor(m2, 4));
;             const float gsum = m1 + m2; const int gq = lane >> 3;
;             int grank = 0;
; #pragma unroll
;             for (int g2 = 0; g2 < 8; ++g2) { const float v = __int_as_float(__builtin_amdgcn_readlane(__float_as_int(gsum), g2 * 8)); grank += (v > gsum || (v == gsum && g2 < gq)) ? 1 : 0; }
;             const bool keep = grank < 4; const float val = keep ? bb : -INFINITY;
;             int rank = 0;
; #pragma unroll 8
;             for (int e2 = 0; e2 < 64; ++e2) { const float v = __int_as_float(__builtin_amdgcn_readlane(__float_as_int(val), e2)); rank += (v > val || (v == val && e2 < lane)) ? 1 : 0; }
;             const bool sel = rank < TOPK;
;             const float ssum = wave_sum(sel ? sc : 0.f);
;             if (sel) { const int p = atomicAdd((int*)(hist + lane), 1); top_e[t * TOPK + rank] = lane; gate[t * TOPK + rank] = sc / ssum * 2.5f; lpos[t * TOPK + rank] = p; }
	v_readlane_b32 s21, v9, 53
	s_movk_i32 s20, 10
	v_addc_co_u32_e32 v6, vcc, 0, v6, vcc
	v_cmp_gt_i64_e32 vcc, s[22:23], v[8:9]
	v_readlane_b32 s23, v9, 54
	s_movk_i32 s22, 9
	v_addc_co_u32_e32 v6, vcc, 0, v6, vcc
	v_cmp_gt_i64_e32 vcc, s[20:21], v[8:9]
	v_readlane_b32 s21, v9, 55
	s_movk_i32 s20, 8
	v_addc_co_u32_e32 v6, vcc, 0, v6, vcc
	v_cmp_gt_i64_e32 vcc, s[22:23], v[8:9]
	v_readlane_b32 s23, v9, 56
	s_movk_i32 s22, 7
	v_addc_co_u32_e32 v6, vcc, 0, v6, vcc
	v_cmp_gt_i64_e32 vcc, s[20:21], v[8:9]
	v_readlane_b32 s21, v9, 57
	s_movk_i32 s20, 6
	v_addc_co_u32_e32 v6, vcc, 0, v6, vcc
	v_cmp_gt_i64_e32 vcc, s[22:23], v[8:9]
	v_readlane_b32 s23, v9, 58
	s_movk_i32 s22, 5
	v_addc_co_u32_e32 v6, vcc, 0, v6, vcc
	v_cmp_gt_i64_e32 vcc, s[20:21], v[8:9]
	v_readlane_b32 s21, v9, 59
	s_movk_i32 s20, 4
	v_addc_co_u32_e32 v6, vcc, 0, v6, vcc
	v_cmp_gt_i64_e32 vcc, s[22:23], v[8:9]
	v_readlane_b32 s23, v9, 60
	s_movk_i32 s22, 3
	v_addc_co_u32_e32 v6, vcc, 0, v6, vcc
	v_cmp_gt_i64_e32 vcc, s[20:21], v[8:9]
	v_readlane_b32 s21, v9, 61
	s_movk_i32 s20, 2
	v_addc_co_u32_e32 v6, vcc, 0, v6, vcc
	v_cmp_gt_i64_e32 vcc, s[22:23], v[8:9]
	v_readlane_b32 s23, v9, 62
	s_movk_i32 s22, 1
	v_addc_co_u32_e32 v6, vcc, 0, v6, vcc
	v_cmp_gt_i64_e32 vcc, s[20:21], v[8:9]
	v_readlane_b32 s21, v9, 63
	s_movk_i32 s20, 0
	v_addc_co_u32_e32 v6, vcc, 0, v6, vcc
	v_cmp_gt_i64_e32 vcc, s[22:23], v[8:9]
	s_nop 1
	v_addc_co_u32_e32 v6, vcc, 0, v6, vcc
	v_cmp_gt_i64_e32 vcc, s[20:21], v[8:9]
	s_nop 1
	v_addc_co_u32_e32 v6, vcc, 0, v6, vcc
	v_cmp_gt_u32_e32 vcc, 6, v6
	s_nop 1
	v_cndmask_b32_e32 v5, 0, v2, vcc
	ds_bpermute_b32 v7, v1, v5
	s_waitcnt lgkmcnt(0)
	v_add_f32_e32 v5, v5, v7
	ds_bpermute_b32 v7, v201, v5
	s_waitcnt lgkmcnt(0)
	v_add_f32_e32 v5, v5, v7
	ds_bpermute_b32 v7, v220, v5
	s_waitcnt lgkmcnt(0)
	v_add_f32_e32 v5, v5, v7
	ds_bpermute_b32 v7, v221, v5
	s_waitcnt lgkmcnt(0)
	v_add_f32_e32 v5, v5, v7
	ds_bpermute_b32 v7, v222, v5
	s_waitcnt lgkmcnt(0)
	v_add_f32_e32 v5, v5, v7
	ds_bpermute_b32 v7, v223, v5
	s_and_saveexec_b64 s[2:3], vcc
	s_cbranch_execz .LBB0_1336
	s_waitcnt lgkmcnt(0)
	v_add_f32_e32 v5, v5, v7
	v_div_scale_f32 v11, s[4:5], v5, v5, v2
	v_add3_u32 v6, s50, 36, v6
	v_rcp_f32_e32 v12, v11
	v_ashrrev_i32_e32 v7, 31, v6
	v_lshlrev_b64 v[6:7], 2, v[6:7]
	v_lshl_add_u64 v[8:9], s[42:43], 0, v[6:7]
	ds_add_rtn_u32 v10, v227, v243
	global_store_dword v[8:9], v230, off
	v_fma_f32 v8, -v11, v12, 1.0
	v_fmac_f32_e32 v12, v8, v12
	v_div_scale_f32 v8, vcc, v2, v5, v2
	v_mul_f32_e32 v9, v8, v12
	v_fma_f32 v13, -v11, v9, v8
	v_fmac_f32_e32 v9, v13, v12
	v_fma_f32 v8, -v11, v9, v8
	v_div_fmas_f32 v8, v8, v12, v9
	v_div_fixup_f32 v2, v8, v5, v2
	v_mul_f32_e32 v2, 0x40200000, v2
	v_lshl_add_u64 v[8:9], s[44:45], 0, v[6:7]
	v_lshl_add_u64 v[6:7], s[46:47], 0, v[6:7]
	global_store_dword v[8:9], v2, off
	s_waitcnt lgkmcnt(0)
	global_store_dword v[6:7], v10, off
.LBB0_1336:
	s_or_b64 exec, exec, s[2:3]
	v_add_u32_e32 v2, s82, v226
	ds_read_b32 v2, v2
	ds_read_b32 v4, v4 offset:18176
	s_waitcnt lgkmcnt(0)
	v_add_f32_e32 v2, v2, v4
	v_mul_f32_e32 v2, 0xbfb8aa3b, v2
	v_exp_f32_e32 v2, v2
	s_nop 0
	v_add_f32_e32 v2, 1.0, v2
	v_div_scale_f32 v4, s[2:3], v2, v2, 1.0
	v_rcp_f32_e32 v5, v4
	v_div_scale_f32 v6, vcc, 1.0, v2, 1.0
	s_mov_b32 s2, 0
	v_fma_f32 v7, -v4, v5, 1.0
	v_fmac_f32_e32 v5, v7, v5
	v_mul_f32_e32 v7, v6, v5
	v_fma_f32 v8, -v4, v7, v6
	v_fmac_f32_e32 v7, v8, v5
	v_fma_f32 v4, -v4, v7, v6
	v_div_fmas_f32 v4, v4, v5, v7
	v_div_fixup_f32 v2, v4, v2, 1.0
	v_add_f32_e32 v3, v3, v2
	ds_bpermute_b32 v4, v1, v3
	s_waitcnt lgkmcnt(0)
	v_max_f32_e32 v4, v4, v4
	v_max_f32_e32 v4, v3, v4
	ds_bpermute_b32 v5, v201, v4
	s_waitcnt lgkmcnt(0)
	v_max_f32_e32 v5, v5, v5
	v_max_f32_e32 v4, v4, v5
	ds_bpermute_b32 v5, v220, v4
	s_waitcnt lgkmcnt(0)
	v_max_f32_e32 v5, v5, v5
	v_max_f32_e32 v6, v4, v5
	v_cmp_eq_f32_e32 vcc, v3, v6
	s_nop 1
	v_lshrrev_b64 v[4:5], v200, vcc
	v_ffbl_b32_sdwa v4, v4 dst_sel:DWORD dst_unused:UNUSED_PAD src0_sel:BYTE_0
	v_add_u32_e32 v4, v4, v200
	v_cmp_ne_u32_e32 vcc, v230, v4
	s_nop 1
	v_cndmask_b32_e32 v4, v245, v3, vcc
	ds_bpermute_b32 v5, v1, v4
	s_waitcnt lgkmcnt(0)
	v_max_f32_e32 v5, v5, v5
	v_max_f32_e32 v4, v4, v5
	ds_bpermute_b32 v5, v201, v4
	s_waitcnt lgkmcnt(0)
	v_max_f32_e32 v5, v5, v5
	v_max_f32_e32 v4, v4, v5
	ds_bpermute_b32 v5, v220, v4
	s_waitcnt lgkmcnt(0)
; __device__ __forceinline__ void phase_nrr(const Frame& F, const Args& a, int l, const bf16_t* XA, const float* g, const float* modl, unsigned char* XN8) {
;     ...
;             float m1 = bb; m1 = fmaxf(m1, __shfl_xor(m1, 1)); m1 = fmaxf(m1, __shfl_xor(m1, 2)); m1 = fmaxf(m1, __shfl_xor(m1, 4));
;             const unsigned long long eq = __ballot(bb == m1); const int gbase = lane & ~7; const unsigned grpmask = (unsigned)((eq >> gbase) & 0xffull);
;             const int first = gbase + __builtin_ctz(grpmask);
;             float m2 = (lane == first) ? -INFINITY : bb; m2 = fmaxf(m2, __shfl_xor(m2, 1)); m2 = fmaxf(m2, __shfl_xor(m2, 2)); m2 = fmaxf(m2, __shfl_xor(m2, 4));
;             const float gsum = m1 + m2; const int gq = lane >> 3;
;             int grank = 0;
; #pragma unroll
;             for (int g2 = 0; g2 < 8; ++g2) { const float v = __int_as_float(__builtin_amdgcn_readlane(__float_as_int(gsum), g2 * 8)); grank += (v > gsum || (v == gsum && g2 < gq)) ? 1 : 0; }
;             const bool keep = grank < 4; const float val = keep ? bb : -INFINITY;
;             int rank = 0;
; #pragma unroll 8
;             for (int e2 = 0; e2 < 64; ++e2) { const float v = __int_as_float(__builtin_amdgcn_readlane(__float_as_int(val), e2)); rank += (v > val || (v == val && e2 < lane)) ? 1 : 0; }
	v_max_f32_e32 v5, v5, v5
	v_max_f32_e32 v4, v4, v5
	v_add_f32_e32 v4, v6, v4
	s_nop 0
	v_readlane_b32 s3, v4, 0
	v_readlane_b32 s4, v4, 8
	v_readlane_b32 s5, v4, 16
	v_cmp_eq_f32_e64 s[20:21], s3, v4
	v_cmp_gt_f32_e32 vcc, s3, v4
	v_cmp_gt_f32_e64 s[22:23], s4, v4
	v_cmp_eq_f32_e64 s[24:25], s4, v4
	v_cmp_gt_f32_e64 s[26:27], s5, v4
	v_cmp_eq_f32_e64 s[28:29], s5, v4
	s_and_b64 s[4:5], s[0:1], s[20:21]
	v_readlane_b32 s34, v4, 24
	s_and_b64 s[20:21], s[6:7], s[24:25]
	s_or_b64 s[4:5], vcc, s[4:5]
	v_readlane_b32 s40, v4, 32
	v_cmp_gt_f32_e64 s[30:31], s34, v4
	v_cmp_eq_f32_e64 s[34:35], s34, v4
	s_and_b64 s[24:25], s[8:9], s[28:29]
	v_cndmask_b32_e64 v5, 0, 1, s[4:5]
	s_or_b64 s[4:5], s[22:23], s[20:21]
	v_cmp_gt_f32_e64 s[36:37], s40, v4
	v_cmp_eq_f32_e64 s[40:41], s40, v4
	s_and_b64 s[28:29], s[10:11], s[34:35]
	v_cndmask_b32_e64 v6, 0, 1, s[4:5]
	s_or_b64 s[4:5], s[26:27], s[24:25]
	v_readlane_b32 s54, v4, 40
	s_and_b64 s[34:35], s[12:13], s[40:41]
	v_cndmask_b32_e64 v7, 0, 1, s[4:5]
	s_or_b64 s[4:5], s[30:31], s[28:29]
	v_cndmask_b32_e64 v8, 0, 1, s[4:5]
	s_or_b64 s[4:5], s[36:37], s[34:35]
	v_cmp_eq_f32_e64 s[20:21], s54, v4
	v_cndmask_b32_e64 v9, 0, 1, s[4:5]
	v_cmp_gt_f32_e32 vcc, s54, v4
	s_and_b64 s[4:5], s[14:15], s[20:21]
	v_readlane_b32 s3, v4, 48
	s_or_b64 s[4:5], vcc, s[4:5]
	v_cndmask_b32_e64 v10, 0, 1, s[4:5]
	v_cmp_eq_f32_e64 s[20:21], s3, v4
	v_cmp_gt_f32_e32 vcc, s3, v4
	s_and_b64 s[4:5], s[16:17], s[20:21]
	v_readlane_b32 s3, v4, 56
	s_or_b64 s[4:5], vcc, s[4:5]
	v_cndmask_b32_e64 v11, 0, 1, s[4:5]
	v_cmp_gt_f32_e32 vcc, s3, v4
	s_nop 1
	v_cndmask_b32_e64 v4, 0, 1, vcc
	v_add_u32_e32 v4, v6, v4
	v_add3_u32 v4, v4, v5, v7
	v_add3_u32 v4, v4, v8, v9
	v_add3_u32 v4, v4, v10, v11
	v_cmp_gt_u32_e32 vcc, 4, v4
	v_mov_b32_e32 v4, 0
	s_nop 0
	v_cndmask_b32_e32 v3, v245, v3, vcc
	v_ashrrev_i32_e32 v9, 31, v3
	v_sub_u32_e32 v8, 63, v230
	v_and_b32_e32 v9, 0x7fffffff, v9
	v_xor_b32_e32 v9, v3, v9
	s_nop 0
	v_readlane_b32 s23, v9, 0
	s_movk_i32 s22, 63
	v_readlane_b32 s21, v9, 1
	s_movk_i32 s20, 62
	v_cmp_gt_i64_e32 vcc, s[22:23], v[8:9]
	v_readlane_b32 s23, v9, 2
	s_movk_i32 s22, 61
	v_addc_co_u32_e32 v4, vcc, 0, v4, vcc
	v_cmp_gt_i64_e32 vcc, s[20:21], v[8:9]
	v_readlane_b32 s21, v9, 3
	s_movk_i32 s20, 60
	v_addc_co_u32_e32 v4, vcc, 0, v4, vcc
	v_cmp_gt_i64_e32 vcc, s[22:23], v[8:9]
	v_readlane_b32 s23, v9, 4
	s_movk_i32 s22, 59
	v_addc_co_u32_e32 v4, vcc, 0, v4, vcc
	v_cmp_gt_i64_e32 vcc, s[20:21], v[8:9]
	v_readlane_b32 s21, v9, 5
	s_movk_i32 s20, 58
	v_addc_co_u32_e32 v4, vcc, 0, v4, vcc
	v_cmp_gt_i64_e32 vcc, s[22:23], v[8:9]
	v_readlane_b32 s23, v9, 6
	s_movk_i32 s22, 57
	v_addc_co_u32_e32 v4, vcc, 0, v4, vcc
	v_cmp_gt_i64_e32 vcc, s[20:21], v[8:9]
	v_readlane_b32 s21, v9, 7
	s_movk_i32 s20, 56
	v_addc_co_u32_e32 v4, vcc, 0, v4, vcc
	v_cmp_gt_i64_e32 vcc, s[22:23], v[8:9]
	v_readlane_b32 s23, v9, 8
	s_movk_i32 s22, 55
	v_addc_co_u32_e32 v4, vcc, 0, v4, vcc
	v_cmp_gt_i64_e32 vcc, s[20:21], v[8:9]
	v_readlane_b32 s21, v9, 9
	s_movk_i32 s20, 54
	v_addc_co_u32_e32 v4, vcc, 0, v4, vcc
	v_cmp_gt_i64_e32 vcc, s[22:23], v[8:9]
	v_readlane_b32 s23, v9, 10
	s_movk_i32 s22, 53
	v_addc_co_u32_e32 v4, vcc, 0, v4, vcc
	v_cmp_gt_i64_e32 vcc, s[20:21], v[8:9]
	v_readlane_b32 s21, v9, 11
	s_movk_i32 s20, 52
	v_addc_co_u32_e32 v4, vcc, 0, v4, vcc
	v_cmp_gt_i64_e32 vcc, s[22:23], v[8:9]
	v_readlane_b32 s23, v9, 12
	s_movk_i32 s22, 51
	v_addc_co_u32_e32 v4, vcc, 0, v4, vcc
	v_cmp_gt_i64_e32 vcc, s[20:21], v[8:9]
	v_readlane_b32 s21, v9, 13
	s_movk_i32 s20, 50
	v_addc_co_u32_e32 v4, vcc, 0, v4, vcc
	v_cmp_gt_i64_e32 vcc, s[22:23], v[8:9]
	v_readlane_b32 s23, v9, 14
	s_movk_i32 s22, 49
	v_addc_co_u32_e32 v4, vcc, 0, v4, vcc
	v_cmp_gt_i64_e32 vcc, s[20:21], v[8:9]
	v_readlane_b32 s21, v9, 15
	s_movk_i32 s20, 48
	v_addc_co_u32_e32 v4, vcc, 0, v4, vcc
	v_cmp_gt_i64_e32 vcc, s[22:23], v[8:9]
	v_readlane_b32 s23, v9, 16
	s_movk_i32 s22, 47
	v_addc_co_u32_e32 v4, vcc, 0, v4, vcc
	v_cmp_gt_i64_e32 vcc, s[20:21], v[8:9]
	v_readlane_b32 s21, v9, 17
	s_movk_i32 s20, 46
	v_addc_co_u32_e32 v4, vcc, 0, v4, vcc
	v_cmp_gt_i64_e32 vcc, s[22:23], v[8:9]
	v_readlane_b32 s23, v9, 18
	s_movk_i32 s22, 45
	v_addc_co_u32_e32 v4, vcc, 0, v4, vcc
	v_cmp_gt_i64_e32 vcc, s[20:21], v[8:9]
	v_readlane_b32 s21, v9, 19
	s_movk_i32 s20, 44
	v_addc_co_u32_e32 v4, vcc, 0, v4, vcc
	v_cmp_gt_i64_e32 vcc, s[22:23], v[8:9]
	v_readlane_b32 s23, v9, 20
	s_movk_i32 s22, 43
	v_addc_co_u32_e32 v4, vcc, 0, v4, vcc
	v_cmp_gt_i64_e32 vcc, s[20:21], v[8:9]
	v_readlane_b32 s21, v9, 21
	s_movk_i32 s20, 42
	v_addc_co_u32_e32 v4, vcc, 0, v4, vcc
	v_cmp_gt_i64_e32 vcc, s[22:23], v[8:9]
	v_readlane_b32 s23, v9, 22
	s_movk_i32 s22, 41
	v_addc_co_u32_e32 v4, vcc, 0, v4, vcc
	v_cmp_gt_i64_e32 vcc, s[20:21], v[8:9]
	v_readlane_b32 s21, v9, 23
	s_movk_i32 s20, 40
	v_addc_co_u32_e32 v4, vcc, 0, v4, vcc
	v_cmp_gt_i64_e32 vcc, s[22:23], v[8:9]
	v_readlane_b32 s23, v9, 24
	s_movk_i32 s22, 39
	v_addc_co_u32_e32 v4, vcc, 0, v4, vcc
	v_cmp_gt_i64_e32 vcc, s[20:21], v[8:9]
	v_readlane_b32 s21, v9, 25
	s_movk_i32 s20, 38
	v_addc_co_u32_e32 v4, vcc, 0, v4, vcc
	v_cmp_gt_i64_e32 vcc, s[22:23], v[8:9]
	v_readlane_b32 s23, v9, 26
	s_movk_i32 s22, 37
	v_addc_co_u32_e32 v4, vcc, 0, v4, vcc
	v_cmp_gt_i64_e32 vcc, s[20:21], v[8:9]
	v_readlane_b32 s21, v9, 27
	s_movk_i32 s20, 36
	v_addc_co_u32_e32 v4, vcc, 0, v4, vcc
	v_cmp_gt_i64_e32 vcc, s[22:23], v[8:9]
	v_readlane_b32 s23, v9, 28
	s_movk_i32 s22, 35
	v_addc_co_u32_e32 v4, vcc, 0, v4, vcc
	v_cmp_gt_i64_e32 vcc, s[20:21], v[8:9]
	v_readlane_b32 s21, v9, 29
	s_movk_i32 s20, 34
	v_addc_co_u32_e32 v4, vcc, 0, v4, vcc
	v_cmp_gt_i64_e32 vcc, s[22:23], v[8:9]
; __device__ __forceinline__ void phase_nrr(const Frame& F, const Args& a, int l, const bf16_t* XA, const float* g, const float* modl, unsigned char* XN8) {
;     ...
;             int rank = 0;
; #pragma unroll 8
;             for (int e2 = 0; e2 < 64; ++e2) { const float v = __int_as_float(__builtin_amdgcn_readlane(__float_as_int(val), e2)); rank += (v > val || (v == val && e2 < lane)) ? 1 : 0; }
;             const bool sel = rank < TOPK;
;             const float ssum = wave_sum(sel ? sc : 0.f);
;             if (sel) { const int p = atomicAdd((int*)(hist + lane), 1); top_e[t * TOPK + rank] = lane; gate[t * TOPK + rank] = sc / ssum * 2.5f; lpos[t * TOPK + rank] = p; }
	v_readlane_b32 s23, v9, 30
	s_movk_i32 s22, 33
	v_addc_co_u32_e32 v4, vcc, 0, v4, vcc
	v_cmp_gt_i64_e32 vcc, s[20:21], v[8:9]
	v_readlane_b32 s21, v9, 31
	s_movk_i32 s20, 32
	v_addc_co_u32_e32 v4, vcc, 0, v4, vcc
	v_cmp_gt_i64_e32 vcc, s[22:23], v[8:9]
	v_readlane_b32 s23, v9, 32
	s_movk_i32 s22, 31
	v_addc_co_u32_e32 v4, vcc, 0, v4, vcc
	v_cmp_gt_i64_e32 vcc, s[20:21], v[8:9]
	v_readlane_b32 s21, v9, 33
	s_movk_i32 s20, 30
	v_addc_co_u32_e32 v4, vcc, 0, v4, vcc
	v_cmp_gt_i64_e32 vcc, s[22:23], v[8:9]
	v_readlane_b32 s23, v9, 34
	s_movk_i32 s22, 29
	v_addc_co_u32_e32 v4, vcc, 0, v4, vcc
	v_cmp_gt_i64_e32 vcc, s[20:21], v[8:9]
	v_readlane_b32 s21, v9, 35
	s_movk_i32 s20, 28
	v_addc_co_u32_e32 v4, vcc, 0, v4, vcc
	v_cmp_gt_i64_e32 vcc, s[22:23], v[8:9]
	v_readlane_b32 s23, v9, 36
	s_movk_i32 s22, 27
	v_addc_co_u32_e32 v4, vcc, 0, v4, vcc
	v_cmp_gt_i64_e32 vcc, s[20:21], v[8:9]
	v_readlane_b32 s21, v9, 37
	s_movk_i32 s20, 26
	v_addc_co_u32_e32 v4, vcc, 0, v4, vcc
	v_cmp_gt_i64_e32 vcc, s[22:23], v[8:9]
	v_readlane_b32 s23, v9, 38
	s_movk_i32 s22, 25
	v_addc_co_u32_e32 v4, vcc, 0, v4, vcc
	v_cmp_gt_i64_e32 vcc, s[20:21], v[8:9]
	v_readlane_b32 s21, v9, 39
	s_movk_i32 s20, 24
	v_addc_co_u32_e32 v4, vcc, 0, v4, vcc
	v_cmp_gt_i64_e32 vcc, s[22:23], v[8:9]
	v_readlane_b32 s23, v9, 40
	s_movk_i32 s22, 23
	v_addc_co_u32_e32 v4, vcc, 0, v4, vcc
	v_cmp_gt_i64_e32 vcc, s[20:21], v[8:9]
	v_readlane_b32 s21, v9, 41
	s_movk_i32 s20, 22
	v_addc_co_u32_e32 v4, vcc, 0, v4, vcc
	v_cmp_gt_i64_e32 vcc, s[22:23], v[8:9]
	v_readlane_b32 s23, v9, 42
	s_movk_i32 s22, 21
	v_addc_co_u32_e32 v4, vcc, 0, v4, vcc
	v_cmp_gt_i64_e32 vcc, s[20:21], v[8:9]
	v_readlane_b32 s21, v9, 43
	s_movk_i32 s20, 20
	v_addc_co_u32_e32 v4, vcc, 0, v4, vcc
	v_cmp_gt_i64_e32 vcc, s[22:23], v[8:9]
	v_readlane_b32 s23, v9, 44
	s_movk_i32 s22, 19
	v_addc_co_u32_e32 v4, vcc, 0, v4, vcc
	v_cmp_gt_i64_e32 vcc, s[20:21], v[8:9]
	v_readlane_b32 s21, v9, 45
	s_movk_i32 s20, 18
	v_addc_co_u32_e32 v4, vcc, 0, v4, vcc
	v_cmp_gt_i64_e32 vcc, s[22:23], v[8:9]
	v_readlane_b32 s23, v9, 46
	s_movk_i32 s22, 17
	v_addc_co_u32_e32 v4, vcc, 0, v4, vcc
	v_cmp_gt_i64_e32 vcc, s[20:21], v[8:9]
	v_readlane_b32 s21, v9, 47
	s_movk_i32 s20, 16
	v_addc_co_u32_e32 v4, vcc, 0, v4, vcc
	v_cmp_gt_i64_e32 vcc, s[22:23], v[8:9]
	v_readlane_b32 s23, v9, 48
	s_movk_i32 s22, 15
	v_addc_co_u32_e32 v4, vcc, 0, v4, vcc
	v_cmp_gt_i64_e32 vcc, s[20:21], v[8:9]
	v_readlane_b32 s21, v9, 49
	s_movk_i32 s20, 14
	v_addc_co_u32_e32 v4, vcc, 0, v4, vcc
	v_cmp_gt_i64_e32 vcc, s[22:23], v[8:9]
	v_readlane_b32 s23, v9, 50
	s_movk_i32 s22, 13
	v_addc_co_u32_e32 v4, vcc, 0, v4, vcc
	v_cmp_gt_i64_e32 vcc, s[20:21], v[8:9]
	v_readlane_b32 s21, v9, 51
	s_movk_i32 s20, 12
	v_addc_co_u32_e32 v4, vcc, 0, v4, vcc
	v_cmp_gt_i64_e32 vcc, s[22:23], v[8:9]
	v_readlane_b32 s23, v9, 52
	s_movk_i32 s22, 11
	v_addc_co_u32_e32 v4, vcc, 0, v4, vcc
	v_cmp_gt_i64_e32 vcc, s[20:21], v[8:9]
	v_readlane_b32 s21, v9, 53
	s_movk_i32 s20, 10
	v_addc_co_u32_e32 v4, vcc, 0, v4, vcc
	v_cmp_gt_i64_e32 vcc, s[22:23], v[8:9]
	v_readlane_b32 s23, v9, 54
	s_movk_i32 s22, 9
	v_addc_co_u32_e32 v4, vcc, 0, v4, vcc
	v_cmp_gt_i64_e32 vcc, s[20:21], v[8:9]
	v_readlane_b32 s21, v9, 55
	s_movk_i32 s20, 8
	v_addc_co_u32_e32 v4, vcc, 0, v4, vcc
	v_cmp_gt_i64_e32 vcc, s[22:23], v[8:9]
	v_readlane_b32 s23, v9, 56
	s_movk_i32 s22, 7
	v_addc_co_u32_e32 v4, vcc, 0, v4, vcc
	v_cmp_gt_i64_e32 vcc, s[20:21], v[8:9]
	v_readlane_b32 s21, v9, 57
	s_movk_i32 s20, 6
	v_addc_co_u32_e32 v4, vcc, 0, v4, vcc
	v_cmp_gt_i64_e32 vcc, s[22:23], v[8:9]
	v_readlane_b32 s23, v9, 58
	s_movk_i32 s22, 5
	v_addc_co_u32_e32 v4, vcc, 0, v4, vcc
	v_cmp_gt_i64_e32 vcc, s[20:21], v[8:9]
	v_readlane_b32 s21, v9, 59
	s_movk_i32 s20, 4
	v_addc_co_u32_e32 v4, vcc, 0, v4, vcc
	v_cmp_gt_i64_e32 vcc, s[22:23], v[8:9]
	v_readlane_b32 s23, v9, 60
	s_movk_i32 s22, 3
	v_addc_co_u32_e32 v4, vcc, 0, v4, vcc
	v_cmp_gt_i64_e32 vcc, s[20:21], v[8:9]
	v_readlane_b32 s21, v9, 61
	s_movk_i32 s20, 2
	v_addc_co_u32_e32 v4, vcc, 0, v4, vcc
	v_cmp_gt_i64_e32 vcc, s[22:23], v[8:9]
	v_readlane_b32 s23, v9, 62
	s_movk_i32 s22, 1
	v_addc_co_u32_e32 v4, vcc, 0, v4, vcc
	v_cmp_gt_i64_e32 vcc, s[20:21], v[8:9]
	v_readlane_b32 s21, v9, 63
	s_movk_i32 s20, 0
	v_addc_co_u32_e32 v4, vcc, 0, v4, vcc
	v_cmp_gt_i64_e32 vcc, s[22:23], v[8:9]
	s_nop 1
	v_addc_co_u32_e32 v4, vcc, 0, v4, vcc
	v_cmp_gt_i64_e32 vcc, s[20:21], v[8:9]
	s_nop 1
	v_addc_co_u32_e32 v4, vcc, 0, v4, vcc
	v_cmp_gt_u32_e32 vcc, 6, v4
	s_nop 1
	v_cndmask_b32_e32 v3, 0, v2, vcc
	ds_bpermute_b32 v5, v1, v3
	s_waitcnt lgkmcnt(0)
	v_add_f32_e32 v3, v3, v5
	ds_bpermute_b32 v5, v201, v3
	s_waitcnt lgkmcnt(0)
	v_add_f32_e32 v3, v3, v5
	ds_bpermute_b32 v5, v220, v3
	s_waitcnt lgkmcnt(0)
	v_add_f32_e32 v3, v3, v5
	ds_bpermute_b32 v5, v221, v3
	s_waitcnt lgkmcnt(0)
	v_add_f32_e32 v3, v3, v5
	ds_bpermute_b32 v5, v222, v3
	s_waitcnt lgkmcnt(0)
	v_add_f32_e32 v3, v3, v5
	ds_bpermute_b32 v5, v223, v3
	s_and_saveexec_b64 s[2:3], vcc
	s_cbranch_execz .LBB0_1340
	s_waitcnt lgkmcnt(0)
	v_add_f32_e32 v3, v3, v5
	v_div_scale_f32 v9, s[4:5], v3, v3, v2
	v_add3_u32 v4, s50, 42, v4
	v_rcp_f32_e32 v10, v9
	v_ashrrev_i32_e32 v5, 31, v4
	v_lshlrev_b64 v[4:5], 2, v[4:5]
	v_lshl_add_u64 v[6:7], s[42:43], 0, v[4:5]
	ds_add_rtn_u32 v8, v227, v243
	global_store_dword v[6:7], v230, off
	v_fma_f32 v6, -v9, v10, 1.0
	v_fmac_f32_e32 v10, v6, v10
	v_div_scale_f32 v6, vcc, v2, v3, v2
	v_mul_f32_e32 v7, v6, v10
	v_fma_f32 v11, -v9, v7, v6
	v_fmac_f32_e32 v7, v11, v10
	v_fma_f32 v6, -v9, v7, v6
	v_div_fmas_f32 v6, v6, v10, v7
	v_div_fixup_f32 v2, v6, v3, v2
	v_mul_f32_e32 v6, 0x40200000, v2
	v_lshl_add_u64 v[2:3], s[44:45], 0, v[4:5]
	global_store_dword v[2:3], v6, off
	v_lshl_add_u64 v[2:3], s[46:47], 0, v[4:5]
	s_waitcnt lgkmcnt(0)
	global_store_dword v[2:3], v8, off
